# GEMM K-loops: in every load segment the LDS-DMA loads and their scalar setup are issued before the ds_read_b128 block (was after)
# speedup vs baseline: 1.0056x; 1.0056x over previous
; #define PG8_STAGE(bufoff, gbase, voff) do { _Pragma("unroll") for (int _i = 0; _i < 2; ++_i) \
;         __builtin_amdgcn_global_load_lds((const unsigned*)((const char*)(gbase) + (voff)[_i]), (PG8_LAS unsigned*)(lds + (bufoff) + ldsw + _i * 8192), 16, 0, 0); } while (0)
; #define PG8_LDA(dst, b, h) do { _Pragma("unroll") for (int m = 0; m < 4; ++m) _Pragma("unroll") for (int k = 0; k < 2; ++k) dst[m][k] = *(const PG8_LAS bf16x8*)(lds + PG8_SA(b, h) + aoff + m * 2048 + k * 1024); } while (0)
; #define PG8_LDB(dst, b, h) do { _Pragma("unroll") for (int n = 0; n < 2; ++n) _Pragma("unroll") for (int k = 0; k < 2; ++k) dst[n][k] = *(const PG8_LAS bf16x8*)(lds + PG8_SB(b, h) + boff + n * 2048 + k * 1024); } while (0)
; #define PG8_WAIT_V(n) asm volatile("s_waitcnt vmcnt(" #n ")" ::: "memory")
; #define PG8_WAIT_L(n) asm volatile("s_waitcnt lgkmcnt(" #n ")" ::: "memory")
; #define PG8_BAR __builtin_amdgcn_s_barrier()
; #define PG8_SCHED __builtin_amdgcn_sched_barrier(0)
; template <class Epi, class Sched, bool ALIGN_EPI = false, bool SP2 = false>
; __device__ __forceinline__ void gemm_phase(PG8_LAS unsigned char* lds, const Gemm g, const Sched& S, const Epi& E, const int wid) {
;     ...
;         const bool has_next = S.next(ui + 1, nxt);
;         const char* nA = has_next ? (const char*)g.A + (size_t)nxt.pm * tstepA : cA; const char* nB = has_next ? (const char*)g.Bt + (size_t)nxt.pn * tstepB : cB;
;         for (int t = 0; t < nt; t += 2) {
;             const bool last = (t == nt - 2);
;             const char* a1 = cA + (size_t)(t + 1) * kstep;
;             const char* a2 = last ? nA : cA + (size_t)(t + 2) * kstep; const char* b2 = last ? nB : cB + (size_t)(t + 2) * kstep;
;             const char* a3 = a2 + kstep; const char* b3 = b2 + kstep;
;             if (last && has_next) S.a_ready(nxt);
;             if constexpr (SP2) {
;             PG8_LDB(B0, 0, 0); PG8_LDB(B1, 0, 1); PG8_SCHED; PG8_LDA(At, 0, 0); PG8_STAGE(PG8_SA(1, 1), a1 + hstepA, voffA);
;             PG8_WAIT_V(8); PG8_WAIT_L(0); PG8_BAR; PG8_MMA(0, 0, At, B0); PG8_MMA(0, 1, At, B1); PG8_BAR; PG8_SCHED;
;             PG8_LDA(At, 0, 1); PG8_STAGE(PG8_SB(0, 0), b2, voffB); PG8_STAGE(PG8_SB(0, 1), b2 + hstepB, voffB); PG8_STAGE(PG8_SA(0, 0), a2, voffA);
;             PG8_WAIT_V(8); PG8_WAIT_L(0); PG8_BAR; PG8_MMA(1, 0, At, B0); PG8_MMA(1, 1, At, B1); PG8_BAR; PG8_SCHED;
.LBB0_348:
	s_ashr_i32 s27, s26, 31
	s_lshl_b64 s[28:29], s[26:27], 19
	s_add_u32 s28, s0, s28
	s_addc_u32 s29, s1, s29
	s_and_b64 s[30:31], s[4:5], exec
	s_cselect_b32 s7, s29, s9
	s_cselect_b32 s27, s28, s8
	s_ashr_i32 s25, s24, 31
	s_lshl_b64 s[30:31], s[24:25], 19
	s_add_u32 s30, s33, s30
	s_addc_u32 s31, s44, s31
	s_and_b64 s[40:41], s[4:5], exec
	s_cselect_b32 s25, s31, s37
	s_cselect_b32 s35, s30, s36
	s_add_u32 s8, s8, 0x40080
	s_addc_u32 s9, s9, 0
	s_add_u32 s73, s36, 0x100
	s_addc_u32 s74, s37, 0
	s_mov_b32 s75, -2
	s_waitcnt lgkmcnt(0)
	v_add_u32_e32 v252, 0x18000, v178
	v_add_u32_e32 v253, 0x1c000, v178
	s_add_u32 s36, s8, 0xfffc0080
	s_addc_u32 s37, s9, -1
	s_cmp_eq_u32 s75, 12
	s_cselect_b32 s41, s7, s37
	s_cselect_b32 s40, s27, s36
	s_cselect_b32 s37, s25, s74
	s_cselect_b32 s36, s35, s73
	s_add_i32 m0, s46, 0xc000
	s_nop 0
	global_load_lds_dwordx4 v142, s[8:9]
	s_add_i32 m0, s46, 0xe000
	s_nop 0
	global_load_lds_dwordx4 v144, s[8:9]
	ds_read_b128 v[128:131], v183
	ds_read_b128 v[150:153], v183 offset:1024
	ds_read_b128 v[154:157], v183 offset:2048
	ds_read_b128 v[158:161], v183 offset:3072
	ds_read_b128 v[162:165], v184
	ds_read_b128 v[166:169], v184 offset:1024
	ds_read_b128 v[170:173], v184 offset:2048
	ds_read_b128 v[188:191], v184 offset:3072
	ds_read_b128 v[192:195], v185
	ds_read_b128 v[196:199], v185 offset:1024
	ds_read_b128 v[200:203], v185 offset:2048
	ds_read_b128 v[204:207], v185 offset:3072
	ds_read_b128 v[208:211], v185 offset:4096
	ds_read_b128 v[212:215], v185 offset:5120
	ds_read_b128 v[216:219], v185 offset:6144
	ds_read_b128 v[220:223], v185 offset:7168
	s_waitcnt vmcnt(8) lgkmcnt(0)
	s_barrier
	s_setprio 1
	v_mfma_f32_16x16x32_bf16 v[124:127], v[128:131], v[192:195], 0
	v_mfma_f32_16x16x32_bf16 v[120:123], v[154:157], v[192:195], 0
	v_mfma_f32_16x16x32_bf16 v[108:111], v[128:131], v[200:203], 0
	v_mfma_f32_16x16x32_bf16 v[104:107], v[154:157], v[200:203], 0
	v_mfma_f32_16x16x32_bf16 v[92:95], v[128:131], v[208:211], 0
	v_mfma_f32_16x16x32_bf16 v[88:91], v[154:157], v[208:211], 0
	v_mfma_f32_16x16x32_bf16 v[76:79], v[128:131], v[216:219], 0
	v_mfma_f32_16x16x32_bf16 v[72:75], v[154:157], v[216:219], 0
	v_mfma_f32_16x16x32_bf16 v[124:127], v[150:153], v[196:199], v[124:127]
	v_mfma_f32_16x16x32_bf16 v[120:123], v[158:161], v[196:199], v[120:123]
	v_mfma_f32_16x16x32_bf16 v[108:111], v[150:153], v[204:207], v[108:111]
	v_mfma_f32_16x16x32_bf16 v[104:107], v[158:161], v[204:207], v[104:107]
	v_mfma_f32_16x16x32_bf16 v[92:95], v[150:153], v[212:215], v[92:95]
	v_mfma_f32_16x16x32_bf16 v[88:91], v[158:161], v[212:215], v[88:91]
	v_mfma_f32_16x16x32_bf16 v[76:79], v[150:153], v[220:223], v[76:79]
	v_mfma_f32_16x16x32_bf16 v[72:75], v[158:161], v[220:223], v[72:75]
	s_setprio 0
	s_setprio 1
	v_mfma_f32_16x16x32_bf16 v[116:119], v[162:165], v[192:195], 0
	v_mfma_f32_16x16x32_bf16 v[112:115], v[170:173], v[192:195], 0
	v_mfma_f32_16x16x32_bf16 v[100:103], v[162:165], v[200:203], 0
	v_mfma_f32_16x16x32_bf16 v[96:99], v[170:173], v[200:203], 0
	v_mfma_f32_16x16x32_bf16 v[84:87], v[162:165], v[208:211], 0
	v_mfma_f32_16x16x32_bf16 v[80:83], v[170:173], v[208:211], 0
	v_mfma_f32_16x16x32_bf16 v[68:71], v[162:165], v[216:219], 0
	v_mfma_f32_16x16x32_bf16 v[64:67], v[170:173], v[216:219], 0
	v_mfma_f32_16x16x32_bf16 v[116:119], v[166:169], v[196:199], v[116:119]
	v_mfma_f32_16x16x32_bf16 v[112:115], v[188:191], v[196:199], v[112:115]
	v_mfma_f32_16x16x32_bf16 v[100:103], v[166:169], v[204:207], v[100:103]
	v_mfma_f32_16x16x32_bf16 v[96:99], v[188:191], v[204:207], v[96:99]
	v_mfma_f32_16x16x32_bf16 v[84:87], v[166:169], v[212:215], v[84:87]
	v_mfma_f32_16x16x32_bf16 v[80:83], v[188:191], v[212:215], v[80:83]
	v_mfma_f32_16x16x32_bf16 v[68:71], v[166:169], v[220:223], v[68:71]
	v_mfma_f32_16x16x32_bf16 v[64:67], v[188:191], v[220:223], v[64:67]
	s_setprio 0
	s_barrier
	s_add_i32 s76, s69, s45
	s_add_u32 s98, s36, 0x80
	s_addc_u32 s99, s37, 0
	s_mov_b32 m0, s76
	s_nop 0
	global_load_lds_dwordx4 v134, s[36:37]
	s_add_i32 m0, s76, 0x2000
	s_add_u32 s76, s36, 0x40000
	s_addc_u32 s77, s37, 0
	s_add_i32 s78, s70, s45
	global_load_lds_dwordx4 v138, s[36:37]
	s_mov_b32 m0, s78
	s_add_u32 s100, s40, 0x80
	s_addc_u32 s101, s41, 0
	global_load_lds_dwordx4 v134, s[76:77]
	s_add_i32 m0, s78, 0x2000
	s_nop 0
	global_load_lds_dwordx4 v138, s[76:77]
	s_mov_b32 m0, s46
	s_nop 0
	global_load_lds_dwordx4 v132, s[40:41]
	s_mov_b32 m0, s47
	s_nop 0
	global_load_lds_dwordx4 v136, s[40:41]
	ds_read_b128 v[192:195], v185 offset:16384
	ds_read_b128 v[196:199], v185 offset:17408
	ds_read_b128 v[200:203], v185 offset:18432
	ds_read_b128 v[204:207], v185 offset:19456
	ds_read_b128 v[208:211], v185 offset:20480
	ds_read_b128 v[212:215], v185 offset:21504
	ds_read_b128 v[216:219], v185 offset:22528
	ds_read_b128 v[220:223], v185 offset:23552
	s_waitcnt vmcnt(8) lgkmcnt(0)
	s_barrier
; #define PG8_STAGE(bufoff, gbase, voff) do { _Pragma("unroll") for (int _i = 0; _i < 2; ++_i) \
;         __builtin_amdgcn_global_load_lds((const unsigned*)((const char*)(gbase) + (voff)[_i]), (PG8_LAS unsigned*)(lds + (bufoff) + ldsw + _i * 8192), 16, 0, 0); } while (0)
; #define PG8_LDA(dst, b, h) do { _Pragma("unroll") for (int m = 0; m < 4; ++m) _Pragma("unroll") for (int k = 0; k < 2; ++k) dst[m][k] = *(const PG8_LAS bf16x8*)(lds + PG8_SA(b, h) + aoff + m * 2048 + k * 1024); } while (0)
; #define PG8_LDB(dst, b, h) do { _Pragma("unroll") for (int n = 0; n < 2; ++n) _Pragma("unroll") for (int k = 0; k < 2; ++k) dst[n][k] = *(const PG8_LAS bf16x8*)(lds + PG8_SB(b, h) + boff + n * 2048 + k * 1024); } while (0)
; #define PG8_MMA(ai, bj, At, Bt) do { __builtin_amdgcn_s_setprio(1); _Pragma("unroll") for (int m = 0; m < 4; ++m) _Pragma("unroll") for (int n = 0; n < 2; ++n) _Pragma("unroll") for (int k = 0; k < 2; ++k) \
;         acc[ai][bj][m][n] = __builtin_amdgcn_mfma_f32_16x16x32_bf16(Bt[n][k], At[m][k], acc[ai][bj][m][n], 0, 0, 0); __builtin_amdgcn_s_setprio(0); } while (0)
; #define PG8_WAIT_V(n) asm volatile("s_waitcnt vmcnt(" #n ")" ::: "memory")
; #define PG8_WAIT_L(n) asm volatile("s_waitcnt lgkmcnt(" #n ")" ::: "memory")
; #define PG8_BAR __builtin_amdgcn_s_barrier()
; #define PG8_SCHED __builtin_amdgcn_sched_barrier(0)
; template <class Epi, class Sched, bool ALIGN_EPI = false, bool SP2 = false>
; __device__ __forceinline__ void gemm_phase(PG8_LAS unsigned char* lds, const Gemm g, const Sched& S, const Epi& E, const int wid) {
;     ...
;             PG8_WAIT_V(8); PG8_WAIT_L(0); PG8_BAR; PG8_MMA(0, 0, At, B0); PG8_MMA(0, 1, At, B1); PG8_BAR; PG8_SCHED;
;             PG8_LDA(At, 0, 1); PG8_STAGE(PG8_SB(0, 0), b2, voffB); PG8_STAGE(PG8_SB(0, 1), b2 + hstepB, voffB); PG8_STAGE(PG8_SA(0, 0), a2, voffA);
;             PG8_WAIT_V(8); PG8_WAIT_L(0); PG8_BAR; PG8_MMA(1, 0, At, B0); PG8_MMA(1, 1, At, B1); PG8_BAR; PG8_SCHED;
;             PG8_LDB(B0, 1, 0); PG8_LDB(B1, 1, 1); PG8_SCHED; PG8_LDA(At, 1, 0); PG8_STAGE(PG8_SA(0, 1), a2 + hstepA, voffA);
;             PG8_WAIT_V(8); PG8_WAIT_L(0); PG8_BAR; PG8_MMA(0, 0, At, B0); PG8_MMA(0, 1, At, B1); PG8_BAR; PG8_SCHED;
	s_setprio 1
	v_mfma_f32_16x16x32_bf16 v[60:63], v[128:131], v[192:195], 0
	v_mfma_f32_16x16x32_bf16 v[56:59], v[154:157], v[192:195], 0
	v_mfma_f32_16x16x32_bf16 v[44:47], v[128:131], v[200:203], 0
	v_mfma_f32_16x16x32_bf16 v[40:43], v[154:157], v[200:203], 0
	v_mfma_f32_16x16x32_bf16 v[28:31], v[128:131], v[208:211], 0
	v_mfma_f32_16x16x32_bf16 v[24:27], v[154:157], v[208:211], 0
	v_mfma_f32_16x16x32_bf16 v[12:15], v[128:131], v[216:219], 0
	v_mfma_f32_16x16x32_bf16 v[8:11], v[154:157], v[216:219], 0
	v_mfma_f32_16x16x32_bf16 v[60:63], v[150:153], v[196:199], v[60:63]
	v_mfma_f32_16x16x32_bf16 v[56:59], v[158:161], v[196:199], v[56:59]
	v_mfma_f32_16x16x32_bf16 v[44:47], v[150:153], v[204:207], v[44:47]
	v_mfma_f32_16x16x32_bf16 v[40:43], v[158:161], v[204:207], v[40:43]
	v_mfma_f32_16x16x32_bf16 v[28:31], v[150:153], v[212:215], v[28:31]
	v_mfma_f32_16x16x32_bf16 v[24:27], v[158:161], v[212:215], v[24:27]
	v_mfma_f32_16x16x32_bf16 v[12:15], v[150:153], v[220:223], v[12:15]
	v_mfma_f32_16x16x32_bf16 v[8:11], v[158:161], v[220:223], v[8:11]
	s_setprio 0
	s_setprio 1
	v_mfma_f32_16x16x32_bf16 v[52:55], v[162:165], v[192:195], 0
	v_mfma_f32_16x16x32_bf16 v[48:51], v[170:173], v[192:195], 0
	v_mfma_f32_16x16x32_bf16 v[36:39], v[162:165], v[200:203], 0
	v_mfma_f32_16x16x32_bf16 v[32:35], v[170:173], v[200:203], 0
	v_mfma_f32_16x16x32_bf16 v[20:23], v[162:165], v[208:211], 0
	v_mfma_f32_16x16x32_bf16 v[16:19], v[170:173], v[208:211], 0
	v_mfma_f32_16x16x32_bf16 v[4:7], v[162:165], v[216:219], 0
	v_mfma_f32_16x16x32_bf16 v[0:3], v[170:173], v[216:219], 0
	v_mfma_f32_16x16x32_bf16 v[52:55], v[166:169], v[196:199], v[52:55]
	v_mfma_f32_16x16x32_bf16 v[48:51], v[188:191], v[196:199], v[48:51]
	v_mfma_f32_16x16x32_bf16 v[36:39], v[166:169], v[204:207], v[36:39]
	v_mfma_f32_16x16x32_bf16 v[32:35], v[188:191], v[204:207], v[32:35]
	v_mfma_f32_16x16x32_bf16 v[20:23], v[166:169], v[212:215], v[20:23]
	v_mfma_f32_16x16x32_bf16 v[16:19], v[188:191], v[212:215], v[16:19]
	v_mfma_f32_16x16x32_bf16 v[4:7], v[166:169], v[220:223], v[4:7]
	v_mfma_f32_16x16x32_bf16 v[0:3], v[188:191], v[220:223], v[0:3]
	s_setprio 0
	s_barrier
	s_add_i32 s76, 0, 0x18000
	s_add_i32 s77, 0, 0x1c000
	s_add_u32 s40, s40, 0x40000
	s_addc_u32 s41, s41, 0
	s_mov_b32 m0, s48
	s_nop 0
	global_load_lds_dwordx4 v132, s[40:41]
	s_mov_b32 m0, s49
	s_nop 0
	global_load_lds_dwordx4 v136, s[40:41]
	ds_read_b128 v[128:131], v252
	ds_read_b128 v[150:153], v252 offset:1024
	ds_read_b128 v[154:157], v252 offset:2048
	ds_read_b128 v[158:161], v252 offset:3072
	ds_read_b128 v[162:165], v253
	ds_read_b128 v[166:169], v253 offset:1024
	ds_read_b128 v[170:173], v253 offset:2048
	ds_read_b128 v[188:191], v253 offset:3072
	ds_read_b128 v[192:195], v185 offset:32768
	ds_read_b128 v[196:199], v185 offset:33792
	ds_read_b128 v[200:203], v185 offset:34816
	ds_read_b128 v[204:207], v185 offset:35840
	ds_read_b128 v[208:211], v185 offset:36864
	ds_read_b128 v[212:215], v185 offset:37888
	ds_read_b128 v[216:219], v185 offset:38912
	ds_read_b128 v[220:223], v185 offset:39936
	s_waitcnt vmcnt(8) lgkmcnt(0)
	s_barrier
	s_setprio 1
	v_mfma_f32_16x16x32_bf16 v[124:127], v[128:131], v[192:195], v[124:127]
	v_mfma_f32_16x16x32_bf16 v[120:123], v[154:157], v[192:195], v[120:123]
	v_mfma_f32_16x16x32_bf16 v[108:111], v[128:131], v[200:203], v[108:111]
	v_mfma_f32_16x16x32_bf16 v[104:107], v[154:157], v[200:203], v[104:107]
	v_mfma_f32_16x16x32_bf16 v[92:95], v[128:131], v[208:211], v[92:95]
	v_mfma_f32_16x16x32_bf16 v[88:91], v[154:157], v[208:211], v[88:91]
	v_mfma_f32_16x16x32_bf16 v[76:79], v[128:131], v[216:219], v[76:79]
	v_mfma_f32_16x16x32_bf16 v[72:75], v[154:157], v[216:219], v[72:75]
	v_mfma_f32_16x16x32_bf16 v[124:127], v[150:153], v[196:199], v[124:127]
	v_mfma_f32_16x16x32_bf16 v[120:123], v[158:161], v[196:199], v[120:123]
	v_mfma_f32_16x16x32_bf16 v[108:111], v[150:153], v[204:207], v[108:111]
	v_mfma_f32_16x16x32_bf16 v[104:107], v[158:161], v[204:207], v[104:107]
	v_mfma_f32_16x16x32_bf16 v[92:95], v[150:153], v[212:215], v[92:95]
	v_mfma_f32_16x16x32_bf16 v[88:91], v[158:161], v[212:215], v[88:91]
	v_mfma_f32_16x16x32_bf16 v[76:79], v[150:153], v[220:223], v[76:79]
	v_mfma_f32_16x16x32_bf16 v[72:75], v[158:161], v[220:223], v[72:75]
	s_setprio 0
	s_setprio 1
	v_mfma_f32_16x16x32_bf16 v[116:119], v[162:165], v[192:195], v[116:119]
	v_mfma_f32_16x16x32_bf16 v[112:115], v[170:173], v[192:195], v[112:115]
	v_mfma_f32_16x16x32_bf16 v[100:103], v[162:165], v[200:203], v[100:103]
	v_mfma_f32_16x16x32_bf16 v[96:99], v[170:173], v[200:203], v[96:99]
	v_mfma_f32_16x16x32_bf16 v[84:87], v[162:165], v[208:211], v[84:87]
	v_mfma_f32_16x16x32_bf16 v[80:83], v[170:173], v[208:211], v[80:83]
	v_mfma_f32_16x16x32_bf16 v[68:71], v[162:165], v[216:219], v[68:71]
	v_mfma_f32_16x16x32_bf16 v[64:67], v[170:173], v[216:219], v[64:67]
	v_mfma_f32_16x16x32_bf16 v[116:119], v[166:169], v[196:199], v[116:119]
	v_mfma_f32_16x16x32_bf16 v[112:115], v[188:191], v[196:199], v[112:115]
	v_mfma_f32_16x16x32_bf16 v[100:103], v[166:169], v[204:207], v[100:103]
	v_mfma_f32_16x16x32_bf16 v[96:99], v[188:191], v[204:207], v[96:99]
	v_mfma_f32_16x16x32_bf16 v[84:87], v[166:169], v[212:215], v[84:87]
	v_mfma_f32_16x16x32_bf16 v[80:83], v[188:191], v[212:215], v[80:83]
	v_mfma_f32_16x16x32_bf16 v[68:71], v[166:169], v[220:223], v[68:71]
	v_mfma_f32_16x16x32_bf16 v[64:67], v[188:191], v[220:223], v[64:67]
	s_setprio 0
	s_barrier
; #define PG8_STAGE(bufoff, gbase, voff) do { _Pragma("unroll") for (int _i = 0; _i < 2; ++_i) \
;         __builtin_amdgcn_global_load_lds((const unsigned*)((const char*)(gbase) + (voff)[_i]), (PG8_LAS unsigned*)(lds + (bufoff) + ldsw + _i * 8192), 16, 0, 0); } while (0)
; #define PG8_LDA(dst, b, h) do { _Pragma("unroll") for (int m = 0; m < 4; ++m) _Pragma("unroll") for (int k = 0; k < 2; ++k) dst[m][k] = *(const PG8_LAS bf16x8*)(lds + PG8_SA(b, h) + aoff + m * 2048 + k * 1024); } while (0)
; #define PG8_LDB(dst, b, h) do { _Pragma("unroll") for (int n = 0; n < 2; ++n) _Pragma("unroll") for (int k = 0; k < 2; ++k) dst[n][k] = *(const PG8_LAS bf16x8*)(lds + PG8_SB(b, h) + boff + n * 2048 + k * 1024); } while (0)
; #define PG8_MMA(ai, bj, At, Bt) do { __builtin_amdgcn_s_setprio(1); _Pragma("unroll") for (int m = 0; m < 4; ++m) _Pragma("unroll") for (int n = 0; n < 2; ++n) _Pragma("unroll") for (int k = 0; k < 2; ++k) \
;         acc[ai][bj][m][n] = __builtin_amdgcn_mfma_f32_16x16x32_bf16(Bt[n][k], At[m][k], acc[ai][bj][m][n], 0, 0, 0); __builtin_amdgcn_s_setprio(0); } while (0)
; #define PG8_WAIT_V(n) asm volatile("s_waitcnt vmcnt(" #n ")" ::: "memory")
; #define PG8_WAIT_L(n) asm volatile("s_waitcnt lgkmcnt(" #n ")" ::: "memory")
; #define PG8_BAR __builtin_amdgcn_s_barrier()
; #define PG8_SCHED __builtin_amdgcn_sched_barrier(0)
; template <class Epi, class Sched, bool ALIGN_EPI = false, bool SP2 = false>
; __device__ __forceinline__ void gemm_phase(PG8_LAS unsigned char* lds, const Gemm g, const Sched& S, const Epi& E, const int wid) {
;     ...
;             if constexpr (SP2) {
;             PG8_LDB(B0, 0, 0); PG8_LDB(B1, 0, 1); PG8_SCHED; PG8_LDA(At, 0, 0); PG8_STAGE(PG8_SA(1, 1), a1 + hstepA, voffA);
;             PG8_WAIT_V(8); PG8_WAIT_L(0); PG8_BAR; PG8_MMA(0, 0, At, B0); PG8_MMA(0, 1, At, B1); PG8_BAR; PG8_SCHED;
;     ...
;             PG8_WAIT_V(8); PG8_WAIT_L(0); PG8_BAR; PG8_MMA(0, 0, At, B0); PG8_MMA(0, 1, At, B1); PG8_BAR; PG8_SCHED;
;             PG8_LDA(At, 1, 1); PG8_STAGE(PG8_SB(1, 0), b3, voffB); PG8_STAGE(PG8_SB(1, 1), b3 + hstepB, voffB); PG8_STAGE(PG8_SA(1, 0), a3, voffA);
;             PG8_WAIT_V(8); PG8_WAIT_L(0); PG8_BAR; PG8_MMA(1, 0, At, B0); PG8_MMA(1, 1, At, B1); PG8_BAR; PG8_SCHED;
	s_add_i32 s40, s76, s45
	s_mov_b32 m0, s40
	s_nop 0
	global_load_lds_dwordx4 v134, s[98:99]
	s_add_i32 m0, s40, 0x2000
	s_add_u32 s36, s36, 0x40080
	s_addc_u32 s37, s37, 0
	s_add_i32 s40, s77, s45
	global_load_lds_dwordx4 v138, s[98:99]
	s_mov_b32 m0, s40
	s_nop 0
	global_load_lds_dwordx4 v134, s[36:37]
	s_add_i32 m0, s40, 0x2000
	s_nop 0
	global_load_lds_dwordx4 v138, s[36:37]
	s_mov_b32 m0, s64
	s_nop 0
	global_load_lds_dwordx4 v132, s[100:101]
	s_mov_b32 m0, s65
	s_nop 0
	global_load_lds_dwordx4 v136, s[100:101]
	ds_read_b128 v[192:195], v185 offset:49152
	ds_read_b128 v[196:199], v185 offset:50176
	ds_read_b128 v[200:203], v185 offset:51200
	ds_read_b128 v[204:207], v185 offset:52224
	ds_read_b128 v[208:211], v185 offset:53248
	ds_read_b128 v[212:215], v185 offset:54272
	ds_read_b128 v[216:219], v185 offset:55296
	ds_read_b128 v[220:223], v185 offset:56320
	s_waitcnt vmcnt(8) lgkmcnt(0)
	s_barrier
	s_setprio 1
	v_mfma_f32_16x16x32_bf16 v[60:63], v[128:131], v[192:195], v[60:63]
	v_mfma_f32_16x16x32_bf16 v[56:59], v[154:157], v[192:195], v[56:59]
	v_mfma_f32_16x16x32_bf16 v[44:47], v[128:131], v[200:203], v[44:47]
	v_mfma_f32_16x16x32_bf16 v[40:43], v[154:157], v[200:203], v[40:43]
	v_mfma_f32_16x16x32_bf16 v[28:31], v[128:131], v[208:211], v[28:31]
	v_mfma_f32_16x16x32_bf16 v[24:27], v[154:157], v[208:211], v[24:27]
	v_mfma_f32_16x16x32_bf16 v[12:15], v[128:131], v[216:219], v[12:15]
	v_mfma_f32_16x16x32_bf16 v[8:11], v[154:157], v[216:219], v[8:11]
	v_mfma_f32_16x16x32_bf16 v[60:63], v[150:153], v[196:199], v[60:63]
	v_mfma_f32_16x16x32_bf16 v[56:59], v[158:161], v[196:199], v[56:59]
	v_mfma_f32_16x16x32_bf16 v[44:47], v[150:153], v[204:207], v[44:47]
	v_mfma_f32_16x16x32_bf16 v[40:43], v[158:161], v[204:207], v[40:43]
	v_mfma_f32_16x16x32_bf16 v[28:31], v[150:153], v[212:215], v[28:31]
	v_mfma_f32_16x16x32_bf16 v[24:27], v[158:161], v[212:215], v[24:27]
	v_mfma_f32_16x16x32_bf16 v[12:15], v[150:153], v[220:223], v[12:15]
	v_mfma_f32_16x16x32_bf16 v[8:11], v[158:161], v[220:223], v[8:11]
	s_setprio 0
	s_setprio 1
	v_mfma_f32_16x16x32_bf16 v[52:55], v[162:165], v[192:195], v[52:55]
	v_mfma_f32_16x16x32_bf16 v[48:51], v[170:173], v[192:195], v[48:51]
	v_mfma_f32_16x16x32_bf16 v[36:39], v[162:165], v[200:203], v[36:39]
	v_mfma_f32_16x16x32_bf16 v[32:35], v[170:173], v[200:203], v[32:35]
	v_mfma_f32_16x16x32_bf16 v[20:23], v[162:165], v[208:211], v[20:23]
	v_mfma_f32_16x16x32_bf16 v[16:19], v[170:173], v[208:211], v[16:19]
	v_mfma_f32_16x16x32_bf16 v[4:7], v[162:165], v[216:219], v[4:7]
	v_mfma_f32_16x16x32_bf16 v[0:3], v[170:173], v[216:219], v[0:3]
	v_mfma_f32_16x16x32_bf16 v[52:55], v[166:169], v[196:199], v[52:55]
	v_mfma_f32_16x16x32_bf16 v[48:51], v[188:191], v[196:199], v[48:51]
	v_mfma_f32_16x16x32_bf16 v[36:39], v[166:169], v[204:207], v[36:39]
	v_mfma_f32_16x16x32_bf16 v[32:35], v[188:191], v[204:207], v[32:35]
	v_mfma_f32_16x16x32_bf16 v[20:23], v[166:169], v[212:215], v[20:23]
	v_mfma_f32_16x16x32_bf16 v[16:19], v[188:191], v[212:215], v[16:19]
	v_mfma_f32_16x16x32_bf16 v[4:7], v[166:169], v[220:223], v[4:7]
	v_mfma_f32_16x16x32_bf16 v[0:3], v[188:191], v[220:223], v[0:3]
	s_setprio 0
	s_barrier
	s_add_i32 s75, s75, 2
	s_add_u32 s8, s8, 0x100
	s_addc_u32 s9, s9, 0
	s_add_u32 s73, s73, 0x100
	s_addc_u32 s74, s74, 0
	s_cmp_gt_u32 s75, 13
.LBB0_349:
	s_add_u32 s36, s8, 0xfffc0080
	s_addc_u32 s37, s9, -1
	s_cmp_eq_u32 s75, 12
	s_cselect_b32 s41, s7, s37
	s_cselect_b32 s40, s27, s36
	s_cselect_b32 s37, s25, s74
	s_cselect_b32 s36, s35, s73
	s_add_i32 m0, s46, 0xc000
	s_nop 0
	global_load_lds_dwordx4 v142, s[8:9]
	s_add_i32 m0, s46, 0xe000
	s_nop 0
	global_load_lds_dwordx4 v144, s[8:9]
	ds_read_b128 v[128:131], v183
	ds_read_b128 v[150:153], v183 offset:1024
	ds_read_b128 v[154:157], v183 offset:2048
	ds_read_b128 v[158:161], v183 offset:3072
	ds_read_b128 v[162:165], v184
	ds_read_b128 v[166:169], v184 offset:1024
	ds_read_b128 v[170:173], v184 offset:2048
	ds_read_b128 v[188:191], v184 offset:3072
	ds_read_b128 v[192:195], v185
	ds_read_b128 v[196:199], v185 offset:1024
	ds_read_b128 v[200:203], v185 offset:2048
	ds_read_b128 v[204:207], v185 offset:3072
	ds_read_b128 v[208:211], v185 offset:4096
	ds_read_b128 v[212:215], v185 offset:5120
	ds_read_b128 v[216:219], v185 offset:6144
	ds_read_b128 v[220:223], v185 offset:7168
	s_waitcnt vmcnt(8) lgkmcnt(0)
	s_barrier
	s_setprio 1
	v_mfma_f32_16x16x32_bf16 v[124:127], v[128:131], v[192:195], v[124:127]
	v_mfma_f32_16x16x32_bf16 v[120:123], v[154:157], v[192:195], v[120:123]
	v_mfma_f32_16x16x32_bf16 v[108:111], v[128:131], v[200:203], v[108:111]
	v_mfma_f32_16x16x32_bf16 v[104:107], v[154:157], v[200:203], v[104:107]
	v_mfma_f32_16x16x32_bf16 v[92:95], v[128:131], v[208:211], v[92:95]
	v_mfma_f32_16x16x32_bf16 v[88:91], v[154:157], v[208:211], v[88:91]
	v_mfma_f32_16x16x32_bf16 v[76:79], v[128:131], v[216:219], v[76:79]
	v_mfma_f32_16x16x32_bf16 v[72:75], v[154:157], v[216:219], v[72:75]
	v_mfma_f32_16x16x32_bf16 v[124:127], v[150:153], v[196:199], v[124:127]
	v_mfma_f32_16x16x32_bf16 v[120:123], v[158:161], v[196:199], v[120:123]
	v_mfma_f32_16x16x32_bf16 v[108:111], v[150:153], v[204:207], v[108:111]
	v_mfma_f32_16x16x32_bf16 v[104:107], v[158:161], v[204:207], v[104:107]
	v_mfma_f32_16x16x32_bf16 v[92:95], v[150:153], v[212:215], v[92:95]
	v_mfma_f32_16x16x32_bf16 v[88:91], v[158:161], v[212:215], v[88:91]
	v_mfma_f32_16x16x32_bf16 v[76:79], v[150:153], v[220:223], v[76:79]
	v_mfma_f32_16x16x32_bf16 v[72:75], v[158:161], v[220:223], v[72:75]
	s_setprio 0
	s_setprio 1
	v_mfma_f32_16x16x32_bf16 v[116:119], v[162:165], v[192:195], v[116:119]
	v_mfma_f32_16x16x32_bf16 v[112:115], v[170:173], v[192:195], v[112:115]
	v_mfma_f32_16x16x32_bf16 v[100:103], v[162:165], v[200:203], v[100:103]
	v_mfma_f32_16x16x32_bf16 v[96:99], v[170:173], v[200:203], v[96:99]
	v_mfma_f32_16x16x32_bf16 v[84:87], v[162:165], v[208:211], v[84:87]
	v_mfma_f32_16x16x32_bf16 v[80:83], v[170:173], v[208:211], v[80:83]
	v_mfma_f32_16x16x32_bf16 v[68:71], v[162:165], v[216:219], v[68:71]
	v_mfma_f32_16x16x32_bf16 v[64:67], v[170:173], v[216:219], v[64:67]
	v_mfma_f32_16x16x32_bf16 v[116:119], v[166:169], v[196:199], v[116:119]
	v_mfma_f32_16x16x32_bf16 v[112:115], v[188:191], v[196:199], v[112:115]
	v_mfma_f32_16x16x32_bf16 v[100:103], v[166:169], v[204:207], v[100:103]
	v_mfma_f32_16x16x32_bf16 v[96:99], v[188:191], v[204:207], v[96:99]
	v_mfma_f32_16x16x32_bf16 v[84:87], v[166:169], v[212:215], v[84:87]
	v_mfma_f32_16x16x32_bf16 v[80:83], v[188:191], v[212:215], v[80:83]
	v_mfma_f32_16x16x32_bf16 v[68:71], v[166:169], v[220:223], v[68:71]
	v_mfma_f32_16x16x32_bf16 v[64:67], v[188:191], v[220:223], v[64:67]
	s_setprio 0
	s_barrier
; #define PG8_STAGE(bufoff, gbase, voff) do { _Pragma("unroll") for (int _i = 0; _i < 2; ++_i) \
;         __builtin_amdgcn_global_load_lds((const unsigned*)((const char*)(gbase) + (voff)[_i]), (PG8_LAS unsigned*)(lds + (bufoff) + ldsw + _i * 8192), 16, 0, 0); } while (0)
; #define PG8_LDA(dst, b, h) do { _Pragma("unroll") for (int m = 0; m < 4; ++m) _Pragma("unroll") for (int k = 0; k < 2; ++k) dst[m][k] = *(const PG8_LAS bf16x8*)(lds + PG8_SA(b, h) + aoff + m * 2048 + k * 1024); } while (0)
; #define PG8_LDB(dst, b, h) do { _Pragma("unroll") for (int n = 0; n < 2; ++n) _Pragma("unroll") for (int k = 0; k < 2; ++k) dst[n][k] = *(const PG8_LAS bf16x8*)(lds + PG8_SB(b, h) + boff + n * 2048 + k * 1024); } while (0)
; #define PG8_MMA(ai, bj, At, Bt) do { __builtin_amdgcn_s_setprio(1); _Pragma("unroll") for (int m = 0; m < 4; ++m) _Pragma("unroll") for (int n = 0; n < 2; ++n) _Pragma("unroll") for (int k = 0; k < 2; ++k) \
;         acc[ai][bj][m][n] = __builtin_amdgcn_mfma_f32_16x16x32_bf16(Bt[n][k], At[m][k], acc[ai][bj][m][n], 0, 0, 0); __builtin_amdgcn_s_setprio(0); } while (0)
; #define PG8_WAIT_V(n) asm volatile("s_waitcnt vmcnt(" #n ")" ::: "memory")
; #define PG8_WAIT_L(n) asm volatile("s_waitcnt lgkmcnt(" #n ")" ::: "memory")
; #define PG8_BAR __builtin_amdgcn_s_barrier()
; #define PG8_SCHED __builtin_amdgcn_sched_barrier(0)
; template <class Epi, class Sched, bool ALIGN_EPI = false, bool SP2 = false>
; __device__ __forceinline__ void gemm_phase(PG8_LAS unsigned char* lds, const Gemm g, const Sched& S, const Epi& E, const int wid) {
;     ...
;             PG8_WAIT_V(8); PG8_WAIT_L(0); PG8_BAR; PG8_MMA(0, 0, At, B0); PG8_MMA(0, 1, At, B1); PG8_BAR; PG8_SCHED;
;             PG8_LDA(At, 0, 1); PG8_STAGE(PG8_SB(0, 0), b2, voffB); PG8_STAGE(PG8_SB(0, 1), b2 + hstepB, voffB); PG8_STAGE(PG8_SA(0, 0), a2, voffA);
;             PG8_WAIT_V(8); PG8_WAIT_L(0); PG8_BAR; PG8_MMA(1, 0, At, B0); PG8_MMA(1, 1, At, B1); PG8_BAR; PG8_SCHED;
;             PG8_LDB(B0, 1, 0); PG8_LDB(B1, 1, 1); PG8_SCHED; PG8_LDA(At, 1, 0); PG8_STAGE(PG8_SA(0, 1), a2 + hstepA, voffA);
;             PG8_WAIT_V(8); PG8_WAIT_L(0); PG8_BAR; PG8_MMA(0, 0, At, B0); PG8_MMA(0, 1, At, B1); PG8_BAR; PG8_SCHED;
	s_add_i32 s76, s69, s45
	s_add_u32 s98, s36, 0x80
	s_addc_u32 s99, s37, 0
	s_mov_b32 m0, s76
	s_nop 0
	global_load_lds_dwordx4 v134, s[36:37]
	s_add_i32 m0, s76, 0x2000
	s_add_u32 s76, s36, 0x40000
	s_addc_u32 s77, s37, 0
	s_add_i32 s78, s70, s45
	global_load_lds_dwordx4 v138, s[36:37]
	s_mov_b32 m0, s78
	s_add_u32 s100, s40, 0x80
	s_addc_u32 s101, s41, 0
	global_load_lds_dwordx4 v134, s[76:77]
	s_add_i32 m0, s78, 0x2000
	s_nop 0
	global_load_lds_dwordx4 v138, s[76:77]
	s_mov_b32 m0, s46
	s_nop 0
	global_load_lds_dwordx4 v132, s[40:41]
	s_mov_b32 m0, s47
	s_nop 0
	global_load_lds_dwordx4 v136, s[40:41]
	ds_read_b128 v[192:195], v185 offset:16384
	ds_read_b128 v[196:199], v185 offset:17408
	ds_read_b128 v[200:203], v185 offset:18432
	ds_read_b128 v[204:207], v185 offset:19456
	ds_read_b128 v[208:211], v185 offset:20480
	ds_read_b128 v[212:215], v185 offset:21504
	ds_read_b128 v[216:219], v185 offset:22528
	ds_read_b128 v[220:223], v185 offset:23552
	s_waitcnt vmcnt(8) lgkmcnt(0)
	s_barrier
	s_setprio 1
	v_mfma_f32_16x16x32_bf16 v[60:63], v[128:131], v[192:195], v[60:63]
	v_mfma_f32_16x16x32_bf16 v[56:59], v[154:157], v[192:195], v[56:59]
	v_mfma_f32_16x16x32_bf16 v[44:47], v[128:131], v[200:203], v[44:47]
	v_mfma_f32_16x16x32_bf16 v[40:43], v[154:157], v[200:203], v[40:43]
	v_mfma_f32_16x16x32_bf16 v[28:31], v[128:131], v[208:211], v[28:31]
	v_mfma_f32_16x16x32_bf16 v[24:27], v[154:157], v[208:211], v[24:27]
	v_mfma_f32_16x16x32_bf16 v[12:15], v[128:131], v[216:219], v[12:15]
	v_mfma_f32_16x16x32_bf16 v[8:11], v[154:157], v[216:219], v[8:11]
	v_mfma_f32_16x16x32_bf16 v[60:63], v[150:153], v[196:199], v[60:63]
	v_mfma_f32_16x16x32_bf16 v[56:59], v[158:161], v[196:199], v[56:59]
	v_mfma_f32_16x16x32_bf16 v[44:47], v[150:153], v[204:207], v[44:47]
	v_mfma_f32_16x16x32_bf16 v[40:43], v[158:161], v[204:207], v[40:43]
	v_mfma_f32_16x16x32_bf16 v[28:31], v[150:153], v[212:215], v[28:31]
	v_mfma_f32_16x16x32_bf16 v[24:27], v[158:161], v[212:215], v[24:27]
	v_mfma_f32_16x16x32_bf16 v[12:15], v[150:153], v[220:223], v[12:15]
	v_mfma_f32_16x16x32_bf16 v[8:11], v[158:161], v[220:223], v[8:11]
	s_setprio 0
	s_setprio 1
	v_mfma_f32_16x16x32_bf16 v[52:55], v[162:165], v[192:195], v[52:55]
	v_mfma_f32_16x16x32_bf16 v[48:51], v[170:173], v[192:195], v[48:51]
	v_mfma_f32_16x16x32_bf16 v[36:39], v[162:165], v[200:203], v[36:39]
	v_mfma_f32_16x16x32_bf16 v[32:35], v[170:173], v[200:203], v[32:35]
	v_mfma_f32_16x16x32_bf16 v[20:23], v[162:165], v[208:211], v[20:23]
	v_mfma_f32_16x16x32_bf16 v[16:19], v[170:173], v[208:211], v[16:19]
	v_mfma_f32_16x16x32_bf16 v[4:7], v[162:165], v[216:219], v[4:7]
	v_mfma_f32_16x16x32_bf16 v[0:3], v[170:173], v[216:219], v[0:3]
	v_mfma_f32_16x16x32_bf16 v[52:55], v[166:169], v[196:199], v[52:55]
	v_mfma_f32_16x16x32_bf16 v[48:51], v[188:191], v[196:199], v[48:51]
	v_mfma_f32_16x16x32_bf16 v[36:39], v[166:169], v[204:207], v[36:39]
	v_mfma_f32_16x16x32_bf16 v[32:35], v[188:191], v[204:207], v[32:35]
	v_mfma_f32_16x16x32_bf16 v[20:23], v[166:169], v[212:215], v[20:23]
	v_mfma_f32_16x16x32_bf16 v[16:19], v[188:191], v[212:215], v[16:19]
	v_mfma_f32_16x16x32_bf16 v[4:7], v[166:169], v[220:223], v[4:7]
	v_mfma_f32_16x16x32_bf16 v[0:3], v[188:191], v[220:223], v[0:3]
	s_setprio 0
	s_barrier
	s_add_i32 s76, 0, 0x18000
	s_add_i32 s77, 0, 0x1c000
	s_add_u32 s40, s40, 0x40000
	s_addc_u32 s41, s41, 0
	s_mov_b32 m0, s48
	s_nop 0
	global_load_lds_dwordx4 v132, s[40:41]
	s_mov_b32 m0, s49
	s_nop 0
	global_load_lds_dwordx4 v136, s[40:41]
	ds_read_b128 v[128:131], v252
	ds_read_b128 v[150:153], v252 offset:1024
	ds_read_b128 v[154:157], v252 offset:2048
	ds_read_b128 v[158:161], v252 offset:3072
	ds_read_b128 v[162:165], v253
	ds_read_b128 v[166:169], v253 offset:1024
	ds_read_b128 v[170:173], v253 offset:2048
	ds_read_b128 v[188:191], v253 offset:3072
	ds_read_b128 v[192:195], v185 offset:32768
	ds_read_b128 v[196:199], v185 offset:33792
	ds_read_b128 v[200:203], v185 offset:34816
	ds_read_b128 v[204:207], v185 offset:35840
	ds_read_b128 v[208:211], v185 offset:36864
	ds_read_b128 v[212:215], v185 offset:37888
	ds_read_b128 v[216:219], v185 offset:38912
	ds_read_b128 v[220:223], v185 offset:39936
	s_waitcnt vmcnt(8) lgkmcnt(0)
	s_barrier
; #define PG8_STAGE(bufoff, gbase, voff) do { _Pragma("unroll") for (int _i = 0; _i < 2; ++_i) \
;         __builtin_amdgcn_global_load_lds((const unsigned*)((const char*)(gbase) + (voff)[_i]), (PG8_LAS unsigned*)(lds + (bufoff) + ldsw + _i * 8192), 16, 0, 0); } while (0)
; #define PG8_LDA(dst, b, h) do { _Pragma("unroll") for (int m = 0; m < 4; ++m) _Pragma("unroll") for (int k = 0; k < 2; ++k) dst[m][k] = *(const PG8_LAS bf16x8*)(lds + PG8_SA(b, h) + aoff + m * 2048 + k * 1024); } while (0)
; #define PG8_MMA(ai, bj, At, Bt) do { __builtin_amdgcn_s_setprio(1); _Pragma("unroll") for (int m = 0; m < 4; ++m) _Pragma("unroll") for (int n = 0; n < 2; ++n) _Pragma("unroll") for (int k = 0; k < 2; ++k) \
;         acc[ai][bj][m][n] = __builtin_amdgcn_mfma_f32_16x16x32_bf16(Bt[n][k], At[m][k], acc[ai][bj][m][n], 0, 0, 0); __builtin_amdgcn_s_setprio(0); } while (0)
; #define PG8_WAIT_V(n) asm volatile("s_waitcnt vmcnt(" #n ")" ::: "memory")
; #define PG8_WAIT_L(n) asm volatile("s_waitcnt lgkmcnt(" #n ")" ::: "memory")
; #define PG8_BAR __builtin_amdgcn_s_barrier()
; #define PG8_SCHED __builtin_amdgcn_sched_barrier(0)
; template <class Epi, class Sched, bool ALIGN_EPI = false, bool SP2 = false>
; __device__ __forceinline__ void gemm_phase(PG8_LAS unsigned char* lds, const Gemm g, const Sched& S, const Epi& E, const int wid) {
;     ...
;         for (int t = 0; t < nt; t += 2) {
;     ...
;             PG8_WAIT_V(8); PG8_WAIT_L(0); PG8_BAR; PG8_MMA(0, 0, At, B0); PG8_MMA(0, 1, At, B1); PG8_BAR; PG8_SCHED;
;             PG8_LDA(At, 1, 1); PG8_STAGE(PG8_SB(1, 0), b3, voffB); PG8_STAGE(PG8_SB(1, 1), b3 + hstepB, voffB); PG8_STAGE(PG8_SA(1, 0), a3, voffA);
;             PG8_WAIT_V(8); PG8_WAIT_L(0); PG8_BAR; PG8_MMA(1, 0, At, B0); PG8_MMA(1, 1, At, B1); PG8_BAR; PG8_SCHED;
	s_setprio 1
	v_mfma_f32_16x16x32_bf16 v[124:127], v[128:131], v[192:195], v[124:127]
	v_mfma_f32_16x16x32_bf16 v[120:123], v[154:157], v[192:195], v[120:123]
	v_mfma_f32_16x16x32_bf16 v[108:111], v[128:131], v[200:203], v[108:111]
	v_mfma_f32_16x16x32_bf16 v[104:107], v[154:157], v[200:203], v[104:107]
	v_mfma_f32_16x16x32_bf16 v[92:95], v[128:131], v[208:211], v[92:95]
	v_mfma_f32_16x16x32_bf16 v[88:91], v[154:157], v[208:211], v[88:91]
	v_mfma_f32_16x16x32_bf16 v[76:79], v[128:131], v[216:219], v[76:79]
	v_mfma_f32_16x16x32_bf16 v[72:75], v[154:157], v[216:219], v[72:75]
	v_mfma_f32_16x16x32_bf16 v[124:127], v[150:153], v[196:199], v[124:127]
	v_mfma_f32_16x16x32_bf16 v[120:123], v[158:161], v[196:199], v[120:123]
	v_mfma_f32_16x16x32_bf16 v[108:111], v[150:153], v[204:207], v[108:111]
	v_mfma_f32_16x16x32_bf16 v[104:107], v[158:161], v[204:207], v[104:107]
	v_mfma_f32_16x16x32_bf16 v[92:95], v[150:153], v[212:215], v[92:95]
	v_mfma_f32_16x16x32_bf16 v[88:91], v[158:161], v[212:215], v[88:91]
	v_mfma_f32_16x16x32_bf16 v[76:79], v[150:153], v[220:223], v[76:79]
	v_mfma_f32_16x16x32_bf16 v[72:75], v[158:161], v[220:223], v[72:75]
	s_setprio 0
	s_setprio 1
	v_mfma_f32_16x16x32_bf16 v[116:119], v[162:165], v[192:195], v[116:119]
	v_mfma_f32_16x16x32_bf16 v[112:115], v[170:173], v[192:195], v[112:115]
	v_mfma_f32_16x16x32_bf16 v[100:103], v[162:165], v[200:203], v[100:103]
	v_mfma_f32_16x16x32_bf16 v[96:99], v[170:173], v[200:203], v[96:99]
	v_mfma_f32_16x16x32_bf16 v[84:87], v[162:165], v[208:211], v[84:87]
	v_mfma_f32_16x16x32_bf16 v[80:83], v[170:173], v[208:211], v[80:83]
	v_mfma_f32_16x16x32_bf16 v[68:71], v[162:165], v[216:219], v[68:71]
	v_mfma_f32_16x16x32_bf16 v[64:67], v[170:173], v[216:219], v[64:67]
	v_mfma_f32_16x16x32_bf16 v[116:119], v[166:169], v[196:199], v[116:119]
	v_mfma_f32_16x16x32_bf16 v[112:115], v[188:191], v[196:199], v[112:115]
	v_mfma_f32_16x16x32_bf16 v[100:103], v[166:169], v[204:207], v[100:103]
	v_mfma_f32_16x16x32_bf16 v[96:99], v[188:191], v[204:207], v[96:99]
	v_mfma_f32_16x16x32_bf16 v[84:87], v[166:169], v[212:215], v[84:87]
	v_mfma_f32_16x16x32_bf16 v[80:83], v[188:191], v[212:215], v[80:83]
	v_mfma_f32_16x16x32_bf16 v[68:71], v[166:169], v[220:223], v[68:71]
	v_mfma_f32_16x16x32_bf16 v[64:67], v[188:191], v[220:223], v[64:67]
	s_setprio 0
	s_barrier
	s_add_i32 s40, s76, s45
	s_mov_b32 m0, s40
	s_nop 0
	global_load_lds_dwordx4 v134, s[98:99]
	s_add_i32 m0, s40, 0x2000
	s_add_u32 s36, s36, 0x40080
	s_addc_u32 s37, s37, 0
	s_add_i32 s40, s77, s45
	global_load_lds_dwordx4 v138, s[98:99]
	s_mov_b32 m0, s40
	s_nop 0
	global_load_lds_dwordx4 v134, s[36:37]
	s_add_i32 m0, s40, 0x2000
	s_nop 0
	global_load_lds_dwordx4 v138, s[36:37]
	s_mov_b32 m0, s64
	s_nop 0
	global_load_lds_dwordx4 v132, s[100:101]
	s_mov_b32 m0, s65
	s_nop 0
	global_load_lds_dwordx4 v136, s[100:101]
	ds_read_b128 v[192:195], v185 offset:49152
	ds_read_b128 v[196:199], v185 offset:50176
	ds_read_b128 v[200:203], v185 offset:51200
	ds_read_b128 v[204:207], v185 offset:52224
	ds_read_b128 v[208:211], v185 offset:53248
	ds_read_b128 v[212:215], v185 offset:54272
	ds_read_b128 v[216:219], v185 offset:55296
	ds_read_b128 v[220:223], v185 offset:56320
	s_waitcnt vmcnt(8) lgkmcnt(0)
	s_barrier
	s_setprio 1
	v_mfma_f32_16x16x32_bf16 v[60:63], v[128:131], v[192:195], v[60:63]
	v_mfma_f32_16x16x32_bf16 v[56:59], v[154:157], v[192:195], v[56:59]
	v_mfma_f32_16x16x32_bf16 v[44:47], v[128:131], v[200:203], v[44:47]
	v_mfma_f32_16x16x32_bf16 v[40:43], v[154:157], v[200:203], v[40:43]
	v_mfma_f32_16x16x32_bf16 v[28:31], v[128:131], v[208:211], v[28:31]
	v_mfma_f32_16x16x32_bf16 v[24:27], v[154:157], v[208:211], v[24:27]
	v_mfma_f32_16x16x32_bf16 v[12:15], v[128:131], v[216:219], v[12:15]
	v_mfma_f32_16x16x32_bf16 v[8:11], v[154:157], v[216:219], v[8:11]
	v_mfma_f32_16x16x32_bf16 v[60:63], v[150:153], v[196:199], v[60:63]
	v_mfma_f32_16x16x32_bf16 v[56:59], v[158:161], v[196:199], v[56:59]
	v_mfma_f32_16x16x32_bf16 v[44:47], v[150:153], v[204:207], v[44:47]
	v_mfma_f32_16x16x32_bf16 v[40:43], v[158:161], v[204:207], v[40:43]
	v_mfma_f32_16x16x32_bf16 v[28:31], v[150:153], v[212:215], v[28:31]
	v_mfma_f32_16x16x32_bf16 v[24:27], v[158:161], v[212:215], v[24:27]
	v_mfma_f32_16x16x32_bf16 v[12:15], v[150:153], v[220:223], v[12:15]
	v_mfma_f32_16x16x32_bf16 v[8:11], v[158:161], v[220:223], v[8:11]
	s_setprio 0
	s_setprio 1
	v_mfma_f32_16x16x32_bf16 v[52:55], v[162:165], v[192:195], v[52:55]
	v_mfma_f32_16x16x32_bf16 v[48:51], v[170:173], v[192:195], v[48:51]
	v_mfma_f32_16x16x32_bf16 v[36:39], v[162:165], v[200:203], v[36:39]
	v_mfma_f32_16x16x32_bf16 v[32:35], v[170:173], v[200:203], v[32:35]
	v_mfma_f32_16x16x32_bf16 v[20:23], v[162:165], v[208:211], v[20:23]
	v_mfma_f32_16x16x32_bf16 v[16:19], v[170:173], v[208:211], v[16:19]
	v_mfma_f32_16x16x32_bf16 v[4:7], v[162:165], v[216:219], v[4:7]
	v_mfma_f32_16x16x32_bf16 v[0:3], v[170:173], v[216:219], v[0:3]
	v_mfma_f32_16x16x32_bf16 v[52:55], v[166:169], v[196:199], v[52:55]
	v_mfma_f32_16x16x32_bf16 v[48:51], v[188:191], v[196:199], v[48:51]
	v_mfma_f32_16x16x32_bf16 v[36:39], v[166:169], v[204:207], v[36:39]
	v_mfma_f32_16x16x32_bf16 v[32:35], v[188:191], v[204:207], v[32:35]
	v_mfma_f32_16x16x32_bf16 v[20:23], v[166:169], v[212:215], v[20:23]
	v_mfma_f32_16x16x32_bf16 v[16:19], v[188:191], v[212:215], v[16:19]
	v_mfma_f32_16x16x32_bf16 v[4:7], v[166:169], v[220:223], v[4:7]
	v_mfma_f32_16x16x32_bf16 v[0:3], v[188:191], v[220:223], v[0:3]
	s_setprio 0
	s_barrier
	s_add_i32 s75, s75, 2
	s_add_u32 s8, s8, 0x100
	s_addc_u32 s9, s9, 0
	s_add_u32 s73, s73, 0x100
	s_addc_u32 s74, s74, 0
	s_cmp_gt_u32 s75, 13
	s_cbranch_scc0 .LBB0_349
	s_and_b64 vcc, exec, s[20:21]
	s_cbranch_vccz .LBB0_352
	s_barrier

; #define PG8_STAGE(bufoff, gbase, voff) do { _Pragma("unroll") for (int _i = 0; _i < 2; ++_i) \
;         __builtin_amdgcn_global_load_lds((const unsigned*)((const char*)(gbase) + (voff)[_i]), (PG8_LAS unsigned*)(lds + (bufoff) + ldsw + _i * 8192), 16, 0, 0); } while (0)
; #define PG8_WAIT_V(n) asm volatile("s_waitcnt vmcnt(" #n ")" ::: "memory")
; #define PG8_WAIT_L(n) asm volatile("s_waitcnt lgkmcnt(" #n ")" ::: "memory")
; #define PG8_BAR __builtin_amdgcn_s_barrier()
; template <class Epi, class Sched, bool ALIGN_EPI = false, bool SP2 = false>
; __device__ __forceinline__ void gemm_phase(PG8_LAS unsigned char* lds, const Gemm g, const Sched& S, const Epi& E, const int wid) {
;     ...
;         const bool has_next = S.next(ui + 1, nxt);
;         const char* nA = has_next ? (const char*)g.A + (size_t)nxt.pm * tstepA : cA; const char* nB = has_next ? (const char*)g.Bt + (size_t)nxt.pn * tstepB : cB;
;         for (int t = 0; t < nt; t += 2) {
;             const bool last = (t == nt - 2);
;             const char* a1 = cA + (size_t)(t + 1) * kstep;
;             const char* a2 = last ? nA : cA + (size_t)(t + 2) * kstep; const char* b2 = last ? nB : cB + (size_t)(t + 2) * kstep;
;             const char* a3 = a2 + kstep; const char* b3 = b2 + kstep;
;             if (last && has_next) S.a_ready(nxt);
;             if constexpr (SP2) {
;             PG8_LDB(B0, 0, 0); PG8_LDB(B1, 0, 1); PG8_SCHED; PG8_LDA(At, 0, 0); PG8_STAGE(PG8_SA(1, 1), a1 + hstepA, voffA);
;             PG8_WAIT_V(8); PG8_WAIT_L(0); PG8_BAR; PG8_MMA(0, 0, At, B0); PG8_MMA(0, 1, At, B1); PG8_BAR; PG8_SCHED;
;             PG8_LDA(At, 0, 1); PG8_STAGE(PG8_SB(0, 0), b2, voffB); PG8_STAGE(PG8_SB(0, 1), b2 + hstepB, voffB); PG8_STAGE(PG8_SA(0, 0), a2, voffA);
;             PG8_WAIT_V(8); PG8_WAIT_L(0); PG8_BAR; PG8_MMA(1, 0, At, B0); PG8_MMA(1, 1, At, B1); PG8_BAR; PG8_SCHED;
;             PG8_LDB(B0, 1, 0); PG8_LDB(B1, 1, 1); PG8_SCHED; PG8_LDA(At, 1, 0); PG8_STAGE(PG8_SA(0, 1), a2 + hstepA, voffA);
;             PG8_WAIT_V(8); PG8_WAIT_L(0); PG8_BAR; PG8_MMA(0, 0, At, B0); PG8_MMA(0, 1, At, B1); PG8_BAR; PG8_SCHED;
;             PG8_LDA(At, 1, 1); PG8_STAGE(PG8_SB(1, 0), b3, voffB); PG8_STAGE(PG8_SB(1, 1), b3 + hstepB, voffB); PG8_STAGE(PG8_SA(1, 0), a3, voffA);
;             PG8_WAIT_V(8); PG8_WAIT_L(0); PG8_BAR; PG8_MMA(1, 0, At, B0); PG8_MMA(1, 1, At, B1); PG8_BAR; PG8_SCHED;
.LBB0_1779:
	s_ashr_i32 s21, s20, 31
	s_lshl_b64 s[22:23], s[20:21], 19
	s_add_u32 s22, s0, s22
	s_addc_u32 s23, s1, s23
	s_and_b64 s[24:25], s[4:5], exec
	s_cselect_b32 s21, s23, s31
	s_cselect_b32 s27, s22, s30
	s_ashr_i32 s19, s18, 31
	s_lshl_b64 s[24:25], s[18:19], 19
	s_add_u32 s24, s33, s24
	s_addc_u32 s25, s38, s25
	s_and_b64 s[36:37], s[4:5], exec
	s_cselect_b32 s19, s25, s35
	s_cselect_b32 s29, s24, s34
	s_add_u32 s30, s30, 0x40080
	s_addc_u32 s31, s31, 0
	s_add_u32 s68, s34, 0x100
	s_addc_u32 s69, s35, 0
	s_mov_b32 s70, -2
	s_waitcnt lgkmcnt(0)
	v_add_u32_e32 v252, 0x18000, v189
	v_add_u32_e32 v253, 0x1c000, v189
	s_add_u32 s34, s30, 0xfffc0080
	s_addc_u32 s35, s31, -1
	s_cmp_eq_u32 s70, 12
	s_cselect_b32 s37, s21, s35
	s_cselect_b32 s36, s27, s34
	s_cselect_b32 s35, s19, s69
	s_cselect_b32 s34, s29, s68
	s_add_i32 m0, s40, 0xc000
	s_nop 0
	global_load_lds_dwordx4 v164, s[30:31]
	s_add_i32 m0, s40, 0xe000
	s_nop 0
	global_load_lds_dwordx4 v166, s[30:31]
	ds_read_b128 v[128:131], v190
	ds_read_b128 v[132:135], v190 offset:1024
	ds_read_b128 v[136:139], v190 offset:2048
	ds_read_b128 v[140:143], v190 offset:3072
	ds_read_b128 v[144:147], v191
	ds_read_b128 v[148:151], v191 offset:1024
	ds_read_b128 v[172:175], v191 offset:2048
	ds_read_b128 v[176:179], v191 offset:3072
	ds_read_b128 v[180:183], v192
	ds_read_b128 v[184:187], v192 offset:1024
	ds_read_b128 v[194:197], v192 offset:2048
	ds_read_b128 v[198:201], v192 offset:3072
	ds_read_b128 v[202:205], v192 offset:4096
	ds_read_b128 v[206:209], v192 offset:5120
	ds_read_b128 v[210:213], v192 offset:6144
	ds_read_b128 v[214:217], v192 offset:7168
	s_waitcnt vmcnt(8) lgkmcnt(0)
	s_barrier
	s_setprio 1
	v_mfma_f32_16x16x32_bf16 v[124:127], v[128:131], v[180:183], 0
	v_mfma_f32_16x16x32_bf16 v[120:123], v[136:139], v[180:183], 0
	v_mfma_f32_16x16x32_bf16 v[108:111], v[128:131], v[194:197], 0
	v_mfma_f32_16x16x32_bf16 v[104:107], v[136:139], v[194:197], 0
	v_mfma_f32_16x16x32_bf16 v[92:95], v[128:131], v[202:205], 0
	v_mfma_f32_16x16x32_bf16 v[88:91], v[136:139], v[202:205], 0
	v_mfma_f32_16x16x32_bf16 v[76:79], v[128:131], v[210:213], 0
	v_mfma_f32_16x16x32_bf16 v[72:75], v[136:139], v[210:213], 0
	v_mfma_f32_16x16x32_bf16 v[124:127], v[132:135], v[184:187], v[124:127]
	v_mfma_f32_16x16x32_bf16 v[120:123], v[140:143], v[184:187], v[120:123]
	v_mfma_f32_16x16x32_bf16 v[108:111], v[132:135], v[198:201], v[108:111]
	v_mfma_f32_16x16x32_bf16 v[104:107], v[140:143], v[198:201], v[104:107]
	v_mfma_f32_16x16x32_bf16 v[92:95], v[132:135], v[206:209], v[92:95]
	v_mfma_f32_16x16x32_bf16 v[88:91], v[140:143], v[206:209], v[88:91]
	v_mfma_f32_16x16x32_bf16 v[76:79], v[132:135], v[214:217], v[76:79]
	v_mfma_f32_16x16x32_bf16 v[72:75], v[140:143], v[214:217], v[72:75]
	s_setprio 0
	s_setprio 1
	v_mfma_f32_16x16x32_bf16 v[116:119], v[144:147], v[180:183], 0
	v_mfma_f32_16x16x32_bf16 v[112:115], v[172:175], v[180:183], 0
	v_mfma_f32_16x16x32_bf16 v[100:103], v[144:147], v[194:197], 0
	v_mfma_f32_16x16x32_bf16 v[96:99], v[172:175], v[194:197], 0
	v_mfma_f32_16x16x32_bf16 v[84:87], v[144:147], v[202:205], 0
	v_mfma_f32_16x16x32_bf16 v[80:83], v[172:175], v[202:205], 0
	v_mfma_f32_16x16x32_bf16 v[68:71], v[144:147], v[210:213], 0
	v_mfma_f32_16x16x32_bf16 v[64:67], v[172:175], v[210:213], 0
	v_mfma_f32_16x16x32_bf16 v[116:119], v[148:151], v[184:187], v[116:119]
	v_mfma_f32_16x16x32_bf16 v[112:115], v[176:179], v[184:187], v[112:115]
	v_mfma_f32_16x16x32_bf16 v[100:103], v[148:151], v[198:201], v[100:103]
	v_mfma_f32_16x16x32_bf16 v[96:99], v[176:179], v[198:201], v[96:99]
	v_mfma_f32_16x16x32_bf16 v[84:87], v[148:151], v[206:209], v[84:87]
	v_mfma_f32_16x16x32_bf16 v[80:83], v[176:179], v[206:209], v[80:83]
	v_mfma_f32_16x16x32_bf16 v[68:71], v[148:151], v[214:217], v[68:71]
	v_mfma_f32_16x16x32_bf16 v[64:67], v[176:179], v[214:217], v[64:67]
	s_setprio 0
	s_barrier
	s_add_i32 s71, s65, s39
	s_add_u32 s98, s34, 0x80
	s_addc_u32 s99, s35, 0
	s_mov_b32 m0, s71
	s_nop 0
	global_load_lds_dwordx4 v154, s[34:35]
	s_add_i32 m0, s71, 0x2000
	s_add_u32 s72, s34, 0x40000
	s_addc_u32 s73, s35, 0
	s_add_i32 s71, s66, s39
	global_load_lds_dwordx4 v158, s[34:35]
	s_mov_b32 m0, s71
	s_add_u32 s100, s36, 0x80
	s_addc_u32 s101, s37, 0
	global_load_lds_dwordx4 v154, s[72:73]
	s_add_i32 m0, s71, 0x2000
	s_nop 0
	global_load_lds_dwordx4 v158, s[72:73]
	s_mov_b32 m0, s40
	s_nop 0
	global_load_lds_dwordx4 v152, s[36:37]
	s_mov_b32 m0, s41
	s_nop 0
	global_load_lds_dwordx4 v156, s[36:37]
	ds_read_b128 v[180:183], v192 offset:16384
	ds_read_b128 v[184:187], v192 offset:17408
	ds_read_b128 v[194:197], v192 offset:18432
	ds_read_b128 v[198:201], v192 offset:19456
	ds_read_b128 v[202:205], v192 offset:20480
	ds_read_b128 v[206:209], v192 offset:21504
	ds_read_b128 v[210:213], v192 offset:22528
	ds_read_b128 v[214:217], v192 offset:23552
	s_waitcnt vmcnt(8) lgkmcnt(0)
	s_barrier
; #define PG8_STAGE(bufoff, gbase, voff) do { _Pragma("unroll") for (int _i = 0; _i < 2; ++_i) \
;         __builtin_amdgcn_global_load_lds((const unsigned*)((const char*)(gbase) + (voff)[_i]), (PG8_LAS unsigned*)(lds + (bufoff) + ldsw + _i * 8192), 16, 0, 0); } while (0)
; #define PG8_LDA(dst, b, h) do { _Pragma("unroll") for (int m = 0; m < 4; ++m) _Pragma("unroll") for (int k = 0; k < 2; ++k) dst[m][k] = *(const PG8_LAS bf16x8*)(lds + PG8_SA(b, h) + aoff + m * 2048 + k * 1024); } while (0)
; #define PG8_LDB(dst, b, h) do { _Pragma("unroll") for (int n = 0; n < 2; ++n) _Pragma("unroll") for (int k = 0; k < 2; ++k) dst[n][k] = *(const PG8_LAS bf16x8*)(lds + PG8_SB(b, h) + boff + n * 2048 + k * 1024); } while (0)
; #define PG8_MMA(ai, bj, At, Bt) do { __builtin_amdgcn_s_setprio(1); _Pragma("unroll") for (int m = 0; m < 4; ++m) _Pragma("unroll") for (int n = 0; n < 2; ++n) _Pragma("unroll") for (int k = 0; k < 2; ++k) \
;         acc[ai][bj][m][n] = __builtin_amdgcn_mfma_f32_16x16x32_bf16(Bt[n][k], At[m][k], acc[ai][bj][m][n], 0, 0, 0); __builtin_amdgcn_s_setprio(0); } while (0)
; template <class Epi, class Sched, bool ALIGN_EPI = false, bool SP2 = false>
; __device__ __forceinline__ void gemm_phase(PG8_LAS unsigned char* lds, const Gemm g, const Sched& S, const Epi& E, const int wid) {
;     ...
;             if constexpr (SP2) {
;             PG8_LDB(B0, 0, 0); PG8_LDB(B1, 0, 1); PG8_SCHED; PG8_LDA(At, 0, 0); PG8_STAGE(PG8_SA(1, 1), a1 + hstepA, voffA);
;             PG8_WAIT_V(8); PG8_WAIT_L(0); PG8_BAR; PG8_MMA(0, 0, At, B0); PG8_MMA(0, 1, At, B1); PG8_BAR; PG8_SCHED;
;             PG8_LDA(At, 0, 1); PG8_STAGE(PG8_SB(0, 0), b2, voffB); PG8_STAGE(PG8_SB(0, 1), b2 + hstepB, voffB); PG8_STAGE(PG8_SA(0, 0), a2, voffA);
;             PG8_WAIT_V(8); PG8_WAIT_L(0); PG8_BAR; PG8_MMA(1, 0, At, B0); PG8_MMA(1, 1, At, B1); PG8_BAR; PG8_SCHED;
;             PG8_LDB(B0, 1, 0); PG8_LDB(B1, 1, 1); PG8_SCHED; PG8_LDA(At, 1, 0); PG8_STAGE(PG8_SA(0, 1), a2 + hstepA, voffA);
;             PG8_WAIT_V(8); PG8_WAIT_L(0); PG8_BAR; PG8_MMA(0, 0, At, B0); PG8_MMA(0, 1, At, B1); PG8_BAR; PG8_SCHED;
;             PG8_LDA(At, 1, 1); PG8_STAGE(PG8_SB(1, 0), b3, voffB); PG8_STAGE(PG8_SB(1, 1), b3 + hstepB, voffB); PG8_STAGE(PG8_SA(1, 0), a3, voffA);
;             PG8_WAIT_V(8); PG8_WAIT_L(0); PG8_BAR; PG8_MMA(1, 0, At, B0); PG8_MMA(1, 1, At, B1); PG8_BAR; PG8_SCHED;
	s_setprio 1
	v_mfma_f32_16x16x32_bf16 v[60:63], v[128:131], v[180:183], 0
	v_mfma_f32_16x16x32_bf16 v[56:59], v[136:139], v[180:183], 0
	v_mfma_f32_16x16x32_bf16 v[44:47], v[128:131], v[194:197], 0
	v_mfma_f32_16x16x32_bf16 v[40:43], v[136:139], v[194:197], 0
	v_mfma_f32_16x16x32_bf16 v[28:31], v[128:131], v[202:205], 0
	v_mfma_f32_16x16x32_bf16 v[24:27], v[136:139], v[202:205], 0
	v_mfma_f32_16x16x32_bf16 v[12:15], v[128:131], v[210:213], 0
	v_mfma_f32_16x16x32_bf16 v[8:11], v[136:139], v[210:213], 0
	v_mfma_f32_16x16x32_bf16 v[60:63], v[132:135], v[184:187], v[60:63]
	v_mfma_f32_16x16x32_bf16 v[56:59], v[140:143], v[184:187], v[56:59]
	v_mfma_f32_16x16x32_bf16 v[44:47], v[132:135], v[198:201], v[44:47]
	v_mfma_f32_16x16x32_bf16 v[40:43], v[140:143], v[198:201], v[40:43]
	v_mfma_f32_16x16x32_bf16 v[28:31], v[132:135], v[206:209], v[28:31]
	v_mfma_f32_16x16x32_bf16 v[24:27], v[140:143], v[206:209], v[24:27]
	v_mfma_f32_16x16x32_bf16 v[12:15], v[132:135], v[214:217], v[12:15]
	v_mfma_f32_16x16x32_bf16 v[8:11], v[140:143], v[214:217], v[8:11]
	s_setprio 0
	s_setprio 1
	v_mfma_f32_16x16x32_bf16 v[52:55], v[144:147], v[180:183], 0
	v_mfma_f32_16x16x32_bf16 v[48:51], v[172:175], v[180:183], 0
	v_mfma_f32_16x16x32_bf16 v[36:39], v[144:147], v[194:197], 0
	v_mfma_f32_16x16x32_bf16 v[32:35], v[172:175], v[194:197], 0
	v_mfma_f32_16x16x32_bf16 v[20:23], v[144:147], v[202:205], 0
	v_mfma_f32_16x16x32_bf16 v[16:19], v[172:175], v[202:205], 0
	v_mfma_f32_16x16x32_bf16 v[4:7], v[144:147], v[210:213], 0
	v_mfma_f32_16x16x32_bf16 v[0:3], v[172:175], v[210:213], 0
	v_mfma_f32_16x16x32_bf16 v[52:55], v[148:151], v[184:187], v[52:55]
	v_mfma_f32_16x16x32_bf16 v[48:51], v[176:179], v[184:187], v[48:51]
	v_mfma_f32_16x16x32_bf16 v[36:39], v[148:151], v[198:201], v[36:39]
	v_mfma_f32_16x16x32_bf16 v[32:35], v[176:179], v[198:201], v[32:35]
	v_mfma_f32_16x16x32_bf16 v[20:23], v[148:151], v[206:209], v[20:23]
	v_mfma_f32_16x16x32_bf16 v[16:19], v[176:179], v[206:209], v[16:19]
	v_mfma_f32_16x16x32_bf16 v[4:7], v[148:151], v[214:217], v[4:7]
	v_mfma_f32_16x16x32_bf16 v[0:3], v[176:179], v[214:217], v[0:3]
	s_setprio 0
	s_barrier
	s_add_i32 s71, 0, 0x18000
	s_add_i32 s72, 0, 0x1c000
	s_add_u32 s36, s36, 0x40000
	s_addc_u32 s37, s37, 0
	s_mov_b32 m0, s44
	s_nop 0
	global_load_lds_dwordx4 v152, s[36:37]
	s_mov_b32 m0, s45
	s_nop 0
	global_load_lds_dwordx4 v156, s[36:37]
	ds_read_b128 v[128:131], v252
	ds_read_b128 v[132:135], v252 offset:1024
	ds_read_b128 v[136:139], v252 offset:2048
	ds_read_b128 v[140:143], v252 offset:3072
	ds_read_b128 v[144:147], v253
	ds_read_b128 v[148:151], v253 offset:1024
	ds_read_b128 v[172:175], v253 offset:2048
	ds_read_b128 v[176:179], v253 offset:3072
	ds_read_b128 v[180:183], v192 offset:32768
	ds_read_b128 v[184:187], v192 offset:33792
	ds_read_b128 v[194:197], v192 offset:34816
	ds_read_b128 v[198:201], v192 offset:35840
	ds_read_b128 v[202:205], v192 offset:36864
	ds_read_b128 v[206:209], v192 offset:37888
	ds_read_b128 v[210:213], v192 offset:38912
	ds_read_b128 v[214:217], v192 offset:39936
	s_waitcnt vmcnt(8) lgkmcnt(0)
	s_barrier
	s_setprio 1
	v_mfma_f32_16x16x32_bf16 v[124:127], v[128:131], v[180:183], v[124:127]
	v_mfma_f32_16x16x32_bf16 v[120:123], v[136:139], v[180:183], v[120:123]
	v_mfma_f32_16x16x32_bf16 v[108:111], v[128:131], v[194:197], v[108:111]
	v_mfma_f32_16x16x32_bf16 v[104:107], v[136:139], v[194:197], v[104:107]
	v_mfma_f32_16x16x32_bf16 v[92:95], v[128:131], v[202:205], v[92:95]
	v_mfma_f32_16x16x32_bf16 v[88:91], v[136:139], v[202:205], v[88:91]
	v_mfma_f32_16x16x32_bf16 v[76:79], v[128:131], v[210:213], v[76:79]
	v_mfma_f32_16x16x32_bf16 v[72:75], v[136:139], v[210:213], v[72:75]
	v_mfma_f32_16x16x32_bf16 v[124:127], v[132:135], v[184:187], v[124:127]
	v_mfma_f32_16x16x32_bf16 v[120:123], v[140:143], v[184:187], v[120:123]
	v_mfma_f32_16x16x32_bf16 v[108:111], v[132:135], v[198:201], v[108:111]
	v_mfma_f32_16x16x32_bf16 v[104:107], v[140:143], v[198:201], v[104:107]
	v_mfma_f32_16x16x32_bf16 v[92:95], v[132:135], v[206:209], v[92:95]
	v_mfma_f32_16x16x32_bf16 v[88:91], v[140:143], v[206:209], v[88:91]
	v_mfma_f32_16x16x32_bf16 v[76:79], v[132:135], v[214:217], v[76:79]
	v_mfma_f32_16x16x32_bf16 v[72:75], v[140:143], v[214:217], v[72:75]
	s_setprio 0
	s_setprio 1
	v_mfma_f32_16x16x32_bf16 v[116:119], v[144:147], v[180:183], v[116:119]
	v_mfma_f32_16x16x32_bf16 v[112:115], v[172:175], v[180:183], v[112:115]
	v_mfma_f32_16x16x32_bf16 v[100:103], v[144:147], v[194:197], v[100:103]
	v_mfma_f32_16x16x32_bf16 v[96:99], v[172:175], v[194:197], v[96:99]
	v_mfma_f32_16x16x32_bf16 v[84:87], v[144:147], v[202:205], v[84:87]
	v_mfma_f32_16x16x32_bf16 v[80:83], v[172:175], v[202:205], v[80:83]
	v_mfma_f32_16x16x32_bf16 v[68:71], v[144:147], v[210:213], v[68:71]
	v_mfma_f32_16x16x32_bf16 v[64:67], v[172:175], v[210:213], v[64:67]
	v_mfma_f32_16x16x32_bf16 v[116:119], v[148:151], v[184:187], v[116:119]
	v_mfma_f32_16x16x32_bf16 v[112:115], v[176:179], v[184:187], v[112:115]
	v_mfma_f32_16x16x32_bf16 v[100:103], v[148:151], v[198:201], v[100:103]
	v_mfma_f32_16x16x32_bf16 v[96:99], v[176:179], v[198:201], v[96:99]
	v_mfma_f32_16x16x32_bf16 v[84:87], v[148:151], v[206:209], v[84:87]
	v_mfma_f32_16x16x32_bf16 v[80:83], v[176:179], v[206:209], v[80:83]
	v_mfma_f32_16x16x32_bf16 v[68:71], v[148:151], v[214:217], v[68:71]
	v_mfma_f32_16x16x32_bf16 v[64:67], v[176:179], v[214:217], v[64:67]
	s_setprio 0
	s_barrier
; #define PG8_STAGE(bufoff, gbase, voff) do { _Pragma("unroll") for (int _i = 0; _i < 2; ++_i) \
;         __builtin_amdgcn_global_load_lds((const unsigned*)((const char*)(gbase) + (voff)[_i]), (PG8_LAS unsigned*)(lds + (bufoff) + ldsw + _i * 8192), 16, 0, 0); } while (0)
; #define PG8_LDA(dst, b, h) do { _Pragma("unroll") for (int m = 0; m < 4; ++m) _Pragma("unroll") for (int k = 0; k < 2; ++k) dst[m][k] = *(const PG8_LAS bf16x8*)(lds + PG8_SA(b, h) + aoff + m * 2048 + k * 1024); } while (0)
; #define PG8_LDB(dst, b, h) do { _Pragma("unroll") for (int n = 0; n < 2; ++n) _Pragma("unroll") for (int k = 0; k < 2; ++k) dst[n][k] = *(const PG8_LAS bf16x8*)(lds + PG8_SB(b, h) + boff + n * 2048 + k * 1024); } while (0)
; #define PG8_MMA(ai, bj, At, Bt) do { __builtin_amdgcn_s_setprio(1); _Pragma("unroll") for (int m = 0; m < 4; ++m) _Pragma("unroll") for (int n = 0; n < 2; ++n) _Pragma("unroll") for (int k = 0; k < 2; ++k) \
;         acc[ai][bj][m][n] = __builtin_amdgcn_mfma_f32_16x16x32_bf16(Bt[n][k], At[m][k], acc[ai][bj][m][n], 0, 0, 0); __builtin_amdgcn_s_setprio(0); } while (0)
; template <class Epi, class Sched, bool ALIGN_EPI = false, bool SP2 = false>
; __device__ __forceinline__ void gemm_phase(PG8_LAS unsigned char* lds, const Gemm g, const Sched& S, const Epi& E, const int wid) {
;     ...
;             if constexpr (SP2) {
;             PG8_LDB(B0, 0, 0); PG8_LDB(B1, 0, 1); PG8_SCHED; PG8_LDA(At, 0, 0); PG8_STAGE(PG8_SA(1, 1), a1 + hstepA, voffA);
;             PG8_WAIT_V(8); PG8_WAIT_L(0); PG8_BAR; PG8_MMA(0, 0, At, B0); PG8_MMA(0, 1, At, B1); PG8_BAR; PG8_SCHED;
;             PG8_LDA(At, 0, 1); PG8_STAGE(PG8_SB(0, 0), b2, voffB); PG8_STAGE(PG8_SB(0, 1), b2 + hstepB, voffB); PG8_STAGE(PG8_SA(0, 0), a2, voffA);
;             PG8_WAIT_V(8); PG8_WAIT_L(0); PG8_BAR; PG8_MMA(1, 0, At, B0); PG8_MMA(1, 1, At, B1); PG8_BAR; PG8_SCHED;
;             PG8_LDB(B0, 1, 0); PG8_LDB(B1, 1, 1); PG8_SCHED; PG8_LDA(At, 1, 0); PG8_STAGE(PG8_SA(0, 1), a2 + hstepA, voffA);
;             PG8_WAIT_V(8); PG8_WAIT_L(0); PG8_BAR; PG8_MMA(0, 0, At, B0); PG8_MMA(0, 1, At, B1); PG8_BAR; PG8_SCHED;
;             PG8_LDA(At, 1, 1); PG8_STAGE(PG8_SB(1, 0), b3, voffB); PG8_STAGE(PG8_SB(1, 1), b3 + hstepB, voffB); PG8_STAGE(PG8_SA(1, 0), a3, voffA);
;             PG8_WAIT_V(8); PG8_WAIT_L(0); PG8_BAR; PG8_MMA(1, 0, At, B0); PG8_MMA(1, 1, At, B1); PG8_BAR; PG8_SCHED;
	s_add_i32 s36, s71, s39
	s_mov_b32 m0, s36
	s_nop 0
	global_load_lds_dwordx4 v154, s[98:99]
	s_add_i32 m0, s36, 0x2000
	s_add_u32 s34, s34, 0x40080
	s_addc_u32 s35, s35, 0
	s_add_i32 s36, s72, s39
	global_load_lds_dwordx4 v158, s[98:99]
	s_mov_b32 m0, s36
	s_nop 0
	global_load_lds_dwordx4 v154, s[34:35]
	s_add_i32 m0, s36, 0x2000
	s_nop 0
	global_load_lds_dwordx4 v158, s[34:35]
	s_mov_b32 m0, s47
	s_nop 0
	global_load_lds_dwordx4 v152, s[100:101]
	s_mov_b32 m0, s48
	s_nop 0
	global_load_lds_dwordx4 v156, s[100:101]
	ds_read_b128 v[180:183], v192 offset:49152
	ds_read_b128 v[184:187], v192 offset:50176
	ds_read_b128 v[194:197], v192 offset:51200
	ds_read_b128 v[198:201], v192 offset:52224
	ds_read_b128 v[202:205], v192 offset:53248
	ds_read_b128 v[206:209], v192 offset:54272
	ds_read_b128 v[210:213], v192 offset:55296
	ds_read_b128 v[214:217], v192 offset:56320
	s_waitcnt vmcnt(8) lgkmcnt(0)
	s_barrier
	s_setprio 1
	v_mfma_f32_16x16x32_bf16 v[60:63], v[128:131], v[180:183], v[60:63]
	v_mfma_f32_16x16x32_bf16 v[56:59], v[136:139], v[180:183], v[56:59]
	v_mfma_f32_16x16x32_bf16 v[44:47], v[128:131], v[194:197], v[44:47]
	v_mfma_f32_16x16x32_bf16 v[40:43], v[136:139], v[194:197], v[40:43]
	v_mfma_f32_16x16x32_bf16 v[28:31], v[128:131], v[202:205], v[28:31]
	v_mfma_f32_16x16x32_bf16 v[24:27], v[136:139], v[202:205], v[24:27]
	v_mfma_f32_16x16x32_bf16 v[12:15], v[128:131], v[210:213], v[12:15]
	v_mfma_f32_16x16x32_bf16 v[8:11], v[136:139], v[210:213], v[8:11]
	v_mfma_f32_16x16x32_bf16 v[60:63], v[132:135], v[184:187], v[60:63]
	v_mfma_f32_16x16x32_bf16 v[56:59], v[140:143], v[184:187], v[56:59]
	v_mfma_f32_16x16x32_bf16 v[44:47], v[132:135], v[198:201], v[44:47]
	v_mfma_f32_16x16x32_bf16 v[40:43], v[140:143], v[198:201], v[40:43]
	v_mfma_f32_16x16x32_bf16 v[28:31], v[132:135], v[206:209], v[28:31]
	v_mfma_f32_16x16x32_bf16 v[24:27], v[140:143], v[206:209], v[24:27]
	v_mfma_f32_16x16x32_bf16 v[12:15], v[132:135], v[214:217], v[12:15]
	v_mfma_f32_16x16x32_bf16 v[8:11], v[140:143], v[214:217], v[8:11]
	s_setprio 0
	s_setprio 1
	v_mfma_f32_16x16x32_bf16 v[52:55], v[144:147], v[180:183], v[52:55]
	v_mfma_f32_16x16x32_bf16 v[48:51], v[172:175], v[180:183], v[48:51]
	v_mfma_f32_16x16x32_bf16 v[36:39], v[144:147], v[194:197], v[36:39]
	v_mfma_f32_16x16x32_bf16 v[32:35], v[172:175], v[194:197], v[32:35]
	v_mfma_f32_16x16x32_bf16 v[20:23], v[144:147], v[202:205], v[20:23]
	v_mfma_f32_16x16x32_bf16 v[16:19], v[172:175], v[202:205], v[16:19]
	v_mfma_f32_16x16x32_bf16 v[4:7], v[144:147], v[210:213], v[4:7]
	v_mfma_f32_16x16x32_bf16 v[0:3], v[172:175], v[210:213], v[0:3]
	v_mfma_f32_16x16x32_bf16 v[52:55], v[148:151], v[184:187], v[52:55]
	v_mfma_f32_16x16x32_bf16 v[48:51], v[176:179], v[184:187], v[48:51]
	v_mfma_f32_16x16x32_bf16 v[36:39], v[148:151], v[198:201], v[36:39]
	v_mfma_f32_16x16x32_bf16 v[32:35], v[176:179], v[198:201], v[32:35]
	v_mfma_f32_16x16x32_bf16 v[20:23], v[148:151], v[206:209], v[20:23]
	v_mfma_f32_16x16x32_bf16 v[16:19], v[176:179], v[206:209], v[16:19]
	v_mfma_f32_16x16x32_bf16 v[4:7], v[148:151], v[214:217], v[4:7]
	v_mfma_f32_16x16x32_bf16 v[0:3], v[176:179], v[214:217], v[0:3]
	s_setprio 0
	s_barrier
	s_add_i32 s70, s70, 2
	s_add_u32 s30, s30, 0x100
	s_addc_u32 s31, s31, 0
	s_add_u32 s68, s68, 0x100
	s_addc_u32 s69, s69, 0
	s_cmp_gt_u32 s70, 13
.LBB0_1780:
	s_add_u32 s34, s30, 0xfffc0080
	s_addc_u32 s35, s31, -1
	s_cmp_eq_u32 s70, 12
	s_cselect_b32 s37, s21, s35
	s_cselect_b32 s36, s27, s34
	s_cselect_b32 s35, s19, s69
	s_cselect_b32 s34, s29, s68
	s_add_i32 m0, s40, 0xc000
	s_nop 0
	global_load_lds_dwordx4 v164, s[30:31]
	s_add_i32 m0, s40, 0xe000
	s_nop 0
	global_load_lds_dwordx4 v166, s[30:31]
	ds_read_b128 v[128:131], v190
	ds_read_b128 v[132:135], v190 offset:1024
	ds_read_b128 v[136:139], v190 offset:2048
	ds_read_b128 v[140:143], v190 offset:3072
	ds_read_b128 v[144:147], v191
	ds_read_b128 v[148:151], v191 offset:1024
	ds_read_b128 v[172:175], v191 offset:2048
	ds_read_b128 v[176:179], v191 offset:3072
	ds_read_b128 v[180:183], v192
	ds_read_b128 v[184:187], v192 offset:1024
	ds_read_b128 v[194:197], v192 offset:2048
	ds_read_b128 v[198:201], v192 offset:3072
	ds_read_b128 v[202:205], v192 offset:4096
	ds_read_b128 v[206:209], v192 offset:5120
	ds_read_b128 v[210:213], v192 offset:6144
	ds_read_b128 v[214:217], v192 offset:7168
	s_waitcnt vmcnt(8) lgkmcnt(0)
	s_barrier
	s_setprio 1
	v_mfma_f32_16x16x32_bf16 v[124:127], v[128:131], v[180:183], v[124:127]
	v_mfma_f32_16x16x32_bf16 v[120:123], v[136:139], v[180:183], v[120:123]
	v_mfma_f32_16x16x32_bf16 v[108:111], v[128:131], v[194:197], v[108:111]
	v_mfma_f32_16x16x32_bf16 v[104:107], v[136:139], v[194:197], v[104:107]
	v_mfma_f32_16x16x32_bf16 v[92:95], v[128:131], v[202:205], v[92:95]
	v_mfma_f32_16x16x32_bf16 v[88:91], v[136:139], v[202:205], v[88:91]
	v_mfma_f32_16x16x32_bf16 v[76:79], v[128:131], v[210:213], v[76:79]
	v_mfma_f32_16x16x32_bf16 v[72:75], v[136:139], v[210:213], v[72:75]
	v_mfma_f32_16x16x32_bf16 v[124:127], v[132:135], v[184:187], v[124:127]
	v_mfma_f32_16x16x32_bf16 v[120:123], v[140:143], v[184:187], v[120:123]
	v_mfma_f32_16x16x32_bf16 v[108:111], v[132:135], v[198:201], v[108:111]
	v_mfma_f32_16x16x32_bf16 v[104:107], v[140:143], v[198:201], v[104:107]
	v_mfma_f32_16x16x32_bf16 v[92:95], v[132:135], v[206:209], v[92:95]
	v_mfma_f32_16x16x32_bf16 v[88:91], v[140:143], v[206:209], v[88:91]
	v_mfma_f32_16x16x32_bf16 v[76:79], v[132:135], v[214:217], v[76:79]
	v_mfma_f32_16x16x32_bf16 v[72:75], v[140:143], v[214:217], v[72:75]
	s_setprio 0
	s_setprio 1
	v_mfma_f32_16x16x32_bf16 v[116:119], v[144:147], v[180:183], v[116:119]
	v_mfma_f32_16x16x32_bf16 v[112:115], v[172:175], v[180:183], v[112:115]
	v_mfma_f32_16x16x32_bf16 v[100:103], v[144:147], v[194:197], v[100:103]
	v_mfma_f32_16x16x32_bf16 v[96:99], v[172:175], v[194:197], v[96:99]
	v_mfma_f32_16x16x32_bf16 v[84:87], v[144:147], v[202:205], v[84:87]
	v_mfma_f32_16x16x32_bf16 v[80:83], v[172:175], v[202:205], v[80:83]
	v_mfma_f32_16x16x32_bf16 v[68:71], v[144:147], v[210:213], v[68:71]
	v_mfma_f32_16x16x32_bf16 v[64:67], v[172:175], v[210:213], v[64:67]
	v_mfma_f32_16x16x32_bf16 v[116:119], v[148:151], v[184:187], v[116:119]
	v_mfma_f32_16x16x32_bf16 v[112:115], v[176:179], v[184:187], v[112:115]
	v_mfma_f32_16x16x32_bf16 v[100:103], v[148:151], v[198:201], v[100:103]
	v_mfma_f32_16x16x32_bf16 v[96:99], v[176:179], v[198:201], v[96:99]
	v_mfma_f32_16x16x32_bf16 v[84:87], v[148:151], v[206:209], v[84:87]
	v_mfma_f32_16x16x32_bf16 v[80:83], v[176:179], v[206:209], v[80:83]
	v_mfma_f32_16x16x32_bf16 v[68:71], v[148:151], v[214:217], v[68:71]
	v_mfma_f32_16x16x32_bf16 v[64:67], v[176:179], v[214:217], v[64:67]
	s_setprio 0
	s_barrier
; #define PG8_STAGE(bufoff, gbase, voff) do { _Pragma("unroll") for (int _i = 0; _i < 2; ++_i) \
;         __builtin_amdgcn_global_load_lds((const unsigned*)((const char*)(gbase) + (voff)[_i]), (PG8_LAS unsigned*)(lds + (bufoff) + ldsw + _i * 8192), 16, 0, 0); } while (0)
; #define PG8_LDA(dst, b, h) do { _Pragma("unroll") for (int m = 0; m < 4; ++m) _Pragma("unroll") for (int k = 0; k < 2; ++k) dst[m][k] = *(const PG8_LAS bf16x8*)(lds + PG8_SA(b, h) + aoff + m * 2048 + k * 1024); } while (0)
; #define PG8_LDB(dst, b, h) do { _Pragma("unroll") for (int n = 0; n < 2; ++n) _Pragma("unroll") for (int k = 0; k < 2; ++k) dst[n][k] = *(const PG8_LAS bf16x8*)(lds + PG8_SB(b, h) + boff + n * 2048 + k * 1024); } while (0)
; #define PG8_MMA(ai, bj, At, Bt) do { __builtin_amdgcn_s_setprio(1); _Pragma("unroll") for (int m = 0; m < 4; ++m) _Pragma("unroll") for (int n = 0; n < 2; ++n) _Pragma("unroll") for (int k = 0; k < 2; ++k) \
;         acc[ai][bj][m][n] = __builtin_amdgcn_mfma_f32_16x16x32_bf16(Bt[n][k], At[m][k], acc[ai][bj][m][n], 0, 0, 0); __builtin_amdgcn_s_setprio(0); } while (0)
; template <class Epi, class Sched, bool ALIGN_EPI = false, bool SP2 = false>
; __device__ __forceinline__ void gemm_phase(PG8_LAS unsigned char* lds, const Gemm g, const Sched& S, const Epi& E, const int wid) {
;     ...
;             if constexpr (SP2) {
;             PG8_LDB(B0, 0, 0); PG8_LDB(B1, 0, 1); PG8_SCHED; PG8_LDA(At, 0, 0); PG8_STAGE(PG8_SA(1, 1), a1 + hstepA, voffA);
;             PG8_WAIT_V(8); PG8_WAIT_L(0); PG8_BAR; PG8_MMA(0, 0, At, B0); PG8_MMA(0, 1, At, B1); PG8_BAR; PG8_SCHED;
;             PG8_LDA(At, 0, 1); PG8_STAGE(PG8_SB(0, 0), b2, voffB); PG8_STAGE(PG8_SB(0, 1), b2 + hstepB, voffB); PG8_STAGE(PG8_SA(0, 0), a2, voffA);
;             PG8_WAIT_V(8); PG8_WAIT_L(0); PG8_BAR; PG8_MMA(1, 0, At, B0); PG8_MMA(1, 1, At, B1); PG8_BAR; PG8_SCHED;
;             PG8_LDB(B0, 1, 0); PG8_LDB(B1, 1, 1); PG8_SCHED; PG8_LDA(At, 1, 0); PG8_STAGE(PG8_SA(0, 1), a2 + hstepA, voffA);
;             PG8_WAIT_V(8); PG8_WAIT_L(0); PG8_BAR; PG8_MMA(0, 0, At, B0); PG8_MMA(0, 1, At, B1); PG8_BAR; PG8_SCHED;
;             PG8_LDA(At, 1, 1); PG8_STAGE(PG8_SB(1, 0), b3, voffB); PG8_STAGE(PG8_SB(1, 1), b3 + hstepB, voffB); PG8_STAGE(PG8_SA(1, 0), a3, voffA);
;             PG8_WAIT_V(8); PG8_WAIT_L(0); PG8_BAR; PG8_MMA(1, 0, At, B0); PG8_MMA(1, 1, At, B1); PG8_BAR; PG8_SCHED;
	s_add_i32 s71, s65, s39
	s_add_u32 s98, s34, 0x80
	s_addc_u32 s99, s35, 0
	s_mov_b32 m0, s71
	s_nop 0
	global_load_lds_dwordx4 v154, s[34:35]
	s_add_i32 m0, s71, 0x2000
	s_add_u32 s72, s34, 0x40000
	s_addc_u32 s73, s35, 0
	s_add_i32 s71, s66, s39
	global_load_lds_dwordx4 v158, s[34:35]
	s_mov_b32 m0, s71
	s_add_u32 s100, s36, 0x80
	s_addc_u32 s101, s37, 0
	global_load_lds_dwordx4 v154, s[72:73]
	s_add_i32 m0, s71, 0x2000
	s_nop 0
	global_load_lds_dwordx4 v158, s[72:73]
	s_mov_b32 m0, s40
	s_nop 0
	global_load_lds_dwordx4 v152, s[36:37]
	s_mov_b32 m0, s41
	s_nop 0
	global_load_lds_dwordx4 v156, s[36:37]
	ds_read_b128 v[180:183], v192 offset:16384
	ds_read_b128 v[184:187], v192 offset:17408
	ds_read_b128 v[194:197], v192 offset:18432
	ds_read_b128 v[198:201], v192 offset:19456
	ds_read_b128 v[202:205], v192 offset:20480
	ds_read_b128 v[206:209], v192 offset:21504
	ds_read_b128 v[210:213], v192 offset:22528
	ds_read_b128 v[214:217], v192 offset:23552
	s_waitcnt vmcnt(8) lgkmcnt(0)
	s_barrier
	s_setprio 1
	v_mfma_f32_16x16x32_bf16 v[60:63], v[128:131], v[180:183], v[60:63]
	v_mfma_f32_16x16x32_bf16 v[56:59], v[136:139], v[180:183], v[56:59]
	v_mfma_f32_16x16x32_bf16 v[44:47], v[128:131], v[194:197], v[44:47]
	v_mfma_f32_16x16x32_bf16 v[40:43], v[136:139], v[194:197], v[40:43]
	v_mfma_f32_16x16x32_bf16 v[28:31], v[128:131], v[202:205], v[28:31]
	v_mfma_f32_16x16x32_bf16 v[24:27], v[136:139], v[202:205], v[24:27]
	v_mfma_f32_16x16x32_bf16 v[12:15], v[128:131], v[210:213], v[12:15]
	v_mfma_f32_16x16x32_bf16 v[8:11], v[136:139], v[210:213], v[8:11]
	v_mfma_f32_16x16x32_bf16 v[60:63], v[132:135], v[184:187], v[60:63]
	v_mfma_f32_16x16x32_bf16 v[56:59], v[140:143], v[184:187], v[56:59]
	v_mfma_f32_16x16x32_bf16 v[44:47], v[132:135], v[198:201], v[44:47]
	v_mfma_f32_16x16x32_bf16 v[40:43], v[140:143], v[198:201], v[40:43]
	v_mfma_f32_16x16x32_bf16 v[28:31], v[132:135], v[206:209], v[28:31]
	v_mfma_f32_16x16x32_bf16 v[24:27], v[140:143], v[206:209], v[24:27]
	v_mfma_f32_16x16x32_bf16 v[12:15], v[132:135], v[214:217], v[12:15]
	v_mfma_f32_16x16x32_bf16 v[8:11], v[140:143], v[214:217], v[8:11]
	s_setprio 0
	s_setprio 1
	v_mfma_f32_16x16x32_bf16 v[52:55], v[144:147], v[180:183], v[52:55]
	v_mfma_f32_16x16x32_bf16 v[48:51], v[172:175], v[180:183], v[48:51]
	v_mfma_f32_16x16x32_bf16 v[36:39], v[144:147], v[194:197], v[36:39]
	v_mfma_f32_16x16x32_bf16 v[32:35], v[172:175], v[194:197], v[32:35]
	v_mfma_f32_16x16x32_bf16 v[20:23], v[144:147], v[202:205], v[20:23]
	v_mfma_f32_16x16x32_bf16 v[16:19], v[172:175], v[202:205], v[16:19]
	v_mfma_f32_16x16x32_bf16 v[4:7], v[144:147], v[210:213], v[4:7]
	v_mfma_f32_16x16x32_bf16 v[0:3], v[172:175], v[210:213], v[0:3]
	v_mfma_f32_16x16x32_bf16 v[52:55], v[148:151], v[184:187], v[52:55]
	v_mfma_f32_16x16x32_bf16 v[48:51], v[176:179], v[184:187], v[48:51]
	v_mfma_f32_16x16x32_bf16 v[36:39], v[148:151], v[198:201], v[36:39]
	v_mfma_f32_16x16x32_bf16 v[32:35], v[176:179], v[198:201], v[32:35]
	v_mfma_f32_16x16x32_bf16 v[20:23], v[148:151], v[206:209], v[20:23]
	v_mfma_f32_16x16x32_bf16 v[16:19], v[176:179], v[206:209], v[16:19]
	v_mfma_f32_16x16x32_bf16 v[4:7], v[148:151], v[214:217], v[4:7]
	v_mfma_f32_16x16x32_bf16 v[0:3], v[176:179], v[214:217], v[0:3]
	s_setprio 0
	s_barrier
	s_add_i32 s71, 0, 0x18000
	s_add_i32 s72, 0, 0x1c000
	s_add_u32 s36, s36, 0x40000
	s_addc_u32 s37, s37, 0
	s_mov_b32 m0, s44
	s_nop 0
	global_load_lds_dwordx4 v152, s[36:37]
	s_mov_b32 m0, s45
	s_nop 0
	global_load_lds_dwordx4 v156, s[36:37]
	ds_read_b128 v[128:131], v252
	ds_read_b128 v[132:135], v252 offset:1024
	ds_read_b128 v[136:139], v252 offset:2048
	ds_read_b128 v[140:143], v252 offset:3072
	ds_read_b128 v[144:147], v253
	ds_read_b128 v[148:151], v253 offset:1024
	ds_read_b128 v[172:175], v253 offset:2048
	ds_read_b128 v[176:179], v253 offset:3072
	ds_read_b128 v[180:183], v192 offset:32768
	ds_read_b128 v[184:187], v192 offset:33792
	ds_read_b128 v[194:197], v192 offset:34816
	ds_read_b128 v[198:201], v192 offset:35840
	ds_read_b128 v[202:205], v192 offset:36864
	ds_read_b128 v[206:209], v192 offset:37888
	ds_read_b128 v[210:213], v192 offset:38912
	ds_read_b128 v[214:217], v192 offset:39936
	s_waitcnt vmcnt(8) lgkmcnt(0)
	s_barrier
; #define PG8_STAGE(bufoff, gbase, voff) do { _Pragma("unroll") for (int _i = 0; _i < 2; ++_i) \
;         __builtin_amdgcn_global_load_lds((const unsigned*)((const char*)(gbase) + (voff)[_i]), (PG8_LAS unsigned*)(lds + (bufoff) + ldsw + _i * 8192), 16, 0, 0); } while (0)
; #define PG8_LDA(dst, b, h) do { _Pragma("unroll") for (int m = 0; m < 4; ++m) _Pragma("unroll") for (int k = 0; k < 2; ++k) dst[m][k] = *(const PG8_LAS bf16x8*)(lds + PG8_SA(b, h) + aoff + m * 2048 + k * 1024); } while (0)
; #define PG8_LDB(dst, b, h) do { _Pragma("unroll") for (int n = 0; n < 2; ++n) _Pragma("unroll") for (int k = 0; k < 2; ++k) dst[n][k] = *(const PG8_LAS bf16x8*)(lds + PG8_SB(b, h) + boff + n * 2048 + k * 1024); } while (0)
; #define PG8_WAIT_V(n) asm volatile("s_waitcnt vmcnt(" #n ")" ::: "memory")
; #define PG8_WAIT_L(n) asm volatile("s_waitcnt lgkmcnt(" #n ")" ::: "memory")
; #define PG8_BAR __builtin_amdgcn_s_barrier()
; template <class Epi, class Sched, bool ALIGN_EPI = false, bool SP2 = false>
; __device__ __forceinline__ void gemm_phase(PG8_LAS unsigned char* lds, const Gemm g, const Sched& S, const Epi& E, const int wid) {
;     ...
;             if constexpr (SP2) {
;             PG8_LDB(B0, 0, 0); PG8_LDB(B1, 0, 1); PG8_SCHED; PG8_LDA(At, 0, 0); PG8_STAGE(PG8_SA(1, 1), a1 + hstepA, voffA);
;             PG8_WAIT_V(8); PG8_WAIT_L(0); PG8_BAR; PG8_MMA(0, 0, At, B0); PG8_MMA(0, 1, At, B1); PG8_BAR; PG8_SCHED;
;             PG8_LDA(At, 0, 1); PG8_STAGE(PG8_SB(0, 0), b2, voffB); PG8_STAGE(PG8_SB(0, 1), b2 + hstepB, voffB); PG8_STAGE(PG8_SA(0, 0), a2, voffA);
;             PG8_WAIT_V(8); PG8_WAIT_L(0); PG8_BAR; PG8_MMA(1, 0, At, B0); PG8_MMA(1, 1, At, B1); PG8_BAR; PG8_SCHED;
;             PG8_LDB(B0, 1, 0); PG8_LDB(B1, 1, 1); PG8_SCHED; PG8_LDA(At, 1, 0); PG8_STAGE(PG8_SA(0, 1), a2 + hstepA, voffA);
;             PG8_WAIT_V(8); PG8_WAIT_L(0); PG8_BAR; PG8_MMA(0, 0, At, B0); PG8_MMA(0, 1, At, B1); PG8_BAR; PG8_SCHED;
;             PG8_LDA(At, 1, 1); PG8_STAGE(PG8_SB(1, 0), b3, voffB); PG8_STAGE(PG8_SB(1, 1), b3 + hstepB, voffB); PG8_STAGE(PG8_SA(1, 0), a3, voffA);
;             PG8_WAIT_V(8); PG8_WAIT_L(0); PG8_BAR; PG8_MMA(1, 0, At, B0); PG8_MMA(1, 1, At, B1); PG8_BAR; PG8_SCHED;
;     ...
;         if constexpr (ALIGN_EPI) { if (wr == 0) PG8_BAR; }
;         if constexpr (!Epi::AFTER_DRAIN) { E(acc, cur, wr, wc, fr, fq); S.done(cur); }
;         if (!has_next) break;
	s_setprio 1
	v_mfma_f32_16x16x32_bf16 v[124:127], v[128:131], v[180:183], v[124:127]
	v_mfma_f32_16x16x32_bf16 v[120:123], v[136:139], v[180:183], v[120:123]
	v_mfma_f32_16x16x32_bf16 v[108:111], v[128:131], v[194:197], v[108:111]
	v_mfma_f32_16x16x32_bf16 v[104:107], v[136:139], v[194:197], v[104:107]
	v_mfma_f32_16x16x32_bf16 v[92:95], v[128:131], v[202:205], v[92:95]
	v_mfma_f32_16x16x32_bf16 v[88:91], v[136:139], v[202:205], v[88:91]
	v_mfma_f32_16x16x32_bf16 v[76:79], v[128:131], v[210:213], v[76:79]
	v_mfma_f32_16x16x32_bf16 v[72:75], v[136:139], v[210:213], v[72:75]
	v_mfma_f32_16x16x32_bf16 v[124:127], v[132:135], v[184:187], v[124:127]
	v_mfma_f32_16x16x32_bf16 v[120:123], v[140:143], v[184:187], v[120:123]
	v_mfma_f32_16x16x32_bf16 v[108:111], v[132:135], v[198:201], v[108:111]
	v_mfma_f32_16x16x32_bf16 v[104:107], v[140:143], v[198:201], v[104:107]
	v_mfma_f32_16x16x32_bf16 v[92:95], v[132:135], v[206:209], v[92:95]
	v_mfma_f32_16x16x32_bf16 v[88:91], v[140:143], v[206:209], v[88:91]
	v_mfma_f32_16x16x32_bf16 v[76:79], v[132:135], v[214:217], v[76:79]
	v_mfma_f32_16x16x32_bf16 v[72:75], v[140:143], v[214:217], v[72:75]
	s_setprio 0
	s_setprio 1
	v_mfma_f32_16x16x32_bf16 v[116:119], v[144:147], v[180:183], v[116:119]
	v_mfma_f32_16x16x32_bf16 v[112:115], v[172:175], v[180:183], v[112:115]
	v_mfma_f32_16x16x32_bf16 v[100:103], v[144:147], v[194:197], v[100:103]
	v_mfma_f32_16x16x32_bf16 v[96:99], v[172:175], v[194:197], v[96:99]
	v_mfma_f32_16x16x32_bf16 v[84:87], v[144:147], v[202:205], v[84:87]
	v_mfma_f32_16x16x32_bf16 v[80:83], v[172:175], v[202:205], v[80:83]
	v_mfma_f32_16x16x32_bf16 v[68:71], v[144:147], v[210:213], v[68:71]
	v_mfma_f32_16x16x32_bf16 v[64:67], v[172:175], v[210:213], v[64:67]
	v_mfma_f32_16x16x32_bf16 v[116:119], v[148:151], v[184:187], v[116:119]
	v_mfma_f32_16x16x32_bf16 v[112:115], v[176:179], v[184:187], v[112:115]
	v_mfma_f32_16x16x32_bf16 v[100:103], v[148:151], v[198:201], v[100:103]
	v_mfma_f32_16x16x32_bf16 v[96:99], v[176:179], v[198:201], v[96:99]
	v_mfma_f32_16x16x32_bf16 v[84:87], v[148:151], v[206:209], v[84:87]
	v_mfma_f32_16x16x32_bf16 v[80:83], v[176:179], v[206:209], v[80:83]
	v_mfma_f32_16x16x32_bf16 v[68:71], v[148:151], v[214:217], v[68:71]
	v_mfma_f32_16x16x32_bf16 v[64:67], v[176:179], v[214:217], v[64:67]
	s_setprio 0
	s_barrier
	s_add_i32 s36, s71, s39
	s_mov_b32 m0, s36
	s_nop 0
	global_load_lds_dwordx4 v154, s[98:99]
	s_add_i32 m0, s36, 0x2000
	s_add_u32 s34, s34, 0x40080
	s_addc_u32 s35, s35, 0
	s_add_i32 s36, s72, s39
	global_load_lds_dwordx4 v158, s[98:99]
	s_mov_b32 m0, s36
	s_nop 0
	global_load_lds_dwordx4 v154, s[34:35]
	s_add_i32 m0, s36, 0x2000
	s_nop 0
	global_load_lds_dwordx4 v158, s[34:35]
	s_mov_b32 m0, s47
	s_nop 0
	global_load_lds_dwordx4 v152, s[100:101]
	s_mov_b32 m0, s48
	s_nop 0
	global_load_lds_dwordx4 v156, s[100:101]
	ds_read_b128 v[180:183], v192 offset:49152
	ds_read_b128 v[184:187], v192 offset:50176
	ds_read_b128 v[194:197], v192 offset:51200
	ds_read_b128 v[198:201], v192 offset:52224
	ds_read_b128 v[202:205], v192 offset:53248
	ds_read_b128 v[206:209], v192 offset:54272
	ds_read_b128 v[210:213], v192 offset:55296
	ds_read_b128 v[214:217], v192 offset:56320
	s_waitcnt vmcnt(8) lgkmcnt(0)
	s_barrier
	s_setprio 1
	v_mfma_f32_16x16x32_bf16 v[60:63], v[128:131], v[180:183], v[60:63]
	v_mfma_f32_16x16x32_bf16 v[56:59], v[136:139], v[180:183], v[56:59]
	v_mfma_f32_16x16x32_bf16 v[44:47], v[128:131], v[194:197], v[44:47]
	v_mfma_f32_16x16x32_bf16 v[40:43], v[136:139], v[194:197], v[40:43]
	v_mfma_f32_16x16x32_bf16 v[28:31], v[128:131], v[202:205], v[28:31]
	v_mfma_f32_16x16x32_bf16 v[24:27], v[136:139], v[202:205], v[24:27]
	v_mfma_f32_16x16x32_bf16 v[12:15], v[128:131], v[210:213], v[12:15]
	v_mfma_f32_16x16x32_bf16 v[8:11], v[136:139], v[210:213], v[8:11]
	v_mfma_f32_16x16x32_bf16 v[60:63], v[132:135], v[184:187], v[60:63]
	v_mfma_f32_16x16x32_bf16 v[56:59], v[140:143], v[184:187], v[56:59]
	v_mfma_f32_16x16x32_bf16 v[44:47], v[132:135], v[198:201], v[44:47]
	v_mfma_f32_16x16x32_bf16 v[40:43], v[140:143], v[198:201], v[40:43]
	v_mfma_f32_16x16x32_bf16 v[28:31], v[132:135], v[206:209], v[28:31]
	v_mfma_f32_16x16x32_bf16 v[24:27], v[140:143], v[206:209], v[24:27]
	v_mfma_f32_16x16x32_bf16 v[12:15], v[132:135], v[214:217], v[12:15]
	v_mfma_f32_16x16x32_bf16 v[8:11], v[140:143], v[214:217], v[8:11]
	s_setprio 0
	s_setprio 1
	v_mfma_f32_16x16x32_bf16 v[52:55], v[144:147], v[180:183], v[52:55]
	v_mfma_f32_16x16x32_bf16 v[48:51], v[172:175], v[180:183], v[48:51]
	v_mfma_f32_16x16x32_bf16 v[36:39], v[144:147], v[194:197], v[36:39]
	v_mfma_f32_16x16x32_bf16 v[32:35], v[172:175], v[194:197], v[32:35]
	v_mfma_f32_16x16x32_bf16 v[20:23], v[144:147], v[202:205], v[20:23]
	v_mfma_f32_16x16x32_bf16 v[16:19], v[172:175], v[202:205], v[16:19]
	v_mfma_f32_16x16x32_bf16 v[4:7], v[144:147], v[210:213], v[4:7]
	v_mfma_f32_16x16x32_bf16 v[0:3], v[172:175], v[210:213], v[0:3]
	v_mfma_f32_16x16x32_bf16 v[52:55], v[148:151], v[184:187], v[52:55]
	v_mfma_f32_16x16x32_bf16 v[48:51], v[176:179], v[184:187], v[48:51]
	v_mfma_f32_16x16x32_bf16 v[36:39], v[148:151], v[198:201], v[36:39]
	v_mfma_f32_16x16x32_bf16 v[32:35], v[176:179], v[198:201], v[32:35]
	v_mfma_f32_16x16x32_bf16 v[20:23], v[148:151], v[206:209], v[20:23]
	v_mfma_f32_16x16x32_bf16 v[16:19], v[176:179], v[206:209], v[16:19]
	v_mfma_f32_16x16x32_bf16 v[4:7], v[148:151], v[214:217], v[4:7]
	v_mfma_f32_16x16x32_bf16 v[0:3], v[176:179], v[214:217], v[0:3]
	s_setprio 0
	s_barrier
	s_add_i32 s70, s70, 2
	s_add_u32 s30, s30, 0x100
	s_addc_u32 s31, s31, 0
	s_add_u32 s68, s68, 0x100
	s_addc_u32 s69, s69, 0
	s_cmp_gt_u32 s70, 13
	s_cbranch_scc0 .LBB0_1780
	s_and_b64 vcc, exec, s[16:17]
	s_cbranch_vccz .LBB0_1783
	s_barrier

; #define PG8_STAGE(bufoff, gbase, voff) do { _Pragma("unroll") for (int _i = 0; _i < 2; ++_i) \
;         __builtin_amdgcn_global_load_lds((const unsigned*)((const char*)(gbase) + (voff)[_i]), (PG8_LAS unsigned*)(lds + (bufoff) + ldsw + _i * 8192), 16, 0, 0); } while (0)
; #define PG8_WAIT_V(n) asm volatile("s_waitcnt vmcnt(" #n ")" ::: "memory")
; #define PG8_WAIT_L(n) asm volatile("s_waitcnt lgkmcnt(" #n ")" ::: "memory")
; #define PG8_BAR __builtin_amdgcn_s_barrier()
; template <class Epi, class Sched, bool ALIGN_EPI = false, bool SP2 = false>
; __device__ __forceinline__ void gemm_phase(PG8_LAS unsigned char* lds, const Gemm g, const Sched& S, const Epi& E, const int wid) {
;     ...
;         const bool has_next = S.next(ui + 1, nxt);
;         const char* nA = has_next ? (const char*)g.A + (size_t)nxt.pm * tstepA : cA; const char* nB = has_next ? (const char*)g.Bt + (size_t)nxt.pn * tstepB : cB;
;         for (int t = 0; t < nt; t += 2) {
;             const bool last = (t == nt - 2);
;             const char* a1 = cA + (size_t)(t + 1) * kstep;
;             const char* a2 = last ? nA : cA + (size_t)(t + 2) * kstep; const char* b2 = last ? nB : cB + (size_t)(t + 2) * kstep;
;             const char* a3 = a2 + kstep; const char* b3 = b2 + kstep;
;             if (last && has_next) S.a_ready(nxt);
;             if constexpr (SP2) {
;             PG8_LDB(B0, 0, 0); PG8_LDB(B1, 0, 1); PG8_SCHED; PG8_LDA(At, 0, 0); PG8_STAGE(PG8_SA(1, 1), a1 + hstepA, voffA);
;             PG8_WAIT_V(8); PG8_WAIT_L(0); PG8_BAR; PG8_MMA(0, 0, At, B0); PG8_MMA(0, 1, At, B1); PG8_BAR; PG8_SCHED;
;             PG8_LDA(At, 0, 1); PG8_STAGE(PG8_SB(0, 0), b2, voffB); PG8_STAGE(PG8_SB(0, 1), b2 + hstepB, voffB); PG8_STAGE(PG8_SA(0, 0), a2, voffA);
;             PG8_WAIT_V(8); PG8_WAIT_L(0); PG8_BAR; PG8_MMA(1, 0, At, B0); PG8_MMA(1, 1, At, B1); PG8_BAR; PG8_SCHED;
;             PG8_LDB(B0, 1, 0); PG8_LDB(B1, 1, 1); PG8_SCHED; PG8_LDA(At, 1, 0); PG8_STAGE(PG8_SA(0, 1), a2 + hstepA, voffA);
;             PG8_WAIT_V(8); PG8_WAIT_L(0); PG8_BAR; PG8_MMA(0, 0, At, B0); PG8_MMA(0, 1, At, B1); PG8_BAR; PG8_SCHED;
;             PG8_LDA(At, 1, 1); PG8_STAGE(PG8_SB(1, 0), b3, voffB); PG8_STAGE(PG8_SB(1, 1), b3 + hstepB, voffB); PG8_STAGE(PG8_SA(1, 0), a3, voffA);
;             PG8_WAIT_V(8); PG8_WAIT_L(0); PG8_BAR; PG8_MMA(1, 0, At, B0); PG8_MMA(1, 1, At, B1); PG8_BAR; PG8_SCHED;
.LBB0_1866:
	s_ashr_i32 s17, s16, 31
	s_lshl_b64 s[18:19], s[16:17], 19
	s_add_u32 s18, s0, s18
	s_addc_u32 s19, s1, s19
	s_and_b64 s[20:21], s[2:3], exec
	s_cselect_b32 s17, s19, s25
	s_cselect_b32 s49, s18, s24
	s_ashr_i32 s15, s14, 31
	s_lshl_b64 s[20:21], s[14:15], 19
	s_add_u32 s20, s30, s20
	s_addc_u32 s21, s31, s21
	s_and_b64 s[28:29], s[2:3], exec
	s_cselect_b32 s15, s21, s27
	s_cselect_b32 s64, s20, s26
	s_add_u32 s24, s24, 0x40080
	s_addc_u32 s25, s25, 0
	s_add_u32 s65, s26, 0x100
	s_addc_u32 s66, s27, 0
	s_mov_b32 s67, -2
	v_add_u32_e32 v252, 0x18000, v165
	v_add_u32_e32 v253, 0x1c000, v165
	s_add_u32 s26, s24, 0xfffc0080
	s_addc_u32 s27, s25, -1
	s_cmp_eq_u32 s67, 12
	s_cselect_b32 s29, s17, s27
	s_cselect_b32 s28, s49, s26
	s_cselect_b32 s27, s15, s66
	s_cselect_b32 s26, s64, s65
	s_add_i32 m0, s36, 0xc000
	s_nop 0
	global_load_lds_dwordx4 v140, s[24:25]
	s_add_i32 m0, s36, 0xe000
	s_nop 0
	global_load_lds_dwordx4 v142, s[24:25]
	ds_read_b128 v[148:151], v166
	ds_read_b128 v[152:155], v166 offset:1024
	ds_read_b128 v[156:159], v166 offset:2048
	ds_read_b128 v[160:163], v166 offset:3072
	ds_read_b128 v[172:175], v167
	ds_read_b128 v[176:179], v167 offset:1024
	ds_read_b128 v[180:183], v167 offset:2048
	ds_read_b128 v[184:187], v167 offset:3072
	ds_read_b128 v[188:191], v168
	ds_read_b128 v[192:195], v168 offset:1024
	ds_read_b128 v[196:199], v168 offset:2048
	ds_read_b128 v[200:203], v168 offset:3072
	ds_read_b128 v[204:207], v168 offset:4096
	ds_read_b128 v[208:211], v168 offset:5120
	ds_read_b128 v[212:215], v168 offset:6144
	ds_read_b128 v[216:219], v168 offset:7168
	s_waitcnt vmcnt(8) lgkmcnt(0)
	v_lshl_add_u32 v220, s22, 8, v164
	v_add_u32_e32 v236, 0x80, v220
	v_ashrrev_i32_e32 v221, 31, v220
	v_ashrrev_i32_e32 v237, 31, v236
	v_lshlrev_b64 v[220:221], 6, v[220:221]
	v_lshlrev_b64 v[236:237], 6, v[236:237]
	v_lshl_add_u64 v[220:221], v[138:139], 0, v[220:221]
	v_lshl_add_u64 v[236:237], v[138:139], 0, v[236:237]
	global_load_dwordx4 v[224:227], v[220:221], off offset:1024
	global_load_dwordx4 v[228:231], v[220:221], off offset:2048
	global_load_dwordx4 v[232:235], v[220:221], off offset:3072
	global_load_dwordx4 v[240:243], v[236:237], off offset:1024
	global_load_dwordx4 v[244:247], v[236:237], off offset:2048
	global_load_dwordx4 v[248:251], v[236:237], off offset:3072
	s_nop 0
	global_load_dwordx4 v[220:223], v[220:221], off
	s_nop 0
	global_load_dwordx4 v[236:239], v[236:237], off
	s_barrier
	s_setprio 1
	v_mfma_f32_16x16x32_bf16 v[124:127], v[148:151], v[188:191], 0
	v_mfma_f32_16x16x32_bf16 v[116:119], v[156:159], v[188:191], 0
	v_mfma_f32_16x16x32_bf16 v[108:111], v[148:151], v[196:199], 0
	v_mfma_f32_16x16x32_bf16 v[100:103], v[156:159], v[196:199], 0
	v_mfma_f32_16x16x32_bf16 v[92:95], v[148:151], v[204:207], 0
	v_mfma_f32_16x16x32_bf16 v[84:87], v[156:159], v[204:207], 0
	v_mfma_f32_16x16x32_bf16 v[76:79], v[148:151], v[212:215], 0
	v_mfma_f32_16x16x32_bf16 v[68:71], v[156:159], v[212:215], 0
	v_mfma_f32_16x16x32_bf16 v[124:127], v[152:155], v[192:195], v[124:127]
	v_mfma_f32_16x16x32_bf16 v[116:119], v[160:163], v[192:195], v[116:119]
	v_mfma_f32_16x16x32_bf16 v[108:111], v[152:155], v[200:203], v[108:111]
	v_mfma_f32_16x16x32_bf16 v[100:103], v[160:163], v[200:203], v[100:103]
	v_mfma_f32_16x16x32_bf16 v[92:95], v[152:155], v[208:211], v[92:95]
	v_mfma_f32_16x16x32_bf16 v[84:87], v[160:163], v[208:211], v[84:87]
	v_mfma_f32_16x16x32_bf16 v[76:79], v[152:155], v[216:219], v[76:79]
	v_mfma_f32_16x16x32_bf16 v[68:71], v[160:163], v[216:219], v[68:71]
	s_setprio 0
	s_setprio 1
	v_mfma_f32_16x16x32_bf16 v[120:123], v[172:175], v[188:191], 0
	v_mfma_f32_16x16x32_bf16 v[112:115], v[180:183], v[188:191], 0
	v_mfma_f32_16x16x32_bf16 v[104:107], v[172:175], v[196:199], 0
	v_mfma_f32_16x16x32_bf16 v[96:99], v[180:183], v[196:199], 0
	v_mfma_f32_16x16x32_bf16 v[88:91], v[172:175], v[204:207], 0
	v_mfma_f32_16x16x32_bf16 v[80:83], v[180:183], v[204:207], 0
	v_mfma_f32_16x16x32_bf16 v[72:75], v[172:175], v[212:215], 0
	v_mfma_f32_16x16x32_bf16 v[64:67], v[180:183], v[212:215], 0
	v_mfma_f32_16x16x32_bf16 v[120:123], v[176:179], v[192:195], v[120:123]
	v_mfma_f32_16x16x32_bf16 v[112:115], v[184:187], v[192:195], v[112:115]
	v_mfma_f32_16x16x32_bf16 v[104:107], v[176:179], v[200:203], v[104:107]
	v_mfma_f32_16x16x32_bf16 v[96:99], v[184:187], v[200:203], v[96:99]
	v_mfma_f32_16x16x32_bf16 v[88:91], v[176:179], v[208:211], v[88:91]
	v_mfma_f32_16x16x32_bf16 v[80:83], v[184:187], v[208:211], v[80:83]
	v_mfma_f32_16x16x32_bf16 v[72:75], v[176:179], v[216:219], v[72:75]
	v_mfma_f32_16x16x32_bf16 v[64:67], v[184:187], v[216:219], v[64:67]
	s_setprio 0
	s_barrier
	s_add_i32 s68, s45, s33
	s_add_u32 s98, s26, 0x80
	s_addc_u32 s99, s27, 0
	s_mov_b32 m0, s68
	s_nop 0
	global_load_lds_dwordx4 v132, s[26:27]
	s_add_i32 m0, s68, 0x2000
	s_add_u32 s68, s26, 0x40000
	s_addc_u32 s69, s27, 0
	s_add_i32 s70, s46, s33
	global_load_lds_dwordx4 v128, s[26:27]
	s_mov_b32 m0, s70
	s_add_u32 s100, s28, 0x80
	s_addc_u32 s101, s29, 0
	global_load_lds_dwordx4 v132, s[68:69]
	s_add_i32 m0, s70, 0x2000
	s_nop 0
	global_load_lds_dwordx4 v128, s[68:69]
	s_mov_b32 m0, s36
	s_nop 0
	global_load_lds_dwordx4 v134, s[28:29]
	s_mov_b32 m0, s37
	s_nop 0
	global_load_lds_dwordx4 v130, s[28:29]
	ds_read_b128 v[188:191], v168 offset:16384
	ds_read_b128 v[192:195], v168 offset:17408
	ds_read_b128 v[196:199], v168 offset:18432
	ds_read_b128 v[200:203], v168 offset:19456
	ds_read_b128 v[204:207], v168 offset:20480
	ds_read_b128 v[208:211], v168 offset:21504
	ds_read_b128 v[212:215], v168 offset:22528
	ds_read_b128 v[216:219], v168 offset:23552
	s_waitcnt vmcnt(8) lgkmcnt(0)
	s_barrier
; #define PG8_STAGE(bufoff, gbase, voff) do { _Pragma("unroll") for (int _i = 0; _i < 2; ++_i) \
;         __builtin_amdgcn_global_load_lds((const unsigned*)((const char*)(gbase) + (voff)[_i]), (PG8_LAS unsigned*)(lds + (bufoff) + ldsw + _i * 8192), 16, 0, 0); } while (0)
; #define PG8_LDA(dst, b, h) do { _Pragma("unroll") for (int m = 0; m < 4; ++m) _Pragma("unroll") for (int k = 0; k < 2; ++k) dst[m][k] = *(const PG8_LAS bf16x8*)(lds + PG8_SA(b, h) + aoff + m * 2048 + k * 1024); } while (0)
; #define PG8_LDB(dst, b, h) do { _Pragma("unroll") for (int n = 0; n < 2; ++n) _Pragma("unroll") for (int k = 0; k < 2; ++k) dst[n][k] = *(const PG8_LAS bf16x8*)(lds + PG8_SB(b, h) + boff + n * 2048 + k * 1024); } while (0)
; #define PG8_MMA(ai, bj, At, Bt) do { __builtin_amdgcn_s_setprio(1); _Pragma("unroll") for (int m = 0; m < 4; ++m) _Pragma("unroll") for (int n = 0; n < 2; ++n) _Pragma("unroll") for (int k = 0; k < 2; ++k) \
;         acc[ai][bj][m][n] = __builtin_amdgcn_mfma_f32_16x16x32_bf16(Bt[n][k], At[m][k], acc[ai][bj][m][n], 0, 0, 0); __builtin_amdgcn_s_setprio(0); } while (0)
; template <class Epi, class Sched, bool ALIGN_EPI = false, bool SP2 = false>
; __device__ __forceinline__ void gemm_phase(PG8_LAS unsigned char* lds, const Gemm g, const Sched& S, const Epi& E, const int wid) {
;     ...
;             if constexpr (SP2) {
;             PG8_LDB(B0, 0, 0); PG8_LDB(B1, 0, 1); PG8_SCHED; PG8_LDA(At, 0, 0); PG8_STAGE(PG8_SA(1, 1), a1 + hstepA, voffA);
;             PG8_WAIT_V(8); PG8_WAIT_L(0); PG8_BAR; PG8_MMA(0, 0, At, B0); PG8_MMA(0, 1, At, B1); PG8_BAR; PG8_SCHED;
;             PG8_LDA(At, 0, 1); PG8_STAGE(PG8_SB(0, 0), b2, voffB); PG8_STAGE(PG8_SB(0, 1), b2 + hstepB, voffB); PG8_STAGE(PG8_SA(0, 0), a2, voffA);
;             PG8_WAIT_V(8); PG8_WAIT_L(0); PG8_BAR; PG8_MMA(1, 0, At, B0); PG8_MMA(1, 1, At, B1); PG8_BAR; PG8_SCHED;
;             PG8_LDB(B0, 1, 0); PG8_LDB(B1, 1, 1); PG8_SCHED; PG8_LDA(At, 1, 0); PG8_STAGE(PG8_SA(0, 1), a2 + hstepA, voffA);
;             PG8_WAIT_V(8); PG8_WAIT_L(0); PG8_BAR; PG8_MMA(0, 0, At, B0); PG8_MMA(0, 1, At, B1); PG8_BAR; PG8_SCHED;
;             PG8_LDA(At, 1, 1); PG8_STAGE(PG8_SB(1, 0), b3, voffB); PG8_STAGE(PG8_SB(1, 1), b3 + hstepB, voffB); PG8_STAGE(PG8_SA(1, 0), a3, voffA);
;             PG8_WAIT_V(8); PG8_WAIT_L(0); PG8_BAR; PG8_MMA(1, 0, At, B0); PG8_MMA(1, 1, At, B1); PG8_BAR; PG8_SCHED;
	s_setprio 1
	v_mfma_f32_16x16x32_bf16 v[60:63], v[148:151], v[188:191], 0
	v_mfma_f32_16x16x32_bf16 v[52:55], v[156:159], v[188:191], 0
	v_mfma_f32_16x16x32_bf16 v[44:47], v[148:151], v[196:199], 0
	v_mfma_f32_16x16x32_bf16 v[36:39], v[156:159], v[196:199], 0
	v_mfma_f32_16x16x32_bf16 v[28:31], v[148:151], v[204:207], 0
	v_mfma_f32_16x16x32_bf16 v[20:23], v[156:159], v[204:207], 0
	v_mfma_f32_16x16x32_bf16 v[12:15], v[148:151], v[212:215], 0
	v_mfma_f32_16x16x32_bf16 v[4:7], v[156:159], v[212:215], 0
	v_mfma_f32_16x16x32_bf16 v[60:63], v[152:155], v[192:195], v[60:63]
	v_mfma_f32_16x16x32_bf16 v[52:55], v[160:163], v[192:195], v[52:55]
	v_mfma_f32_16x16x32_bf16 v[44:47], v[152:155], v[200:203], v[44:47]
	v_mfma_f32_16x16x32_bf16 v[36:39], v[160:163], v[200:203], v[36:39]
	v_mfma_f32_16x16x32_bf16 v[28:31], v[152:155], v[208:211], v[28:31]
	v_mfma_f32_16x16x32_bf16 v[20:23], v[160:163], v[208:211], v[20:23]
	v_mfma_f32_16x16x32_bf16 v[12:15], v[152:155], v[216:219], v[12:15]
	v_mfma_f32_16x16x32_bf16 v[4:7], v[160:163], v[216:219], v[4:7]
	s_setprio 0
	s_setprio 1
	v_mfma_f32_16x16x32_bf16 v[56:59], v[172:175], v[188:191], 0
	v_mfma_f32_16x16x32_bf16 v[48:51], v[180:183], v[188:191], 0
	v_mfma_f32_16x16x32_bf16 v[40:43], v[172:175], v[196:199], 0
	v_mfma_f32_16x16x32_bf16 v[32:35], v[180:183], v[196:199], 0
	v_mfma_f32_16x16x32_bf16 v[24:27], v[172:175], v[204:207], 0
	v_mfma_f32_16x16x32_bf16 v[16:19], v[180:183], v[204:207], 0
	v_mfma_f32_16x16x32_bf16 v[8:11], v[172:175], v[212:215], 0
	v_mfma_f32_16x16x32_bf16 v[0:3], v[180:183], v[212:215], 0
	v_mfma_f32_16x16x32_bf16 v[56:59], v[176:179], v[192:195], v[56:59]
	v_mfma_f32_16x16x32_bf16 v[48:51], v[184:187], v[192:195], v[48:51]
	v_mfma_f32_16x16x32_bf16 v[40:43], v[176:179], v[200:203], v[40:43]
	v_mfma_f32_16x16x32_bf16 v[32:35], v[184:187], v[200:203], v[32:35]
	v_mfma_f32_16x16x32_bf16 v[24:27], v[176:179], v[208:211], v[24:27]
	v_mfma_f32_16x16x32_bf16 v[16:19], v[184:187], v[208:211], v[16:19]
	v_mfma_f32_16x16x32_bf16 v[8:11], v[176:179], v[216:219], v[8:11]
	v_mfma_f32_16x16x32_bf16 v[0:3], v[184:187], v[216:219], v[0:3]
	s_setprio 0
	s_barrier
	s_add_i32 s68, 0, 0x18000
	s_add_i32 s69, 0, 0x1c000
	s_add_u32 s28, s28, 0x40000
	s_addc_u32 s29, s29, 0
	s_mov_b32 m0, s38
	s_nop 0
	global_load_lds_dwordx4 v134, s[28:29]
	s_mov_b32 m0, s39
	s_nop 0
	global_load_lds_dwordx4 v130, s[28:29]
	ds_read_b128 v[148:151], v252
	ds_read_b128 v[152:155], v252 offset:1024
	ds_read_b128 v[156:159], v252 offset:2048
	ds_read_b128 v[160:163], v252 offset:3072
	ds_read_b128 v[172:175], v253
	ds_read_b128 v[176:179], v253 offset:1024
	ds_read_b128 v[180:183], v253 offset:2048
	ds_read_b128 v[184:187], v253 offset:3072
	ds_read_b128 v[188:191], v168 offset:32768
	ds_read_b128 v[192:195], v168 offset:33792
	ds_read_b128 v[196:199], v168 offset:34816
	ds_read_b128 v[200:203], v168 offset:35840
	ds_read_b128 v[204:207], v168 offset:36864
	ds_read_b128 v[208:211], v168 offset:37888
	ds_read_b128 v[212:215], v168 offset:38912
	ds_read_b128 v[216:219], v168 offset:39936
	s_waitcnt vmcnt(8) lgkmcnt(0)
	s_barrier
	s_setprio 1
	v_mfma_f32_16x16x32_bf16 v[124:127], v[148:151], v[188:191], v[124:127]
	v_mfma_f32_16x16x32_bf16 v[116:119], v[156:159], v[188:191], v[116:119]
	v_mfma_f32_16x16x32_bf16 v[108:111], v[148:151], v[196:199], v[108:111]
	v_mfma_f32_16x16x32_bf16 v[100:103], v[156:159], v[196:199], v[100:103]
	v_mfma_f32_16x16x32_bf16 v[92:95], v[148:151], v[204:207], v[92:95]
	v_mfma_f32_16x16x32_bf16 v[84:87], v[156:159], v[204:207], v[84:87]
	v_mfma_f32_16x16x32_bf16 v[76:79], v[148:151], v[212:215], v[76:79]
	v_mfma_f32_16x16x32_bf16 v[68:71], v[156:159], v[212:215], v[68:71]
	v_mfma_f32_16x16x32_bf16 v[124:127], v[152:155], v[192:195], v[124:127]
	v_mfma_f32_16x16x32_bf16 v[116:119], v[160:163], v[192:195], v[116:119]
	v_mfma_f32_16x16x32_bf16 v[108:111], v[152:155], v[200:203], v[108:111]
	v_mfma_f32_16x16x32_bf16 v[100:103], v[160:163], v[200:203], v[100:103]
	v_mfma_f32_16x16x32_bf16 v[92:95], v[152:155], v[208:211], v[92:95]
	v_mfma_f32_16x16x32_bf16 v[84:87], v[160:163], v[208:211], v[84:87]
	v_mfma_f32_16x16x32_bf16 v[76:79], v[152:155], v[216:219], v[76:79]
	v_mfma_f32_16x16x32_bf16 v[68:71], v[160:163], v[216:219], v[68:71]
	s_setprio 0
	s_setprio 1
	v_mfma_f32_16x16x32_bf16 v[120:123], v[172:175], v[188:191], v[120:123]
	v_mfma_f32_16x16x32_bf16 v[112:115], v[180:183], v[188:191], v[112:115]
	v_mfma_f32_16x16x32_bf16 v[104:107], v[172:175], v[196:199], v[104:107]
	v_mfma_f32_16x16x32_bf16 v[96:99], v[180:183], v[196:199], v[96:99]
	v_mfma_f32_16x16x32_bf16 v[88:91], v[172:175], v[204:207], v[88:91]
	v_mfma_f32_16x16x32_bf16 v[80:83], v[180:183], v[204:207], v[80:83]
	v_mfma_f32_16x16x32_bf16 v[72:75], v[172:175], v[212:215], v[72:75]
	v_mfma_f32_16x16x32_bf16 v[64:67], v[180:183], v[212:215], v[64:67]
	v_mfma_f32_16x16x32_bf16 v[120:123], v[176:179], v[192:195], v[120:123]
	v_mfma_f32_16x16x32_bf16 v[112:115], v[184:187], v[192:195], v[112:115]
	v_mfma_f32_16x16x32_bf16 v[104:107], v[176:179], v[200:203], v[104:107]
	v_mfma_f32_16x16x32_bf16 v[96:99], v[184:187], v[200:203], v[96:99]
	v_mfma_f32_16x16x32_bf16 v[88:91], v[176:179], v[208:211], v[88:91]
	v_mfma_f32_16x16x32_bf16 v[80:83], v[184:187], v[208:211], v[80:83]
	v_mfma_f32_16x16x32_bf16 v[72:75], v[176:179], v[216:219], v[72:75]
	v_mfma_f32_16x16x32_bf16 v[64:67], v[184:187], v[216:219], v[64:67]
	s_setprio 0
	s_barrier
; #define PG8_STAGE(bufoff, gbase, voff) do { _Pragma("unroll") for (int _i = 0; _i < 2; ++_i) \
;         __builtin_amdgcn_global_load_lds((const unsigned*)((const char*)(gbase) + (voff)[_i]), (PG8_LAS unsigned*)(lds + (bufoff) + ldsw + _i * 8192), 16, 0, 0); } while (0)
; #define PG8_LDA(dst, b, h) do { _Pragma("unroll") for (int m = 0; m < 4; ++m) _Pragma("unroll") for (int k = 0; k < 2; ++k) dst[m][k] = *(const PG8_LAS bf16x8*)(lds + PG8_SA(b, h) + aoff + m * 2048 + k * 1024); } while (0)
; #define PG8_LDB(dst, b, h) do { _Pragma("unroll") for (int n = 0; n < 2; ++n) _Pragma("unroll") for (int k = 0; k < 2; ++k) dst[n][k] = *(const PG8_LAS bf16x8*)(lds + PG8_SB(b, h) + boff + n * 2048 + k * 1024); } while (0)
; #define PG8_MMA(ai, bj, At, Bt) do { __builtin_amdgcn_s_setprio(1); _Pragma("unroll") for (int m = 0; m < 4; ++m) _Pragma("unroll") for (int n = 0; n < 2; ++n) _Pragma("unroll") for (int k = 0; k < 2; ++k) \
;         acc[ai][bj][m][n] = __builtin_amdgcn_mfma_f32_16x16x32_bf16(Bt[n][k], At[m][k], acc[ai][bj][m][n], 0, 0, 0); __builtin_amdgcn_s_setprio(0); } while (0)
; template <class Epi, class Sched, bool ALIGN_EPI = false, bool SP2 = false>
; __device__ __forceinline__ void gemm_phase(PG8_LAS unsigned char* lds, const Gemm g, const Sched& S, const Epi& E, const int wid) {
;     ...
;             if constexpr (SP2) {
;             PG8_LDB(B0, 0, 0); PG8_LDB(B1, 0, 1); PG8_SCHED; PG8_LDA(At, 0, 0); PG8_STAGE(PG8_SA(1, 1), a1 + hstepA, voffA);
;             PG8_WAIT_V(8); PG8_WAIT_L(0); PG8_BAR; PG8_MMA(0, 0, At, B0); PG8_MMA(0, 1, At, B1); PG8_BAR; PG8_SCHED;
;             PG8_LDA(At, 0, 1); PG8_STAGE(PG8_SB(0, 0), b2, voffB); PG8_STAGE(PG8_SB(0, 1), b2 + hstepB, voffB); PG8_STAGE(PG8_SA(0, 0), a2, voffA);
;             PG8_WAIT_V(8); PG8_WAIT_L(0); PG8_BAR; PG8_MMA(1, 0, At, B0); PG8_MMA(1, 1, At, B1); PG8_BAR; PG8_SCHED;
;             PG8_LDB(B0, 1, 0); PG8_LDB(B1, 1, 1); PG8_SCHED; PG8_LDA(At, 1, 0); PG8_STAGE(PG8_SA(0, 1), a2 + hstepA, voffA);
;             PG8_WAIT_V(8); PG8_WAIT_L(0); PG8_BAR; PG8_MMA(0, 0, At, B0); PG8_MMA(0, 1, At, B1); PG8_BAR; PG8_SCHED;
;             PG8_LDA(At, 1, 1); PG8_STAGE(PG8_SB(1, 0), b3, voffB); PG8_STAGE(PG8_SB(1, 1), b3 + hstepB, voffB); PG8_STAGE(PG8_SA(1, 0), a3, voffA);
;             PG8_WAIT_V(8); PG8_WAIT_L(0); PG8_BAR; PG8_MMA(1, 0, At, B0); PG8_MMA(1, 1, At, B1); PG8_BAR; PG8_SCHED;
	s_add_i32 s28, s68, s33
	s_mov_b32 m0, s28
	s_nop 0
	global_load_lds_dwordx4 v132, s[98:99]
	s_add_i32 m0, s28, 0x2000
	s_add_u32 s26, s26, 0x40080
	s_addc_u32 s27, s27, 0
	s_add_i32 s28, s69, s33
	global_load_lds_dwordx4 v128, s[98:99]
	s_mov_b32 m0, s28
	s_nop 0
	global_load_lds_dwordx4 v132, s[26:27]
	s_add_i32 m0, s28, 0x2000
	s_nop 0
	global_load_lds_dwordx4 v128, s[26:27]
	s_mov_b32 m0, s40
	s_nop 0
	global_load_lds_dwordx4 v134, s[100:101]
	s_mov_b32 m0, s41
	s_nop 0
	global_load_lds_dwordx4 v130, s[100:101]
	ds_read_b128 v[188:191], v168 offset:49152
	ds_read_b128 v[192:195], v168 offset:50176
	ds_read_b128 v[196:199], v168 offset:51200
	ds_read_b128 v[200:203], v168 offset:52224
	ds_read_b128 v[204:207], v168 offset:53248
	ds_read_b128 v[208:211], v168 offset:54272
	ds_read_b128 v[212:215], v168 offset:55296
	ds_read_b128 v[216:219], v168 offset:56320
	s_waitcnt vmcnt(8) lgkmcnt(0)
	s_barrier
	s_setprio 1
	v_mfma_f32_16x16x32_bf16 v[60:63], v[148:151], v[188:191], v[60:63]
	v_mfma_f32_16x16x32_bf16 v[52:55], v[156:159], v[188:191], v[52:55]
	v_mfma_f32_16x16x32_bf16 v[44:47], v[148:151], v[196:199], v[44:47]
	v_mfma_f32_16x16x32_bf16 v[36:39], v[156:159], v[196:199], v[36:39]
	v_mfma_f32_16x16x32_bf16 v[28:31], v[148:151], v[204:207], v[28:31]
	v_mfma_f32_16x16x32_bf16 v[20:23], v[156:159], v[204:207], v[20:23]
	v_mfma_f32_16x16x32_bf16 v[12:15], v[148:151], v[212:215], v[12:15]
	v_mfma_f32_16x16x32_bf16 v[4:7], v[156:159], v[212:215], v[4:7]
	v_mfma_f32_16x16x32_bf16 v[60:63], v[152:155], v[192:195], v[60:63]
	v_mfma_f32_16x16x32_bf16 v[52:55], v[160:163], v[192:195], v[52:55]
	v_mfma_f32_16x16x32_bf16 v[44:47], v[152:155], v[200:203], v[44:47]
	v_mfma_f32_16x16x32_bf16 v[36:39], v[160:163], v[200:203], v[36:39]
	v_mfma_f32_16x16x32_bf16 v[28:31], v[152:155], v[208:211], v[28:31]
	v_mfma_f32_16x16x32_bf16 v[20:23], v[160:163], v[208:211], v[20:23]
	v_mfma_f32_16x16x32_bf16 v[12:15], v[152:155], v[216:219], v[12:15]
	v_mfma_f32_16x16x32_bf16 v[4:7], v[160:163], v[216:219], v[4:7]
	s_setprio 0
	s_setprio 1
	v_mfma_f32_16x16x32_bf16 v[56:59], v[172:175], v[188:191], v[56:59]
	v_mfma_f32_16x16x32_bf16 v[48:51], v[180:183], v[188:191], v[48:51]
	v_mfma_f32_16x16x32_bf16 v[40:43], v[172:175], v[196:199], v[40:43]
	v_mfma_f32_16x16x32_bf16 v[32:35], v[180:183], v[196:199], v[32:35]
	v_mfma_f32_16x16x32_bf16 v[24:27], v[172:175], v[204:207], v[24:27]
	v_mfma_f32_16x16x32_bf16 v[16:19], v[180:183], v[204:207], v[16:19]
	v_mfma_f32_16x16x32_bf16 v[8:11], v[172:175], v[212:215], v[8:11]
	v_mfma_f32_16x16x32_bf16 v[0:3], v[180:183], v[212:215], v[0:3]
	v_mfma_f32_16x16x32_bf16 v[56:59], v[176:179], v[192:195], v[56:59]
	v_mfma_f32_16x16x32_bf16 v[48:51], v[184:187], v[192:195], v[48:51]
	v_mfma_f32_16x16x32_bf16 v[40:43], v[176:179], v[200:203], v[40:43]
	v_mfma_f32_16x16x32_bf16 v[32:35], v[184:187], v[200:203], v[32:35]
	v_mfma_f32_16x16x32_bf16 v[24:27], v[176:179], v[208:211], v[24:27]
	v_mfma_f32_16x16x32_bf16 v[16:19], v[184:187], v[208:211], v[16:19]
	v_mfma_f32_16x16x32_bf16 v[8:11], v[176:179], v[216:219], v[8:11]
	v_mfma_f32_16x16x32_bf16 v[0:3], v[184:187], v[216:219], v[0:3]
	s_setprio 0
	s_barrier
	s_add_i32 s67, s67, 2
	s_add_u32 s24, s24, 0x100
	s_addc_u32 s25, s25, 0
	s_add_u32 s65, s65, 0x100
	s_addc_u32 s66, s66, 0
	s_cmp_gt_u32 s67, 13
.LBB0_1867:
	s_add_u32 s26, s24, 0xfffc0080
	s_addc_u32 s27, s25, -1
	s_cmp_eq_u32 s67, 12
	s_cselect_b32 s29, s17, s27
	s_cselect_b32 s28, s49, s26
	s_cselect_b32 s27, s15, s66
	s_cselect_b32 s26, s64, s65
	s_add_i32 m0, s36, 0xc000
	s_nop 0
	global_load_lds_dwordx4 v140, s[24:25]
	s_add_i32 m0, s36, 0xe000
	s_nop 0
	global_load_lds_dwordx4 v142, s[24:25]
	ds_read_b128 v[148:151], v166
	ds_read_b128 v[152:155], v166 offset:1024
	ds_read_b128 v[156:159], v166 offset:2048
	ds_read_b128 v[160:163], v166 offset:3072
	ds_read_b128 v[172:175], v167
	ds_read_b128 v[176:179], v167 offset:1024
	ds_read_b128 v[180:183], v167 offset:2048
	ds_read_b128 v[184:187], v167 offset:3072
	ds_read_b128 v[188:191], v168
	ds_read_b128 v[192:195], v168 offset:1024
	ds_read_b128 v[196:199], v168 offset:2048
	ds_read_b128 v[200:203], v168 offset:3072
	ds_read_b128 v[204:207], v168 offset:4096
	ds_read_b128 v[208:211], v168 offset:5120
	ds_read_b128 v[212:215], v168 offset:6144
	ds_read_b128 v[216:219], v168 offset:7168
	s_waitcnt vmcnt(8) lgkmcnt(0)
	s_barrier
	s_setprio 1
	v_mfma_f32_16x16x32_bf16 v[124:127], v[148:151], v[188:191], v[124:127]
	v_mfma_f32_16x16x32_bf16 v[116:119], v[156:159], v[188:191], v[116:119]
	v_mfma_f32_16x16x32_bf16 v[108:111], v[148:151], v[196:199], v[108:111]
	v_mfma_f32_16x16x32_bf16 v[100:103], v[156:159], v[196:199], v[100:103]
	v_mfma_f32_16x16x32_bf16 v[92:95], v[148:151], v[204:207], v[92:95]
	v_mfma_f32_16x16x32_bf16 v[84:87], v[156:159], v[204:207], v[84:87]
	v_mfma_f32_16x16x32_bf16 v[76:79], v[148:151], v[212:215], v[76:79]
	v_mfma_f32_16x16x32_bf16 v[68:71], v[156:159], v[212:215], v[68:71]
	v_mfma_f32_16x16x32_bf16 v[124:127], v[152:155], v[192:195], v[124:127]
	v_mfma_f32_16x16x32_bf16 v[116:119], v[160:163], v[192:195], v[116:119]
	v_mfma_f32_16x16x32_bf16 v[108:111], v[152:155], v[200:203], v[108:111]
	v_mfma_f32_16x16x32_bf16 v[100:103], v[160:163], v[200:203], v[100:103]
	v_mfma_f32_16x16x32_bf16 v[92:95], v[152:155], v[208:211], v[92:95]
	v_mfma_f32_16x16x32_bf16 v[84:87], v[160:163], v[208:211], v[84:87]
	v_mfma_f32_16x16x32_bf16 v[76:79], v[152:155], v[216:219], v[76:79]
	v_mfma_f32_16x16x32_bf16 v[68:71], v[160:163], v[216:219], v[68:71]
	s_setprio 0
	s_setprio 1
	v_mfma_f32_16x16x32_bf16 v[120:123], v[172:175], v[188:191], v[120:123]
	v_mfma_f32_16x16x32_bf16 v[112:115], v[180:183], v[188:191], v[112:115]
	v_mfma_f32_16x16x32_bf16 v[104:107], v[172:175], v[196:199], v[104:107]
	v_mfma_f32_16x16x32_bf16 v[96:99], v[180:183], v[196:199], v[96:99]
	v_mfma_f32_16x16x32_bf16 v[88:91], v[172:175], v[204:207], v[88:91]
	v_mfma_f32_16x16x32_bf16 v[80:83], v[180:183], v[204:207], v[80:83]
	v_mfma_f32_16x16x32_bf16 v[72:75], v[172:175], v[212:215], v[72:75]
	v_mfma_f32_16x16x32_bf16 v[64:67], v[180:183], v[212:215], v[64:67]
	v_mfma_f32_16x16x32_bf16 v[120:123], v[176:179], v[192:195], v[120:123]
	v_mfma_f32_16x16x32_bf16 v[112:115], v[184:187], v[192:195], v[112:115]
	v_mfma_f32_16x16x32_bf16 v[104:107], v[176:179], v[200:203], v[104:107]
	v_mfma_f32_16x16x32_bf16 v[96:99], v[184:187], v[200:203], v[96:99]
	v_mfma_f32_16x16x32_bf16 v[88:91], v[176:179], v[208:211], v[88:91]
	v_mfma_f32_16x16x32_bf16 v[80:83], v[184:187], v[208:211], v[80:83]
	v_mfma_f32_16x16x32_bf16 v[72:75], v[176:179], v[216:219], v[72:75]
	v_mfma_f32_16x16x32_bf16 v[64:67], v[184:187], v[216:219], v[64:67]
	s_setprio 0
	s_barrier
; #define PG8_STAGE(bufoff, gbase, voff) do { _Pragma("unroll") for (int _i = 0; _i < 2; ++_i) \
;         __builtin_amdgcn_global_load_lds((const unsigned*)((const char*)(gbase) + (voff)[_i]), (PG8_LAS unsigned*)(lds + (bufoff) + ldsw + _i * 8192), 16, 0, 0); } while (0)
; #define PG8_LDA(dst, b, h) do { _Pragma("unroll") for (int m = 0; m < 4; ++m) _Pragma("unroll") for (int k = 0; k < 2; ++k) dst[m][k] = *(const PG8_LAS bf16x8*)(lds + PG8_SA(b, h) + aoff + m * 2048 + k * 1024); } while (0)
; #define PG8_LDB(dst, b, h) do { _Pragma("unroll") for (int n = 0; n < 2; ++n) _Pragma("unroll") for (int k = 0; k < 2; ++k) dst[n][k] = *(const PG8_LAS bf16x8*)(lds + PG8_SB(b, h) + boff + n * 2048 + k * 1024); } while (0)
; #define PG8_MMA(ai, bj, At, Bt) do { __builtin_amdgcn_s_setprio(1); _Pragma("unroll") for (int m = 0; m < 4; ++m) _Pragma("unroll") for (int n = 0; n < 2; ++n) _Pragma("unroll") for (int k = 0; k < 2; ++k) \
;         acc[ai][bj][m][n] = __builtin_amdgcn_mfma_f32_16x16x32_bf16(Bt[n][k], At[m][k], acc[ai][bj][m][n], 0, 0, 0); __builtin_amdgcn_s_setprio(0); } while (0)
; template <class Epi, class Sched, bool ALIGN_EPI = false, bool SP2 = false>
; __device__ __forceinline__ void gemm_phase(PG8_LAS unsigned char* lds, const Gemm g, const Sched& S, const Epi& E, const int wid) {
;     ...
;             if constexpr (SP2) {
;             PG8_LDB(B0, 0, 0); PG8_LDB(B1, 0, 1); PG8_SCHED; PG8_LDA(At, 0, 0); PG8_STAGE(PG8_SA(1, 1), a1 + hstepA, voffA);
;             PG8_WAIT_V(8); PG8_WAIT_L(0); PG8_BAR; PG8_MMA(0, 0, At, B0); PG8_MMA(0, 1, At, B1); PG8_BAR; PG8_SCHED;
;             PG8_LDA(At, 0, 1); PG8_STAGE(PG8_SB(0, 0), b2, voffB); PG8_STAGE(PG8_SB(0, 1), b2 + hstepB, voffB); PG8_STAGE(PG8_SA(0, 0), a2, voffA);
;             PG8_WAIT_V(8); PG8_WAIT_L(0); PG8_BAR; PG8_MMA(1, 0, At, B0); PG8_MMA(1, 1, At, B1); PG8_BAR; PG8_SCHED;
;             PG8_LDB(B0, 1, 0); PG8_LDB(B1, 1, 1); PG8_SCHED; PG8_LDA(At, 1, 0); PG8_STAGE(PG8_SA(0, 1), a2 + hstepA, voffA);
;             PG8_WAIT_V(8); PG8_WAIT_L(0); PG8_BAR; PG8_MMA(0, 0, At, B0); PG8_MMA(0, 1, At, B1); PG8_BAR; PG8_SCHED;
;             PG8_LDA(At, 1, 1); PG8_STAGE(PG8_SB(1, 0), b3, voffB); PG8_STAGE(PG8_SB(1, 1), b3 + hstepB, voffB); PG8_STAGE(PG8_SA(1, 0), a3, voffA);
;             PG8_WAIT_V(8); PG8_WAIT_L(0); PG8_BAR; PG8_MMA(1, 0, At, B0); PG8_MMA(1, 1, At, B1); PG8_BAR; PG8_SCHED;
	s_add_i32 s68, s45, s33
	s_add_u32 s98, s26, 0x80
	s_addc_u32 s99, s27, 0
	s_mov_b32 m0, s68
	s_nop 0
	global_load_lds_dwordx4 v132, s[26:27]
	s_add_i32 m0, s68, 0x2000
	s_add_u32 s68, s26, 0x40000
	s_addc_u32 s69, s27, 0
	s_add_i32 s70, s46, s33
	global_load_lds_dwordx4 v128, s[26:27]
	s_mov_b32 m0, s70
	s_add_u32 s100, s28, 0x80
	s_addc_u32 s101, s29, 0
	global_load_lds_dwordx4 v132, s[68:69]
	s_add_i32 m0, s70, 0x2000
	s_nop 0
	global_load_lds_dwordx4 v128, s[68:69]
	s_mov_b32 m0, s36
	s_nop 0
	global_load_lds_dwordx4 v134, s[28:29]
	s_mov_b32 m0, s37
	s_nop 0
	global_load_lds_dwordx4 v130, s[28:29]
	ds_read_b128 v[188:191], v168 offset:16384
	ds_read_b128 v[192:195], v168 offset:17408
	ds_read_b128 v[196:199], v168 offset:18432
	ds_read_b128 v[200:203], v168 offset:19456
	ds_read_b128 v[204:207], v168 offset:20480
	ds_read_b128 v[208:211], v168 offset:21504
	ds_read_b128 v[212:215], v168 offset:22528
	ds_read_b128 v[216:219], v168 offset:23552
	s_waitcnt vmcnt(8) lgkmcnt(0)
	s_barrier
	s_setprio 1
	v_mfma_f32_16x16x32_bf16 v[60:63], v[148:151], v[188:191], v[60:63]
	v_mfma_f32_16x16x32_bf16 v[52:55], v[156:159], v[188:191], v[52:55]
	v_mfma_f32_16x16x32_bf16 v[44:47], v[148:151], v[196:199], v[44:47]
	v_mfma_f32_16x16x32_bf16 v[36:39], v[156:159], v[196:199], v[36:39]
	v_mfma_f32_16x16x32_bf16 v[28:31], v[148:151], v[204:207], v[28:31]
	v_mfma_f32_16x16x32_bf16 v[20:23], v[156:159], v[204:207], v[20:23]
	v_mfma_f32_16x16x32_bf16 v[12:15], v[148:151], v[212:215], v[12:15]
	v_mfma_f32_16x16x32_bf16 v[4:7], v[156:159], v[212:215], v[4:7]
	v_mfma_f32_16x16x32_bf16 v[60:63], v[152:155], v[192:195], v[60:63]
	v_mfma_f32_16x16x32_bf16 v[52:55], v[160:163], v[192:195], v[52:55]
	v_mfma_f32_16x16x32_bf16 v[44:47], v[152:155], v[200:203], v[44:47]
	v_mfma_f32_16x16x32_bf16 v[36:39], v[160:163], v[200:203], v[36:39]
	v_mfma_f32_16x16x32_bf16 v[28:31], v[152:155], v[208:211], v[28:31]
	v_mfma_f32_16x16x32_bf16 v[20:23], v[160:163], v[208:211], v[20:23]
	v_mfma_f32_16x16x32_bf16 v[12:15], v[152:155], v[216:219], v[12:15]
	v_mfma_f32_16x16x32_bf16 v[4:7], v[160:163], v[216:219], v[4:7]
	s_setprio 0
	s_setprio 1
	v_mfma_f32_16x16x32_bf16 v[56:59], v[172:175], v[188:191], v[56:59]
	v_mfma_f32_16x16x32_bf16 v[48:51], v[180:183], v[188:191], v[48:51]
	v_mfma_f32_16x16x32_bf16 v[40:43], v[172:175], v[196:199], v[40:43]
	v_mfma_f32_16x16x32_bf16 v[32:35], v[180:183], v[196:199], v[32:35]
	v_mfma_f32_16x16x32_bf16 v[24:27], v[172:175], v[204:207], v[24:27]
	v_mfma_f32_16x16x32_bf16 v[16:19], v[180:183], v[204:207], v[16:19]
	v_mfma_f32_16x16x32_bf16 v[8:11], v[172:175], v[212:215], v[8:11]
	v_mfma_f32_16x16x32_bf16 v[0:3], v[180:183], v[212:215], v[0:3]
	v_mfma_f32_16x16x32_bf16 v[56:59], v[176:179], v[192:195], v[56:59]
	v_mfma_f32_16x16x32_bf16 v[48:51], v[184:187], v[192:195], v[48:51]
	v_mfma_f32_16x16x32_bf16 v[40:43], v[176:179], v[200:203], v[40:43]
	v_mfma_f32_16x16x32_bf16 v[32:35], v[184:187], v[200:203], v[32:35]
	v_mfma_f32_16x16x32_bf16 v[24:27], v[176:179], v[208:211], v[24:27]
	v_mfma_f32_16x16x32_bf16 v[16:19], v[184:187], v[208:211], v[16:19]
	v_mfma_f32_16x16x32_bf16 v[8:11], v[176:179], v[216:219], v[8:11]
	v_mfma_f32_16x16x32_bf16 v[0:3], v[184:187], v[216:219], v[0:3]
	s_setprio 0
	s_barrier
	s_add_i32 s68, 0, 0x18000
	s_add_i32 s69, 0, 0x1c000
	s_add_u32 s28, s28, 0x40000
	s_addc_u32 s29, s29, 0
	s_mov_b32 m0, s38
	s_nop 0
	global_load_lds_dwordx4 v134, s[28:29]
	s_mov_b32 m0, s39
	s_nop 0
	global_load_lds_dwordx4 v130, s[28:29]
	ds_read_b128 v[148:151], v252
	ds_read_b128 v[152:155], v252 offset:1024
	ds_read_b128 v[156:159], v252 offset:2048
	ds_read_b128 v[160:163], v252 offset:3072
	ds_read_b128 v[172:175], v253
	ds_read_b128 v[176:179], v253 offset:1024
	ds_read_b128 v[180:183], v253 offset:2048
	ds_read_b128 v[184:187], v253 offset:3072
	ds_read_b128 v[188:191], v168 offset:32768
	ds_read_b128 v[192:195], v168 offset:33792
	ds_read_b128 v[196:199], v168 offset:34816
	ds_read_b128 v[200:203], v168 offset:35840
	ds_read_b128 v[204:207], v168 offset:36864
	ds_read_b128 v[208:211], v168 offset:37888
	ds_read_b128 v[212:215], v168 offset:38912
	ds_read_b128 v[216:219], v168 offset:39936
	s_waitcnt vmcnt(8) lgkmcnt(0)
	s_barrier
; #define PG8_STAGE(bufoff, gbase, voff) do { _Pragma("unroll") for (int _i = 0; _i < 2; ++_i) \
;         __builtin_amdgcn_global_load_lds((const unsigned*)((const char*)(gbase) + (voff)[_i]), (PG8_LAS unsigned*)(lds + (bufoff) + ldsw + _i * 8192), 16, 0, 0); } while (0)
; #define PG8_LDA(dst, b, h) do { _Pragma("unroll") for (int m = 0; m < 4; ++m) _Pragma("unroll") for (int k = 0; k < 2; ++k) dst[m][k] = *(const PG8_LAS bf16x8*)(lds + PG8_SA(b, h) + aoff + m * 2048 + k * 1024); } while (0)
; #define PG8_LDB(dst, b, h) do { _Pragma("unroll") for (int n = 0; n < 2; ++n) _Pragma("unroll") for (int k = 0; k < 2; ++k) dst[n][k] = *(const PG8_LAS bf16x8*)(lds + PG8_SB(b, h) + boff + n * 2048 + k * 1024); } while (0)
; #define PG8_WAIT_V(n) asm volatile("s_waitcnt vmcnt(" #n ")" ::: "memory")
; #define PG8_WAIT_L(n) asm volatile("s_waitcnt lgkmcnt(" #n ")" ::: "memory")
; #define PG8_BAR __builtin_amdgcn_s_barrier()
; template <class Epi, class Sched, bool ALIGN_EPI = false, bool SP2 = false>
; __device__ __forceinline__ void gemm_phase(PG8_LAS unsigned char* lds, const Gemm g, const Sched& S, const Epi& E, const int wid) {
;     ...
;             if constexpr (SP2) {
;             PG8_LDB(B0, 0, 0); PG8_LDB(B1, 0, 1); PG8_SCHED; PG8_LDA(At, 0, 0); PG8_STAGE(PG8_SA(1, 1), a1 + hstepA, voffA);
;             PG8_WAIT_V(8); PG8_WAIT_L(0); PG8_BAR; PG8_MMA(0, 0, At, B0); PG8_MMA(0, 1, At, B1); PG8_BAR; PG8_SCHED;
;             PG8_LDA(At, 0, 1); PG8_STAGE(PG8_SB(0, 0), b2, voffB); PG8_STAGE(PG8_SB(0, 1), b2 + hstepB, voffB); PG8_STAGE(PG8_SA(0, 0), a2, voffA);
;             PG8_WAIT_V(8); PG8_WAIT_L(0); PG8_BAR; PG8_MMA(1, 0, At, B0); PG8_MMA(1, 1, At, B1); PG8_BAR; PG8_SCHED;
;             PG8_LDB(B0, 1, 0); PG8_LDB(B1, 1, 1); PG8_SCHED; PG8_LDA(At, 1, 0); PG8_STAGE(PG8_SA(0, 1), a2 + hstepA, voffA);
;             PG8_WAIT_V(8); PG8_WAIT_L(0); PG8_BAR; PG8_MMA(0, 0, At, B0); PG8_MMA(0, 1, At, B1); PG8_BAR; PG8_SCHED;
;             PG8_LDA(At, 1, 1); PG8_STAGE(PG8_SB(1, 0), b3, voffB); PG8_STAGE(PG8_SB(1, 1), b3 + hstepB, voffB); PG8_STAGE(PG8_SA(1, 0), a3, voffA);
;             PG8_WAIT_V(8); PG8_WAIT_L(0); PG8_BAR; PG8_MMA(1, 0, At, B0); PG8_MMA(1, 1, At, B1); PG8_BAR; PG8_SCHED;
;     ...
;         if constexpr (ALIGN_EPI) { if (wr == 0) PG8_BAR; }
;         if constexpr (!Epi::AFTER_DRAIN) { E(acc, cur, wr, wc, fr, fq); S.done(cur); }
;         if (!has_next) break;
	s_setprio 1
	v_mfma_f32_16x16x32_bf16 v[124:127], v[148:151], v[188:191], v[124:127]
	v_mfma_f32_16x16x32_bf16 v[116:119], v[156:159], v[188:191], v[116:119]
	v_mfma_f32_16x16x32_bf16 v[108:111], v[148:151], v[196:199], v[108:111]
	v_mfma_f32_16x16x32_bf16 v[100:103], v[156:159], v[196:199], v[100:103]
	v_mfma_f32_16x16x32_bf16 v[92:95], v[148:151], v[204:207], v[92:95]
	v_mfma_f32_16x16x32_bf16 v[84:87], v[156:159], v[204:207], v[84:87]
	v_mfma_f32_16x16x32_bf16 v[76:79], v[148:151], v[212:215], v[76:79]
	v_mfma_f32_16x16x32_bf16 v[68:71], v[156:159], v[212:215], v[68:71]
	v_mfma_f32_16x16x32_bf16 v[124:127], v[152:155], v[192:195], v[124:127]
	v_mfma_f32_16x16x32_bf16 v[116:119], v[160:163], v[192:195], v[116:119]
	v_mfma_f32_16x16x32_bf16 v[108:111], v[152:155], v[200:203], v[108:111]
	v_mfma_f32_16x16x32_bf16 v[100:103], v[160:163], v[200:203], v[100:103]
	v_mfma_f32_16x16x32_bf16 v[92:95], v[152:155], v[208:211], v[92:95]
	v_mfma_f32_16x16x32_bf16 v[84:87], v[160:163], v[208:211], v[84:87]
	v_mfma_f32_16x16x32_bf16 v[76:79], v[152:155], v[216:219], v[76:79]
	v_mfma_f32_16x16x32_bf16 v[68:71], v[160:163], v[216:219], v[68:71]
	s_setprio 0
	s_setprio 1
	v_mfma_f32_16x16x32_bf16 v[120:123], v[172:175], v[188:191], v[120:123]
	v_mfma_f32_16x16x32_bf16 v[112:115], v[180:183], v[188:191], v[112:115]
	v_mfma_f32_16x16x32_bf16 v[104:107], v[172:175], v[196:199], v[104:107]
	v_mfma_f32_16x16x32_bf16 v[96:99], v[180:183], v[196:199], v[96:99]
	v_mfma_f32_16x16x32_bf16 v[88:91], v[172:175], v[204:207], v[88:91]
	v_mfma_f32_16x16x32_bf16 v[80:83], v[180:183], v[204:207], v[80:83]
	v_mfma_f32_16x16x32_bf16 v[72:75], v[172:175], v[212:215], v[72:75]
	v_mfma_f32_16x16x32_bf16 v[64:67], v[180:183], v[212:215], v[64:67]
	v_mfma_f32_16x16x32_bf16 v[120:123], v[176:179], v[192:195], v[120:123]
	v_mfma_f32_16x16x32_bf16 v[112:115], v[184:187], v[192:195], v[112:115]
	v_mfma_f32_16x16x32_bf16 v[104:107], v[176:179], v[200:203], v[104:107]
	v_mfma_f32_16x16x32_bf16 v[96:99], v[184:187], v[200:203], v[96:99]
	v_mfma_f32_16x16x32_bf16 v[88:91], v[176:179], v[208:211], v[88:91]
	v_mfma_f32_16x16x32_bf16 v[80:83], v[184:187], v[208:211], v[80:83]
	v_mfma_f32_16x16x32_bf16 v[72:75], v[176:179], v[216:219], v[72:75]
	v_mfma_f32_16x16x32_bf16 v[64:67], v[184:187], v[216:219], v[64:67]
	s_setprio 0
	s_barrier
	s_add_i32 s28, s68, s33
	s_mov_b32 m0, s28
	s_nop 0
	global_load_lds_dwordx4 v132, s[98:99]
	s_add_i32 m0, s28, 0x2000
	s_add_u32 s26, s26, 0x40080
	s_addc_u32 s27, s27, 0
	s_add_i32 s28, s69, s33
	global_load_lds_dwordx4 v128, s[98:99]
	s_mov_b32 m0, s28
	s_nop 0
	global_load_lds_dwordx4 v132, s[26:27]
	s_add_i32 m0, s28, 0x2000
	s_nop 0
	global_load_lds_dwordx4 v128, s[26:27]
	s_mov_b32 m0, s40
	s_nop 0
	global_load_lds_dwordx4 v134, s[100:101]
	s_mov_b32 m0, s41
	s_nop 0
	global_load_lds_dwordx4 v130, s[100:101]
	ds_read_b128 v[188:191], v168 offset:49152
	ds_read_b128 v[192:195], v168 offset:50176
	ds_read_b128 v[196:199], v168 offset:51200
	ds_read_b128 v[200:203], v168 offset:52224
	ds_read_b128 v[204:207], v168 offset:53248
	ds_read_b128 v[208:211], v168 offset:54272
	ds_read_b128 v[212:215], v168 offset:55296
	ds_read_b128 v[216:219], v168 offset:56320
	s_waitcnt vmcnt(8) lgkmcnt(0)
	s_barrier
	s_setprio 1
	v_mfma_f32_16x16x32_bf16 v[60:63], v[148:151], v[188:191], v[60:63]
	v_mfma_f32_16x16x32_bf16 v[52:55], v[156:159], v[188:191], v[52:55]
	v_mfma_f32_16x16x32_bf16 v[44:47], v[148:151], v[196:199], v[44:47]
	v_mfma_f32_16x16x32_bf16 v[36:39], v[156:159], v[196:199], v[36:39]
	v_mfma_f32_16x16x32_bf16 v[28:31], v[148:151], v[204:207], v[28:31]
	v_mfma_f32_16x16x32_bf16 v[20:23], v[156:159], v[204:207], v[20:23]
	v_mfma_f32_16x16x32_bf16 v[12:15], v[148:151], v[212:215], v[12:15]
	v_mfma_f32_16x16x32_bf16 v[4:7], v[156:159], v[212:215], v[4:7]
	v_mfma_f32_16x16x32_bf16 v[60:63], v[152:155], v[192:195], v[60:63]
	v_mfma_f32_16x16x32_bf16 v[52:55], v[160:163], v[192:195], v[52:55]
	v_mfma_f32_16x16x32_bf16 v[44:47], v[152:155], v[200:203], v[44:47]
	v_mfma_f32_16x16x32_bf16 v[36:39], v[160:163], v[200:203], v[36:39]
	v_mfma_f32_16x16x32_bf16 v[28:31], v[152:155], v[208:211], v[28:31]
	v_mfma_f32_16x16x32_bf16 v[20:23], v[160:163], v[208:211], v[20:23]
	v_mfma_f32_16x16x32_bf16 v[12:15], v[152:155], v[216:219], v[12:15]
	v_mfma_f32_16x16x32_bf16 v[4:7], v[160:163], v[216:219], v[4:7]
	s_setprio 0
	s_setprio 1
	v_mfma_f32_16x16x32_bf16 v[56:59], v[172:175], v[188:191], v[56:59]
	v_mfma_f32_16x16x32_bf16 v[48:51], v[180:183], v[188:191], v[48:51]
	v_mfma_f32_16x16x32_bf16 v[40:43], v[172:175], v[196:199], v[40:43]
	v_mfma_f32_16x16x32_bf16 v[32:35], v[180:183], v[196:199], v[32:35]
	v_mfma_f32_16x16x32_bf16 v[24:27], v[172:175], v[204:207], v[24:27]
	v_mfma_f32_16x16x32_bf16 v[16:19], v[180:183], v[204:207], v[16:19]
	v_mfma_f32_16x16x32_bf16 v[8:11], v[172:175], v[212:215], v[8:11]
	v_mfma_f32_16x16x32_bf16 v[0:3], v[180:183], v[212:215], v[0:3]
	v_mfma_f32_16x16x32_bf16 v[56:59], v[176:179], v[192:195], v[56:59]
	v_mfma_f32_16x16x32_bf16 v[48:51], v[184:187], v[192:195], v[48:51]
	v_mfma_f32_16x16x32_bf16 v[40:43], v[176:179], v[200:203], v[40:43]
	v_mfma_f32_16x16x32_bf16 v[32:35], v[184:187], v[200:203], v[32:35]
	v_mfma_f32_16x16x32_bf16 v[24:27], v[176:179], v[208:211], v[24:27]
	v_mfma_f32_16x16x32_bf16 v[16:19], v[184:187], v[208:211], v[16:19]
	v_mfma_f32_16x16x32_bf16 v[8:11], v[176:179], v[216:219], v[8:11]
	v_mfma_f32_16x16x32_bf16 v[0:3], v[184:187], v[216:219], v[0:3]
	s_setprio 0
	s_barrier
	s_add_i32 s67, s67, 2
	s_add_u32 s24, s24, 0x100
	s_addc_u32 s25, s25, 0
	s_add_u32 s65, s65, 0x100
	s_addc_u32 s66, s66, 0
	s_cmp_gt_u32 s67, 13
	s_cbranch_scc0 .LBB0_1867
	s_and_b64 vcc, exec, s[12:13]
	s_cbranch_vccz .LBB0_1870
	s_barrier

; #define PG8_STAGE(bufoff, gbase, voff) do { _Pragma("unroll") for (int _i = 0; _i < 2; ++_i) \
;         __builtin_amdgcn_global_load_lds((const unsigned*)((const char*)(gbase) + (voff)[_i]), (PG8_LAS unsigned*)(lds + (bufoff) + ldsw + _i * 8192), 16, 0, 0); } while (0)
; #define PG8_WAIT_V(n) asm volatile("s_waitcnt vmcnt(" #n ")" ::: "memory")
; #define PG8_WAIT_L(n) asm volatile("s_waitcnt lgkmcnt(" #n ")" ::: "memory")
; #define PG8_BAR __builtin_amdgcn_s_barrier()
; template <class Epi, class Sched, bool ALIGN_EPI = false, bool SP2 = false>
; __device__ __forceinline__ void gemm_phase(PG8_LAS unsigned char* lds, const Gemm g, const Sched& S, const Epi& E, const int wid) {
;     ...
;         const bool has_next = S.next(ui + 1, nxt);
;         const char* nA = has_next ? (const char*)g.A + (size_t)nxt.pm * tstepA : cA; const char* nB = has_next ? (const char*)g.Bt + (size_t)nxt.pn * tstepB : cB;
;         for (int t = 0; t < nt; t += 2) {
;             const bool last = (t == nt - 2);
;             const char* a1 = cA + (size_t)(t + 1) * kstep;
;             const char* a2 = last ? nA : cA + (size_t)(t + 2) * kstep; const char* b2 = last ? nB : cB + (size_t)(t + 2) * kstep;
;             const char* a3 = a2 + kstep; const char* b3 = b2 + kstep;
;             if (last && has_next) S.a_ready(nxt);
;             if constexpr (SP2) {
;             PG8_LDB(B0, 0, 0); PG8_LDB(B1, 0, 1); PG8_SCHED; PG8_LDA(At, 0, 0); PG8_STAGE(PG8_SA(1, 1), a1 + hstepA, voffA);
;             PG8_WAIT_V(8); PG8_WAIT_L(0); PG8_BAR; PG8_MMA(0, 0, At, B0); PG8_MMA(0, 1, At, B1); PG8_BAR; PG8_SCHED;
;             PG8_LDA(At, 0, 1); PG8_STAGE(PG8_SB(0, 0), b2, voffB); PG8_STAGE(PG8_SB(0, 1), b2 + hstepB, voffB); PG8_STAGE(PG8_SA(0, 0), a2, voffA);
;             PG8_WAIT_V(8); PG8_WAIT_L(0); PG8_BAR; PG8_MMA(1, 0, At, B0); PG8_MMA(1, 1, At, B1); PG8_BAR; PG8_SCHED;
;             PG8_LDB(B0, 1, 0); PG8_LDB(B1, 1, 1); PG8_SCHED; PG8_LDA(At, 1, 0); PG8_STAGE(PG8_SA(0, 1), a2 + hstepA, voffA);
;             PG8_WAIT_V(8); PG8_WAIT_L(0); PG8_BAR; PG8_MMA(0, 0, At, B0); PG8_MMA(0, 1, At, B1); PG8_BAR; PG8_SCHED;
;             PG8_LDA(At, 1, 1); PG8_STAGE(PG8_SB(1, 0), b3, voffB); PG8_STAGE(PG8_SB(1, 1), b3 + hstepB, voffB); PG8_STAGE(PG8_SA(1, 0), a3, voffA);
;             PG8_WAIT_V(8); PG8_WAIT_L(0); PG8_BAR; PG8_MMA(1, 0, At, B0); PG8_MMA(1, 1, At, B1); PG8_BAR; PG8_SCHED;
.LBB0_1951:
	s_add_u32 s66, s24, 0x100
	s_addc_u32 s67, s25, 0
	s_mov_b32 s68, -2
	s_waitcnt lgkmcnt(0)
	v_add_u32_e32 v252, 0x18000, v189
	v_add_u32_e32 v253, 0x1c000, v189
	s_add_u32 s24, s22, 0x100
	s_addc_u32 s25, s23, 0
	s_cmp_eq_u32 s68, 40
	s_cselect_b32 s29, s7, s25
	s_cselect_b32 s28, s6, s24
	s_cselect_b32 s27, s21, s67
	s_cselect_b32 s26, s20, s66
	s_add_i32 m0, s34, 0xc000
	s_nop 0
	global_load_lds_dwordx4 v164, s[22:23]
	s_add_i32 m0, s34, 0xe000
	s_nop 0
	global_load_lds_dwordx4 v166, s[22:23]
	ds_read_b128 v[128:131], v190
	ds_read_b128 v[132:135], v190 offset:1024
	ds_read_b128 v[136:139], v190 offset:2048
	ds_read_b128 v[140:143], v190 offset:3072
	ds_read_b128 v[144:147], v191
	ds_read_b128 v[148:151], v191 offset:1024
	ds_read_b128 v[172:175], v191 offset:2048
	ds_read_b128 v[176:179], v191 offset:3072
	ds_read_b128 v[180:183], v192
	ds_read_b128 v[184:187], v192 offset:1024
	ds_read_b128 v[194:197], v192 offset:2048
	ds_read_b128 v[198:201], v192 offset:3072
	ds_read_b128 v[202:205], v192 offset:4096
	ds_read_b128 v[206:209], v192 offset:5120
	ds_read_b128 v[210:213], v192 offset:6144
	ds_read_b128 v[214:217], v192 offset:7168
	s_waitcnt vmcnt(8) lgkmcnt(0)
	s_barrier
	s_setprio 1
	v_mfma_f32_16x16x32_bf16 v[124:127], v[128:131], v[180:183], 0
	v_mfma_f32_16x16x32_bf16 v[120:123], v[136:139], v[180:183], 0
	v_mfma_f32_16x16x32_bf16 v[108:111], v[128:131], v[194:197], 0
	v_mfma_f32_16x16x32_bf16 v[104:107], v[136:139], v[194:197], 0
	v_mfma_f32_16x16x32_bf16 v[92:95], v[128:131], v[202:205], 0
	v_mfma_f32_16x16x32_bf16 v[88:91], v[136:139], v[202:205], 0
	v_mfma_f32_16x16x32_bf16 v[76:79], v[128:131], v[210:213], 0
	v_mfma_f32_16x16x32_bf16 v[72:75], v[136:139], v[210:213], 0
	v_mfma_f32_16x16x32_bf16 v[124:127], v[132:135], v[184:187], v[124:127]
	v_mfma_f32_16x16x32_bf16 v[120:123], v[140:143], v[184:187], v[120:123]
	v_mfma_f32_16x16x32_bf16 v[108:111], v[132:135], v[198:201], v[108:111]
	v_mfma_f32_16x16x32_bf16 v[104:107], v[140:143], v[198:201], v[104:107]
	v_mfma_f32_16x16x32_bf16 v[92:95], v[132:135], v[206:209], v[92:95]
	v_mfma_f32_16x16x32_bf16 v[88:91], v[140:143], v[206:209], v[88:91]
	v_mfma_f32_16x16x32_bf16 v[76:79], v[132:135], v[214:217], v[76:79]
	v_mfma_f32_16x16x32_bf16 v[72:75], v[140:143], v[214:217], v[72:75]
	s_setprio 0
	s_setprio 1
	v_mfma_f32_16x16x32_bf16 v[116:119], v[144:147], v[180:183], 0
	v_mfma_f32_16x16x32_bf16 v[112:115], v[172:175], v[180:183], 0
	v_mfma_f32_16x16x32_bf16 v[100:103], v[144:147], v[194:197], 0
	v_mfma_f32_16x16x32_bf16 v[96:99], v[172:175], v[194:197], 0
	v_mfma_f32_16x16x32_bf16 v[84:87], v[144:147], v[202:205], 0
	v_mfma_f32_16x16x32_bf16 v[80:83], v[172:175], v[202:205], 0
	v_mfma_f32_16x16x32_bf16 v[68:71], v[144:147], v[210:213], 0
	v_mfma_f32_16x16x32_bf16 v[64:67], v[172:175], v[210:213], 0
	v_mfma_f32_16x16x32_bf16 v[116:119], v[148:151], v[184:187], v[116:119]
	v_mfma_f32_16x16x32_bf16 v[112:115], v[176:179], v[184:187], v[112:115]
	v_mfma_f32_16x16x32_bf16 v[100:103], v[148:151], v[198:201], v[100:103]
	v_mfma_f32_16x16x32_bf16 v[96:99], v[176:179], v[198:201], v[96:99]
	v_mfma_f32_16x16x32_bf16 v[84:87], v[148:151], v[206:209], v[84:87]
	v_mfma_f32_16x16x32_bf16 v[80:83], v[176:179], v[206:209], v[80:83]
	v_mfma_f32_16x16x32_bf16 v[68:71], v[148:151], v[214:217], v[68:71]
	v_mfma_f32_16x16x32_bf16 v[64:67], v[176:179], v[214:217], v[64:67]
	s_setprio 0
	s_barrier
	s_add_i32 s22, s45, s33
	s_add_u32 s98, s26, 0x80
	s_addc_u32 s99, s27, 0
	s_mov_b32 m0, s22
	s_nop 0
	global_load_lds_dwordx4 v154, s[26:27]
	s_add_i32 m0, s22, 0x2000
	s_add_u32 s22, s26, 0xb0000
	s_addc_u32 s23, s27, 0
	s_add_i32 s69, s46, s33
	global_load_lds_dwordx4 v158, s[26:27]
	s_mov_b32 m0, s69
	s_add_u32 s100, s28, 0x80
	s_addc_u32 s101, s29, 0
	global_load_lds_dwordx4 v154, s[22:23]
	s_add_i32 m0, s69, 0x2000
	s_nop 0
	global_load_lds_dwordx4 v158, s[22:23]
	s_mov_b32 m0, s34
	s_nop 0
	global_load_lds_dwordx4 v152, s[28:29]
	s_mov_b32 m0, s35
	s_nop 0
	global_load_lds_dwordx4 v156, s[28:29]
	ds_read_b128 v[180:183], v192 offset:16384
	ds_read_b128 v[184:187], v192 offset:17408
	ds_read_b128 v[194:197], v192 offset:18432
	ds_read_b128 v[198:201], v192 offset:19456
	ds_read_b128 v[202:205], v192 offset:20480
	ds_read_b128 v[206:209], v192 offset:21504
	ds_read_b128 v[210:213], v192 offset:22528
	ds_read_b128 v[214:217], v192 offset:23552
	s_waitcnt vmcnt(8) lgkmcnt(0)
	s_barrier
	s_setprio 1
	v_mfma_f32_16x16x32_bf16 v[60:63], v[128:131], v[180:183], 0
	v_mfma_f32_16x16x32_bf16 v[56:59], v[136:139], v[180:183], 0
	v_mfma_f32_16x16x32_bf16 v[44:47], v[128:131], v[194:197], 0
	v_mfma_f32_16x16x32_bf16 v[40:43], v[136:139], v[194:197], 0
	v_mfma_f32_16x16x32_bf16 v[28:31], v[128:131], v[202:205], 0
	v_mfma_f32_16x16x32_bf16 v[24:27], v[136:139], v[202:205], 0
	v_mfma_f32_16x16x32_bf16 v[12:15], v[128:131], v[210:213], 0
	v_mfma_f32_16x16x32_bf16 v[8:11], v[136:139], v[210:213], 0
	v_mfma_f32_16x16x32_bf16 v[60:63], v[132:135], v[184:187], v[60:63]
	v_mfma_f32_16x16x32_bf16 v[56:59], v[140:143], v[184:187], v[56:59]
	v_mfma_f32_16x16x32_bf16 v[44:47], v[132:135], v[198:201], v[44:47]
	v_mfma_f32_16x16x32_bf16 v[40:43], v[140:143], v[198:201], v[40:43]
	v_mfma_f32_16x16x32_bf16 v[28:31], v[132:135], v[206:209], v[28:31]
	v_mfma_f32_16x16x32_bf16 v[24:27], v[140:143], v[206:209], v[24:27]
	v_mfma_f32_16x16x32_bf16 v[12:15], v[132:135], v[214:217], v[12:15]
	v_mfma_f32_16x16x32_bf16 v[8:11], v[140:143], v[214:217], v[8:11]
	s_setprio 0
	s_setprio 1
	v_mfma_f32_16x16x32_bf16 v[52:55], v[144:147], v[180:183], 0
	v_mfma_f32_16x16x32_bf16 v[48:51], v[172:175], v[180:183], 0
	v_mfma_f32_16x16x32_bf16 v[36:39], v[144:147], v[194:197], 0
	v_mfma_f32_16x16x32_bf16 v[32:35], v[172:175], v[194:197], 0
	v_mfma_f32_16x16x32_bf16 v[20:23], v[144:147], v[202:205], 0
	v_mfma_f32_16x16x32_bf16 v[16:19], v[172:175], v[202:205], 0
	v_mfma_f32_16x16x32_bf16 v[4:7], v[144:147], v[210:213], 0
	v_mfma_f32_16x16x32_bf16 v[0:3], v[172:175], v[210:213], 0
	v_mfma_f32_16x16x32_bf16 v[52:55], v[148:151], v[184:187], v[52:55]
	v_mfma_f32_16x16x32_bf16 v[48:51], v[176:179], v[184:187], v[48:51]
	v_mfma_f32_16x16x32_bf16 v[36:39], v[148:151], v[198:201], v[36:39]
	v_mfma_f32_16x16x32_bf16 v[32:35], v[176:179], v[198:201], v[32:35]
	v_mfma_f32_16x16x32_bf16 v[20:23], v[148:151], v[206:209], v[20:23]
	v_mfma_f32_16x16x32_bf16 v[16:19], v[176:179], v[206:209], v[16:19]
	v_mfma_f32_16x16x32_bf16 v[4:7], v[148:151], v[214:217], v[4:7]
	v_mfma_f32_16x16x32_bf16 v[0:3], v[176:179], v[214:217], v[0:3]
	s_setprio 0
	s_barrier
; #define PG8_STAGE(bufoff, gbase, voff) do { _Pragma("unroll") for (int _i = 0; _i < 2; ++_i) \
;         __builtin_amdgcn_global_load_lds((const unsigned*)((const char*)(gbase) + (voff)[_i]), (PG8_LAS unsigned*)(lds + (bufoff) + ldsw + _i * 8192), 16, 0, 0); } while (0)
; #define PG8_LDA(dst, b, h) do { _Pragma("unroll") for (int m = 0; m < 4; ++m) _Pragma("unroll") for (int k = 0; k < 2; ++k) dst[m][k] = *(const PG8_LAS bf16x8*)(lds + PG8_SA(b, h) + aoff + m * 2048 + k * 1024); } while (0)
; #define PG8_LDB(dst, b, h) do { _Pragma("unroll") for (int n = 0; n < 2; ++n) _Pragma("unroll") for (int k = 0; k < 2; ++k) dst[n][k] = *(const PG8_LAS bf16x8*)(lds + PG8_SB(b, h) + boff + n * 2048 + k * 1024); } while (0)
; #define PG8_MMA(ai, bj, At, Bt) do { __builtin_amdgcn_s_setprio(1); _Pragma("unroll") for (int m = 0; m < 4; ++m) _Pragma("unroll") for (int n = 0; n < 2; ++n) _Pragma("unroll") for (int k = 0; k < 2; ++k) \
;         acc[ai][bj][m][n] = __builtin_amdgcn_mfma_f32_16x16x32_bf16(Bt[n][k], At[m][k], acc[ai][bj][m][n], 0, 0, 0); __builtin_amdgcn_s_setprio(0); } while (0)
; template <class Epi, class Sched, bool ALIGN_EPI = false, bool SP2 = false>
; __device__ __forceinline__ void gemm_phase(PG8_LAS unsigned char* lds, const Gemm g, const Sched& S, const Epi& E, const int wid) {
;     ...
;             if constexpr (SP2) {
;             PG8_LDB(B0, 0, 0); PG8_LDB(B1, 0, 1); PG8_SCHED; PG8_LDA(At, 0, 0); PG8_STAGE(PG8_SA(1, 1), a1 + hstepA, voffA);
;             PG8_WAIT_V(8); PG8_WAIT_L(0); PG8_BAR; PG8_MMA(0, 0, At, B0); PG8_MMA(0, 1, At, B1); PG8_BAR; PG8_SCHED;
;             PG8_LDA(At, 0, 1); PG8_STAGE(PG8_SB(0, 0), b2, voffB); PG8_STAGE(PG8_SB(0, 1), b2 + hstepB, voffB); PG8_STAGE(PG8_SA(0, 0), a2, voffA);
;             PG8_WAIT_V(8); PG8_WAIT_L(0); PG8_BAR; PG8_MMA(1, 0, At, B0); PG8_MMA(1, 1, At, B1); PG8_BAR; PG8_SCHED;
;             PG8_LDB(B0, 1, 0); PG8_LDB(B1, 1, 1); PG8_SCHED; PG8_LDA(At, 1, 0); PG8_STAGE(PG8_SA(0, 1), a2 + hstepA, voffA);
;             PG8_WAIT_V(8); PG8_WAIT_L(0); PG8_BAR; PG8_MMA(0, 0, At, B0); PG8_MMA(0, 1, At, B1); PG8_BAR; PG8_SCHED;
;             PG8_LDA(At, 1, 1); PG8_STAGE(PG8_SB(1, 0), b3, voffB); PG8_STAGE(PG8_SB(1, 1), b3 + hstepB, voffB); PG8_STAGE(PG8_SA(1, 0), a3, voffA);
;             PG8_WAIT_V(8); PG8_WAIT_L(0); PG8_BAR; PG8_MMA(1, 0, At, B0); PG8_MMA(1, 1, At, B1); PG8_BAR; PG8_SCHED;
	s_add_i32 s69, 0, 0x18000
	s_add_i32 s70, 0, 0x1c000
	s_add_u32 s22, s28, 0xb0000
	s_addc_u32 s23, s29, 0
	s_mov_b32 m0, s36
	s_nop 0
	global_load_lds_dwordx4 v152, s[22:23]
	s_mov_b32 m0, s37
	s_nop 0
	global_load_lds_dwordx4 v156, s[22:23]
	ds_read_b128 v[128:131], v252
	ds_read_b128 v[132:135], v252 offset:1024
	ds_read_b128 v[136:139], v252 offset:2048
	ds_read_b128 v[140:143], v252 offset:3072
	ds_read_b128 v[144:147], v253
	ds_read_b128 v[148:151], v253 offset:1024
	ds_read_b128 v[172:175], v253 offset:2048
	ds_read_b128 v[176:179], v253 offset:3072
	ds_read_b128 v[180:183], v192 offset:32768
	ds_read_b128 v[184:187], v192 offset:33792
	ds_read_b128 v[194:197], v192 offset:34816
	ds_read_b128 v[198:201], v192 offset:35840
	ds_read_b128 v[202:205], v192 offset:36864
	ds_read_b128 v[206:209], v192 offset:37888
	ds_read_b128 v[210:213], v192 offset:38912
	ds_read_b128 v[214:217], v192 offset:39936
	s_waitcnt vmcnt(8) lgkmcnt(0)
	s_barrier
	s_setprio 1
	v_mfma_f32_16x16x32_bf16 v[124:127], v[128:131], v[180:183], v[124:127]
	v_mfma_f32_16x16x32_bf16 v[120:123], v[136:139], v[180:183], v[120:123]
	v_mfma_f32_16x16x32_bf16 v[108:111], v[128:131], v[194:197], v[108:111]
	v_mfma_f32_16x16x32_bf16 v[104:107], v[136:139], v[194:197], v[104:107]
	v_mfma_f32_16x16x32_bf16 v[92:95], v[128:131], v[202:205], v[92:95]
	v_mfma_f32_16x16x32_bf16 v[88:91], v[136:139], v[202:205], v[88:91]
	v_mfma_f32_16x16x32_bf16 v[76:79], v[128:131], v[210:213], v[76:79]
	v_mfma_f32_16x16x32_bf16 v[72:75], v[136:139], v[210:213], v[72:75]
	v_mfma_f32_16x16x32_bf16 v[124:127], v[132:135], v[184:187], v[124:127]
	v_mfma_f32_16x16x32_bf16 v[120:123], v[140:143], v[184:187], v[120:123]
	v_mfma_f32_16x16x32_bf16 v[108:111], v[132:135], v[198:201], v[108:111]
	v_mfma_f32_16x16x32_bf16 v[104:107], v[140:143], v[198:201], v[104:107]
	v_mfma_f32_16x16x32_bf16 v[92:95], v[132:135], v[206:209], v[92:95]
	v_mfma_f32_16x16x32_bf16 v[88:91], v[140:143], v[206:209], v[88:91]
	v_mfma_f32_16x16x32_bf16 v[76:79], v[132:135], v[214:217], v[76:79]
	v_mfma_f32_16x16x32_bf16 v[72:75], v[140:143], v[214:217], v[72:75]
	s_setprio 0
	s_setprio 1
	v_mfma_f32_16x16x32_bf16 v[116:119], v[144:147], v[180:183], v[116:119]
	v_mfma_f32_16x16x32_bf16 v[112:115], v[172:175], v[180:183], v[112:115]
	v_mfma_f32_16x16x32_bf16 v[100:103], v[144:147], v[194:197], v[100:103]
	v_mfma_f32_16x16x32_bf16 v[96:99], v[172:175], v[194:197], v[96:99]
	v_mfma_f32_16x16x32_bf16 v[84:87], v[144:147], v[202:205], v[84:87]
	v_mfma_f32_16x16x32_bf16 v[80:83], v[172:175], v[202:205], v[80:83]
	v_mfma_f32_16x16x32_bf16 v[68:71], v[144:147], v[210:213], v[68:71]
	v_mfma_f32_16x16x32_bf16 v[64:67], v[172:175], v[210:213], v[64:67]
	v_mfma_f32_16x16x32_bf16 v[116:119], v[148:151], v[184:187], v[116:119]
	v_mfma_f32_16x16x32_bf16 v[112:115], v[176:179], v[184:187], v[112:115]
	v_mfma_f32_16x16x32_bf16 v[100:103], v[148:151], v[198:201], v[100:103]
	v_mfma_f32_16x16x32_bf16 v[96:99], v[176:179], v[198:201], v[96:99]
	v_mfma_f32_16x16x32_bf16 v[84:87], v[148:151], v[206:209], v[84:87]
	v_mfma_f32_16x16x32_bf16 v[80:83], v[176:179], v[206:209], v[80:83]
	v_mfma_f32_16x16x32_bf16 v[68:71], v[148:151], v[214:217], v[68:71]
	v_mfma_f32_16x16x32_bf16 v[64:67], v[176:179], v[214:217], v[64:67]
	s_setprio 0
	s_barrier
	s_add_i32 s22, s69, s33
	s_mov_b32 m0, s22
	s_nop 0
	global_load_lds_dwordx4 v154, s[98:99]
	s_add_i32 m0, s22, 0x2000
	s_add_u32 s22, s26, 0xb0080
	s_addc_u32 s23, s27, 0
	s_add_i32 s26, s70, s33
	global_load_lds_dwordx4 v158, s[98:99]
	s_mov_b32 m0, s26
	s_nop 0
	global_load_lds_dwordx4 v154, s[22:23]
	s_add_i32 m0, s26, 0x2000
	s_nop 0
	global_load_lds_dwordx4 v158, s[22:23]
	s_mov_b32 m0, s39
	s_nop 0
	global_load_lds_dwordx4 v152, s[100:101]
	s_mov_b32 m0, s40
	s_nop 0
	global_load_lds_dwordx4 v156, s[100:101]
	ds_read_b128 v[180:183], v192 offset:49152
	ds_read_b128 v[184:187], v192 offset:50176
	ds_read_b128 v[194:197], v192 offset:51200
	ds_read_b128 v[198:201], v192 offset:52224
	ds_read_b128 v[202:205], v192 offset:53248
	ds_read_b128 v[206:209], v192 offset:54272
	ds_read_b128 v[210:213], v192 offset:55296
	ds_read_b128 v[214:217], v192 offset:56320
	s_waitcnt vmcnt(8) lgkmcnt(0)
	s_barrier
	s_setprio 1
	v_mfma_f32_16x16x32_bf16 v[60:63], v[128:131], v[180:183], v[60:63]
	v_mfma_f32_16x16x32_bf16 v[56:59], v[136:139], v[180:183], v[56:59]
	v_mfma_f32_16x16x32_bf16 v[44:47], v[128:131], v[194:197], v[44:47]
	v_mfma_f32_16x16x32_bf16 v[40:43], v[136:139], v[194:197], v[40:43]
	v_mfma_f32_16x16x32_bf16 v[28:31], v[128:131], v[202:205], v[28:31]
	v_mfma_f32_16x16x32_bf16 v[24:27], v[136:139], v[202:205], v[24:27]
	v_mfma_f32_16x16x32_bf16 v[12:15], v[128:131], v[210:213], v[12:15]
	v_mfma_f32_16x16x32_bf16 v[8:11], v[136:139], v[210:213], v[8:11]
	v_mfma_f32_16x16x32_bf16 v[60:63], v[132:135], v[184:187], v[60:63]
	v_mfma_f32_16x16x32_bf16 v[56:59], v[140:143], v[184:187], v[56:59]
	v_mfma_f32_16x16x32_bf16 v[44:47], v[132:135], v[198:201], v[44:47]
	v_mfma_f32_16x16x32_bf16 v[40:43], v[140:143], v[198:201], v[40:43]
	v_mfma_f32_16x16x32_bf16 v[28:31], v[132:135], v[206:209], v[28:31]
	v_mfma_f32_16x16x32_bf16 v[24:27], v[140:143], v[206:209], v[24:27]
	v_mfma_f32_16x16x32_bf16 v[12:15], v[132:135], v[214:217], v[12:15]
	v_mfma_f32_16x16x32_bf16 v[8:11], v[140:143], v[214:217], v[8:11]
	s_setprio 0
	s_setprio 1
	v_mfma_f32_16x16x32_bf16 v[52:55], v[144:147], v[180:183], v[52:55]
	v_mfma_f32_16x16x32_bf16 v[48:51], v[172:175], v[180:183], v[48:51]
	v_mfma_f32_16x16x32_bf16 v[36:39], v[144:147], v[194:197], v[36:39]
	v_mfma_f32_16x16x32_bf16 v[32:35], v[172:175], v[194:197], v[32:35]
	v_mfma_f32_16x16x32_bf16 v[20:23], v[144:147], v[202:205], v[20:23]
	v_mfma_f32_16x16x32_bf16 v[16:19], v[172:175], v[202:205], v[16:19]
	v_mfma_f32_16x16x32_bf16 v[4:7], v[144:147], v[210:213], v[4:7]
	v_mfma_f32_16x16x32_bf16 v[0:3], v[172:175], v[210:213], v[0:3]
	v_mfma_f32_16x16x32_bf16 v[52:55], v[148:151], v[184:187], v[52:55]
	v_mfma_f32_16x16x32_bf16 v[48:51], v[176:179], v[184:187], v[48:51]
	v_mfma_f32_16x16x32_bf16 v[36:39], v[148:151], v[198:201], v[36:39]
	v_mfma_f32_16x16x32_bf16 v[32:35], v[176:179], v[198:201], v[32:35]
	v_mfma_f32_16x16x32_bf16 v[20:23], v[148:151], v[206:209], v[20:23]
	v_mfma_f32_16x16x32_bf16 v[16:19], v[176:179], v[206:209], v[16:19]
	v_mfma_f32_16x16x32_bf16 v[4:7], v[148:151], v[214:217], v[4:7]
	v_mfma_f32_16x16x32_bf16 v[0:3], v[176:179], v[214:217], v[0:3]
	s_setprio 0
	s_barrier
	s_add_i32 s68, s68, 2
	s_add_u32 s66, s66, 0x100
	s_addc_u32 s67, s67, 0
	s_cmp_gt_u32 s68, 41
	s_mov_b64 s[22:23], s[24:25]
; #define PG8_STAGE(bufoff, gbase, voff) do { _Pragma("unroll") for (int _i = 0; _i < 2; ++_i) \
;         __builtin_amdgcn_global_load_lds((const unsigned*)((const char*)(gbase) + (voff)[_i]), (PG8_LAS unsigned*)(lds + (bufoff) + ldsw + _i * 8192), 16, 0, 0); } while (0)
; #define PG8_LDA(dst, b, h) do { _Pragma("unroll") for (int m = 0; m < 4; ++m) _Pragma("unroll") for (int k = 0; k < 2; ++k) dst[m][k] = *(const PG8_LAS bf16x8*)(lds + PG8_SA(b, h) + aoff + m * 2048 + k * 1024); } while (0)
; #define PG8_LDB(dst, b, h) do { _Pragma("unroll") for (int n = 0; n < 2; ++n) _Pragma("unroll") for (int k = 0; k < 2; ++k) dst[n][k] = *(const PG8_LAS bf16x8*)(lds + PG8_SB(b, h) + boff + n * 2048 + k * 1024); } while (0)
; #define PG8_MMA(ai, bj, At, Bt) do { __builtin_amdgcn_s_setprio(1); _Pragma("unroll") for (int m = 0; m < 4; ++m) _Pragma("unroll") for (int n = 0; n < 2; ++n) _Pragma("unroll") for (int k = 0; k < 2; ++k) \
;         acc[ai][bj][m][n] = __builtin_amdgcn_mfma_f32_16x16x32_bf16(Bt[n][k], At[m][k], acc[ai][bj][m][n], 0, 0, 0); __builtin_amdgcn_s_setprio(0); } while (0)
; template <class Epi, class Sched, bool ALIGN_EPI = false, bool SP2 = false>
; __device__ __forceinline__ void gemm_phase(PG8_LAS unsigned char* lds, const Gemm g, const Sched& S, const Epi& E, const int wid) {
;     ...
;             if constexpr (SP2) {
;             PG8_LDB(B0, 0, 0); PG8_LDB(B1, 0, 1); PG8_SCHED; PG8_LDA(At, 0, 0); PG8_STAGE(PG8_SA(1, 1), a1 + hstepA, voffA);
;             PG8_WAIT_V(8); PG8_WAIT_L(0); PG8_BAR; PG8_MMA(0, 0, At, B0); PG8_MMA(0, 1, At, B1); PG8_BAR; PG8_SCHED;
;             PG8_LDA(At, 0, 1); PG8_STAGE(PG8_SB(0, 0), b2, voffB); PG8_STAGE(PG8_SB(0, 1), b2 + hstepB, voffB); PG8_STAGE(PG8_SA(0, 0), a2, voffA);
;             PG8_WAIT_V(8); PG8_WAIT_L(0); PG8_BAR; PG8_MMA(1, 0, At, B0); PG8_MMA(1, 1, At, B1); PG8_BAR; PG8_SCHED;
;             PG8_LDB(B0, 1, 0); PG8_LDB(B1, 1, 1); PG8_SCHED; PG8_LDA(At, 1, 0); PG8_STAGE(PG8_SA(0, 1), a2 + hstepA, voffA);
;             PG8_WAIT_V(8); PG8_WAIT_L(0); PG8_BAR; PG8_MMA(0, 0, At, B0); PG8_MMA(0, 1, At, B1); PG8_BAR; PG8_SCHED;
;             PG8_LDA(At, 1, 1); PG8_STAGE(PG8_SB(1, 0), b3, voffB); PG8_STAGE(PG8_SB(1, 1), b3 + hstepB, voffB); PG8_STAGE(PG8_SA(1, 0), a3, voffA);
;             PG8_WAIT_V(8); PG8_WAIT_L(0); PG8_BAR; PG8_MMA(1, 0, At, B0); PG8_MMA(1, 1, At, B1); PG8_BAR; PG8_SCHED;
.LBB0_1952:
	s_add_u32 s24, s22, 0x100
	s_addc_u32 s25, s23, 0
	s_cmp_eq_u32 s68, 40
	s_cselect_b32 s29, s7, s25
	s_cselect_b32 s28, s6, s24
	s_cselect_b32 s27, s21, s67
	s_cselect_b32 s26, s20, s66
	s_add_i32 m0, s34, 0xc000
	s_nop 0
	global_load_lds_dwordx4 v164, s[22:23]
	s_add_i32 m0, s34, 0xe000
	s_nop 0
	global_load_lds_dwordx4 v166, s[22:23]
	ds_read_b128 v[128:131], v190
	ds_read_b128 v[132:135], v190 offset:1024
	ds_read_b128 v[136:139], v190 offset:2048
	ds_read_b128 v[140:143], v190 offset:3072
	ds_read_b128 v[144:147], v191
	ds_read_b128 v[148:151], v191 offset:1024
	ds_read_b128 v[172:175], v191 offset:2048
	ds_read_b128 v[176:179], v191 offset:3072
	ds_read_b128 v[180:183], v192
	ds_read_b128 v[184:187], v192 offset:1024
	ds_read_b128 v[194:197], v192 offset:2048
	ds_read_b128 v[198:201], v192 offset:3072
	ds_read_b128 v[202:205], v192 offset:4096
	ds_read_b128 v[206:209], v192 offset:5120
	ds_read_b128 v[210:213], v192 offset:6144
	ds_read_b128 v[214:217], v192 offset:7168
	s_waitcnt vmcnt(8) lgkmcnt(0)
	s_barrier
	s_setprio 1
	v_mfma_f32_16x16x32_bf16 v[124:127], v[128:131], v[180:183], v[124:127]
	v_mfma_f32_16x16x32_bf16 v[120:123], v[136:139], v[180:183], v[120:123]
	v_mfma_f32_16x16x32_bf16 v[108:111], v[128:131], v[194:197], v[108:111]
	v_mfma_f32_16x16x32_bf16 v[104:107], v[136:139], v[194:197], v[104:107]
	v_mfma_f32_16x16x32_bf16 v[92:95], v[128:131], v[202:205], v[92:95]
	v_mfma_f32_16x16x32_bf16 v[88:91], v[136:139], v[202:205], v[88:91]
	v_mfma_f32_16x16x32_bf16 v[76:79], v[128:131], v[210:213], v[76:79]
	v_mfma_f32_16x16x32_bf16 v[72:75], v[136:139], v[210:213], v[72:75]
	v_mfma_f32_16x16x32_bf16 v[124:127], v[132:135], v[184:187], v[124:127]
	v_mfma_f32_16x16x32_bf16 v[120:123], v[140:143], v[184:187], v[120:123]
	v_mfma_f32_16x16x32_bf16 v[108:111], v[132:135], v[198:201], v[108:111]
	v_mfma_f32_16x16x32_bf16 v[104:107], v[140:143], v[198:201], v[104:107]
	v_mfma_f32_16x16x32_bf16 v[92:95], v[132:135], v[206:209], v[92:95]
	v_mfma_f32_16x16x32_bf16 v[88:91], v[140:143], v[206:209], v[88:91]
	v_mfma_f32_16x16x32_bf16 v[76:79], v[132:135], v[214:217], v[76:79]
	v_mfma_f32_16x16x32_bf16 v[72:75], v[140:143], v[214:217], v[72:75]
	s_setprio 0
	s_setprio 1
	v_mfma_f32_16x16x32_bf16 v[116:119], v[144:147], v[180:183], v[116:119]
	v_mfma_f32_16x16x32_bf16 v[112:115], v[172:175], v[180:183], v[112:115]
	v_mfma_f32_16x16x32_bf16 v[100:103], v[144:147], v[194:197], v[100:103]
	v_mfma_f32_16x16x32_bf16 v[96:99], v[172:175], v[194:197], v[96:99]
	v_mfma_f32_16x16x32_bf16 v[84:87], v[144:147], v[202:205], v[84:87]
	v_mfma_f32_16x16x32_bf16 v[80:83], v[172:175], v[202:205], v[80:83]
	v_mfma_f32_16x16x32_bf16 v[68:71], v[144:147], v[210:213], v[68:71]
	v_mfma_f32_16x16x32_bf16 v[64:67], v[172:175], v[210:213], v[64:67]
	v_mfma_f32_16x16x32_bf16 v[116:119], v[148:151], v[184:187], v[116:119]
	v_mfma_f32_16x16x32_bf16 v[112:115], v[176:179], v[184:187], v[112:115]
	v_mfma_f32_16x16x32_bf16 v[100:103], v[148:151], v[198:201], v[100:103]
	v_mfma_f32_16x16x32_bf16 v[96:99], v[176:179], v[198:201], v[96:99]
	v_mfma_f32_16x16x32_bf16 v[84:87], v[148:151], v[206:209], v[84:87]
	v_mfma_f32_16x16x32_bf16 v[80:83], v[176:179], v[206:209], v[80:83]
	v_mfma_f32_16x16x32_bf16 v[68:71], v[148:151], v[214:217], v[68:71]
	v_mfma_f32_16x16x32_bf16 v[64:67], v[176:179], v[214:217], v[64:67]
	s_setprio 0
	s_barrier
	s_add_i32 s22, s45, s33
	s_add_u32 s98, s26, 0x80
	s_addc_u32 s99, s27, 0
	s_mov_b32 m0, s22
	s_nop 0
	global_load_lds_dwordx4 v154, s[26:27]
	s_add_i32 m0, s22, 0x2000
	s_add_u32 s22, s26, 0xb0000
	s_addc_u32 s23, s27, 0
	s_add_i32 s69, s46, s33
	global_load_lds_dwordx4 v158, s[26:27]
	s_mov_b32 m0, s69
	s_add_u32 s100, s28, 0x80
	s_addc_u32 s101, s29, 0
	global_load_lds_dwordx4 v154, s[22:23]
	s_add_i32 m0, s69, 0x2000
	s_nop 0
	global_load_lds_dwordx4 v158, s[22:23]
	s_mov_b32 m0, s34
	s_nop 0
	global_load_lds_dwordx4 v152, s[28:29]
	s_mov_b32 m0, s35
	s_nop 0
	global_load_lds_dwordx4 v156, s[28:29]
	ds_read_b128 v[180:183], v192 offset:16384
	ds_read_b128 v[184:187], v192 offset:17408
	ds_read_b128 v[194:197], v192 offset:18432
	ds_read_b128 v[198:201], v192 offset:19456
	ds_read_b128 v[202:205], v192 offset:20480
	ds_read_b128 v[206:209], v192 offset:21504
	ds_read_b128 v[210:213], v192 offset:22528
	ds_read_b128 v[214:217], v192 offset:23552
	s_waitcnt vmcnt(8) lgkmcnt(0)
	s_barrier
	s_setprio 1
	v_mfma_f32_16x16x32_bf16 v[60:63], v[128:131], v[180:183], v[60:63]
	v_mfma_f32_16x16x32_bf16 v[56:59], v[136:139], v[180:183], v[56:59]
	v_mfma_f32_16x16x32_bf16 v[44:47], v[128:131], v[194:197], v[44:47]
	v_mfma_f32_16x16x32_bf16 v[40:43], v[136:139], v[194:197], v[40:43]
	v_mfma_f32_16x16x32_bf16 v[28:31], v[128:131], v[202:205], v[28:31]
	v_mfma_f32_16x16x32_bf16 v[24:27], v[136:139], v[202:205], v[24:27]
	v_mfma_f32_16x16x32_bf16 v[12:15], v[128:131], v[210:213], v[12:15]
	v_mfma_f32_16x16x32_bf16 v[8:11], v[136:139], v[210:213], v[8:11]
	v_mfma_f32_16x16x32_bf16 v[60:63], v[132:135], v[184:187], v[60:63]
	v_mfma_f32_16x16x32_bf16 v[56:59], v[140:143], v[184:187], v[56:59]
	v_mfma_f32_16x16x32_bf16 v[44:47], v[132:135], v[198:201], v[44:47]
	v_mfma_f32_16x16x32_bf16 v[40:43], v[140:143], v[198:201], v[40:43]
	v_mfma_f32_16x16x32_bf16 v[28:31], v[132:135], v[206:209], v[28:31]
	v_mfma_f32_16x16x32_bf16 v[24:27], v[140:143], v[206:209], v[24:27]
	v_mfma_f32_16x16x32_bf16 v[12:15], v[132:135], v[214:217], v[12:15]
	v_mfma_f32_16x16x32_bf16 v[8:11], v[140:143], v[214:217], v[8:11]
	s_setprio 0
	s_setprio 1
	v_mfma_f32_16x16x32_bf16 v[52:55], v[144:147], v[180:183], v[52:55]
	v_mfma_f32_16x16x32_bf16 v[48:51], v[172:175], v[180:183], v[48:51]
	v_mfma_f32_16x16x32_bf16 v[36:39], v[144:147], v[194:197], v[36:39]
	v_mfma_f32_16x16x32_bf16 v[32:35], v[172:175], v[194:197], v[32:35]
	v_mfma_f32_16x16x32_bf16 v[20:23], v[144:147], v[202:205], v[20:23]
	v_mfma_f32_16x16x32_bf16 v[16:19], v[172:175], v[202:205], v[16:19]
	v_mfma_f32_16x16x32_bf16 v[4:7], v[144:147], v[210:213], v[4:7]
	v_mfma_f32_16x16x32_bf16 v[0:3], v[172:175], v[210:213], v[0:3]
	v_mfma_f32_16x16x32_bf16 v[52:55], v[148:151], v[184:187], v[52:55]
	v_mfma_f32_16x16x32_bf16 v[48:51], v[176:179], v[184:187], v[48:51]
	v_mfma_f32_16x16x32_bf16 v[36:39], v[148:151], v[198:201], v[36:39]
	v_mfma_f32_16x16x32_bf16 v[32:35], v[176:179], v[198:201], v[32:35]
	v_mfma_f32_16x16x32_bf16 v[20:23], v[148:151], v[206:209], v[20:23]
	v_mfma_f32_16x16x32_bf16 v[16:19], v[176:179], v[206:209], v[16:19]
	v_mfma_f32_16x16x32_bf16 v[4:7], v[148:151], v[214:217], v[4:7]
	v_mfma_f32_16x16x32_bf16 v[0:3], v[176:179], v[214:217], v[0:3]
	s_setprio 0
	s_barrier
; #define PG8_STAGE(bufoff, gbase, voff) do { _Pragma("unroll") for (int _i = 0; _i < 2; ++_i) \
;         __builtin_amdgcn_global_load_lds((const unsigned*)((const char*)(gbase) + (voff)[_i]), (PG8_LAS unsigned*)(lds + (bufoff) + ldsw + _i * 8192), 16, 0, 0); } while (0)
; #define PG8_LDA(dst, b, h) do { _Pragma("unroll") for (int m = 0; m < 4; ++m) _Pragma("unroll") for (int k = 0; k < 2; ++k) dst[m][k] = *(const PG8_LAS bf16x8*)(lds + PG8_SA(b, h) + aoff + m * 2048 + k * 1024); } while (0)
; #define PG8_LDB(dst, b, h) do { _Pragma("unroll") for (int n = 0; n < 2; ++n) _Pragma("unroll") for (int k = 0; k < 2; ++k) dst[n][k] = *(const PG8_LAS bf16x8*)(lds + PG8_SB(b, h) + boff + n * 2048 + k * 1024); } while (0)
; #define PG8_WAIT_V(n) asm volatile("s_waitcnt vmcnt(" #n ")" ::: "memory")
; #define PG8_WAIT_L(n) asm volatile("s_waitcnt lgkmcnt(" #n ")" ::: "memory")
; #define PG8_BAR __builtin_amdgcn_s_barrier()
; template <class Epi, class Sched, bool ALIGN_EPI = false, bool SP2 = false>
; __device__ __forceinline__ void gemm_phase(PG8_LAS unsigned char* lds, const Gemm g, const Sched& S, const Epi& E, const int wid) {
;     ...
;             if constexpr (SP2) {
;             PG8_LDB(B0, 0, 0); PG8_LDB(B1, 0, 1); PG8_SCHED; PG8_LDA(At, 0, 0); PG8_STAGE(PG8_SA(1, 1), a1 + hstepA, voffA);
;             PG8_WAIT_V(8); PG8_WAIT_L(0); PG8_BAR; PG8_MMA(0, 0, At, B0); PG8_MMA(0, 1, At, B1); PG8_BAR; PG8_SCHED;
;             PG8_LDA(At, 0, 1); PG8_STAGE(PG8_SB(0, 0), b2, voffB); PG8_STAGE(PG8_SB(0, 1), b2 + hstepB, voffB); PG8_STAGE(PG8_SA(0, 0), a2, voffA);
;             PG8_WAIT_V(8); PG8_WAIT_L(0); PG8_BAR; PG8_MMA(1, 0, At, B0); PG8_MMA(1, 1, At, B1); PG8_BAR; PG8_SCHED;
;             PG8_LDB(B0, 1, 0); PG8_LDB(B1, 1, 1); PG8_SCHED; PG8_LDA(At, 1, 0); PG8_STAGE(PG8_SA(0, 1), a2 + hstepA, voffA);
;             PG8_WAIT_V(8); PG8_WAIT_L(0); PG8_BAR; PG8_MMA(0, 0, At, B0); PG8_MMA(0, 1, At, B1); PG8_BAR; PG8_SCHED;
;             PG8_LDA(At, 1, 1); PG8_STAGE(PG8_SB(1, 0), b3, voffB); PG8_STAGE(PG8_SB(1, 1), b3 + hstepB, voffB); PG8_STAGE(PG8_SA(1, 0), a3, voffA);
;             PG8_WAIT_V(8); PG8_WAIT_L(0); PG8_BAR; PG8_MMA(1, 0, At, B0); PG8_MMA(1, 1, At, B1); PG8_BAR; PG8_SCHED;
;     ...
;         if constexpr (ALIGN_EPI) { if (wr == 0) PG8_BAR; }
;         if constexpr (!Epi::AFTER_DRAIN) { E(acc, cur, wr, wc, fr, fq); S.done(cur); }
;         if (!has_next) break;
	s_add_i32 s69, 0, 0x18000
	s_add_i32 s70, 0, 0x1c000
	s_add_u32 s22, s28, 0xb0000
	s_addc_u32 s23, s29, 0
	s_mov_b32 m0, s36
	s_nop 0
	global_load_lds_dwordx4 v152, s[22:23]
	s_mov_b32 m0, s37
	s_nop 0
	global_load_lds_dwordx4 v156, s[22:23]
	ds_read_b128 v[128:131], v252
	ds_read_b128 v[132:135], v252 offset:1024
	ds_read_b128 v[136:139], v252 offset:2048
	ds_read_b128 v[140:143], v252 offset:3072
	ds_read_b128 v[144:147], v253
	ds_read_b128 v[148:151], v253 offset:1024
	ds_read_b128 v[172:175], v253 offset:2048
	ds_read_b128 v[176:179], v253 offset:3072
	ds_read_b128 v[180:183], v192 offset:32768
	ds_read_b128 v[184:187], v192 offset:33792
	ds_read_b128 v[194:197], v192 offset:34816
	ds_read_b128 v[198:201], v192 offset:35840
	ds_read_b128 v[202:205], v192 offset:36864
	ds_read_b128 v[206:209], v192 offset:37888
	ds_read_b128 v[210:213], v192 offset:38912
	ds_read_b128 v[214:217], v192 offset:39936
	s_waitcnt vmcnt(8) lgkmcnt(0)
	s_barrier
	s_setprio 1
	v_mfma_f32_16x16x32_bf16 v[124:127], v[128:131], v[180:183], v[124:127]
	v_mfma_f32_16x16x32_bf16 v[120:123], v[136:139], v[180:183], v[120:123]
	v_mfma_f32_16x16x32_bf16 v[108:111], v[128:131], v[194:197], v[108:111]
	v_mfma_f32_16x16x32_bf16 v[104:107], v[136:139], v[194:197], v[104:107]
	v_mfma_f32_16x16x32_bf16 v[92:95], v[128:131], v[202:205], v[92:95]
	v_mfma_f32_16x16x32_bf16 v[88:91], v[136:139], v[202:205], v[88:91]
	v_mfma_f32_16x16x32_bf16 v[76:79], v[128:131], v[210:213], v[76:79]
	v_mfma_f32_16x16x32_bf16 v[72:75], v[136:139], v[210:213], v[72:75]
	v_mfma_f32_16x16x32_bf16 v[124:127], v[132:135], v[184:187], v[124:127]
	v_mfma_f32_16x16x32_bf16 v[120:123], v[140:143], v[184:187], v[120:123]
	v_mfma_f32_16x16x32_bf16 v[108:111], v[132:135], v[198:201], v[108:111]
	v_mfma_f32_16x16x32_bf16 v[104:107], v[140:143], v[198:201], v[104:107]
	v_mfma_f32_16x16x32_bf16 v[92:95], v[132:135], v[206:209], v[92:95]
	v_mfma_f32_16x16x32_bf16 v[88:91], v[140:143], v[206:209], v[88:91]
	v_mfma_f32_16x16x32_bf16 v[76:79], v[132:135], v[214:217], v[76:79]
	v_mfma_f32_16x16x32_bf16 v[72:75], v[140:143], v[214:217], v[72:75]
	s_setprio 0
	s_setprio 1
	v_mfma_f32_16x16x32_bf16 v[116:119], v[144:147], v[180:183], v[116:119]
	v_mfma_f32_16x16x32_bf16 v[112:115], v[172:175], v[180:183], v[112:115]
	v_mfma_f32_16x16x32_bf16 v[100:103], v[144:147], v[194:197], v[100:103]
	v_mfma_f32_16x16x32_bf16 v[96:99], v[172:175], v[194:197], v[96:99]
	v_mfma_f32_16x16x32_bf16 v[84:87], v[144:147], v[202:205], v[84:87]
	v_mfma_f32_16x16x32_bf16 v[80:83], v[172:175], v[202:205], v[80:83]
	v_mfma_f32_16x16x32_bf16 v[68:71], v[144:147], v[210:213], v[68:71]
	v_mfma_f32_16x16x32_bf16 v[64:67], v[172:175], v[210:213], v[64:67]
	v_mfma_f32_16x16x32_bf16 v[116:119], v[148:151], v[184:187], v[116:119]
	v_mfma_f32_16x16x32_bf16 v[112:115], v[176:179], v[184:187], v[112:115]
	v_mfma_f32_16x16x32_bf16 v[100:103], v[148:151], v[198:201], v[100:103]
	v_mfma_f32_16x16x32_bf16 v[96:99], v[176:179], v[198:201], v[96:99]
	v_mfma_f32_16x16x32_bf16 v[84:87], v[148:151], v[206:209], v[84:87]
	v_mfma_f32_16x16x32_bf16 v[80:83], v[176:179], v[206:209], v[80:83]
	v_mfma_f32_16x16x32_bf16 v[68:71], v[148:151], v[214:217], v[68:71]
	v_mfma_f32_16x16x32_bf16 v[64:67], v[176:179], v[214:217], v[64:67]
	s_setprio 0
	s_barrier
	s_add_i32 s22, s69, s33
	s_mov_b32 m0, s22
	s_nop 0
	global_load_lds_dwordx4 v154, s[98:99]
	s_add_i32 m0, s22, 0x2000
	s_add_u32 s22, s26, 0xb0080
	s_addc_u32 s23, s27, 0
	s_add_i32 s26, s70, s33
	global_load_lds_dwordx4 v158, s[98:99]
	s_mov_b32 m0, s26
	s_nop 0
	global_load_lds_dwordx4 v154, s[22:23]
	s_add_i32 m0, s26, 0x2000
	s_nop 0
	global_load_lds_dwordx4 v158, s[22:23]
	s_mov_b32 m0, s39
	s_nop 0
	global_load_lds_dwordx4 v152, s[100:101]
	s_mov_b32 m0, s40
	s_nop 0
	global_load_lds_dwordx4 v156, s[100:101]
	ds_read_b128 v[180:183], v192 offset:49152
	ds_read_b128 v[184:187], v192 offset:50176
	ds_read_b128 v[194:197], v192 offset:51200
	ds_read_b128 v[198:201], v192 offset:52224
	ds_read_b128 v[202:205], v192 offset:53248
	ds_read_b128 v[206:209], v192 offset:54272
	ds_read_b128 v[210:213], v192 offset:55296
	ds_read_b128 v[214:217], v192 offset:56320
	s_waitcnt vmcnt(8) lgkmcnt(0)
	s_barrier
	s_setprio 1
	v_mfma_f32_16x16x32_bf16 v[60:63], v[128:131], v[180:183], v[60:63]
	v_mfma_f32_16x16x32_bf16 v[56:59], v[136:139], v[180:183], v[56:59]
	v_mfma_f32_16x16x32_bf16 v[44:47], v[128:131], v[194:197], v[44:47]
	v_mfma_f32_16x16x32_bf16 v[40:43], v[136:139], v[194:197], v[40:43]
	v_mfma_f32_16x16x32_bf16 v[28:31], v[128:131], v[202:205], v[28:31]
	v_mfma_f32_16x16x32_bf16 v[24:27], v[136:139], v[202:205], v[24:27]
	v_mfma_f32_16x16x32_bf16 v[12:15], v[128:131], v[210:213], v[12:15]
	v_mfma_f32_16x16x32_bf16 v[8:11], v[136:139], v[210:213], v[8:11]
	v_mfma_f32_16x16x32_bf16 v[60:63], v[132:135], v[184:187], v[60:63]
	v_mfma_f32_16x16x32_bf16 v[56:59], v[140:143], v[184:187], v[56:59]
	v_mfma_f32_16x16x32_bf16 v[44:47], v[132:135], v[198:201], v[44:47]
	v_mfma_f32_16x16x32_bf16 v[40:43], v[140:143], v[198:201], v[40:43]
	v_mfma_f32_16x16x32_bf16 v[28:31], v[132:135], v[206:209], v[28:31]
	v_mfma_f32_16x16x32_bf16 v[24:27], v[140:143], v[206:209], v[24:27]
	v_mfma_f32_16x16x32_bf16 v[12:15], v[132:135], v[214:217], v[12:15]
	v_mfma_f32_16x16x32_bf16 v[8:11], v[140:143], v[214:217], v[8:11]
	s_setprio 0
	s_setprio 1
	v_mfma_f32_16x16x32_bf16 v[52:55], v[144:147], v[180:183], v[52:55]
	v_mfma_f32_16x16x32_bf16 v[48:51], v[172:175], v[180:183], v[48:51]
	v_mfma_f32_16x16x32_bf16 v[36:39], v[144:147], v[194:197], v[36:39]
	v_mfma_f32_16x16x32_bf16 v[32:35], v[172:175], v[194:197], v[32:35]
	v_mfma_f32_16x16x32_bf16 v[20:23], v[144:147], v[202:205], v[20:23]
	v_mfma_f32_16x16x32_bf16 v[16:19], v[172:175], v[202:205], v[16:19]
	v_mfma_f32_16x16x32_bf16 v[4:7], v[144:147], v[210:213], v[4:7]
	v_mfma_f32_16x16x32_bf16 v[0:3], v[172:175], v[210:213], v[0:3]
	v_mfma_f32_16x16x32_bf16 v[52:55], v[148:151], v[184:187], v[52:55]
	v_mfma_f32_16x16x32_bf16 v[48:51], v[176:179], v[184:187], v[48:51]
	v_mfma_f32_16x16x32_bf16 v[36:39], v[148:151], v[198:201], v[36:39]
	v_mfma_f32_16x16x32_bf16 v[32:35], v[176:179], v[198:201], v[32:35]
	v_mfma_f32_16x16x32_bf16 v[20:23], v[148:151], v[206:209], v[20:23]
	v_mfma_f32_16x16x32_bf16 v[16:19], v[176:179], v[206:209], v[16:19]
	v_mfma_f32_16x16x32_bf16 v[4:7], v[148:151], v[214:217], v[4:7]
	v_mfma_f32_16x16x32_bf16 v[0:3], v[176:179], v[214:217], v[0:3]
	s_setprio 0
	s_barrier
	s_add_i32 s68, s68, 2
	s_add_u32 s66, s66, 0x100
	s_addc_u32 s67, s67, 0
	s_cmp_gt_u32 s68, 41
	s_mov_b64 s[22:23], s[24:25]
	s_cbranch_scc0 .LBB0_1952
	s_and_b64 vcc, exec, s[18:19]
	s_cbranch_vccz .LBB0_1955
	s_barrier

; #define PG8_STAGE(bufoff, gbase, voff) do { _Pragma("unroll") for (int _i = 0; _i < 2; ++_i) \
;         __builtin_amdgcn_global_load_lds((const unsigned*)((const char*)(gbase) + (voff)[_i]), (PG8_LAS unsigned*)(lds + (bufoff) + ldsw + _i * 8192), 16, 0, 0); } while (0)
; #define PG8_WAIT_V(n) asm volatile("s_waitcnt vmcnt(" #n ")" ::: "memory")
; #define PG8_WAIT_L(n) asm volatile("s_waitcnt lgkmcnt(" #n ")" ::: "memory")
; #define PG8_BAR __builtin_amdgcn_s_barrier()
; template <class Epi, class Sched, bool ALIGN_EPI = false, bool SP2 = false>
; __device__ __forceinline__ void gemm_phase(PG8_LAS unsigned char* lds, const Gemm g, const Sched& S, const Epi& E, const int wid) {
;     ...
;         const bool has_next = S.next(ui + 1, nxt);
;         const char* nA = has_next ? (const char*)g.A + (size_t)nxt.pm * tstepA : cA; const char* nB = has_next ? (const char*)g.Bt + (size_t)nxt.pn * tstepB : cB;
;         for (int t = 0; t < nt; t += 2) {
;             const bool last = (t == nt - 2);
;             const char* a1 = cA + (size_t)(t + 1) * kstep;
;             const char* a2 = last ? nA : cA + (size_t)(t + 2) * kstep; const char* b2 = last ? nB : cB + (size_t)(t + 2) * kstep;
;             const char* a3 = a2 + kstep; const char* b3 = b2 + kstep;
;             if (last && has_next) S.a_ready(nxt);
;             if constexpr (SP2) {
;             PG8_LDB(B0, 0, 0); PG8_LDB(B1, 0, 1); PG8_SCHED; PG8_LDA(At, 0, 0); PG8_STAGE(PG8_SA(1, 1), a1 + hstepA, voffA);
;             PG8_WAIT_V(8); PG8_WAIT_L(0); PG8_BAR; PG8_MMA(0, 0, At, B0); PG8_MMA(0, 1, At, B1); PG8_BAR; PG8_SCHED;
;             PG8_LDA(At, 0, 1); PG8_STAGE(PG8_SB(0, 0), b2, voffB); PG8_STAGE(PG8_SB(0, 1), b2 + hstepB, voffB); PG8_STAGE(PG8_SA(0, 0), a2, voffA);
;             PG8_WAIT_V(8); PG8_WAIT_L(0); PG8_BAR; PG8_MMA(1, 0, At, B0); PG8_MMA(1, 1, At, B1); PG8_BAR; PG8_SCHED;
;             PG8_LDB(B0, 1, 0); PG8_LDB(B1, 1, 1); PG8_SCHED; PG8_LDA(At, 1, 0); PG8_STAGE(PG8_SA(0, 1), a2 + hstepA, voffA);
;             PG8_WAIT_V(8); PG8_WAIT_L(0); PG8_BAR; PG8_MMA(0, 0, At, B0); PG8_MMA(0, 1, At, B1); PG8_BAR; PG8_SCHED;
;             PG8_LDA(At, 1, 1); PG8_STAGE(PG8_SB(1, 0), b3, voffB); PG8_STAGE(PG8_SB(1, 1), b3 + hstepB, voffB); PG8_STAGE(PG8_SA(1, 0), a3, voffA);
;             PG8_WAIT_V(8); PG8_WAIT_L(0); PG8_BAR; PG8_MMA(1, 0, At, B0); PG8_MMA(1, 1, At, B1); PG8_BAR; PG8_SCHED;
.LBB0_2048:
	s_ashr_i32 s31, s30, 31
	s_lshl_b64 s[34:35], s[30:31], 19
	s_add_u32 s34, s0, s34
	s_addc_u32 s35, s1, s35
	s_and_b64 s[36:37], s[4:5], exec
	s_cselect_b32 s7, s35, s9
	s_cselect_b32 s11, s34, s8
	s_ashr_i32 s29, s28, 31
	s_lshl_b64 s[36:37], s[28:29], 19
	s_add_u32 s36, s33, s36
	s_addc_u32 s37, s44, s37
	s_and_b64 s[38:39], s[4:5], exec
	s_cselect_b32 s29, s37, s13
	s_cselect_b32 s31, s36, s12
	s_add_u32 s8, s8, 0x40080
	s_addc_u32 s9, s9, 0
	s_add_u32 s40, s12, 0x100
	s_addc_u32 s41, s13, 0
	s_mov_b32 s71, -2
	s_waitcnt lgkmcnt(0)
	v_add_u32_e32 v252, 0x18000, v174
	v_add_u32_e32 v253, 0x1c000, v174
	s_add_u32 s12, s8, 0xfffc0080
	s_addc_u32 s13, s9, -1
	s_cmp_eq_u32 s71, 12
	s_cselect_b32 s39, s7, s13
	s_cselect_b32 s38, s11, s12
	s_cselect_b32 s13, s29, s41
	s_cselect_b32 s12, s31, s40
	s_add_i32 m0, s46, 0xc000
	s_nop 0
	global_load_lds_dwordx4 v138, s[8:9]
	s_add_i32 m0, s46, 0xe000
	s_nop 0
	global_load_lds_dwordx4 v140, s[8:9]
	ds_read_b128 v[146:149], v179
	ds_read_b128 v[150:153], v179 offset:1024
	ds_read_b128 v[154:157], v179 offset:2048
	ds_read_b128 v[158:161], v179 offset:3072
	ds_read_b128 v[162:165], v180
	ds_read_b128 v[166:169], v180 offset:1024
	ds_read_b128 v[184:187], v180 offset:2048
	ds_read_b128 v[188:191], v180 offset:3072
	ds_read_b128 v[192:195], v181
	ds_read_b128 v[196:199], v181 offset:1024
	ds_read_b128 v[200:203], v181 offset:2048
	ds_read_b128 v[204:207], v181 offset:3072
	ds_read_b128 v[208:211], v181 offset:4096
	ds_read_b128 v[212:215], v181 offset:5120
	ds_read_b128 v[216:219], v181 offset:6144
	ds_read_b128 v[220:223], v181 offset:7168
	s_waitcnt vmcnt(8) lgkmcnt(0)
	s_barrier
	s_setprio 1
	v_mfma_f32_16x16x32_bf16 v[124:127], v[146:149], v[192:195], 0
	v_mfma_f32_16x16x32_bf16 v[120:123], v[154:157], v[192:195], 0
	v_mfma_f32_16x16x32_bf16 v[108:111], v[146:149], v[200:203], 0
	v_mfma_f32_16x16x32_bf16 v[104:107], v[154:157], v[200:203], 0
	v_mfma_f32_16x16x32_bf16 v[92:95], v[146:149], v[208:211], 0
	v_mfma_f32_16x16x32_bf16 v[88:91], v[154:157], v[208:211], 0
	v_mfma_f32_16x16x32_bf16 v[76:79], v[146:149], v[216:219], 0
	v_mfma_f32_16x16x32_bf16 v[72:75], v[154:157], v[216:219], 0
	v_mfma_f32_16x16x32_bf16 v[124:127], v[150:153], v[196:199], v[124:127]
	v_mfma_f32_16x16x32_bf16 v[120:123], v[158:161], v[196:199], v[120:123]
	v_mfma_f32_16x16x32_bf16 v[108:111], v[150:153], v[204:207], v[108:111]
	v_mfma_f32_16x16x32_bf16 v[104:107], v[158:161], v[204:207], v[104:107]
	v_mfma_f32_16x16x32_bf16 v[92:95], v[150:153], v[212:215], v[92:95]
	v_mfma_f32_16x16x32_bf16 v[88:91], v[158:161], v[212:215], v[88:91]
	v_mfma_f32_16x16x32_bf16 v[76:79], v[150:153], v[220:223], v[76:79]
	v_mfma_f32_16x16x32_bf16 v[72:75], v[158:161], v[220:223], v[72:75]
	s_setprio 0
	s_setprio 1
	v_mfma_f32_16x16x32_bf16 v[116:119], v[162:165], v[192:195], 0
	v_mfma_f32_16x16x32_bf16 v[112:115], v[184:187], v[192:195], 0
	v_mfma_f32_16x16x32_bf16 v[100:103], v[162:165], v[200:203], 0
	v_mfma_f32_16x16x32_bf16 v[96:99], v[184:187], v[200:203], 0
	v_mfma_f32_16x16x32_bf16 v[84:87], v[162:165], v[208:211], 0
	v_mfma_f32_16x16x32_bf16 v[80:83], v[184:187], v[208:211], 0
	v_mfma_f32_16x16x32_bf16 v[68:71], v[162:165], v[216:219], 0
	v_mfma_f32_16x16x32_bf16 v[64:67], v[184:187], v[216:219], 0
	v_mfma_f32_16x16x32_bf16 v[116:119], v[166:169], v[196:199], v[116:119]
	v_mfma_f32_16x16x32_bf16 v[112:115], v[188:191], v[196:199], v[112:115]
	v_mfma_f32_16x16x32_bf16 v[100:103], v[166:169], v[204:207], v[100:103]
	v_mfma_f32_16x16x32_bf16 v[96:99], v[188:191], v[204:207], v[96:99]
	v_mfma_f32_16x16x32_bf16 v[84:87], v[166:169], v[212:215], v[84:87]
	v_mfma_f32_16x16x32_bf16 v[80:83], v[188:191], v[212:215], v[80:83]
	v_mfma_f32_16x16x32_bf16 v[68:71], v[166:169], v[220:223], v[68:71]
	v_mfma_f32_16x16x32_bf16 v[64:67], v[188:191], v[220:223], v[64:67]
	s_setprio 0
	s_barrier
	s_add_i32 s72, s69, s45
	s_add_u32 s98, s12, 0x80
	s_addc_u32 s99, s13, 0
	s_mov_b32 m0, s72
	s_nop 0
	global_load_lds_dwordx4 v130, s[12:13]
	s_add_i32 m0, s72, 0x2000
	s_add_u32 s72, s12, 0x40000
	s_addc_u32 s73, s13, 0
	s_add_i32 s74, s70, s45
	global_load_lds_dwordx4 v134, s[12:13]
	s_mov_b32 m0, s74
	s_add_u32 s100, s38, 0x80
	s_addc_u32 s101, s39, 0
	global_load_lds_dwordx4 v130, s[72:73]
	s_add_i32 m0, s74, 0x2000
	s_nop 0
	global_load_lds_dwordx4 v134, s[72:73]
	s_mov_b32 m0, s46
	s_nop 0
	global_load_lds_dwordx4 v128, s[38:39]
	s_mov_b32 m0, s47
	s_nop 0
	global_load_lds_dwordx4 v132, s[38:39]
	ds_read_b128 v[192:195], v181 offset:16384
	ds_read_b128 v[196:199], v181 offset:17408
	ds_read_b128 v[200:203], v181 offset:18432
	ds_read_b128 v[204:207], v181 offset:19456
	ds_read_b128 v[208:211], v181 offset:20480
	ds_read_b128 v[212:215], v181 offset:21504
	ds_read_b128 v[216:219], v181 offset:22528
	ds_read_b128 v[220:223], v181 offset:23552
	s_waitcnt vmcnt(8) lgkmcnt(0)
	s_barrier
; #define PG8_STAGE(bufoff, gbase, voff) do { _Pragma("unroll") for (int _i = 0; _i < 2; ++_i) \
;         __builtin_amdgcn_global_load_lds((const unsigned*)((const char*)(gbase) + (voff)[_i]), (PG8_LAS unsigned*)(lds + (bufoff) + ldsw + _i * 8192), 16, 0, 0); } while (0)
; #define PG8_LDA(dst, b, h) do { _Pragma("unroll") for (int m = 0; m < 4; ++m) _Pragma("unroll") for (int k = 0; k < 2; ++k) dst[m][k] = *(const PG8_LAS bf16x8*)(lds + PG8_SA(b, h) + aoff + m * 2048 + k * 1024); } while (0)
; #define PG8_LDB(dst, b, h) do { _Pragma("unroll") for (int n = 0; n < 2; ++n) _Pragma("unroll") for (int k = 0; k < 2; ++k) dst[n][k] = *(const PG8_LAS bf16x8*)(lds + PG8_SB(b, h) + boff + n * 2048 + k * 1024); } while (0)
; #define PG8_MMA(ai, bj, At, Bt) do { __builtin_amdgcn_s_setprio(1); _Pragma("unroll") for (int m = 0; m < 4; ++m) _Pragma("unroll") for (int n = 0; n < 2; ++n) _Pragma("unroll") for (int k = 0; k < 2; ++k) \
;         acc[ai][bj][m][n] = __builtin_amdgcn_mfma_f32_16x16x32_bf16(Bt[n][k], At[m][k], acc[ai][bj][m][n], 0, 0, 0); __builtin_amdgcn_s_setprio(0); } while (0)
; template <class Epi, class Sched, bool ALIGN_EPI = false, bool SP2 = false>
; __device__ __forceinline__ void gemm_phase(PG8_LAS unsigned char* lds, const Gemm g, const Sched& S, const Epi& E, const int wid) {
;     ...
;             if constexpr (SP2) {
;             PG8_LDB(B0, 0, 0); PG8_LDB(B1, 0, 1); PG8_SCHED; PG8_LDA(At, 0, 0); PG8_STAGE(PG8_SA(1, 1), a1 + hstepA, voffA);
;             PG8_WAIT_V(8); PG8_WAIT_L(0); PG8_BAR; PG8_MMA(0, 0, At, B0); PG8_MMA(0, 1, At, B1); PG8_BAR; PG8_SCHED;
;             PG8_LDA(At, 0, 1); PG8_STAGE(PG8_SB(0, 0), b2, voffB); PG8_STAGE(PG8_SB(0, 1), b2 + hstepB, voffB); PG8_STAGE(PG8_SA(0, 0), a2, voffA);
;             PG8_WAIT_V(8); PG8_WAIT_L(0); PG8_BAR; PG8_MMA(1, 0, At, B0); PG8_MMA(1, 1, At, B1); PG8_BAR; PG8_SCHED;
;             PG8_LDB(B0, 1, 0); PG8_LDB(B1, 1, 1); PG8_SCHED; PG8_LDA(At, 1, 0); PG8_STAGE(PG8_SA(0, 1), a2 + hstepA, voffA);
;             PG8_WAIT_V(8); PG8_WAIT_L(0); PG8_BAR; PG8_MMA(0, 0, At, B0); PG8_MMA(0, 1, At, B1); PG8_BAR; PG8_SCHED;
;             PG8_LDA(At, 1, 1); PG8_STAGE(PG8_SB(1, 0), b3, voffB); PG8_STAGE(PG8_SB(1, 1), b3 + hstepB, voffB); PG8_STAGE(PG8_SA(1, 0), a3, voffA);
;             PG8_WAIT_V(8); PG8_WAIT_L(0); PG8_BAR; PG8_MMA(1, 0, At, B0); PG8_MMA(1, 1, At, B1); PG8_BAR; PG8_SCHED;
	s_setprio 1
	v_mfma_f32_16x16x32_bf16 v[60:63], v[146:149], v[192:195], 0
	v_mfma_f32_16x16x32_bf16 v[56:59], v[154:157], v[192:195], 0
	v_mfma_f32_16x16x32_bf16 v[44:47], v[146:149], v[200:203], 0
	v_mfma_f32_16x16x32_bf16 v[40:43], v[154:157], v[200:203], 0
	v_mfma_f32_16x16x32_bf16 v[28:31], v[146:149], v[208:211], 0
	v_mfma_f32_16x16x32_bf16 v[24:27], v[154:157], v[208:211], 0
	v_mfma_f32_16x16x32_bf16 v[12:15], v[146:149], v[216:219], 0
	v_mfma_f32_16x16x32_bf16 v[8:11], v[154:157], v[216:219], 0
	v_mfma_f32_16x16x32_bf16 v[60:63], v[150:153], v[196:199], v[60:63]
	v_mfma_f32_16x16x32_bf16 v[56:59], v[158:161], v[196:199], v[56:59]
	v_mfma_f32_16x16x32_bf16 v[44:47], v[150:153], v[204:207], v[44:47]
	v_mfma_f32_16x16x32_bf16 v[40:43], v[158:161], v[204:207], v[40:43]
	v_mfma_f32_16x16x32_bf16 v[28:31], v[150:153], v[212:215], v[28:31]
	v_mfma_f32_16x16x32_bf16 v[24:27], v[158:161], v[212:215], v[24:27]
	v_mfma_f32_16x16x32_bf16 v[12:15], v[150:153], v[220:223], v[12:15]
	v_mfma_f32_16x16x32_bf16 v[8:11], v[158:161], v[220:223], v[8:11]
	s_setprio 0
	s_setprio 1
	v_mfma_f32_16x16x32_bf16 v[52:55], v[162:165], v[192:195], 0
	v_mfma_f32_16x16x32_bf16 v[48:51], v[184:187], v[192:195], 0
	v_mfma_f32_16x16x32_bf16 v[36:39], v[162:165], v[200:203], 0
	v_mfma_f32_16x16x32_bf16 v[32:35], v[184:187], v[200:203], 0
	v_mfma_f32_16x16x32_bf16 v[20:23], v[162:165], v[208:211], 0
	v_mfma_f32_16x16x32_bf16 v[16:19], v[184:187], v[208:211], 0
	v_mfma_f32_16x16x32_bf16 v[4:7], v[162:165], v[216:219], 0
	v_mfma_f32_16x16x32_bf16 v[0:3], v[184:187], v[216:219], 0
	v_mfma_f32_16x16x32_bf16 v[52:55], v[166:169], v[196:199], v[52:55]
	v_mfma_f32_16x16x32_bf16 v[48:51], v[188:191], v[196:199], v[48:51]
	v_mfma_f32_16x16x32_bf16 v[36:39], v[166:169], v[204:207], v[36:39]
	v_mfma_f32_16x16x32_bf16 v[32:35], v[188:191], v[204:207], v[32:35]
	v_mfma_f32_16x16x32_bf16 v[20:23], v[166:169], v[212:215], v[20:23]
	v_mfma_f32_16x16x32_bf16 v[16:19], v[188:191], v[212:215], v[16:19]
	v_mfma_f32_16x16x32_bf16 v[4:7], v[166:169], v[220:223], v[4:7]
	v_mfma_f32_16x16x32_bf16 v[0:3], v[188:191], v[220:223], v[0:3]
	s_setprio 0
	s_barrier
	s_add_i32 s72, 0, 0x18000
	s_add_i32 s73, 0, 0x1c000
	s_add_u32 s38, s38, 0x40000
	s_addc_u32 s39, s39, 0
	s_mov_b32 m0, s48
	s_nop 0
	global_load_lds_dwordx4 v128, s[38:39]
	s_mov_b32 m0, s49
	s_nop 0
	global_load_lds_dwordx4 v132, s[38:39]
	ds_read_b128 v[146:149], v252
	ds_read_b128 v[150:153], v252 offset:1024
	ds_read_b128 v[154:157], v252 offset:2048
	ds_read_b128 v[158:161], v252 offset:3072
	ds_read_b128 v[162:165], v253
	ds_read_b128 v[166:169], v253 offset:1024
	ds_read_b128 v[184:187], v253 offset:2048
	ds_read_b128 v[188:191], v253 offset:3072
	ds_read_b128 v[192:195], v181 offset:32768
	ds_read_b128 v[196:199], v181 offset:33792
	ds_read_b128 v[200:203], v181 offset:34816
	ds_read_b128 v[204:207], v181 offset:35840
	ds_read_b128 v[208:211], v181 offset:36864
	ds_read_b128 v[212:215], v181 offset:37888
	ds_read_b128 v[216:219], v181 offset:38912
	ds_read_b128 v[220:223], v181 offset:39936
	s_waitcnt vmcnt(8) lgkmcnt(0)
	s_barrier
	s_setprio 1
	v_mfma_f32_16x16x32_bf16 v[124:127], v[146:149], v[192:195], v[124:127]
	v_mfma_f32_16x16x32_bf16 v[120:123], v[154:157], v[192:195], v[120:123]
	v_mfma_f32_16x16x32_bf16 v[108:111], v[146:149], v[200:203], v[108:111]
	v_mfma_f32_16x16x32_bf16 v[104:107], v[154:157], v[200:203], v[104:107]
	v_mfma_f32_16x16x32_bf16 v[92:95], v[146:149], v[208:211], v[92:95]
	v_mfma_f32_16x16x32_bf16 v[88:91], v[154:157], v[208:211], v[88:91]
	v_mfma_f32_16x16x32_bf16 v[76:79], v[146:149], v[216:219], v[76:79]
	v_mfma_f32_16x16x32_bf16 v[72:75], v[154:157], v[216:219], v[72:75]
	v_mfma_f32_16x16x32_bf16 v[124:127], v[150:153], v[196:199], v[124:127]
	v_mfma_f32_16x16x32_bf16 v[120:123], v[158:161], v[196:199], v[120:123]
	v_mfma_f32_16x16x32_bf16 v[108:111], v[150:153], v[204:207], v[108:111]
	v_mfma_f32_16x16x32_bf16 v[104:107], v[158:161], v[204:207], v[104:107]
	v_mfma_f32_16x16x32_bf16 v[92:95], v[150:153], v[212:215], v[92:95]
	v_mfma_f32_16x16x32_bf16 v[88:91], v[158:161], v[212:215], v[88:91]
	v_mfma_f32_16x16x32_bf16 v[76:79], v[150:153], v[220:223], v[76:79]
	v_mfma_f32_16x16x32_bf16 v[72:75], v[158:161], v[220:223], v[72:75]
	s_setprio 0
	s_setprio 1
	v_mfma_f32_16x16x32_bf16 v[116:119], v[162:165], v[192:195], v[116:119]
	v_mfma_f32_16x16x32_bf16 v[112:115], v[184:187], v[192:195], v[112:115]
	v_mfma_f32_16x16x32_bf16 v[100:103], v[162:165], v[200:203], v[100:103]
	v_mfma_f32_16x16x32_bf16 v[96:99], v[184:187], v[200:203], v[96:99]
	v_mfma_f32_16x16x32_bf16 v[84:87], v[162:165], v[208:211], v[84:87]
	v_mfma_f32_16x16x32_bf16 v[80:83], v[184:187], v[208:211], v[80:83]
	v_mfma_f32_16x16x32_bf16 v[68:71], v[162:165], v[216:219], v[68:71]
	v_mfma_f32_16x16x32_bf16 v[64:67], v[184:187], v[216:219], v[64:67]
	v_mfma_f32_16x16x32_bf16 v[116:119], v[166:169], v[196:199], v[116:119]
	v_mfma_f32_16x16x32_bf16 v[112:115], v[188:191], v[196:199], v[112:115]
	v_mfma_f32_16x16x32_bf16 v[100:103], v[166:169], v[204:207], v[100:103]
	v_mfma_f32_16x16x32_bf16 v[96:99], v[188:191], v[204:207], v[96:99]
	v_mfma_f32_16x16x32_bf16 v[84:87], v[166:169], v[212:215], v[84:87]
	v_mfma_f32_16x16x32_bf16 v[80:83], v[188:191], v[212:215], v[80:83]
	v_mfma_f32_16x16x32_bf16 v[68:71], v[166:169], v[220:223], v[68:71]
	v_mfma_f32_16x16x32_bf16 v[64:67], v[188:191], v[220:223], v[64:67]
	s_setprio 0
	s_barrier
; #define PG8_STAGE(bufoff, gbase, voff) do { _Pragma("unroll") for (int _i = 0; _i < 2; ++_i) \
;         __builtin_amdgcn_global_load_lds((const unsigned*)((const char*)(gbase) + (voff)[_i]), (PG8_LAS unsigned*)(lds + (bufoff) + ldsw + _i * 8192), 16, 0, 0); } while (0)
; #define PG8_LDA(dst, b, h) do { _Pragma("unroll") for (int m = 0; m < 4; ++m) _Pragma("unroll") for (int k = 0; k < 2; ++k) dst[m][k] = *(const PG8_LAS bf16x8*)(lds + PG8_SA(b, h) + aoff + m * 2048 + k * 1024); } while (0)
; #define PG8_LDB(dst, b, h) do { _Pragma("unroll") for (int n = 0; n < 2; ++n) _Pragma("unroll") for (int k = 0; k < 2; ++k) dst[n][k] = *(const PG8_LAS bf16x8*)(lds + PG8_SB(b, h) + boff + n * 2048 + k * 1024); } while (0)
; #define PG8_MMA(ai, bj, At, Bt) do { __builtin_amdgcn_s_setprio(1); _Pragma("unroll") for (int m = 0; m < 4; ++m) _Pragma("unroll") for (int n = 0; n < 2; ++n) _Pragma("unroll") for (int k = 0; k < 2; ++k) \
;         acc[ai][bj][m][n] = __builtin_amdgcn_mfma_f32_16x16x32_bf16(Bt[n][k], At[m][k], acc[ai][bj][m][n], 0, 0, 0); __builtin_amdgcn_s_setprio(0); } while (0)
; template <class Epi, class Sched, bool ALIGN_EPI = false, bool SP2 = false>
; __device__ __forceinline__ void gemm_phase(PG8_LAS unsigned char* lds, const Gemm g, const Sched& S, const Epi& E, const int wid) {
;     ...
;             if constexpr (SP2) {
;             PG8_LDB(B0, 0, 0); PG8_LDB(B1, 0, 1); PG8_SCHED; PG8_LDA(At, 0, 0); PG8_STAGE(PG8_SA(1, 1), a1 + hstepA, voffA);
;             PG8_WAIT_V(8); PG8_WAIT_L(0); PG8_BAR; PG8_MMA(0, 0, At, B0); PG8_MMA(0, 1, At, B1); PG8_BAR; PG8_SCHED;
;             PG8_LDA(At, 0, 1); PG8_STAGE(PG8_SB(0, 0), b2, voffB); PG8_STAGE(PG8_SB(0, 1), b2 + hstepB, voffB); PG8_STAGE(PG8_SA(0, 0), a2, voffA);
;             PG8_WAIT_V(8); PG8_WAIT_L(0); PG8_BAR; PG8_MMA(1, 0, At, B0); PG8_MMA(1, 1, At, B1); PG8_BAR; PG8_SCHED;
;             PG8_LDB(B0, 1, 0); PG8_LDB(B1, 1, 1); PG8_SCHED; PG8_LDA(At, 1, 0); PG8_STAGE(PG8_SA(0, 1), a2 + hstepA, voffA);
;             PG8_WAIT_V(8); PG8_WAIT_L(0); PG8_BAR; PG8_MMA(0, 0, At, B0); PG8_MMA(0, 1, At, B1); PG8_BAR; PG8_SCHED;
;             PG8_LDA(At, 1, 1); PG8_STAGE(PG8_SB(1, 0), b3, voffB); PG8_STAGE(PG8_SB(1, 1), b3 + hstepB, voffB); PG8_STAGE(PG8_SA(1, 0), a3, voffA);
;             PG8_WAIT_V(8); PG8_WAIT_L(0); PG8_BAR; PG8_MMA(1, 0, At, B0); PG8_MMA(1, 1, At, B1); PG8_BAR; PG8_SCHED;
	s_add_i32 s38, s72, s45
	s_mov_b32 m0, s38
	s_nop 0
	global_load_lds_dwordx4 v130, s[98:99]
	s_add_i32 m0, s38, 0x2000
	s_add_u32 s12, s12, 0x40080
	s_addc_u32 s13, s13, 0
	s_add_i32 s38, s73, s45
	global_load_lds_dwordx4 v134, s[98:99]
	s_mov_b32 m0, s38
	s_nop 0
	global_load_lds_dwordx4 v130, s[12:13]
	s_add_i32 m0, s38, 0x2000
	s_nop 0
	global_load_lds_dwordx4 v134, s[12:13]
	s_mov_b32 m0, s65
	s_nop 0
	global_load_lds_dwordx4 v128, s[100:101]
	s_mov_b32 m0, s66
	s_nop 0
	global_load_lds_dwordx4 v132, s[100:101]
	ds_read_b128 v[192:195], v181 offset:49152
	ds_read_b128 v[196:199], v181 offset:50176
	ds_read_b128 v[200:203], v181 offset:51200
	ds_read_b128 v[204:207], v181 offset:52224
	ds_read_b128 v[208:211], v181 offset:53248
	ds_read_b128 v[212:215], v181 offset:54272
	ds_read_b128 v[216:219], v181 offset:55296
	ds_read_b128 v[220:223], v181 offset:56320
	s_waitcnt vmcnt(8) lgkmcnt(0)
	s_barrier
	s_setprio 1
	v_mfma_f32_16x16x32_bf16 v[60:63], v[146:149], v[192:195], v[60:63]
	v_mfma_f32_16x16x32_bf16 v[56:59], v[154:157], v[192:195], v[56:59]
	v_mfma_f32_16x16x32_bf16 v[44:47], v[146:149], v[200:203], v[44:47]
	v_mfma_f32_16x16x32_bf16 v[40:43], v[154:157], v[200:203], v[40:43]
	v_mfma_f32_16x16x32_bf16 v[28:31], v[146:149], v[208:211], v[28:31]
	v_mfma_f32_16x16x32_bf16 v[24:27], v[154:157], v[208:211], v[24:27]
	v_mfma_f32_16x16x32_bf16 v[12:15], v[146:149], v[216:219], v[12:15]
	v_mfma_f32_16x16x32_bf16 v[8:11], v[154:157], v[216:219], v[8:11]
	v_mfma_f32_16x16x32_bf16 v[60:63], v[150:153], v[196:199], v[60:63]
	v_mfma_f32_16x16x32_bf16 v[56:59], v[158:161], v[196:199], v[56:59]
	v_mfma_f32_16x16x32_bf16 v[44:47], v[150:153], v[204:207], v[44:47]
	v_mfma_f32_16x16x32_bf16 v[40:43], v[158:161], v[204:207], v[40:43]
	v_mfma_f32_16x16x32_bf16 v[28:31], v[150:153], v[212:215], v[28:31]
	v_mfma_f32_16x16x32_bf16 v[24:27], v[158:161], v[212:215], v[24:27]
	v_mfma_f32_16x16x32_bf16 v[12:15], v[150:153], v[220:223], v[12:15]
	v_mfma_f32_16x16x32_bf16 v[8:11], v[158:161], v[220:223], v[8:11]
	s_setprio 0
	s_setprio 1
	v_mfma_f32_16x16x32_bf16 v[52:55], v[162:165], v[192:195], v[52:55]
	v_mfma_f32_16x16x32_bf16 v[48:51], v[184:187], v[192:195], v[48:51]
	v_mfma_f32_16x16x32_bf16 v[36:39], v[162:165], v[200:203], v[36:39]
	v_mfma_f32_16x16x32_bf16 v[32:35], v[184:187], v[200:203], v[32:35]
	v_mfma_f32_16x16x32_bf16 v[20:23], v[162:165], v[208:211], v[20:23]
	v_mfma_f32_16x16x32_bf16 v[16:19], v[184:187], v[208:211], v[16:19]
	v_mfma_f32_16x16x32_bf16 v[4:7], v[162:165], v[216:219], v[4:7]
	v_mfma_f32_16x16x32_bf16 v[0:3], v[184:187], v[216:219], v[0:3]
	v_mfma_f32_16x16x32_bf16 v[52:55], v[166:169], v[196:199], v[52:55]
	v_mfma_f32_16x16x32_bf16 v[48:51], v[188:191], v[196:199], v[48:51]
	v_mfma_f32_16x16x32_bf16 v[36:39], v[166:169], v[204:207], v[36:39]
	v_mfma_f32_16x16x32_bf16 v[32:35], v[188:191], v[204:207], v[32:35]
	v_mfma_f32_16x16x32_bf16 v[20:23], v[166:169], v[212:215], v[20:23]
	v_mfma_f32_16x16x32_bf16 v[16:19], v[188:191], v[212:215], v[16:19]
	v_mfma_f32_16x16x32_bf16 v[4:7], v[166:169], v[220:223], v[4:7]
	v_mfma_f32_16x16x32_bf16 v[0:3], v[188:191], v[220:223], v[0:3]
	s_setprio 0
	s_barrier
	s_add_i32 s71, s71, 2
	s_add_u32 s8, s8, 0x100
	s_addc_u32 s9, s9, 0
	s_add_u32 s40, s40, 0x100
	s_addc_u32 s41, s41, 0
	s_cmp_gt_u32 s71, 13
.LBB0_2049:
	s_add_u32 s12, s8, 0xfffc0080
	s_addc_u32 s13, s9, -1
	s_cmp_eq_u32 s71, 12
	s_cselect_b32 s39, s7, s13
	s_cselect_b32 s38, s11, s12
	s_cselect_b32 s13, s29, s41
	s_cselect_b32 s12, s31, s40
	s_add_i32 m0, s46, 0xc000
	s_nop 0
	global_load_lds_dwordx4 v138, s[8:9]
	s_add_i32 m0, s46, 0xe000
	s_nop 0
	global_load_lds_dwordx4 v140, s[8:9]
	ds_read_b128 v[146:149], v179
	ds_read_b128 v[150:153], v179 offset:1024
	ds_read_b128 v[154:157], v179 offset:2048
	ds_read_b128 v[158:161], v179 offset:3072
	ds_read_b128 v[162:165], v180
	ds_read_b128 v[166:169], v180 offset:1024
	ds_read_b128 v[184:187], v180 offset:2048
	ds_read_b128 v[188:191], v180 offset:3072
	ds_read_b128 v[192:195], v181
	ds_read_b128 v[196:199], v181 offset:1024
	ds_read_b128 v[200:203], v181 offset:2048
	ds_read_b128 v[204:207], v181 offset:3072
	ds_read_b128 v[208:211], v181 offset:4096
	ds_read_b128 v[212:215], v181 offset:5120
	ds_read_b128 v[216:219], v181 offset:6144
	ds_read_b128 v[220:223], v181 offset:7168
	s_waitcnt vmcnt(8) lgkmcnt(0)
	s_barrier
	s_setprio 1
	v_mfma_f32_16x16x32_bf16 v[124:127], v[146:149], v[192:195], v[124:127]
	v_mfma_f32_16x16x32_bf16 v[120:123], v[154:157], v[192:195], v[120:123]
	v_mfma_f32_16x16x32_bf16 v[108:111], v[146:149], v[200:203], v[108:111]
	v_mfma_f32_16x16x32_bf16 v[104:107], v[154:157], v[200:203], v[104:107]
	v_mfma_f32_16x16x32_bf16 v[92:95], v[146:149], v[208:211], v[92:95]
	v_mfma_f32_16x16x32_bf16 v[88:91], v[154:157], v[208:211], v[88:91]
	v_mfma_f32_16x16x32_bf16 v[76:79], v[146:149], v[216:219], v[76:79]
	v_mfma_f32_16x16x32_bf16 v[72:75], v[154:157], v[216:219], v[72:75]
	v_mfma_f32_16x16x32_bf16 v[124:127], v[150:153], v[196:199], v[124:127]
	v_mfma_f32_16x16x32_bf16 v[120:123], v[158:161], v[196:199], v[120:123]
	v_mfma_f32_16x16x32_bf16 v[108:111], v[150:153], v[204:207], v[108:111]
	v_mfma_f32_16x16x32_bf16 v[104:107], v[158:161], v[204:207], v[104:107]
	v_mfma_f32_16x16x32_bf16 v[92:95], v[150:153], v[212:215], v[92:95]
	v_mfma_f32_16x16x32_bf16 v[88:91], v[158:161], v[212:215], v[88:91]
	v_mfma_f32_16x16x32_bf16 v[76:79], v[150:153], v[220:223], v[76:79]
	v_mfma_f32_16x16x32_bf16 v[72:75], v[158:161], v[220:223], v[72:75]
	s_setprio 0
	s_setprio 1
	v_mfma_f32_16x16x32_bf16 v[116:119], v[162:165], v[192:195], v[116:119]
	v_mfma_f32_16x16x32_bf16 v[112:115], v[184:187], v[192:195], v[112:115]
	v_mfma_f32_16x16x32_bf16 v[100:103], v[162:165], v[200:203], v[100:103]
	v_mfma_f32_16x16x32_bf16 v[96:99], v[184:187], v[200:203], v[96:99]
	v_mfma_f32_16x16x32_bf16 v[84:87], v[162:165], v[208:211], v[84:87]
	v_mfma_f32_16x16x32_bf16 v[80:83], v[184:187], v[208:211], v[80:83]
	v_mfma_f32_16x16x32_bf16 v[68:71], v[162:165], v[216:219], v[68:71]
	v_mfma_f32_16x16x32_bf16 v[64:67], v[184:187], v[216:219], v[64:67]
	v_mfma_f32_16x16x32_bf16 v[116:119], v[166:169], v[196:199], v[116:119]
	v_mfma_f32_16x16x32_bf16 v[112:115], v[188:191], v[196:199], v[112:115]
	v_mfma_f32_16x16x32_bf16 v[100:103], v[166:169], v[204:207], v[100:103]
	v_mfma_f32_16x16x32_bf16 v[96:99], v[188:191], v[204:207], v[96:99]
	v_mfma_f32_16x16x32_bf16 v[84:87], v[166:169], v[212:215], v[84:87]
	v_mfma_f32_16x16x32_bf16 v[80:83], v[188:191], v[212:215], v[80:83]
	v_mfma_f32_16x16x32_bf16 v[68:71], v[166:169], v[220:223], v[68:71]
	v_mfma_f32_16x16x32_bf16 v[64:67], v[188:191], v[220:223], v[64:67]
	s_setprio 0
	s_barrier
; #define PG8_STAGE(bufoff, gbase, voff) do { _Pragma("unroll") for (int _i = 0; _i < 2; ++_i) \
;         __builtin_amdgcn_global_load_lds((const unsigned*)((const char*)(gbase) + (voff)[_i]), (PG8_LAS unsigned*)(lds + (bufoff) + ldsw + _i * 8192), 16, 0, 0); } while (0)
; #define PG8_LDA(dst, b, h) do { _Pragma("unroll") for (int m = 0; m < 4; ++m) _Pragma("unroll") for (int k = 0; k < 2; ++k) dst[m][k] = *(const PG8_LAS bf16x8*)(lds + PG8_SA(b, h) + aoff + m * 2048 + k * 1024); } while (0)
; #define PG8_LDB(dst, b, h) do { _Pragma("unroll") for (int n = 0; n < 2; ++n) _Pragma("unroll") for (int k = 0; k < 2; ++k) dst[n][k] = *(const PG8_LAS bf16x8*)(lds + PG8_SB(b, h) + boff + n * 2048 + k * 1024); } while (0)
; #define PG8_MMA(ai, bj, At, Bt) do { __builtin_amdgcn_s_setprio(1); _Pragma("unroll") for (int m = 0; m < 4; ++m) _Pragma("unroll") for (int n = 0; n < 2; ++n) _Pragma("unroll") for (int k = 0; k < 2; ++k) \
;         acc[ai][bj][m][n] = __builtin_amdgcn_mfma_f32_16x16x32_bf16(Bt[n][k], At[m][k], acc[ai][bj][m][n], 0, 0, 0); __builtin_amdgcn_s_setprio(0); } while (0)
; template <class Epi, class Sched, bool ALIGN_EPI = false, bool SP2 = false>
; __device__ __forceinline__ void gemm_phase(PG8_LAS unsigned char* lds, const Gemm g, const Sched& S, const Epi& E, const int wid) {
;     ...
;             if constexpr (SP2) {
;             PG8_LDB(B0, 0, 0); PG8_LDB(B1, 0, 1); PG8_SCHED; PG8_LDA(At, 0, 0); PG8_STAGE(PG8_SA(1, 1), a1 + hstepA, voffA);
;             PG8_WAIT_V(8); PG8_WAIT_L(0); PG8_BAR; PG8_MMA(0, 0, At, B0); PG8_MMA(0, 1, At, B1); PG8_BAR; PG8_SCHED;
;             PG8_LDA(At, 0, 1); PG8_STAGE(PG8_SB(0, 0), b2, voffB); PG8_STAGE(PG8_SB(0, 1), b2 + hstepB, voffB); PG8_STAGE(PG8_SA(0, 0), a2, voffA);
;             PG8_WAIT_V(8); PG8_WAIT_L(0); PG8_BAR; PG8_MMA(1, 0, At, B0); PG8_MMA(1, 1, At, B1); PG8_BAR; PG8_SCHED;
;             PG8_LDB(B0, 1, 0); PG8_LDB(B1, 1, 1); PG8_SCHED; PG8_LDA(At, 1, 0); PG8_STAGE(PG8_SA(0, 1), a2 + hstepA, voffA);
;             PG8_WAIT_V(8); PG8_WAIT_L(0); PG8_BAR; PG8_MMA(0, 0, At, B0); PG8_MMA(0, 1, At, B1); PG8_BAR; PG8_SCHED;
;             PG8_LDA(At, 1, 1); PG8_STAGE(PG8_SB(1, 0), b3, voffB); PG8_STAGE(PG8_SB(1, 1), b3 + hstepB, voffB); PG8_STAGE(PG8_SA(1, 0), a3, voffA);
;             PG8_WAIT_V(8); PG8_WAIT_L(0); PG8_BAR; PG8_MMA(1, 0, At, B0); PG8_MMA(1, 1, At, B1); PG8_BAR; PG8_SCHED;
	s_add_i32 s72, s69, s45
	s_add_u32 s98, s12, 0x80
	s_addc_u32 s99, s13, 0
	s_mov_b32 m0, s72
	s_nop 0
	global_load_lds_dwordx4 v130, s[12:13]
	s_add_i32 m0, s72, 0x2000
	s_add_u32 s72, s12, 0x40000
	s_addc_u32 s73, s13, 0
	s_add_i32 s74, s70, s45
	global_load_lds_dwordx4 v134, s[12:13]
	s_mov_b32 m0, s74
	s_add_u32 s100, s38, 0x80
	s_addc_u32 s101, s39, 0
	global_load_lds_dwordx4 v130, s[72:73]
	s_add_i32 m0, s74, 0x2000
	s_nop 0
	global_load_lds_dwordx4 v134, s[72:73]
	s_mov_b32 m0, s46
	s_nop 0
	global_load_lds_dwordx4 v128, s[38:39]
	s_mov_b32 m0, s47
	s_nop 0
	global_load_lds_dwordx4 v132, s[38:39]
	ds_read_b128 v[192:195], v181 offset:16384
	ds_read_b128 v[196:199], v181 offset:17408
	ds_read_b128 v[200:203], v181 offset:18432
	ds_read_b128 v[204:207], v181 offset:19456
	ds_read_b128 v[208:211], v181 offset:20480
	ds_read_b128 v[212:215], v181 offset:21504
	ds_read_b128 v[216:219], v181 offset:22528
	ds_read_b128 v[220:223], v181 offset:23552
	s_waitcnt vmcnt(8) lgkmcnt(0)
	s_barrier
	s_setprio 1
	v_mfma_f32_16x16x32_bf16 v[60:63], v[146:149], v[192:195], v[60:63]
	v_mfma_f32_16x16x32_bf16 v[56:59], v[154:157], v[192:195], v[56:59]
	v_mfma_f32_16x16x32_bf16 v[44:47], v[146:149], v[200:203], v[44:47]
	v_mfma_f32_16x16x32_bf16 v[40:43], v[154:157], v[200:203], v[40:43]
	v_mfma_f32_16x16x32_bf16 v[28:31], v[146:149], v[208:211], v[28:31]
	v_mfma_f32_16x16x32_bf16 v[24:27], v[154:157], v[208:211], v[24:27]
	v_mfma_f32_16x16x32_bf16 v[12:15], v[146:149], v[216:219], v[12:15]
	v_mfma_f32_16x16x32_bf16 v[8:11], v[154:157], v[216:219], v[8:11]
	v_mfma_f32_16x16x32_bf16 v[60:63], v[150:153], v[196:199], v[60:63]
	v_mfma_f32_16x16x32_bf16 v[56:59], v[158:161], v[196:199], v[56:59]
	v_mfma_f32_16x16x32_bf16 v[44:47], v[150:153], v[204:207], v[44:47]
	v_mfma_f32_16x16x32_bf16 v[40:43], v[158:161], v[204:207], v[40:43]
	v_mfma_f32_16x16x32_bf16 v[28:31], v[150:153], v[212:215], v[28:31]
	v_mfma_f32_16x16x32_bf16 v[24:27], v[158:161], v[212:215], v[24:27]
	v_mfma_f32_16x16x32_bf16 v[12:15], v[150:153], v[220:223], v[12:15]
	v_mfma_f32_16x16x32_bf16 v[8:11], v[158:161], v[220:223], v[8:11]
	s_setprio 0
	s_setprio 1
	v_mfma_f32_16x16x32_bf16 v[52:55], v[162:165], v[192:195], v[52:55]
	v_mfma_f32_16x16x32_bf16 v[48:51], v[184:187], v[192:195], v[48:51]
	v_mfma_f32_16x16x32_bf16 v[36:39], v[162:165], v[200:203], v[36:39]
	v_mfma_f32_16x16x32_bf16 v[32:35], v[184:187], v[200:203], v[32:35]
	v_mfma_f32_16x16x32_bf16 v[20:23], v[162:165], v[208:211], v[20:23]
	v_mfma_f32_16x16x32_bf16 v[16:19], v[184:187], v[208:211], v[16:19]
	v_mfma_f32_16x16x32_bf16 v[4:7], v[162:165], v[216:219], v[4:7]
	v_mfma_f32_16x16x32_bf16 v[0:3], v[184:187], v[216:219], v[0:3]
	v_mfma_f32_16x16x32_bf16 v[52:55], v[166:169], v[196:199], v[52:55]
	v_mfma_f32_16x16x32_bf16 v[48:51], v[188:191], v[196:199], v[48:51]
	v_mfma_f32_16x16x32_bf16 v[36:39], v[166:169], v[204:207], v[36:39]
	v_mfma_f32_16x16x32_bf16 v[32:35], v[188:191], v[204:207], v[32:35]
	v_mfma_f32_16x16x32_bf16 v[20:23], v[166:169], v[212:215], v[20:23]
	v_mfma_f32_16x16x32_bf16 v[16:19], v[188:191], v[212:215], v[16:19]
	v_mfma_f32_16x16x32_bf16 v[4:7], v[166:169], v[220:223], v[4:7]
	v_mfma_f32_16x16x32_bf16 v[0:3], v[188:191], v[220:223], v[0:3]
	s_setprio 0
	s_barrier
	s_add_i32 s72, 0, 0x18000
	s_add_i32 s73, 0, 0x1c000
	s_add_u32 s38, s38, 0x40000
	s_addc_u32 s39, s39, 0
	s_mov_b32 m0, s48
	s_nop 0
	global_load_lds_dwordx4 v128, s[38:39]
	s_mov_b32 m0, s49
	s_nop 0
	global_load_lds_dwordx4 v132, s[38:39]
	ds_read_b128 v[146:149], v252
	ds_read_b128 v[150:153], v252 offset:1024
	ds_read_b128 v[154:157], v252 offset:2048
	ds_read_b128 v[158:161], v252 offset:3072
	ds_read_b128 v[162:165], v253
	ds_read_b128 v[166:169], v253 offset:1024
	ds_read_b128 v[184:187], v253 offset:2048
	ds_read_b128 v[188:191], v253 offset:3072
	ds_read_b128 v[192:195], v181 offset:32768
	ds_read_b128 v[196:199], v181 offset:33792
	ds_read_b128 v[200:203], v181 offset:34816
	ds_read_b128 v[204:207], v181 offset:35840
	ds_read_b128 v[208:211], v181 offset:36864
	ds_read_b128 v[212:215], v181 offset:37888
	ds_read_b128 v[216:219], v181 offset:38912
	ds_read_b128 v[220:223], v181 offset:39936
	s_waitcnt vmcnt(8) lgkmcnt(0)
	s_barrier
; #define PG8_STAGE(bufoff, gbase, voff) do { _Pragma("unroll") for (int _i = 0; _i < 2; ++_i) \
;         __builtin_amdgcn_global_load_lds((const unsigned*)((const char*)(gbase) + (voff)[_i]), (PG8_LAS unsigned*)(lds + (bufoff) + ldsw + _i * 8192), 16, 0, 0); } while (0)
; #define PG8_LDA(dst, b, h) do { _Pragma("unroll") for (int m = 0; m < 4; ++m) _Pragma("unroll") for (int k = 0; k < 2; ++k) dst[m][k] = *(const PG8_LAS bf16x8*)(lds + PG8_SA(b, h) + aoff + m * 2048 + k * 1024); } while (0)
; #define PG8_LDB(dst, b, h) do { _Pragma("unroll") for (int n = 0; n < 2; ++n) _Pragma("unroll") for (int k = 0; k < 2; ++k) dst[n][k] = *(const PG8_LAS bf16x8*)(lds + PG8_SB(b, h) + boff + n * 2048 + k * 1024); } while (0)
; #define PG8_WAIT_V(n) asm volatile("s_waitcnt vmcnt(" #n ")" ::: "memory")
; #define PG8_WAIT_L(n) asm volatile("s_waitcnt lgkmcnt(" #n ")" ::: "memory")
; #define PG8_BAR __builtin_amdgcn_s_barrier()
; template <class Epi, class Sched, bool ALIGN_EPI = false, bool SP2 = false>
; __device__ __forceinline__ void gemm_phase(PG8_LAS unsigned char* lds, const Gemm g, const Sched& S, const Epi& E, const int wid) {
;     ...
;             if constexpr (SP2) {
;             PG8_LDB(B0, 0, 0); PG8_LDB(B1, 0, 1); PG8_SCHED; PG8_LDA(At, 0, 0); PG8_STAGE(PG8_SA(1, 1), a1 + hstepA, voffA);
;             PG8_WAIT_V(8); PG8_WAIT_L(0); PG8_BAR; PG8_MMA(0, 0, At, B0); PG8_MMA(0, 1, At, B1); PG8_BAR; PG8_SCHED;
;             PG8_LDA(At, 0, 1); PG8_STAGE(PG8_SB(0, 0), b2, voffB); PG8_STAGE(PG8_SB(0, 1), b2 + hstepB, voffB); PG8_STAGE(PG8_SA(0, 0), a2, voffA);
;             PG8_WAIT_V(8); PG8_WAIT_L(0); PG8_BAR; PG8_MMA(1, 0, At, B0); PG8_MMA(1, 1, At, B1); PG8_BAR; PG8_SCHED;
;             PG8_LDB(B0, 1, 0); PG8_LDB(B1, 1, 1); PG8_SCHED; PG8_LDA(At, 1, 0); PG8_STAGE(PG8_SA(0, 1), a2 + hstepA, voffA);
;             PG8_WAIT_V(8); PG8_WAIT_L(0); PG8_BAR; PG8_MMA(0, 0, At, B0); PG8_MMA(0, 1, At, B1); PG8_BAR; PG8_SCHED;
;             PG8_LDA(At, 1, 1); PG8_STAGE(PG8_SB(1, 0), b3, voffB); PG8_STAGE(PG8_SB(1, 1), b3 + hstepB, voffB); PG8_STAGE(PG8_SA(1, 0), a3, voffA);
;             PG8_WAIT_V(8); PG8_WAIT_L(0); PG8_BAR; PG8_MMA(1, 0, At, B0); PG8_MMA(1, 1, At, B1); PG8_BAR; PG8_SCHED;
;     ...
;         if constexpr (ALIGN_EPI) { if (wr == 0) PG8_BAR; }
;         if constexpr (!Epi::AFTER_DRAIN) { E(acc, cur, wr, wc, fr, fq); S.done(cur); }
;         if (!has_next) break;
	s_setprio 1
	v_mfma_f32_16x16x32_bf16 v[124:127], v[146:149], v[192:195], v[124:127]
	v_mfma_f32_16x16x32_bf16 v[120:123], v[154:157], v[192:195], v[120:123]
	v_mfma_f32_16x16x32_bf16 v[108:111], v[146:149], v[200:203], v[108:111]
	v_mfma_f32_16x16x32_bf16 v[104:107], v[154:157], v[200:203], v[104:107]
	v_mfma_f32_16x16x32_bf16 v[92:95], v[146:149], v[208:211], v[92:95]
	v_mfma_f32_16x16x32_bf16 v[88:91], v[154:157], v[208:211], v[88:91]
	v_mfma_f32_16x16x32_bf16 v[76:79], v[146:149], v[216:219], v[76:79]
	v_mfma_f32_16x16x32_bf16 v[72:75], v[154:157], v[216:219], v[72:75]
	v_mfma_f32_16x16x32_bf16 v[124:127], v[150:153], v[196:199], v[124:127]
	v_mfma_f32_16x16x32_bf16 v[120:123], v[158:161], v[196:199], v[120:123]
	v_mfma_f32_16x16x32_bf16 v[108:111], v[150:153], v[204:207], v[108:111]
	v_mfma_f32_16x16x32_bf16 v[104:107], v[158:161], v[204:207], v[104:107]
	v_mfma_f32_16x16x32_bf16 v[92:95], v[150:153], v[212:215], v[92:95]
	v_mfma_f32_16x16x32_bf16 v[88:91], v[158:161], v[212:215], v[88:91]
	v_mfma_f32_16x16x32_bf16 v[76:79], v[150:153], v[220:223], v[76:79]
	v_mfma_f32_16x16x32_bf16 v[72:75], v[158:161], v[220:223], v[72:75]
	s_setprio 0
	s_setprio 1
	v_mfma_f32_16x16x32_bf16 v[116:119], v[162:165], v[192:195], v[116:119]
	v_mfma_f32_16x16x32_bf16 v[112:115], v[184:187], v[192:195], v[112:115]
	v_mfma_f32_16x16x32_bf16 v[100:103], v[162:165], v[200:203], v[100:103]
	v_mfma_f32_16x16x32_bf16 v[96:99], v[184:187], v[200:203], v[96:99]
	v_mfma_f32_16x16x32_bf16 v[84:87], v[162:165], v[208:211], v[84:87]
	v_mfma_f32_16x16x32_bf16 v[80:83], v[184:187], v[208:211], v[80:83]
	v_mfma_f32_16x16x32_bf16 v[68:71], v[162:165], v[216:219], v[68:71]
	v_mfma_f32_16x16x32_bf16 v[64:67], v[184:187], v[216:219], v[64:67]
	v_mfma_f32_16x16x32_bf16 v[116:119], v[166:169], v[196:199], v[116:119]
	v_mfma_f32_16x16x32_bf16 v[112:115], v[188:191], v[196:199], v[112:115]
	v_mfma_f32_16x16x32_bf16 v[100:103], v[166:169], v[204:207], v[100:103]
	v_mfma_f32_16x16x32_bf16 v[96:99], v[188:191], v[204:207], v[96:99]
	v_mfma_f32_16x16x32_bf16 v[84:87], v[166:169], v[212:215], v[84:87]
	v_mfma_f32_16x16x32_bf16 v[80:83], v[188:191], v[212:215], v[80:83]
	v_mfma_f32_16x16x32_bf16 v[68:71], v[166:169], v[220:223], v[68:71]
	v_mfma_f32_16x16x32_bf16 v[64:67], v[188:191], v[220:223], v[64:67]
	s_setprio 0
	s_barrier
	s_add_i32 s38, s72, s45
	s_mov_b32 m0, s38
	s_nop 0
	global_load_lds_dwordx4 v130, s[98:99]
	s_add_i32 m0, s38, 0x2000
	s_add_u32 s12, s12, 0x40080
	s_addc_u32 s13, s13, 0
	s_add_i32 s38, s73, s45
	global_load_lds_dwordx4 v134, s[98:99]
	s_mov_b32 m0, s38
	s_nop 0
	global_load_lds_dwordx4 v130, s[12:13]
	s_add_i32 m0, s38, 0x2000
	s_nop 0
	global_load_lds_dwordx4 v134, s[12:13]
	s_mov_b32 m0, s65
	s_nop 0
	global_load_lds_dwordx4 v128, s[100:101]
	s_mov_b32 m0, s66
	s_nop 0
	global_load_lds_dwordx4 v132, s[100:101]
	ds_read_b128 v[192:195], v181 offset:49152
	ds_read_b128 v[196:199], v181 offset:50176
	ds_read_b128 v[200:203], v181 offset:51200
	ds_read_b128 v[204:207], v181 offset:52224
	ds_read_b128 v[208:211], v181 offset:53248
	ds_read_b128 v[212:215], v181 offset:54272
	ds_read_b128 v[216:219], v181 offset:55296
	ds_read_b128 v[220:223], v181 offset:56320
	s_waitcnt vmcnt(8) lgkmcnt(0)
	s_barrier
	s_setprio 1
	v_mfma_f32_16x16x32_bf16 v[60:63], v[146:149], v[192:195], v[60:63]
	v_mfma_f32_16x16x32_bf16 v[56:59], v[154:157], v[192:195], v[56:59]
	v_mfma_f32_16x16x32_bf16 v[44:47], v[146:149], v[200:203], v[44:47]
	v_mfma_f32_16x16x32_bf16 v[40:43], v[154:157], v[200:203], v[40:43]
	v_mfma_f32_16x16x32_bf16 v[28:31], v[146:149], v[208:211], v[28:31]
	v_mfma_f32_16x16x32_bf16 v[24:27], v[154:157], v[208:211], v[24:27]
	v_mfma_f32_16x16x32_bf16 v[12:15], v[146:149], v[216:219], v[12:15]
	v_mfma_f32_16x16x32_bf16 v[8:11], v[154:157], v[216:219], v[8:11]
	v_mfma_f32_16x16x32_bf16 v[60:63], v[150:153], v[196:199], v[60:63]
	v_mfma_f32_16x16x32_bf16 v[56:59], v[158:161], v[196:199], v[56:59]
	v_mfma_f32_16x16x32_bf16 v[44:47], v[150:153], v[204:207], v[44:47]
	v_mfma_f32_16x16x32_bf16 v[40:43], v[158:161], v[204:207], v[40:43]
	v_mfma_f32_16x16x32_bf16 v[28:31], v[150:153], v[212:215], v[28:31]
	v_mfma_f32_16x16x32_bf16 v[24:27], v[158:161], v[212:215], v[24:27]
	v_mfma_f32_16x16x32_bf16 v[12:15], v[150:153], v[220:223], v[12:15]
	v_mfma_f32_16x16x32_bf16 v[8:11], v[158:161], v[220:223], v[8:11]
	s_setprio 0
	s_setprio 1
	v_mfma_f32_16x16x32_bf16 v[52:55], v[162:165], v[192:195], v[52:55]
	v_mfma_f32_16x16x32_bf16 v[48:51], v[184:187], v[192:195], v[48:51]
	v_mfma_f32_16x16x32_bf16 v[36:39], v[162:165], v[200:203], v[36:39]
	v_mfma_f32_16x16x32_bf16 v[32:35], v[184:187], v[200:203], v[32:35]
	v_mfma_f32_16x16x32_bf16 v[20:23], v[162:165], v[208:211], v[20:23]
	v_mfma_f32_16x16x32_bf16 v[16:19], v[184:187], v[208:211], v[16:19]
	v_mfma_f32_16x16x32_bf16 v[4:7], v[162:165], v[216:219], v[4:7]
	v_mfma_f32_16x16x32_bf16 v[0:3], v[184:187], v[216:219], v[0:3]
	v_mfma_f32_16x16x32_bf16 v[52:55], v[166:169], v[196:199], v[52:55]
	v_mfma_f32_16x16x32_bf16 v[48:51], v[188:191], v[196:199], v[48:51]
	v_mfma_f32_16x16x32_bf16 v[36:39], v[166:169], v[204:207], v[36:39]
	v_mfma_f32_16x16x32_bf16 v[32:35], v[188:191], v[204:207], v[32:35]
	v_mfma_f32_16x16x32_bf16 v[20:23], v[166:169], v[212:215], v[20:23]
	v_mfma_f32_16x16x32_bf16 v[16:19], v[188:191], v[212:215], v[16:19]
	v_mfma_f32_16x16x32_bf16 v[4:7], v[166:169], v[220:223], v[4:7]
	v_mfma_f32_16x16x32_bf16 v[0:3], v[188:191], v[220:223], v[0:3]
	s_setprio 0
	s_barrier
	s_add_i32 s71, s71, 2
	s_add_u32 s8, s8, 0x100
	s_addc_u32 s9, s9, 0
	s_add_u32 s40, s40, 0x100
	s_addc_u32 s41, s41, 0
	s_cmp_gt_u32 s71, 13
	s_cbranch_scc0 .LBB0_2049
	s_and_b64 vcc, exec, s[20:21]
	s_cbranch_vccz .LBB0_2052
	s_barrier

; #define PG8_STAGE(bufoff, gbase, voff) do { _Pragma("unroll") for (int _i = 0; _i < 2; ++_i) \
;         __builtin_amdgcn_global_load_lds((const unsigned*)((const char*)(gbase) + (voff)[_i]), (PG8_LAS unsigned*)(lds + (bufoff) + ldsw + _i * 8192), 16, 0, 0); } while (0)
; #define PG8_WAIT_V(n) asm volatile("s_waitcnt vmcnt(" #n ")" ::: "memory")
; #define PG8_WAIT_L(n) asm volatile("s_waitcnt lgkmcnt(" #n ")" ::: "memory")
; #define PG8_BAR __builtin_amdgcn_s_barrier()
; template <class Epi, class Sched, bool ALIGN_EPI = false, bool SP2 = false>
; __device__ __forceinline__ void gemm_phase(PG8_LAS unsigned char* lds, const Gemm g, const Sched& S, const Epi& E, const int wid) {
;     ...
;         const bool has_next = S.next(ui + 1, nxt);
;         const char* nA = has_next ? (const char*)g.A + (size_t)nxt.pm * tstepA : cA; const char* nB = has_next ? (const char*)g.Bt + (size_t)nxt.pn * tstepB : cB;
;         for (int t = 0; t < nt; t += 2) {
;             const bool last = (t == nt - 2);
;             const char* a1 = cA + (size_t)(t + 1) * kstep;
;             const char* a2 = last ? nA : cA + (size_t)(t + 2) * kstep; const char* b2 = last ? nB : cB + (size_t)(t + 2) * kstep;
;             const char* a3 = a2 + kstep; const char* b3 = b2 + kstep;
;             if (last && has_next) S.a_ready(nxt);
;             if constexpr (SP2) {
;             PG8_LDB(B0, 0, 0); PG8_LDB(B1, 0, 1); PG8_SCHED; PG8_LDA(At, 0, 0); PG8_STAGE(PG8_SA(1, 1), a1 + hstepA, voffA);
;             PG8_WAIT_V(8); PG8_WAIT_L(0); PG8_BAR; PG8_MMA(0, 0, At, B0); PG8_MMA(0, 1, At, B1); PG8_BAR; PG8_SCHED;
;             PG8_LDA(At, 0, 1); PG8_STAGE(PG8_SB(0, 0), b2, voffB); PG8_STAGE(PG8_SB(0, 1), b2 + hstepB, voffB); PG8_STAGE(PG8_SA(0, 0), a2, voffA);
;             PG8_WAIT_V(8); PG8_WAIT_L(0); PG8_BAR; PG8_MMA(1, 0, At, B0); PG8_MMA(1, 1, At, B1); PG8_BAR; PG8_SCHED;
;             PG8_LDB(B0, 1, 0); PG8_LDB(B1, 1, 1); PG8_SCHED; PG8_LDA(At, 1, 0); PG8_STAGE(PG8_SA(0, 1), a2 + hstepA, voffA);
;             PG8_WAIT_V(8); PG8_WAIT_L(0); PG8_BAR; PG8_MMA(0, 0, At, B0); PG8_MMA(0, 1, At, B1); PG8_BAR; PG8_SCHED;
;             PG8_LDA(At, 1, 1); PG8_STAGE(PG8_SB(1, 0), b3, voffB); PG8_STAGE(PG8_SB(1, 1), b3 + hstepB, voffB); PG8_STAGE(PG8_SA(1, 0), a3, voffA);
;             PG8_WAIT_V(8); PG8_WAIT_L(0); PG8_BAR; PG8_MMA(1, 0, At, B0); PG8_MMA(1, 1, At, B1); PG8_BAR; PG8_SCHED;
.LBB0_2279:
	s_ashr_i32 s19, s18, 31
	s_lshl_b64 s[20:21], s[18:19], 20
	s_add_u32 s20, s65, s20
	s_addc_u32 s21, s66, s21
	s_and_b64 s[22:23], s[2:3], exec
	s_cselect_b32 s19, s21, s29
	s_cselect_b32 s81, s20, s28
	s_ashr_i32 s17, s16, 31
	s_lshl_b64 s[22:23], s[16:17], 17
	s_add_u32 s22, s67, s22
	s_addc_u32 s23, s68, s23
	s_and_b64 s[30:31], s[2:3], exec
	s_cselect_b32 s17, s23, s27
	s_cselect_b32 s82, s22, s26
	s_mov_b32 s36, 0
	s_mov_b64 s[30:31], -1
	s_mov_b64 s[34:35], 0
	v_add_u32_e32 v252, 0x18000, v156
	v_add_u32_e32 v253, 0x1c000, v156
	s_add_u32 s37, s28, s36
	s_addc_u32 s44, s29, 0
	s_add_u32 s40, s37, 0x100
	s_addc_u32 s41, s44, 0
	s_and_b64 s[38:39], s[34:35], exec
	s_cselect_b32 s39, s19, s41
	s_cselect_b32 s38, s81, s40
	s_add_u32 s36, s26, s36
	s_addc_u32 s40, s27, 0
	s_add_u32 s36, s36, 0x100
	s_addc_u32 s40, s40, 0
	s_and_b64 s[34:35], s[34:35], exec
	s_cselect_b32 s41, s17, s40
	s_cselect_b32 s40, s82, s36
	s_add_u32 s46, s37, 0x80080
	s_addc_u32 s47, s44, 0
	s_add_i32 s93, s77, s0
	s_add_i32 m0, s70, 0xc000
	s_add_i32 s94, s70, 0xe000
	s_add_i32 s89, s93, 0x2000
	s_add_u32 s44, s40, 0x10000
	s_addc_u32 s45, s41, 0
	s_add_i32 s92, s78, s0
	s_add_i32 s91, s92, 0x2000
	s_add_i32 s88, 0, 0x18000
	s_add_i32 s87, 0, 0x1c000
	s_add_u32 s36, s38, 0x80000
	s_addc_u32 s37, s39, 0
	s_add_i32 s86, s88, s0
	s_add_i32 s84, s86, 0x2000
	s_add_u32 s34, s40, 0x10080
	s_addc_u32 s35, s41, 0
	s_add_i32 s85, s87, s0
	s_add_i32 s83, s85, 0x2000
	global_load_lds_dwordx4 v134, s[46:47]
	s_mov_b32 m0, s94
	s_nop 0
	global_load_lds_dwordx4 v130, s[46:47]
	ds_read_b128 v[142:145], v157
	ds_read_b128 v[146:149], v157 offset:1024
	ds_read_b128 v[150:153], v157 offset:2048
	ds_read_b128 v[162:165], v157 offset:3072
	ds_read_b128 v[166:169], v158
	ds_read_b128 v[170:173], v158 offset:1024
	ds_read_b128 v[174:177], v158 offset:2048
	ds_read_b128 v[178:181], v158 offset:3072
	ds_read_b128 v[182:185], v159
	ds_read_b128 v[186:189], v159 offset:1024
	ds_read_b128 v[190:193], v159 offset:2048
	ds_read_b128 v[194:197], v159 offset:3072
	ds_read_b128 v[198:201], v159 offset:4096
	ds_read_b128 v[202:205], v159 offset:5120
	ds_read_b128 v[206:209], v159 offset:6144
	ds_read_b128 v[210:213], v159 offset:7168
	s_waitcnt vmcnt(8) lgkmcnt(0)
	s_barrier
	s_setprio 1
	v_mfma_f32_16x16x32_bf16 v[124:127], v[142:145], v[182:185], 0
	v_mfma_f32_16x16x32_bf16 v[120:123], v[150:153], v[182:185], 0
	v_mfma_f32_16x16x32_bf16 v[116:119], v[142:145], v[190:193], 0
	v_mfma_f32_16x16x32_bf16 v[112:115], v[150:153], v[190:193], 0
	v_mfma_f32_16x16x32_bf16 v[100:103], v[142:145], v[198:201], 0
	v_mfma_f32_16x16x32_bf16 v[96:99], v[150:153], v[198:201], 0
	v_mfma_f32_16x16x32_bf16 v[84:87], v[142:145], v[206:209], 0
	v_mfma_f32_16x16x32_bf16 v[80:83], v[150:153], v[206:209], 0
	v_mfma_f32_16x16x32_bf16 v[124:127], v[146:149], v[186:189], v[124:127]
	v_mfma_f32_16x16x32_bf16 v[120:123], v[162:165], v[186:189], v[120:123]
	v_mfma_f32_16x16x32_bf16 v[116:119], v[146:149], v[194:197], v[116:119]
	v_mfma_f32_16x16x32_bf16 v[112:115], v[162:165], v[194:197], v[112:115]
	v_mfma_f32_16x16x32_bf16 v[100:103], v[146:149], v[202:205], v[100:103]
	v_mfma_f32_16x16x32_bf16 v[96:99], v[162:165], v[202:205], v[96:99]
	v_mfma_f32_16x16x32_bf16 v[84:87], v[146:149], v[210:213], v[84:87]
	v_mfma_f32_16x16x32_bf16 v[80:83], v[162:165], v[210:213], v[80:83]
	s_setprio 0
	s_setprio 1
	v_mfma_f32_16x16x32_bf16 v[108:111], v[166:169], v[182:185], 0
	v_mfma_f32_16x16x32_bf16 v[104:107], v[174:177], v[182:185], 0
	v_mfma_f32_16x16x32_bf16 v[92:95], v[166:169], v[190:193], 0
	v_mfma_f32_16x16x32_bf16 v[88:91], v[174:177], v[190:193], 0
	v_mfma_f32_16x16x32_bf16 v[76:79], v[166:169], v[198:201], 0
	v_mfma_f32_16x16x32_bf16 v[72:75], v[174:177], v[198:201], 0
	v_mfma_f32_16x16x32_bf16 v[68:71], v[166:169], v[206:209], 0
	v_mfma_f32_16x16x32_bf16 v[64:67], v[174:177], v[206:209], 0
	v_mfma_f32_16x16x32_bf16 v[108:111], v[170:173], v[186:189], v[108:111]
	v_mfma_f32_16x16x32_bf16 v[104:107], v[178:181], v[186:189], v[104:107]
	v_mfma_f32_16x16x32_bf16 v[92:95], v[170:173], v[194:197], v[92:95]
	v_mfma_f32_16x16x32_bf16 v[88:91], v[178:181], v[194:197], v[88:91]
	v_mfma_f32_16x16x32_bf16 v[76:79], v[170:173], v[202:205], v[76:79]
	v_mfma_f32_16x16x32_bf16 v[72:75], v[178:181], v[202:205], v[72:75]
	v_mfma_f32_16x16x32_bf16 v[68:71], v[170:173], v[210:213], v[68:71]
	v_mfma_f32_16x16x32_bf16 v[64:67], v[178:181], v[210:213], v[64:67]
	s_setprio 0
	s_barrier
	s_mov_b32 m0, s93
	s_add_u32 s98, s40, 0x80
	s_addc_u32 s99, s41, 0
	global_load_lds_dwordx4 v132, s[40:41]
	s_mov_b32 m0, s89
	s_nop 0
	global_load_lds_dwordx4 v128, s[40:41]
	s_mov_b32 m0, s92
	s_add_u32 s100, s38, 0x80
	s_addc_u32 s101, s39, 0
	global_load_lds_dwordx4 v132, s[44:45]
	s_mov_b32 m0, s91
	s_nop 0
	global_load_lds_dwordx4 v128, s[44:45]
	s_mov_b32 m0, s70
	s_nop 0
	global_load_lds_dwordx4 v134, s[38:39]
	s_mov_b32 m0, s71
	s_nop 0
	global_load_lds_dwordx4 v130, s[38:39]
	ds_read_b128 v[182:185], v159 offset:16384
	ds_read_b128 v[186:189], v159 offset:17408
	ds_read_b128 v[190:193], v159 offset:18432
	ds_read_b128 v[194:197], v159 offset:19456
	ds_read_b128 v[198:201], v159 offset:20480
	ds_read_b128 v[202:205], v159 offset:21504
	ds_read_b128 v[206:209], v159 offset:22528
	ds_read_b128 v[210:213], v159 offset:23552
	s_waitcnt vmcnt(8) lgkmcnt(0)
	s_barrier
; #define PG8_STAGE(bufoff, gbase, voff) do { _Pragma("unroll") for (int _i = 0; _i < 2; ++_i) \
;         __builtin_amdgcn_global_load_lds((const unsigned*)((const char*)(gbase) + (voff)[_i]), (PG8_LAS unsigned*)(lds + (bufoff) + ldsw + _i * 8192), 16, 0, 0); } while (0)
; #define PG8_LDA(dst, b, h) do { _Pragma("unroll") for (int m = 0; m < 4; ++m) _Pragma("unroll") for (int k = 0; k < 2; ++k) dst[m][k] = *(const PG8_LAS bf16x8*)(lds + PG8_SA(b, h) + aoff + m * 2048 + k * 1024); } while (0)
; #define PG8_LDB(dst, b, h) do { _Pragma("unroll") for (int n = 0; n < 2; ++n) _Pragma("unroll") for (int k = 0; k < 2; ++k) dst[n][k] = *(const PG8_LAS bf16x8*)(lds + PG8_SB(b, h) + boff + n * 2048 + k * 1024); } while (0)
; #define PG8_MMA(ai, bj, At, Bt) do { __builtin_amdgcn_s_setprio(1); _Pragma("unroll") for (int m = 0; m < 4; ++m) _Pragma("unroll") for (int n = 0; n < 2; ++n) _Pragma("unroll") for (int k = 0; k < 2; ++k) \
;         acc[ai][bj][m][n] = __builtin_amdgcn_mfma_f32_16x16x32_bf16(Bt[n][k], At[m][k], acc[ai][bj][m][n], 0, 0, 0); __builtin_amdgcn_s_setprio(0); } while (0)
; template <class Epi, class Sched, bool ALIGN_EPI = false, bool SP2 = false>
; __device__ __forceinline__ void gemm_phase(PG8_LAS unsigned char* lds, const Gemm g, const Sched& S, const Epi& E, const int wid) {
;     ...
;             if constexpr (SP2) {
;             PG8_LDB(B0, 0, 0); PG8_LDB(B1, 0, 1); PG8_SCHED; PG8_LDA(At, 0, 0); PG8_STAGE(PG8_SA(1, 1), a1 + hstepA, voffA);
;             PG8_WAIT_V(8); PG8_WAIT_L(0); PG8_BAR; PG8_MMA(0, 0, At, B0); PG8_MMA(0, 1, At, B1); PG8_BAR; PG8_SCHED;
;             PG8_LDA(At, 0, 1); PG8_STAGE(PG8_SB(0, 0), b2, voffB); PG8_STAGE(PG8_SB(0, 1), b2 + hstepB, voffB); PG8_STAGE(PG8_SA(0, 0), a2, voffA);
;             PG8_WAIT_V(8); PG8_WAIT_L(0); PG8_BAR; PG8_MMA(1, 0, At, B0); PG8_MMA(1, 1, At, B1); PG8_BAR; PG8_SCHED;
;             PG8_LDB(B0, 1, 0); PG8_LDB(B1, 1, 1); PG8_SCHED; PG8_LDA(At, 1, 0); PG8_STAGE(PG8_SA(0, 1), a2 + hstepA, voffA);
;             PG8_WAIT_V(8); PG8_WAIT_L(0); PG8_BAR; PG8_MMA(0, 0, At, B0); PG8_MMA(0, 1, At, B1); PG8_BAR; PG8_SCHED;
;             PG8_LDA(At, 1, 1); PG8_STAGE(PG8_SB(1, 0), b3, voffB); PG8_STAGE(PG8_SB(1, 1), b3 + hstepB, voffB); PG8_STAGE(PG8_SA(1, 0), a3, voffA);
;             PG8_WAIT_V(8); PG8_WAIT_L(0); PG8_BAR; PG8_MMA(1, 0, At, B0); PG8_MMA(1, 1, At, B1); PG8_BAR; PG8_SCHED;
	s_setprio 1
	v_mfma_f32_16x16x32_bf16 v[60:63], v[142:145], v[182:185], 0
	v_mfma_f32_16x16x32_bf16 v[56:59], v[150:153], v[182:185], 0
	v_mfma_f32_16x16x32_bf16 v[52:55], v[142:145], v[190:193], 0
	v_mfma_f32_16x16x32_bf16 v[48:51], v[150:153], v[190:193], 0
	v_mfma_f32_16x16x32_bf16 v[36:39], v[142:145], v[198:201], 0
	v_mfma_f32_16x16x32_bf16 v[32:35], v[150:153], v[198:201], 0
	v_mfma_f32_16x16x32_bf16 v[20:23], v[142:145], v[206:209], 0
	v_mfma_f32_16x16x32_bf16 v[16:19], v[150:153], v[206:209], 0
	v_mfma_f32_16x16x32_bf16 v[60:63], v[146:149], v[186:189], v[60:63]
	v_mfma_f32_16x16x32_bf16 v[56:59], v[162:165], v[186:189], v[56:59]
	v_mfma_f32_16x16x32_bf16 v[52:55], v[146:149], v[194:197], v[52:55]
	v_mfma_f32_16x16x32_bf16 v[48:51], v[162:165], v[194:197], v[48:51]
	v_mfma_f32_16x16x32_bf16 v[36:39], v[146:149], v[202:205], v[36:39]
	v_mfma_f32_16x16x32_bf16 v[32:35], v[162:165], v[202:205], v[32:35]
	v_mfma_f32_16x16x32_bf16 v[20:23], v[146:149], v[210:213], v[20:23]
	v_mfma_f32_16x16x32_bf16 v[16:19], v[162:165], v[210:213], v[16:19]
	s_setprio 0
	s_setprio 1
	v_mfma_f32_16x16x32_bf16 v[44:47], v[166:169], v[182:185], 0
	v_mfma_f32_16x16x32_bf16 v[40:43], v[174:177], v[182:185], 0
	v_mfma_f32_16x16x32_bf16 v[28:31], v[166:169], v[190:193], 0
	v_mfma_f32_16x16x32_bf16 v[24:27], v[174:177], v[190:193], 0
	v_mfma_f32_16x16x32_bf16 v[12:15], v[166:169], v[198:201], 0
	v_mfma_f32_16x16x32_bf16 v[8:11], v[174:177], v[198:201], 0
	v_mfma_f32_16x16x32_bf16 v[4:7], v[166:169], v[206:209], 0
	v_mfma_f32_16x16x32_bf16 v[0:3], v[174:177], v[206:209], 0
	v_mfma_f32_16x16x32_bf16 v[44:47], v[170:173], v[186:189], v[44:47]
	v_mfma_f32_16x16x32_bf16 v[40:43], v[178:181], v[186:189], v[40:43]
	v_mfma_f32_16x16x32_bf16 v[28:31], v[170:173], v[194:197], v[28:31]
	v_mfma_f32_16x16x32_bf16 v[24:27], v[178:181], v[194:197], v[24:27]
	v_mfma_f32_16x16x32_bf16 v[12:15], v[170:173], v[202:205], v[12:15]
	v_mfma_f32_16x16x32_bf16 v[8:11], v[178:181], v[202:205], v[8:11]
	v_mfma_f32_16x16x32_bf16 v[4:7], v[170:173], v[210:213], v[4:7]
	v_mfma_f32_16x16x32_bf16 v[0:3], v[178:181], v[210:213], v[0:3]
	s_setprio 0
	s_barrier
	s_mov_b32 m0, s72
	s_nop 0
	global_load_lds_dwordx4 v134, s[36:37]
	s_mov_b32 m0, s73
	s_nop 0
	global_load_lds_dwordx4 v130, s[36:37]
	ds_read_b128 v[142:145], v252
	ds_read_b128 v[146:149], v252 offset:1024
	ds_read_b128 v[150:153], v252 offset:2048
	ds_read_b128 v[162:165], v252 offset:3072
	ds_read_b128 v[166:169], v253
	ds_read_b128 v[170:173], v253 offset:1024
	ds_read_b128 v[174:177], v253 offset:2048
	ds_read_b128 v[178:181], v253 offset:3072
	ds_read_b128 v[182:185], v159 offset:32768
	ds_read_b128 v[186:189], v159 offset:33792
	ds_read_b128 v[190:193], v159 offset:34816
	ds_read_b128 v[194:197], v159 offset:35840
	ds_read_b128 v[198:201], v159 offset:36864
	ds_read_b128 v[202:205], v159 offset:37888
	ds_read_b128 v[206:209], v159 offset:38912
	ds_read_b128 v[210:213], v159 offset:39936
	s_waitcnt vmcnt(8) lgkmcnt(0)
	s_barrier
	s_setprio 1
	v_mfma_f32_16x16x32_bf16 v[124:127], v[142:145], v[182:185], v[124:127]
	v_mfma_f32_16x16x32_bf16 v[120:123], v[150:153], v[182:185], v[120:123]
	v_mfma_f32_16x16x32_bf16 v[116:119], v[142:145], v[190:193], v[116:119]
	v_mfma_f32_16x16x32_bf16 v[112:115], v[150:153], v[190:193], v[112:115]
	v_mfma_f32_16x16x32_bf16 v[100:103], v[142:145], v[198:201], v[100:103]
	v_mfma_f32_16x16x32_bf16 v[96:99], v[150:153], v[198:201], v[96:99]
	v_mfma_f32_16x16x32_bf16 v[84:87], v[142:145], v[206:209], v[84:87]
	v_mfma_f32_16x16x32_bf16 v[80:83], v[150:153], v[206:209], v[80:83]
	v_mfma_f32_16x16x32_bf16 v[124:127], v[146:149], v[186:189], v[124:127]
	v_mfma_f32_16x16x32_bf16 v[120:123], v[162:165], v[186:189], v[120:123]
	v_mfma_f32_16x16x32_bf16 v[116:119], v[146:149], v[194:197], v[116:119]
	v_mfma_f32_16x16x32_bf16 v[112:115], v[162:165], v[194:197], v[112:115]
	v_mfma_f32_16x16x32_bf16 v[100:103], v[146:149], v[202:205], v[100:103]
	v_mfma_f32_16x16x32_bf16 v[96:99], v[162:165], v[202:205], v[96:99]
	v_mfma_f32_16x16x32_bf16 v[84:87], v[146:149], v[210:213], v[84:87]
	v_mfma_f32_16x16x32_bf16 v[80:83], v[162:165], v[210:213], v[80:83]
	s_setprio 0
	s_setprio 1
	v_mfma_f32_16x16x32_bf16 v[108:111], v[166:169], v[182:185], v[108:111]
	v_mfma_f32_16x16x32_bf16 v[104:107], v[174:177], v[182:185], v[104:107]
	v_mfma_f32_16x16x32_bf16 v[92:95], v[166:169], v[190:193], v[92:95]
	v_mfma_f32_16x16x32_bf16 v[88:91], v[174:177], v[190:193], v[88:91]
	v_mfma_f32_16x16x32_bf16 v[76:79], v[166:169], v[198:201], v[76:79]
	v_mfma_f32_16x16x32_bf16 v[72:75], v[174:177], v[198:201], v[72:75]
	v_mfma_f32_16x16x32_bf16 v[68:71], v[166:169], v[206:209], v[68:71]
	v_mfma_f32_16x16x32_bf16 v[64:67], v[174:177], v[206:209], v[64:67]
	v_mfma_f32_16x16x32_bf16 v[108:111], v[170:173], v[186:189], v[108:111]
	v_mfma_f32_16x16x32_bf16 v[104:107], v[178:181], v[186:189], v[104:107]
	v_mfma_f32_16x16x32_bf16 v[92:95], v[170:173], v[194:197], v[92:95]
	v_mfma_f32_16x16x32_bf16 v[88:91], v[178:181], v[194:197], v[88:91]
	v_mfma_f32_16x16x32_bf16 v[76:79], v[170:173], v[202:205], v[76:79]
	v_mfma_f32_16x16x32_bf16 v[72:75], v[178:181], v[202:205], v[72:75]
	v_mfma_f32_16x16x32_bf16 v[68:71], v[170:173], v[210:213], v[68:71]
	v_mfma_f32_16x16x32_bf16 v[64:67], v[178:181], v[210:213], v[64:67]
	s_setprio 0
	s_barrier
; #define PG8_STAGE(bufoff, gbase, voff) do { _Pragma("unroll") for (int _i = 0; _i < 2; ++_i) \
;         __builtin_amdgcn_global_load_lds((const unsigned*)((const char*)(gbase) + (voff)[_i]), (PG8_LAS unsigned*)(lds + (bufoff) + ldsw + _i * 8192), 16, 0, 0); } while (0)
; #define PG8_WAIT_V(n) asm volatile("s_waitcnt vmcnt(" #n ")" ::: "memory")
; #define PG8_WAIT_L(n) asm volatile("s_waitcnt lgkmcnt(" #n ")" ::: "memory")
; #define PG8_BAR __builtin_amdgcn_s_barrier()
; template <class Epi, class Sched, bool ALIGN_EPI = false, bool SP2 = false>
; __device__ __forceinline__ void gemm_phase(PG8_LAS unsigned char* lds, const Gemm g, const Sched& S, const Epi& E, const int wid) {
;     ...
;         const bool has_next = S.next(ui + 1, nxt);
;         const char* nA = has_next ? (const char*)g.A + (size_t)nxt.pm * tstepA : cA; const char* nB = has_next ? (const char*)g.Bt + (size_t)nxt.pn * tstepB : cB;
;         for (int t = 0; t < nt; t += 2) {
;             const bool last = (t == nt - 2);
;             const char* a1 = cA + (size_t)(t + 1) * kstep;
;             const char* a2 = last ? nA : cA + (size_t)(t + 2) * kstep; const char* b2 = last ? nB : cB + (size_t)(t + 2) * kstep;
;             const char* a3 = a2 + kstep; const char* b3 = b2 + kstep;
;             if (last && has_next) S.a_ready(nxt);
;             if constexpr (SP2) {
;             PG8_LDB(B0, 0, 0); PG8_LDB(B1, 0, 1); PG8_SCHED; PG8_LDA(At, 0, 0); PG8_STAGE(PG8_SA(1, 1), a1 + hstepA, voffA);
;             PG8_WAIT_V(8); PG8_WAIT_L(0); PG8_BAR; PG8_MMA(0, 0, At, B0); PG8_MMA(0, 1, At, B1); PG8_BAR; PG8_SCHED;
;             PG8_LDA(At, 0, 1); PG8_STAGE(PG8_SB(0, 0), b2, voffB); PG8_STAGE(PG8_SB(0, 1), b2 + hstepB, voffB); PG8_STAGE(PG8_SA(0, 0), a2, voffA);
;             PG8_WAIT_V(8); PG8_WAIT_L(0); PG8_BAR; PG8_MMA(1, 0, At, B0); PG8_MMA(1, 1, At, B1); PG8_BAR; PG8_SCHED;
;             PG8_LDB(B0, 1, 0); PG8_LDB(B1, 1, 1); PG8_SCHED; PG8_LDA(At, 1, 0); PG8_STAGE(PG8_SA(0, 1), a2 + hstepA, voffA);
;             PG8_WAIT_V(8); PG8_WAIT_L(0); PG8_BAR; PG8_MMA(0, 0, At, B0); PG8_MMA(0, 1, At, B1); PG8_BAR; PG8_SCHED;
;             PG8_LDA(At, 1, 1); PG8_STAGE(PG8_SB(1, 0), b3, voffB); PG8_STAGE(PG8_SB(1, 1), b3 + hstepB, voffB); PG8_STAGE(PG8_SA(1, 0), a3, voffA);
;             PG8_WAIT_V(8); PG8_WAIT_L(0); PG8_BAR; PG8_MMA(1, 0, At, B0); PG8_MMA(1, 1, At, B1); PG8_BAR; PG8_SCHED;
	s_mov_b32 m0, s86
	s_nop 0
	global_load_lds_dwordx4 v132, s[98:99]
	s_mov_b32 m0, s84
	s_nop 0
	global_load_lds_dwordx4 v128, s[98:99]
	s_mov_b32 m0, s85
	s_nop 0
	global_load_lds_dwordx4 v132, s[34:35]
	s_mov_b32 m0, s83
	s_nop 0
	global_load_lds_dwordx4 v128, s[34:35]
	s_mov_b32 m0, s74
	s_nop 0
	global_load_lds_dwordx4 v134, s[100:101]
	s_mov_b32 m0, s75
	s_nop 0
	global_load_lds_dwordx4 v130, s[100:101]
	ds_read_b128 v[182:185], v159 offset:49152
	ds_read_b128 v[186:189], v159 offset:50176
	ds_read_b128 v[190:193], v159 offset:51200
	ds_read_b128 v[194:197], v159 offset:52224
	ds_read_b128 v[198:201], v159 offset:53248
	ds_read_b128 v[202:205], v159 offset:54272
	ds_read_b128 v[206:209], v159 offset:55296
	ds_read_b128 v[210:213], v159 offset:56320
	s_waitcnt vmcnt(8) lgkmcnt(0)
	s_barrier
	s_setprio 1
	v_mfma_f32_16x16x32_bf16 v[60:63], v[142:145], v[182:185], v[60:63]
	v_mfma_f32_16x16x32_bf16 v[56:59], v[150:153], v[182:185], v[56:59]
	v_mfma_f32_16x16x32_bf16 v[52:55], v[142:145], v[190:193], v[52:55]
	v_mfma_f32_16x16x32_bf16 v[48:51], v[150:153], v[190:193], v[48:51]
	v_mfma_f32_16x16x32_bf16 v[36:39], v[142:145], v[198:201], v[36:39]
	v_mfma_f32_16x16x32_bf16 v[32:35], v[150:153], v[198:201], v[32:35]
	v_mfma_f32_16x16x32_bf16 v[20:23], v[142:145], v[206:209], v[20:23]
	v_mfma_f32_16x16x32_bf16 v[16:19], v[150:153], v[206:209], v[16:19]
	v_mfma_f32_16x16x32_bf16 v[60:63], v[146:149], v[186:189], v[60:63]
	v_mfma_f32_16x16x32_bf16 v[56:59], v[162:165], v[186:189], v[56:59]
	v_mfma_f32_16x16x32_bf16 v[52:55], v[146:149], v[194:197], v[52:55]
	v_mfma_f32_16x16x32_bf16 v[48:51], v[162:165], v[194:197], v[48:51]
	v_mfma_f32_16x16x32_bf16 v[36:39], v[146:149], v[202:205], v[36:39]
	v_mfma_f32_16x16x32_bf16 v[32:35], v[162:165], v[202:205], v[32:35]
	v_mfma_f32_16x16x32_bf16 v[20:23], v[146:149], v[210:213], v[20:23]
	v_mfma_f32_16x16x32_bf16 v[16:19], v[162:165], v[210:213], v[16:19]
	s_setprio 0
	s_setprio 1
	v_mfma_f32_16x16x32_bf16 v[44:47], v[166:169], v[182:185], v[44:47]
	v_mfma_f32_16x16x32_bf16 v[40:43], v[174:177], v[182:185], v[40:43]
	v_mfma_f32_16x16x32_bf16 v[28:31], v[166:169], v[190:193], v[28:31]
	v_mfma_f32_16x16x32_bf16 v[24:27], v[174:177], v[190:193], v[24:27]
	v_mfma_f32_16x16x32_bf16 v[12:15], v[166:169], v[198:201], v[12:15]
	v_mfma_f32_16x16x32_bf16 v[8:11], v[174:177], v[198:201], v[8:11]
	v_mfma_f32_16x16x32_bf16 v[4:7], v[166:169], v[206:209], v[4:7]
	v_mfma_f32_16x16x32_bf16 v[0:3], v[174:177], v[206:209], v[0:3]
	v_mfma_f32_16x16x32_bf16 v[44:47], v[170:173], v[186:189], v[44:47]
	v_mfma_f32_16x16x32_bf16 v[40:43], v[178:181], v[186:189], v[40:43]
	v_mfma_f32_16x16x32_bf16 v[28:31], v[170:173], v[194:197], v[28:31]
	v_mfma_f32_16x16x32_bf16 v[24:27], v[178:181], v[194:197], v[24:27]
	v_mfma_f32_16x16x32_bf16 v[12:15], v[170:173], v[202:205], v[12:15]
	v_mfma_f32_16x16x32_bf16 v[8:11], v[178:181], v[202:205], v[8:11]
	v_mfma_f32_16x16x32_bf16 v[4:7], v[170:173], v[210:213], v[4:7]
	v_mfma_f32_16x16x32_bf16 v[0:3], v[178:181], v[210:213], v[0:3]
	s_setprio 0
	s_barrier
	s_movk_i32 s36, 0x100
	s_andn2_b64 vcc, exec, s[30:31]
	s_mov_b64 s[34:35], -1
	s_mov_b64 s[30:31], 0
.LBB0_2280:
	s_add_u32 s37, s28, s36
	s_addc_u32 s44, s29, 0
	s_add_u32 s40, s37, 0x100
	s_addc_u32 s41, s44, 0
	s_and_b64 s[38:39], s[34:35], exec
	s_cselect_b32 s39, s19, s41
	s_cselect_b32 s38, s81, s40
	s_add_u32 s36, s26, s36
	s_addc_u32 s40, s27, 0
	s_add_u32 s36, s36, 0x100
	s_addc_u32 s40, s40, 0
	s_and_b64 s[34:35], s[34:35], exec
	s_cselect_b32 s41, s17, s40
	s_cselect_b32 s40, s82, s36
	s_add_u32 s46, s37, 0x80080
	s_addc_u32 s47, s44, 0
	s_add_i32 s93, s77, s0
	s_add_i32 m0, s70, 0xc000
	s_add_i32 s94, s70, 0xe000
	s_add_i32 s89, s93, 0x2000
	s_add_u32 s44, s40, 0x10000
	s_addc_u32 s45, s41, 0
	s_add_i32 s92, s78, s0
	s_add_i32 s91, s92, 0x2000
	s_add_i32 s88, 0, 0x18000
	s_add_i32 s87, 0, 0x1c000
	s_add_u32 s36, s38, 0x80000
	s_addc_u32 s37, s39, 0
	s_add_i32 s86, s88, s0
	s_add_i32 s84, s86, 0x2000
	s_add_u32 s34, s40, 0x10080
	s_addc_u32 s35, s41, 0
	s_add_i32 s85, s87, s0
	s_add_i32 s83, s85, 0x2000
	global_load_lds_dwordx4 v134, s[46:47]
	s_mov_b32 m0, s94
	s_nop 0
	global_load_lds_dwordx4 v130, s[46:47]
	ds_read_b128 v[142:145], v157
	ds_read_b128 v[146:149], v157 offset:1024
	ds_read_b128 v[150:153], v157 offset:2048
	ds_read_b128 v[162:165], v157 offset:3072
	ds_read_b128 v[166:169], v158
	ds_read_b128 v[170:173], v158 offset:1024
	ds_read_b128 v[174:177], v158 offset:2048
	ds_read_b128 v[178:181], v158 offset:3072
	ds_read_b128 v[182:185], v159
	ds_read_b128 v[186:189], v159 offset:1024
	ds_read_b128 v[190:193], v159 offset:2048
	ds_read_b128 v[194:197], v159 offset:3072
	ds_read_b128 v[198:201], v159 offset:4096
	ds_read_b128 v[202:205], v159 offset:5120
	ds_read_b128 v[206:209], v159 offset:6144
	ds_read_b128 v[210:213], v159 offset:7168
	s_waitcnt vmcnt(8) lgkmcnt(0)
	s_barrier
; #define PG8_STAGE(bufoff, gbase, voff) do { _Pragma("unroll") for (int _i = 0; _i < 2; ++_i) \
;         __builtin_amdgcn_global_load_lds((const unsigned*)((const char*)(gbase) + (voff)[_i]), (PG8_LAS unsigned*)(lds + (bufoff) + ldsw + _i * 8192), 16, 0, 0); } while (0)
; #define PG8_LDA(dst, b, h) do { _Pragma("unroll") for (int m = 0; m < 4; ++m) _Pragma("unroll") for (int k = 0; k < 2; ++k) dst[m][k] = *(const PG8_LAS bf16x8*)(lds + PG8_SA(b, h) + aoff + m * 2048 + k * 1024); } while (0)
; #define PG8_LDB(dst, b, h) do { _Pragma("unroll") for (int n = 0; n < 2; ++n) _Pragma("unroll") for (int k = 0; k < 2; ++k) dst[n][k] = *(const PG8_LAS bf16x8*)(lds + PG8_SB(b, h) + boff + n * 2048 + k * 1024); } while (0)
; #define PG8_MMA(ai, bj, At, Bt) do { __builtin_amdgcn_s_setprio(1); _Pragma("unroll") for (int m = 0; m < 4; ++m) _Pragma("unroll") for (int n = 0; n < 2; ++n) _Pragma("unroll") for (int k = 0; k < 2; ++k) \
;         acc[ai][bj][m][n] = __builtin_amdgcn_mfma_f32_16x16x32_bf16(Bt[n][k], At[m][k], acc[ai][bj][m][n], 0, 0, 0); __builtin_amdgcn_s_setprio(0); } while (0)
; #define PG8_WAIT_V(n) asm volatile("s_waitcnt vmcnt(" #n ")" ::: "memory")
; #define PG8_WAIT_L(n) asm volatile("s_waitcnt lgkmcnt(" #n ")" ::: "memory")
; #define PG8_BAR __builtin_amdgcn_s_barrier()
; #define PG8_SCHED __builtin_amdgcn_sched_barrier(0)
; template <class Epi, class Sched, bool ALIGN_EPI = false, bool SP2 = false>
; __device__ __forceinline__ void gemm_phase(PG8_LAS unsigned char* lds, const Gemm g, const Sched& S, const Epi& E, const int wid) {
;     ...
;             if constexpr (SP2) {
;             PG8_LDB(B0, 0, 0); PG8_LDB(B1, 0, 1); PG8_SCHED; PG8_LDA(At, 0, 0); PG8_STAGE(PG8_SA(1, 1), a1 + hstepA, voffA);
;             PG8_WAIT_V(8); PG8_WAIT_L(0); PG8_BAR; PG8_MMA(0, 0, At, B0); PG8_MMA(0, 1, At, B1); PG8_BAR; PG8_SCHED;
;             PG8_LDA(At, 0, 1); PG8_STAGE(PG8_SB(0, 0), b2, voffB); PG8_STAGE(PG8_SB(0, 1), b2 + hstepB, voffB); PG8_STAGE(PG8_SA(0, 0), a2, voffA);
;             PG8_WAIT_V(8); PG8_WAIT_L(0); PG8_BAR; PG8_MMA(1, 0, At, B0); PG8_MMA(1, 1, At, B1); PG8_BAR; PG8_SCHED;
	s_setprio 1
	v_mfma_f32_16x16x32_bf16 v[124:127], v[142:145], v[182:185], v[124:127]
	v_mfma_f32_16x16x32_bf16 v[120:123], v[150:153], v[182:185], v[120:123]
	v_mfma_f32_16x16x32_bf16 v[116:119], v[142:145], v[190:193], v[116:119]
	v_mfma_f32_16x16x32_bf16 v[112:115], v[150:153], v[190:193], v[112:115]
	v_mfma_f32_16x16x32_bf16 v[100:103], v[142:145], v[198:201], v[100:103]
	v_mfma_f32_16x16x32_bf16 v[96:99], v[150:153], v[198:201], v[96:99]
	v_mfma_f32_16x16x32_bf16 v[84:87], v[142:145], v[206:209], v[84:87]
	v_mfma_f32_16x16x32_bf16 v[80:83], v[150:153], v[206:209], v[80:83]
	v_mfma_f32_16x16x32_bf16 v[124:127], v[146:149], v[186:189], v[124:127]
	v_mfma_f32_16x16x32_bf16 v[120:123], v[162:165], v[186:189], v[120:123]
	v_mfma_f32_16x16x32_bf16 v[116:119], v[146:149], v[194:197], v[116:119]
	v_mfma_f32_16x16x32_bf16 v[112:115], v[162:165], v[194:197], v[112:115]
	v_mfma_f32_16x16x32_bf16 v[100:103], v[146:149], v[202:205], v[100:103]
	v_mfma_f32_16x16x32_bf16 v[96:99], v[162:165], v[202:205], v[96:99]
	v_mfma_f32_16x16x32_bf16 v[84:87], v[146:149], v[210:213], v[84:87]
	v_mfma_f32_16x16x32_bf16 v[80:83], v[162:165], v[210:213], v[80:83]
	s_setprio 0
	s_setprio 1
	v_mfma_f32_16x16x32_bf16 v[108:111], v[166:169], v[182:185], v[108:111]
	v_mfma_f32_16x16x32_bf16 v[104:107], v[174:177], v[182:185], v[104:107]
	v_mfma_f32_16x16x32_bf16 v[92:95], v[166:169], v[190:193], v[92:95]
	v_mfma_f32_16x16x32_bf16 v[88:91], v[174:177], v[190:193], v[88:91]
	v_mfma_f32_16x16x32_bf16 v[76:79], v[166:169], v[198:201], v[76:79]
	v_mfma_f32_16x16x32_bf16 v[72:75], v[174:177], v[198:201], v[72:75]
	v_mfma_f32_16x16x32_bf16 v[68:71], v[166:169], v[206:209], v[68:71]
	v_mfma_f32_16x16x32_bf16 v[64:67], v[174:177], v[206:209], v[64:67]
	v_mfma_f32_16x16x32_bf16 v[108:111], v[170:173], v[186:189], v[108:111]
	v_mfma_f32_16x16x32_bf16 v[104:107], v[178:181], v[186:189], v[104:107]
	v_mfma_f32_16x16x32_bf16 v[92:95], v[170:173], v[194:197], v[92:95]
	v_mfma_f32_16x16x32_bf16 v[88:91], v[178:181], v[194:197], v[88:91]
	v_mfma_f32_16x16x32_bf16 v[76:79], v[170:173], v[202:205], v[76:79]
	v_mfma_f32_16x16x32_bf16 v[72:75], v[178:181], v[202:205], v[72:75]
	v_mfma_f32_16x16x32_bf16 v[68:71], v[170:173], v[210:213], v[68:71]
	v_mfma_f32_16x16x32_bf16 v[64:67], v[178:181], v[210:213], v[64:67]
	s_setprio 0
	s_barrier
	s_mov_b32 m0, s93
	s_add_u32 s98, s40, 0x80
	s_addc_u32 s99, s41, 0
	global_load_lds_dwordx4 v132, s[40:41]
	s_mov_b32 m0, s89
	s_nop 0
	global_load_lds_dwordx4 v128, s[40:41]
	s_mov_b32 m0, s92
	s_add_u32 s100, s38, 0x80
	s_addc_u32 s101, s39, 0
	global_load_lds_dwordx4 v132, s[44:45]
	s_mov_b32 m0, s91
	s_nop 0
	global_load_lds_dwordx4 v128, s[44:45]
	s_mov_b32 m0, s70
	s_nop 0
	global_load_lds_dwordx4 v134, s[38:39]
	s_mov_b32 m0, s71
	s_nop 0
	global_load_lds_dwordx4 v130, s[38:39]
	ds_read_b128 v[182:185], v159 offset:16384
	ds_read_b128 v[186:189], v159 offset:17408
	ds_read_b128 v[190:193], v159 offset:18432
	ds_read_b128 v[194:197], v159 offset:19456
	ds_read_b128 v[198:201], v159 offset:20480
	ds_read_b128 v[202:205], v159 offset:21504
	ds_read_b128 v[206:209], v159 offset:22528
	ds_read_b128 v[210:213], v159 offset:23552
	s_waitcnt vmcnt(8) lgkmcnt(0)
	s_barrier
	s_setprio 1
	v_mfma_f32_16x16x32_bf16 v[60:63], v[142:145], v[182:185], v[60:63]
	v_mfma_f32_16x16x32_bf16 v[56:59], v[150:153], v[182:185], v[56:59]
	v_mfma_f32_16x16x32_bf16 v[52:55], v[142:145], v[190:193], v[52:55]
	v_mfma_f32_16x16x32_bf16 v[48:51], v[150:153], v[190:193], v[48:51]
	v_mfma_f32_16x16x32_bf16 v[36:39], v[142:145], v[198:201], v[36:39]
	v_mfma_f32_16x16x32_bf16 v[32:35], v[150:153], v[198:201], v[32:35]
	v_mfma_f32_16x16x32_bf16 v[20:23], v[142:145], v[206:209], v[20:23]
	v_mfma_f32_16x16x32_bf16 v[16:19], v[150:153], v[206:209], v[16:19]
	v_mfma_f32_16x16x32_bf16 v[60:63], v[146:149], v[186:189], v[60:63]
	v_mfma_f32_16x16x32_bf16 v[56:59], v[162:165], v[186:189], v[56:59]
	v_mfma_f32_16x16x32_bf16 v[52:55], v[146:149], v[194:197], v[52:55]
	v_mfma_f32_16x16x32_bf16 v[48:51], v[162:165], v[194:197], v[48:51]
	v_mfma_f32_16x16x32_bf16 v[36:39], v[146:149], v[202:205], v[36:39]
	v_mfma_f32_16x16x32_bf16 v[32:35], v[162:165], v[202:205], v[32:35]
	v_mfma_f32_16x16x32_bf16 v[20:23], v[146:149], v[210:213], v[20:23]
	v_mfma_f32_16x16x32_bf16 v[16:19], v[162:165], v[210:213], v[16:19]
	s_setprio 0
	s_setprio 1
	v_mfma_f32_16x16x32_bf16 v[44:47], v[166:169], v[182:185], v[44:47]
	v_mfma_f32_16x16x32_bf16 v[40:43], v[174:177], v[182:185], v[40:43]
	v_mfma_f32_16x16x32_bf16 v[28:31], v[166:169], v[190:193], v[28:31]
	v_mfma_f32_16x16x32_bf16 v[24:27], v[174:177], v[190:193], v[24:27]
	v_mfma_f32_16x16x32_bf16 v[12:15], v[166:169], v[198:201], v[12:15]
	v_mfma_f32_16x16x32_bf16 v[8:11], v[174:177], v[198:201], v[8:11]
	v_mfma_f32_16x16x32_bf16 v[4:7], v[166:169], v[206:209], v[4:7]
	v_mfma_f32_16x16x32_bf16 v[0:3], v[174:177], v[206:209], v[0:3]
	v_mfma_f32_16x16x32_bf16 v[44:47], v[170:173], v[186:189], v[44:47]
	v_mfma_f32_16x16x32_bf16 v[40:43], v[178:181], v[186:189], v[40:43]
	v_mfma_f32_16x16x32_bf16 v[28:31], v[170:173], v[194:197], v[28:31]
	v_mfma_f32_16x16x32_bf16 v[24:27], v[178:181], v[194:197], v[24:27]
	v_mfma_f32_16x16x32_bf16 v[12:15], v[170:173], v[202:205], v[12:15]
	v_mfma_f32_16x16x32_bf16 v[8:11], v[178:181], v[202:205], v[8:11]
	v_mfma_f32_16x16x32_bf16 v[4:7], v[170:173], v[210:213], v[4:7]
	v_mfma_f32_16x16x32_bf16 v[0:3], v[178:181], v[210:213], v[0:3]
	s_setprio 0
	s_barrier
; #define PG8_STAGE(bufoff, gbase, voff) do { _Pragma("unroll") for (int _i = 0; _i < 2; ++_i) \
;         __builtin_amdgcn_global_load_lds((const unsigned*)((const char*)(gbase) + (voff)[_i]), (PG8_LAS unsigned*)(lds + (bufoff) + ldsw + _i * 8192), 16, 0, 0); } while (0)
; #define PG8_LDA(dst, b, h) do { _Pragma("unroll") for (int m = 0; m < 4; ++m) _Pragma("unroll") for (int k = 0; k < 2; ++k) dst[m][k] = *(const PG8_LAS bf16x8*)(lds + PG8_SA(b, h) + aoff + m * 2048 + k * 1024); } while (0)
; #define PG8_LDB(dst, b, h) do { _Pragma("unroll") for (int n = 0; n < 2; ++n) _Pragma("unroll") for (int k = 0; k < 2; ++k) dst[n][k] = *(const PG8_LAS bf16x8*)(lds + PG8_SB(b, h) + boff + n * 2048 + k * 1024); } while (0)
; #define PG8_MMA(ai, bj, At, Bt) do { __builtin_amdgcn_s_setprio(1); _Pragma("unroll") for (int m = 0; m < 4; ++m) _Pragma("unroll") for (int n = 0; n < 2; ++n) _Pragma("unroll") for (int k = 0; k < 2; ++k) \
;         acc[ai][bj][m][n] = __builtin_amdgcn_mfma_f32_16x16x32_bf16(Bt[n][k], At[m][k], acc[ai][bj][m][n], 0, 0, 0); __builtin_amdgcn_s_setprio(0); } while (0)
; #define PG8_WAIT_V(n) asm volatile("s_waitcnt vmcnt(" #n ")" ::: "memory")
; #define PG8_WAIT_L(n) asm volatile("s_waitcnt lgkmcnt(" #n ")" ::: "memory")
; #define PG8_BAR __builtin_amdgcn_s_barrier()
; #define PG8_SCHED __builtin_amdgcn_sched_barrier(0)
; template <class Epi, class Sched, bool ALIGN_EPI = false, bool SP2 = false>
; __device__ __forceinline__ void gemm_phase(PG8_LAS unsigned char* lds, const Gemm g, const Sched& S, const Epi& E, const int wid) {
;     ...
;             PG8_LDB(B0, 1, 0); PG8_LDB(B1, 1, 1); PG8_SCHED; PG8_LDA(At, 1, 0); PG8_STAGE(PG8_SA(0, 1), a2 + hstepA, voffA);
;             PG8_WAIT_V(8); PG8_WAIT_L(0); PG8_BAR; PG8_MMA(0, 0, At, B0); PG8_MMA(0, 1, At, B1); PG8_BAR; PG8_SCHED;
;             PG8_LDA(At, 1, 1); PG8_STAGE(PG8_SB(1, 0), b3, voffB); PG8_STAGE(PG8_SB(1, 1), b3 + hstepB, voffB); PG8_STAGE(PG8_SA(1, 0), a3, voffA);
;             PG8_WAIT_V(8); PG8_WAIT_L(0); PG8_BAR; PG8_MMA(1, 0, At, B0); PG8_MMA(1, 1, At, B1); PG8_BAR; PG8_SCHED;
;     ...
;         if constexpr (ALIGN_EPI) { if (wr == 0) PG8_BAR; }
	s_mov_b32 m0, s72
	s_nop 0
	global_load_lds_dwordx4 v134, s[36:37]
	s_mov_b32 m0, s73
	s_nop 0
	global_load_lds_dwordx4 v130, s[36:37]
	ds_read_b128 v[142:145], v252
	ds_read_b128 v[146:149], v252 offset:1024
	ds_read_b128 v[150:153], v252 offset:2048
	ds_read_b128 v[162:165], v252 offset:3072
	ds_read_b128 v[166:169], v253
	ds_read_b128 v[170:173], v253 offset:1024
	ds_read_b128 v[174:177], v253 offset:2048
	ds_read_b128 v[178:181], v253 offset:3072
	ds_read_b128 v[182:185], v159 offset:32768
	ds_read_b128 v[186:189], v159 offset:33792
	ds_read_b128 v[190:193], v159 offset:34816
	ds_read_b128 v[194:197], v159 offset:35840
	ds_read_b128 v[198:201], v159 offset:36864
	ds_read_b128 v[202:205], v159 offset:37888
	ds_read_b128 v[206:209], v159 offset:38912
	ds_read_b128 v[210:213], v159 offset:39936
	s_waitcnt vmcnt(8) lgkmcnt(0)
	s_barrier
	s_setprio 1
	v_mfma_f32_16x16x32_bf16 v[124:127], v[142:145], v[182:185], v[124:127]
	v_mfma_f32_16x16x32_bf16 v[120:123], v[150:153], v[182:185], v[120:123]
	v_mfma_f32_16x16x32_bf16 v[116:119], v[142:145], v[190:193], v[116:119]
	v_mfma_f32_16x16x32_bf16 v[112:115], v[150:153], v[190:193], v[112:115]
	v_mfma_f32_16x16x32_bf16 v[100:103], v[142:145], v[198:201], v[100:103]
	v_mfma_f32_16x16x32_bf16 v[96:99], v[150:153], v[198:201], v[96:99]
	v_mfma_f32_16x16x32_bf16 v[84:87], v[142:145], v[206:209], v[84:87]
	v_mfma_f32_16x16x32_bf16 v[80:83], v[150:153], v[206:209], v[80:83]
	v_mfma_f32_16x16x32_bf16 v[124:127], v[146:149], v[186:189], v[124:127]
	v_mfma_f32_16x16x32_bf16 v[120:123], v[162:165], v[186:189], v[120:123]
	v_mfma_f32_16x16x32_bf16 v[116:119], v[146:149], v[194:197], v[116:119]
	v_mfma_f32_16x16x32_bf16 v[112:115], v[162:165], v[194:197], v[112:115]
	v_mfma_f32_16x16x32_bf16 v[100:103], v[146:149], v[202:205], v[100:103]
	v_mfma_f32_16x16x32_bf16 v[96:99], v[162:165], v[202:205], v[96:99]
	v_mfma_f32_16x16x32_bf16 v[84:87], v[146:149], v[210:213], v[84:87]
	v_mfma_f32_16x16x32_bf16 v[80:83], v[162:165], v[210:213], v[80:83]
	s_setprio 0
	s_setprio 1
	v_mfma_f32_16x16x32_bf16 v[108:111], v[166:169], v[182:185], v[108:111]
	v_mfma_f32_16x16x32_bf16 v[104:107], v[174:177], v[182:185], v[104:107]
	v_mfma_f32_16x16x32_bf16 v[92:95], v[166:169], v[190:193], v[92:95]
	v_mfma_f32_16x16x32_bf16 v[88:91], v[174:177], v[190:193], v[88:91]
	v_mfma_f32_16x16x32_bf16 v[76:79], v[166:169], v[198:201], v[76:79]
	v_mfma_f32_16x16x32_bf16 v[72:75], v[174:177], v[198:201], v[72:75]
	v_mfma_f32_16x16x32_bf16 v[68:71], v[166:169], v[206:209], v[68:71]
	v_mfma_f32_16x16x32_bf16 v[64:67], v[174:177], v[206:209], v[64:67]
	v_mfma_f32_16x16x32_bf16 v[108:111], v[170:173], v[186:189], v[108:111]
	v_mfma_f32_16x16x32_bf16 v[104:107], v[178:181], v[186:189], v[104:107]
	v_mfma_f32_16x16x32_bf16 v[92:95], v[170:173], v[194:197], v[92:95]
	v_mfma_f32_16x16x32_bf16 v[88:91], v[178:181], v[194:197], v[88:91]
	v_mfma_f32_16x16x32_bf16 v[76:79], v[170:173], v[202:205], v[76:79]
	v_mfma_f32_16x16x32_bf16 v[72:75], v[178:181], v[202:205], v[72:75]
	v_mfma_f32_16x16x32_bf16 v[68:71], v[170:173], v[210:213], v[68:71]
	v_mfma_f32_16x16x32_bf16 v[64:67], v[178:181], v[210:213], v[64:67]
	s_setprio 0
	s_barrier
	s_mov_b32 m0, s86
	s_nop 0
	global_load_lds_dwordx4 v132, s[98:99]
	s_mov_b32 m0, s84
	s_nop 0
	global_load_lds_dwordx4 v128, s[98:99]
	s_mov_b32 m0, s85
	s_nop 0
	global_load_lds_dwordx4 v132, s[34:35]
	s_mov_b32 m0, s83
	s_nop 0
	global_load_lds_dwordx4 v128, s[34:35]
	s_mov_b32 m0, s74
	s_nop 0
	global_load_lds_dwordx4 v134, s[100:101]
	s_mov_b32 m0, s75
	s_nop 0
	global_load_lds_dwordx4 v130, s[100:101]
	ds_read_b128 v[182:185], v159 offset:49152
	ds_read_b128 v[186:189], v159 offset:50176
	ds_read_b128 v[190:193], v159 offset:51200
	ds_read_b128 v[194:197], v159 offset:52224
	ds_read_b128 v[198:201], v159 offset:53248
	ds_read_b128 v[202:205], v159 offset:54272
	ds_read_b128 v[206:209], v159 offset:55296
	ds_read_b128 v[210:213], v159 offset:56320
	s_waitcnt vmcnt(8) lgkmcnt(0)
	s_barrier
	s_setprio 1
	v_mfma_f32_16x16x32_bf16 v[60:63], v[142:145], v[182:185], v[60:63]
	v_mfma_f32_16x16x32_bf16 v[56:59], v[150:153], v[182:185], v[56:59]
	v_mfma_f32_16x16x32_bf16 v[52:55], v[142:145], v[190:193], v[52:55]
	v_mfma_f32_16x16x32_bf16 v[48:51], v[150:153], v[190:193], v[48:51]
	v_mfma_f32_16x16x32_bf16 v[36:39], v[142:145], v[198:201], v[36:39]
	v_mfma_f32_16x16x32_bf16 v[32:35], v[150:153], v[198:201], v[32:35]
	v_mfma_f32_16x16x32_bf16 v[20:23], v[142:145], v[206:209], v[20:23]
	v_mfma_f32_16x16x32_bf16 v[16:19], v[150:153], v[206:209], v[16:19]
	v_mfma_f32_16x16x32_bf16 v[60:63], v[146:149], v[186:189], v[60:63]
	v_mfma_f32_16x16x32_bf16 v[56:59], v[162:165], v[186:189], v[56:59]
	v_mfma_f32_16x16x32_bf16 v[52:55], v[146:149], v[194:197], v[52:55]
	v_mfma_f32_16x16x32_bf16 v[48:51], v[162:165], v[194:197], v[48:51]
	v_mfma_f32_16x16x32_bf16 v[36:39], v[146:149], v[202:205], v[36:39]
	v_mfma_f32_16x16x32_bf16 v[32:35], v[162:165], v[202:205], v[32:35]
	v_mfma_f32_16x16x32_bf16 v[20:23], v[146:149], v[210:213], v[20:23]
	v_mfma_f32_16x16x32_bf16 v[16:19], v[162:165], v[210:213], v[16:19]
	s_setprio 0
	s_setprio 1
	v_mfma_f32_16x16x32_bf16 v[44:47], v[166:169], v[182:185], v[44:47]
	v_mfma_f32_16x16x32_bf16 v[40:43], v[174:177], v[182:185], v[40:43]
	v_mfma_f32_16x16x32_bf16 v[28:31], v[166:169], v[190:193], v[28:31]
	v_mfma_f32_16x16x32_bf16 v[24:27], v[174:177], v[190:193], v[24:27]
	v_mfma_f32_16x16x32_bf16 v[12:15], v[166:169], v[198:201], v[12:15]
	v_mfma_f32_16x16x32_bf16 v[8:11], v[174:177], v[198:201], v[8:11]
	v_mfma_f32_16x16x32_bf16 v[4:7], v[166:169], v[206:209], v[4:7]
	v_mfma_f32_16x16x32_bf16 v[0:3], v[174:177], v[206:209], v[0:3]
	v_mfma_f32_16x16x32_bf16 v[44:47], v[170:173], v[186:189], v[44:47]
	v_mfma_f32_16x16x32_bf16 v[40:43], v[178:181], v[186:189], v[40:43]
	v_mfma_f32_16x16x32_bf16 v[28:31], v[170:173], v[194:197], v[28:31]
	v_mfma_f32_16x16x32_bf16 v[24:27], v[178:181], v[194:197], v[24:27]
	v_mfma_f32_16x16x32_bf16 v[12:15], v[170:173], v[202:205], v[12:15]
	v_mfma_f32_16x16x32_bf16 v[8:11], v[178:181], v[202:205], v[8:11]
	v_mfma_f32_16x16x32_bf16 v[4:7], v[170:173], v[210:213], v[4:7]
	v_mfma_f32_16x16x32_bf16 v[0:3], v[178:181], v[210:213], v[0:3]
	s_setprio 0
	s_barrier
	s_movk_i32 s36, 0x100
	s_andn2_b64 vcc, exec, s[30:31]
	s_mov_b64 s[34:35], -1
	s_mov_b64 s[30:31], 0
	s_cbranch_vccz .LBB0_2280
	s_and_b64 vcc, exec, s[14:15]
	s_cbranch_vccz .LBB0_2283
	s_barrier

; #define PG8_STAGE(bufoff, gbase, voff) do { _Pragma("unroll") for (int _i = 0; _i < 2; ++_i) \
;         __builtin_amdgcn_global_load_lds((const unsigned*)((const char*)(gbase) + (voff)[_i]), (PG8_LAS unsigned*)(lds + (bufoff) + ldsw + _i * 8192), 16, 0, 0); } while (0)
; #define PG8_LDA(dst, b, h) do { _Pragma("unroll") for (int m = 0; m < 4; ++m) _Pragma("unroll") for (int k = 0; k < 2; ++k) dst[m][k] = *(const PG8_LAS bf16x8*)(lds + PG8_SA(b, h) + aoff + m * 2048 + k * 1024); } while (0)
; #define PG8_LDB(dst, b, h) do { _Pragma("unroll") for (int n = 0; n < 2; ++n) _Pragma("unroll") for (int k = 0; k < 2; ++k) dst[n][k] = *(const PG8_LAS bf16x8*)(lds + PG8_SB(b, h) + boff + n * 2048 + k * 1024); } while (0)
; #define PG8_WAIT_V(n) asm volatile("s_waitcnt vmcnt(" #n ")" ::: "memory")
; #define PG8_WAIT_L(n) asm volatile("s_waitcnt lgkmcnt(" #n ")" ::: "memory")
; #define PG8_BAR __builtin_amdgcn_s_barrier()
; #define PG8_SCHED __builtin_amdgcn_sched_barrier(0)
; template <class Epi, class Sched, bool ALIGN_EPI = false, bool SP2 = false>
; __device__ __forceinline__ void gemm_phase(PG8_LAS unsigned char* lds, const Gemm g, const Sched& S, const Epi& E, const int wid) {
;     ...
;         const bool has_next = S.next(ui + 1, nxt);
;         const char* nA = has_next ? (const char*)g.A + (size_t)nxt.pm * tstepA : cA; const char* nB = has_next ? (const char*)g.Bt + (size_t)nxt.pn * tstepB : cB;
;         for (int t = 0; t < nt; t += 2) {
;             const bool last = (t == nt - 2);
;             const char* a1 = cA + (size_t)(t + 1) * kstep;
;             const char* a2 = last ? nA : cA + (size_t)(t + 2) * kstep; const char* b2 = last ? nB : cB + (size_t)(t + 2) * kstep;
;             const char* a3 = a2 + kstep; const char* b3 = b2 + kstep;
;             if (last && has_next) S.a_ready(nxt);
;             if constexpr (SP2) {
;             PG8_LDB(B0, 0, 0); PG8_LDB(B1, 0, 1); PG8_SCHED; PG8_LDA(At, 0, 0); PG8_STAGE(PG8_SA(1, 1), a1 + hstepA, voffA);
;             PG8_WAIT_V(8); PG8_WAIT_L(0); PG8_BAR; PG8_MMA(0, 0, At, B0); PG8_MMA(0, 1, At, B1); PG8_BAR; PG8_SCHED;
;             PG8_LDA(At, 0, 1); PG8_STAGE(PG8_SB(0, 0), b2, voffB); PG8_STAGE(PG8_SB(0, 1), b2 + hstepB, voffB); PG8_STAGE(PG8_SA(0, 0), a2, voffA);
;             PG8_WAIT_V(8); PG8_WAIT_L(0); PG8_BAR; PG8_MMA(1, 0, At, B0); PG8_MMA(1, 1, At, B1); PG8_BAR; PG8_SCHED;
.LBB0_2724:
	s_ashr_i32 s21, s20, 31
	s_lshl_b64 s[22:23], s[20:21], 19
	s_add_u32 s22, s0, s22
	s_addc_u32 s23, s1, s23
	s_and_b64 s[24:25], s[4:5], exec
	s_cselect_b32 s21, s23, s31
	s_cselect_b32 s27, s22, s30
	s_ashr_i32 s19, s18, 31
	s_lshl_b64 s[24:25], s[18:19], 19
	s_add_u32 s24, s33, s24
	s_addc_u32 s25, s38, s25
	s_and_b64 s[36:37], s[4:5], exec
	s_cselect_b32 s19, s25, s35
	s_cselect_b32 s29, s24, s34
	s_add_u32 s30, s30, 0x40080
	s_addc_u32 s31, s31, 0
	s_add_u32 s58, s34, 0x100
	s_addc_u32 s59, s35, 0
	s_mov_b32 s60, -2
	s_waitcnt lgkmcnt(0)
	v_add_u32_e32 v252, 0x18000, v189
	v_add_u32_e32 v253, 0x1c000, v189
	s_add_u32 s34, s30, 0xfffc0080
	s_addc_u32 s35, s31, -1
	s_cmp_eq_u32 s60, 12
	s_cselect_b32 s37, s21, s35
	s_cselect_b32 s36, s27, s34
	s_cselect_b32 s35, s19, s59
	s_cselect_b32 s34, s29, s58
	s_add_i32 m0, s40, 0xc000
	s_nop 0
	global_load_lds_dwordx4 v164, s[30:31]
	s_add_i32 m0, s40, 0xe000
	s_nop 0
	global_load_lds_dwordx4 v166, s[30:31]
	ds_read_b128 v[128:131], v190
	ds_read_b128 v[132:135], v190 offset:1024
	ds_read_b128 v[136:139], v190 offset:2048
	ds_read_b128 v[140:143], v190 offset:3072
	ds_read_b128 v[144:147], v191
	ds_read_b128 v[148:151], v191 offset:1024
	ds_read_b128 v[172:175], v191 offset:2048
	ds_read_b128 v[176:179], v191 offset:3072
	ds_read_b128 v[180:183], v192
	ds_read_b128 v[184:187], v192 offset:1024
	ds_read_b128 v[194:197], v192 offset:2048
	ds_read_b128 v[198:201], v192 offset:3072
	ds_read_b128 v[202:205], v192 offset:4096
	ds_read_b128 v[206:209], v192 offset:5120
	ds_read_b128 v[210:213], v192 offset:6144
	ds_read_b128 v[214:217], v192 offset:7168
	s_waitcnt vmcnt(8) lgkmcnt(0)
	s_barrier
	s_setprio 1
	v_mfma_f32_16x16x32_bf16 v[124:127], v[128:131], v[180:183], 0
	v_mfma_f32_16x16x32_bf16 v[120:123], v[136:139], v[180:183], 0
	v_mfma_f32_16x16x32_bf16 v[108:111], v[128:131], v[194:197], 0
	v_mfma_f32_16x16x32_bf16 v[104:107], v[136:139], v[194:197], 0
	v_mfma_f32_16x16x32_bf16 v[92:95], v[128:131], v[202:205], 0
	v_mfma_f32_16x16x32_bf16 v[88:91], v[136:139], v[202:205], 0
	v_mfma_f32_16x16x32_bf16 v[76:79], v[128:131], v[210:213], 0
	v_mfma_f32_16x16x32_bf16 v[72:75], v[136:139], v[210:213], 0
	v_mfma_f32_16x16x32_bf16 v[124:127], v[132:135], v[184:187], v[124:127]
	v_mfma_f32_16x16x32_bf16 v[120:123], v[140:143], v[184:187], v[120:123]
	v_mfma_f32_16x16x32_bf16 v[108:111], v[132:135], v[198:201], v[108:111]
	v_mfma_f32_16x16x32_bf16 v[104:107], v[140:143], v[198:201], v[104:107]
	v_mfma_f32_16x16x32_bf16 v[92:95], v[132:135], v[206:209], v[92:95]
	v_mfma_f32_16x16x32_bf16 v[88:91], v[140:143], v[206:209], v[88:91]
	v_mfma_f32_16x16x32_bf16 v[76:79], v[132:135], v[214:217], v[76:79]
	v_mfma_f32_16x16x32_bf16 v[72:75], v[140:143], v[214:217], v[72:75]
	s_setprio 0
	s_setprio 1
	v_mfma_f32_16x16x32_bf16 v[116:119], v[144:147], v[180:183], 0
	v_mfma_f32_16x16x32_bf16 v[112:115], v[172:175], v[180:183], 0
	v_mfma_f32_16x16x32_bf16 v[100:103], v[144:147], v[194:197], 0
	v_mfma_f32_16x16x32_bf16 v[96:99], v[172:175], v[194:197], 0
	v_mfma_f32_16x16x32_bf16 v[84:87], v[144:147], v[202:205], 0
	v_mfma_f32_16x16x32_bf16 v[80:83], v[172:175], v[202:205], 0
	v_mfma_f32_16x16x32_bf16 v[68:71], v[144:147], v[210:213], 0
	v_mfma_f32_16x16x32_bf16 v[64:67], v[172:175], v[210:213], 0
	v_mfma_f32_16x16x32_bf16 v[116:119], v[148:151], v[184:187], v[116:119]
	v_mfma_f32_16x16x32_bf16 v[112:115], v[176:179], v[184:187], v[112:115]
	v_mfma_f32_16x16x32_bf16 v[100:103], v[148:151], v[198:201], v[100:103]
	v_mfma_f32_16x16x32_bf16 v[96:99], v[176:179], v[198:201], v[96:99]
	v_mfma_f32_16x16x32_bf16 v[84:87], v[148:151], v[206:209], v[84:87]
	v_mfma_f32_16x16x32_bf16 v[80:83], v[176:179], v[206:209], v[80:83]
	v_mfma_f32_16x16x32_bf16 v[68:71], v[148:151], v[214:217], v[68:71]
	v_mfma_f32_16x16x32_bf16 v[64:67], v[176:179], v[214:217], v[64:67]
	s_setprio 0
	s_barrier
	s_add_i32 s61, s49, s39
	s_add_u32 s98, s34, 0x80
	s_addc_u32 s99, s35, 0
	s_mov_b32 m0, s61
	s_nop 0
	global_load_lds_dwordx4 v154, s[34:35]
	s_add_i32 m0, s61, 0x2000
	s_add_u32 s62, s34, 0x40000
	s_addc_u32 s63, s35, 0
	s_add_i32 s61, s56, s39
	global_load_lds_dwordx4 v158, s[34:35]
	s_mov_b32 m0, s61
	s_add_u32 s100, s36, 0x80
	s_addc_u32 s101, s37, 0
	global_load_lds_dwordx4 v154, s[62:63]
	s_add_i32 m0, s61, 0x2000
	s_nop 0
	global_load_lds_dwordx4 v158, s[62:63]
	s_mov_b32 m0, s40
	s_nop 0
	global_load_lds_dwordx4 v152, s[36:37]
	s_mov_b32 m0, s41
	s_nop 0
	global_load_lds_dwordx4 v156, s[36:37]
	ds_read_b128 v[180:183], v192 offset:16384
	ds_read_b128 v[184:187], v192 offset:17408
	ds_read_b128 v[194:197], v192 offset:18432
	ds_read_b128 v[198:201], v192 offset:19456
	ds_read_b128 v[202:205], v192 offset:20480
	ds_read_b128 v[206:209], v192 offset:21504
	ds_read_b128 v[210:213], v192 offset:22528
	ds_read_b128 v[214:217], v192 offset:23552
	s_waitcnt vmcnt(8) lgkmcnt(0)
	s_barrier
; #define PG8_STAGE(bufoff, gbase, voff) do { _Pragma("unroll") for (int _i = 0; _i < 2; ++_i) \
;         __builtin_amdgcn_global_load_lds((const unsigned*)((const char*)(gbase) + (voff)[_i]), (PG8_LAS unsigned*)(lds + (bufoff) + ldsw + _i * 8192), 16, 0, 0); } while (0)
; #define PG8_LDA(dst, b, h) do { _Pragma("unroll") for (int m = 0; m < 4; ++m) _Pragma("unroll") for (int k = 0; k < 2; ++k) dst[m][k] = *(const PG8_LAS bf16x8*)(lds + PG8_SA(b, h) + aoff + m * 2048 + k * 1024); } while (0)
; #define PG8_LDB(dst, b, h) do { _Pragma("unroll") for (int n = 0; n < 2; ++n) _Pragma("unroll") for (int k = 0; k < 2; ++k) dst[n][k] = *(const PG8_LAS bf16x8*)(lds + PG8_SB(b, h) + boff + n * 2048 + k * 1024); } while (0)
; #define PG8_MMA(ai, bj, At, Bt) do { __builtin_amdgcn_s_setprio(1); _Pragma("unroll") for (int m = 0; m < 4; ++m) _Pragma("unroll") for (int n = 0; n < 2; ++n) _Pragma("unroll") for (int k = 0; k < 2; ++k) \
;         acc[ai][bj][m][n] = __builtin_amdgcn_mfma_f32_16x16x32_bf16(Bt[n][k], At[m][k], acc[ai][bj][m][n], 0, 0, 0); __builtin_amdgcn_s_setprio(0); } while (0)
; #define PG8_WAIT_V(n) asm volatile("s_waitcnt vmcnt(" #n ")" ::: "memory")
; #define PG8_WAIT_L(n) asm volatile("s_waitcnt lgkmcnt(" #n ")" ::: "memory")
; #define PG8_BAR __builtin_amdgcn_s_barrier()
; #define PG8_SCHED __builtin_amdgcn_sched_barrier(0)
; template <class Epi, class Sched, bool ALIGN_EPI = false, bool SP2 = false>
; __device__ __forceinline__ void gemm_phase(PG8_LAS unsigned char* lds, const Gemm g, const Sched& S, const Epi& E, const int wid) {
;     ...
;             PG8_WAIT_V(8); PG8_WAIT_L(0); PG8_BAR; PG8_MMA(1, 0, At, B0); PG8_MMA(1, 1, At, B1); PG8_BAR; PG8_SCHED;
;             PG8_LDB(B0, 1, 0); PG8_LDB(B1, 1, 1); PG8_SCHED; PG8_LDA(At, 1, 0); PG8_STAGE(PG8_SA(0, 1), a2 + hstepA, voffA);
;             PG8_WAIT_V(8); PG8_WAIT_L(0); PG8_BAR; PG8_MMA(0, 0, At, B0); PG8_MMA(0, 1, At, B1); PG8_BAR; PG8_SCHED;
	s_setprio 1
	v_mfma_f32_16x16x32_bf16 v[60:63], v[128:131], v[180:183], 0
	v_mfma_f32_16x16x32_bf16 v[56:59], v[136:139], v[180:183], 0
	v_mfma_f32_16x16x32_bf16 v[44:47], v[128:131], v[194:197], 0
	v_mfma_f32_16x16x32_bf16 v[40:43], v[136:139], v[194:197], 0
	v_mfma_f32_16x16x32_bf16 v[28:31], v[128:131], v[202:205], 0
	v_mfma_f32_16x16x32_bf16 v[24:27], v[136:139], v[202:205], 0
	v_mfma_f32_16x16x32_bf16 v[12:15], v[128:131], v[210:213], 0
	v_mfma_f32_16x16x32_bf16 v[8:11], v[136:139], v[210:213], 0
	v_mfma_f32_16x16x32_bf16 v[60:63], v[132:135], v[184:187], v[60:63]
	v_mfma_f32_16x16x32_bf16 v[56:59], v[140:143], v[184:187], v[56:59]
	v_mfma_f32_16x16x32_bf16 v[44:47], v[132:135], v[198:201], v[44:47]
	v_mfma_f32_16x16x32_bf16 v[40:43], v[140:143], v[198:201], v[40:43]
	v_mfma_f32_16x16x32_bf16 v[28:31], v[132:135], v[206:209], v[28:31]
	v_mfma_f32_16x16x32_bf16 v[24:27], v[140:143], v[206:209], v[24:27]
	v_mfma_f32_16x16x32_bf16 v[12:15], v[132:135], v[214:217], v[12:15]
	v_mfma_f32_16x16x32_bf16 v[8:11], v[140:143], v[214:217], v[8:11]
	s_setprio 0
	s_setprio 1
	v_mfma_f32_16x16x32_bf16 v[52:55], v[144:147], v[180:183], 0
	v_mfma_f32_16x16x32_bf16 v[48:51], v[172:175], v[180:183], 0
	v_mfma_f32_16x16x32_bf16 v[36:39], v[144:147], v[194:197], 0
	v_mfma_f32_16x16x32_bf16 v[32:35], v[172:175], v[194:197], 0
	v_mfma_f32_16x16x32_bf16 v[20:23], v[144:147], v[202:205], 0
	v_mfma_f32_16x16x32_bf16 v[16:19], v[172:175], v[202:205], 0
	v_mfma_f32_16x16x32_bf16 v[4:7], v[144:147], v[210:213], 0
	v_mfma_f32_16x16x32_bf16 v[0:3], v[172:175], v[210:213], 0
	v_mfma_f32_16x16x32_bf16 v[52:55], v[148:151], v[184:187], v[52:55]
	v_mfma_f32_16x16x32_bf16 v[48:51], v[176:179], v[184:187], v[48:51]
	v_mfma_f32_16x16x32_bf16 v[36:39], v[148:151], v[198:201], v[36:39]
	v_mfma_f32_16x16x32_bf16 v[32:35], v[176:179], v[198:201], v[32:35]
	v_mfma_f32_16x16x32_bf16 v[20:23], v[148:151], v[206:209], v[20:23]
	v_mfma_f32_16x16x32_bf16 v[16:19], v[176:179], v[206:209], v[16:19]
	v_mfma_f32_16x16x32_bf16 v[4:7], v[148:151], v[214:217], v[4:7]
	v_mfma_f32_16x16x32_bf16 v[0:3], v[176:179], v[214:217], v[0:3]
	s_setprio 0
	s_barrier
	s_add_i32 s61, 0, 0x18000
	s_add_i32 s62, 0, 0x1c000
	s_add_u32 s36, s36, 0x40000
	s_addc_u32 s37, s37, 0
	s_mov_b32 m0, s42
	s_nop 0
	global_load_lds_dwordx4 v152, s[36:37]
	s_mov_b32 m0, s43
	s_nop 0
	global_load_lds_dwordx4 v156, s[36:37]
	ds_read_b128 v[128:131], v252
	ds_read_b128 v[132:135], v252 offset:1024
	ds_read_b128 v[136:139], v252 offset:2048
	ds_read_b128 v[140:143], v252 offset:3072
	ds_read_b128 v[144:147], v253
	ds_read_b128 v[148:151], v253 offset:1024
	ds_read_b128 v[172:175], v253 offset:2048
	ds_read_b128 v[176:179], v253 offset:3072
	ds_read_b128 v[180:183], v192 offset:32768
	ds_read_b128 v[184:187], v192 offset:33792
	ds_read_b128 v[194:197], v192 offset:34816
	ds_read_b128 v[198:201], v192 offset:35840
	ds_read_b128 v[202:205], v192 offset:36864
	ds_read_b128 v[206:209], v192 offset:37888
	ds_read_b128 v[210:213], v192 offset:38912
	ds_read_b128 v[214:217], v192 offset:39936
	s_waitcnt vmcnt(8) lgkmcnt(0)
	s_barrier
	s_setprio 1
	v_mfma_f32_16x16x32_bf16 v[124:127], v[128:131], v[180:183], v[124:127]
	v_mfma_f32_16x16x32_bf16 v[120:123], v[136:139], v[180:183], v[120:123]
	v_mfma_f32_16x16x32_bf16 v[108:111], v[128:131], v[194:197], v[108:111]
	v_mfma_f32_16x16x32_bf16 v[104:107], v[136:139], v[194:197], v[104:107]
	v_mfma_f32_16x16x32_bf16 v[92:95], v[128:131], v[202:205], v[92:95]
	v_mfma_f32_16x16x32_bf16 v[88:91], v[136:139], v[202:205], v[88:91]
	v_mfma_f32_16x16x32_bf16 v[76:79], v[128:131], v[210:213], v[76:79]
	v_mfma_f32_16x16x32_bf16 v[72:75], v[136:139], v[210:213], v[72:75]
	v_mfma_f32_16x16x32_bf16 v[124:127], v[132:135], v[184:187], v[124:127]
	v_mfma_f32_16x16x32_bf16 v[120:123], v[140:143], v[184:187], v[120:123]
	v_mfma_f32_16x16x32_bf16 v[108:111], v[132:135], v[198:201], v[108:111]
	v_mfma_f32_16x16x32_bf16 v[104:107], v[140:143], v[198:201], v[104:107]
	v_mfma_f32_16x16x32_bf16 v[92:95], v[132:135], v[206:209], v[92:95]
	v_mfma_f32_16x16x32_bf16 v[88:91], v[140:143], v[206:209], v[88:91]
	v_mfma_f32_16x16x32_bf16 v[76:79], v[132:135], v[214:217], v[76:79]
	v_mfma_f32_16x16x32_bf16 v[72:75], v[140:143], v[214:217], v[72:75]
	s_setprio 0
	s_setprio 1
	v_mfma_f32_16x16x32_bf16 v[116:119], v[144:147], v[180:183], v[116:119]
	v_mfma_f32_16x16x32_bf16 v[112:115], v[172:175], v[180:183], v[112:115]
	v_mfma_f32_16x16x32_bf16 v[100:103], v[144:147], v[194:197], v[100:103]
	v_mfma_f32_16x16x32_bf16 v[96:99], v[172:175], v[194:197], v[96:99]
	v_mfma_f32_16x16x32_bf16 v[84:87], v[144:147], v[202:205], v[84:87]
	v_mfma_f32_16x16x32_bf16 v[80:83], v[172:175], v[202:205], v[80:83]
	v_mfma_f32_16x16x32_bf16 v[68:71], v[144:147], v[210:213], v[68:71]
	v_mfma_f32_16x16x32_bf16 v[64:67], v[172:175], v[210:213], v[64:67]
	v_mfma_f32_16x16x32_bf16 v[116:119], v[148:151], v[184:187], v[116:119]
	v_mfma_f32_16x16x32_bf16 v[112:115], v[176:179], v[184:187], v[112:115]
	v_mfma_f32_16x16x32_bf16 v[100:103], v[148:151], v[198:201], v[100:103]
	v_mfma_f32_16x16x32_bf16 v[96:99], v[176:179], v[198:201], v[96:99]
	v_mfma_f32_16x16x32_bf16 v[84:87], v[148:151], v[206:209], v[84:87]
	v_mfma_f32_16x16x32_bf16 v[80:83], v[176:179], v[206:209], v[80:83]
	v_mfma_f32_16x16x32_bf16 v[68:71], v[148:151], v[214:217], v[68:71]
	v_mfma_f32_16x16x32_bf16 v[64:67], v[176:179], v[214:217], v[64:67]
	s_setprio 0
	s_barrier
; #define PG8_STAGE(bufoff, gbase, voff) do { _Pragma("unroll") for (int _i = 0; _i < 2; ++_i) \
;         __builtin_amdgcn_global_load_lds((const unsigned*)((const char*)(gbase) + (voff)[_i]), (PG8_LAS unsigned*)(lds + (bufoff) + ldsw + _i * 8192), 16, 0, 0); } while (0)
; #define PG8_LDA(dst, b, h) do { _Pragma("unroll") for (int m = 0; m < 4; ++m) _Pragma("unroll") for (int k = 0; k < 2; ++k) dst[m][k] = *(const PG8_LAS bf16x8*)(lds + PG8_SA(b, h) + aoff + m * 2048 + k * 1024); } while (0)
; #define PG8_LDB(dst, b, h) do { _Pragma("unroll") for (int n = 0; n < 2; ++n) _Pragma("unroll") for (int k = 0; k < 2; ++k) dst[n][k] = *(const PG8_LAS bf16x8*)(lds + PG8_SB(b, h) + boff + n * 2048 + k * 1024); } while (0)
; #define PG8_MMA(ai, bj, At, Bt) do { __builtin_amdgcn_s_setprio(1); _Pragma("unroll") for (int m = 0; m < 4; ++m) _Pragma("unroll") for (int n = 0; n < 2; ++n) _Pragma("unroll") for (int k = 0; k < 2; ++k) \
;         acc[ai][bj][m][n] = __builtin_amdgcn_mfma_f32_16x16x32_bf16(Bt[n][k], At[m][k], acc[ai][bj][m][n], 0, 0, 0); __builtin_amdgcn_s_setprio(0); } while (0)
; #define PG8_WAIT_V(n) asm volatile("s_waitcnt vmcnt(" #n ")" ::: "memory")
; #define PG8_BAR __builtin_amdgcn_s_barrier()
; template <class Epi, class Sched, bool ALIGN_EPI = false, bool SP2 = false>
; __device__ __forceinline__ void gemm_phase(PG8_LAS unsigned char* lds, const Gemm g, const Sched& S, const Epi& E, const int wid) {
;     ...
;         for (int t = 0; t < nt; t += 2) {
;             const bool last = (t == nt - 2);
;             const char* a1 = cA + (size_t)(t + 1) * kstep;
;             const char* a2 = last ? nA : cA + (size_t)(t + 2) * kstep; const char* b2 = last ? nB : cB + (size_t)(t + 2) * kstep;
;             const char* a3 = a2 + kstep; const char* b3 = b2 + kstep;
;             if (last && has_next) S.a_ready(nxt);
;             if constexpr (SP2) {
;             PG8_LDB(B0, 0, 0); PG8_LDB(B1, 0, 1); PG8_SCHED; PG8_LDA(At, 0, 0); PG8_STAGE(PG8_SA(1, 1), a1 + hstepA, voffA);
;             PG8_WAIT_V(8); PG8_WAIT_L(0); PG8_BAR; PG8_MMA(0, 0, At, B0); PG8_MMA(0, 1, At, B1); PG8_BAR; PG8_SCHED;
;     ...
;             PG8_LDA(At, 1, 1); PG8_STAGE(PG8_SB(1, 0), b3, voffB); PG8_STAGE(PG8_SB(1, 1), b3 + hstepB, voffB); PG8_STAGE(PG8_SA(1, 0), a3, voffA);
;             PG8_WAIT_V(8); PG8_WAIT_L(0); PG8_BAR; PG8_MMA(1, 0, At, B0); PG8_MMA(1, 1, At, B1); PG8_BAR; PG8_SCHED;
	s_add_i32 s36, s61, s39
	s_mov_b32 m0, s36
	s_nop 0
	global_load_lds_dwordx4 v154, s[98:99]
	s_add_i32 m0, s36, 0x2000
	s_add_u32 s34, s34, 0x40080
	s_addc_u32 s35, s35, 0
	s_add_i32 s36, s62, s39
	global_load_lds_dwordx4 v158, s[98:99]
	s_mov_b32 m0, s36
	s_nop 0
	global_load_lds_dwordx4 v154, s[34:35]
	s_add_i32 m0, s36, 0x2000
	s_nop 0
	global_load_lds_dwordx4 v158, s[34:35]
	s_mov_b32 m0, s45
	s_nop 0
	global_load_lds_dwordx4 v152, s[100:101]
	s_mov_b32 m0, s46
	s_nop 0
	global_load_lds_dwordx4 v156, s[100:101]
	ds_read_b128 v[180:183], v192 offset:49152
	ds_read_b128 v[184:187], v192 offset:50176
	ds_read_b128 v[194:197], v192 offset:51200
	ds_read_b128 v[198:201], v192 offset:52224
	ds_read_b128 v[202:205], v192 offset:53248
	ds_read_b128 v[206:209], v192 offset:54272
	ds_read_b128 v[210:213], v192 offset:55296
	ds_read_b128 v[214:217], v192 offset:56320
	s_waitcnt vmcnt(8) lgkmcnt(0)
	s_barrier
	s_setprio 1
	v_mfma_f32_16x16x32_bf16 v[60:63], v[128:131], v[180:183], v[60:63]
	v_mfma_f32_16x16x32_bf16 v[56:59], v[136:139], v[180:183], v[56:59]
	v_mfma_f32_16x16x32_bf16 v[44:47], v[128:131], v[194:197], v[44:47]
	v_mfma_f32_16x16x32_bf16 v[40:43], v[136:139], v[194:197], v[40:43]
	v_mfma_f32_16x16x32_bf16 v[28:31], v[128:131], v[202:205], v[28:31]
	v_mfma_f32_16x16x32_bf16 v[24:27], v[136:139], v[202:205], v[24:27]
	v_mfma_f32_16x16x32_bf16 v[12:15], v[128:131], v[210:213], v[12:15]
	v_mfma_f32_16x16x32_bf16 v[8:11], v[136:139], v[210:213], v[8:11]
	v_mfma_f32_16x16x32_bf16 v[60:63], v[132:135], v[184:187], v[60:63]
	v_mfma_f32_16x16x32_bf16 v[56:59], v[140:143], v[184:187], v[56:59]
	v_mfma_f32_16x16x32_bf16 v[44:47], v[132:135], v[198:201], v[44:47]
	v_mfma_f32_16x16x32_bf16 v[40:43], v[140:143], v[198:201], v[40:43]
	v_mfma_f32_16x16x32_bf16 v[28:31], v[132:135], v[206:209], v[28:31]
	v_mfma_f32_16x16x32_bf16 v[24:27], v[140:143], v[206:209], v[24:27]
	v_mfma_f32_16x16x32_bf16 v[12:15], v[132:135], v[214:217], v[12:15]
	v_mfma_f32_16x16x32_bf16 v[8:11], v[140:143], v[214:217], v[8:11]
	s_setprio 0
	s_setprio 1
	v_mfma_f32_16x16x32_bf16 v[52:55], v[144:147], v[180:183], v[52:55]
	v_mfma_f32_16x16x32_bf16 v[48:51], v[172:175], v[180:183], v[48:51]
	v_mfma_f32_16x16x32_bf16 v[36:39], v[144:147], v[194:197], v[36:39]
	v_mfma_f32_16x16x32_bf16 v[32:35], v[172:175], v[194:197], v[32:35]
	v_mfma_f32_16x16x32_bf16 v[20:23], v[144:147], v[202:205], v[20:23]
	v_mfma_f32_16x16x32_bf16 v[16:19], v[172:175], v[202:205], v[16:19]
	v_mfma_f32_16x16x32_bf16 v[4:7], v[144:147], v[210:213], v[4:7]
	v_mfma_f32_16x16x32_bf16 v[0:3], v[172:175], v[210:213], v[0:3]
	v_mfma_f32_16x16x32_bf16 v[52:55], v[148:151], v[184:187], v[52:55]
	v_mfma_f32_16x16x32_bf16 v[48:51], v[176:179], v[184:187], v[48:51]
	v_mfma_f32_16x16x32_bf16 v[36:39], v[148:151], v[198:201], v[36:39]
	v_mfma_f32_16x16x32_bf16 v[32:35], v[176:179], v[198:201], v[32:35]
	v_mfma_f32_16x16x32_bf16 v[20:23], v[148:151], v[206:209], v[20:23]
	v_mfma_f32_16x16x32_bf16 v[16:19], v[176:179], v[206:209], v[16:19]
	v_mfma_f32_16x16x32_bf16 v[4:7], v[148:151], v[214:217], v[4:7]
	v_mfma_f32_16x16x32_bf16 v[0:3], v[176:179], v[214:217], v[0:3]
	s_setprio 0
	s_barrier
	s_add_i32 s60, s60, 2
	s_add_u32 s30, s30, 0x100
	s_addc_u32 s31, s31, 0
	s_add_u32 s58, s58, 0x100
	s_addc_u32 s59, s59, 0
	s_cmp_gt_u32 s60, 13
.LBB0_2725:
	s_add_u32 s34, s30, 0xfffc0080
	s_addc_u32 s35, s31, -1
	s_cmp_eq_u32 s60, 12
	s_cselect_b32 s37, s21, s35
	s_cselect_b32 s36, s27, s34
	s_cselect_b32 s35, s19, s59
	s_cselect_b32 s34, s29, s58
	s_add_i32 m0, s40, 0xc000
	s_nop 0
	global_load_lds_dwordx4 v164, s[30:31]
	s_add_i32 m0, s40, 0xe000
	s_nop 0
	global_load_lds_dwordx4 v166, s[30:31]
	ds_read_b128 v[128:131], v190
	ds_read_b128 v[132:135], v190 offset:1024
	ds_read_b128 v[136:139], v190 offset:2048
	ds_read_b128 v[140:143], v190 offset:3072
	ds_read_b128 v[144:147], v191
	ds_read_b128 v[148:151], v191 offset:1024
	ds_read_b128 v[172:175], v191 offset:2048
	ds_read_b128 v[176:179], v191 offset:3072
	ds_read_b128 v[180:183], v192
	ds_read_b128 v[184:187], v192 offset:1024
	ds_read_b128 v[194:197], v192 offset:2048
	ds_read_b128 v[198:201], v192 offset:3072
	ds_read_b128 v[202:205], v192 offset:4096
	ds_read_b128 v[206:209], v192 offset:5120
	ds_read_b128 v[210:213], v192 offset:6144
	ds_read_b128 v[214:217], v192 offset:7168
	s_waitcnt vmcnt(8) lgkmcnt(0)
	s_barrier
	s_setprio 1
	v_mfma_f32_16x16x32_bf16 v[124:127], v[128:131], v[180:183], v[124:127]
	v_mfma_f32_16x16x32_bf16 v[120:123], v[136:139], v[180:183], v[120:123]
	v_mfma_f32_16x16x32_bf16 v[108:111], v[128:131], v[194:197], v[108:111]
	v_mfma_f32_16x16x32_bf16 v[104:107], v[136:139], v[194:197], v[104:107]
	v_mfma_f32_16x16x32_bf16 v[92:95], v[128:131], v[202:205], v[92:95]
	v_mfma_f32_16x16x32_bf16 v[88:91], v[136:139], v[202:205], v[88:91]
	v_mfma_f32_16x16x32_bf16 v[76:79], v[128:131], v[210:213], v[76:79]
	v_mfma_f32_16x16x32_bf16 v[72:75], v[136:139], v[210:213], v[72:75]
	v_mfma_f32_16x16x32_bf16 v[124:127], v[132:135], v[184:187], v[124:127]
	v_mfma_f32_16x16x32_bf16 v[120:123], v[140:143], v[184:187], v[120:123]
	v_mfma_f32_16x16x32_bf16 v[108:111], v[132:135], v[198:201], v[108:111]
	v_mfma_f32_16x16x32_bf16 v[104:107], v[140:143], v[198:201], v[104:107]
	v_mfma_f32_16x16x32_bf16 v[92:95], v[132:135], v[206:209], v[92:95]
	v_mfma_f32_16x16x32_bf16 v[88:91], v[140:143], v[206:209], v[88:91]
	v_mfma_f32_16x16x32_bf16 v[76:79], v[132:135], v[214:217], v[76:79]
	v_mfma_f32_16x16x32_bf16 v[72:75], v[140:143], v[214:217], v[72:75]
	s_setprio 0
	s_setprio 1
	v_mfma_f32_16x16x32_bf16 v[116:119], v[144:147], v[180:183], v[116:119]
	v_mfma_f32_16x16x32_bf16 v[112:115], v[172:175], v[180:183], v[112:115]
	v_mfma_f32_16x16x32_bf16 v[100:103], v[144:147], v[194:197], v[100:103]
	v_mfma_f32_16x16x32_bf16 v[96:99], v[172:175], v[194:197], v[96:99]
	v_mfma_f32_16x16x32_bf16 v[84:87], v[144:147], v[202:205], v[84:87]
	v_mfma_f32_16x16x32_bf16 v[80:83], v[172:175], v[202:205], v[80:83]
	v_mfma_f32_16x16x32_bf16 v[68:71], v[144:147], v[210:213], v[68:71]
	v_mfma_f32_16x16x32_bf16 v[64:67], v[172:175], v[210:213], v[64:67]
	v_mfma_f32_16x16x32_bf16 v[116:119], v[148:151], v[184:187], v[116:119]
	v_mfma_f32_16x16x32_bf16 v[112:115], v[176:179], v[184:187], v[112:115]
	v_mfma_f32_16x16x32_bf16 v[100:103], v[148:151], v[198:201], v[100:103]
	v_mfma_f32_16x16x32_bf16 v[96:99], v[176:179], v[198:201], v[96:99]
	v_mfma_f32_16x16x32_bf16 v[84:87], v[148:151], v[206:209], v[84:87]
	v_mfma_f32_16x16x32_bf16 v[80:83], v[176:179], v[206:209], v[80:83]
	v_mfma_f32_16x16x32_bf16 v[68:71], v[148:151], v[214:217], v[68:71]
	v_mfma_f32_16x16x32_bf16 v[64:67], v[176:179], v[214:217], v[64:67]
	s_setprio 0
	s_barrier
; #define PG8_STAGE(bufoff, gbase, voff) do { _Pragma("unroll") for (int _i = 0; _i < 2; ++_i) \
;         __builtin_amdgcn_global_load_lds((const unsigned*)((const char*)(gbase) + (voff)[_i]), (PG8_LAS unsigned*)(lds + (bufoff) + ldsw + _i * 8192), 16, 0, 0); } while (0)
; #define PG8_LDA(dst, b, h) do { _Pragma("unroll") for (int m = 0; m < 4; ++m) _Pragma("unroll") for (int k = 0; k < 2; ++k) dst[m][k] = *(const PG8_LAS bf16x8*)(lds + PG8_SA(b, h) + aoff + m * 2048 + k * 1024); } while (0)
; #define PG8_LDB(dst, b, h) do { _Pragma("unroll") for (int n = 0; n < 2; ++n) _Pragma("unroll") for (int k = 0; k < 2; ++k) dst[n][k] = *(const PG8_LAS bf16x8*)(lds + PG8_SB(b, h) + boff + n * 2048 + k * 1024); } while (0)
; #define PG8_MMA(ai, bj, At, Bt) do { __builtin_amdgcn_s_setprio(1); _Pragma("unroll") for (int m = 0; m < 4; ++m) _Pragma("unroll") for (int n = 0; n < 2; ++n) _Pragma("unroll") for (int k = 0; k < 2; ++k) \
;         acc[ai][bj][m][n] = __builtin_amdgcn_mfma_f32_16x16x32_bf16(Bt[n][k], At[m][k], acc[ai][bj][m][n], 0, 0, 0); __builtin_amdgcn_s_setprio(0); } while (0)
; #define PG8_WAIT_V(n) asm volatile("s_waitcnt vmcnt(" #n ")" ::: "memory")
; #define PG8_WAIT_L(n) asm volatile("s_waitcnt lgkmcnt(" #n ")" ::: "memory")
; #define PG8_BAR __builtin_amdgcn_s_barrier()
; #define PG8_SCHED __builtin_amdgcn_sched_barrier(0)
; template <class Epi, class Sched, bool ALIGN_EPI = false, bool SP2 = false>
; __device__ __forceinline__ void gemm_phase(PG8_LAS unsigned char* lds, const Gemm g, const Sched& S, const Epi& E, const int wid) {
;     ...
;             PG8_WAIT_V(8); PG8_WAIT_L(0); PG8_BAR; PG8_MMA(0, 0, At, B0); PG8_MMA(0, 1, At, B1); PG8_BAR; PG8_SCHED;
;             PG8_LDA(At, 0, 1); PG8_STAGE(PG8_SB(0, 0), b2, voffB); PG8_STAGE(PG8_SB(0, 1), b2 + hstepB, voffB); PG8_STAGE(PG8_SA(0, 0), a2, voffA);
;             PG8_WAIT_V(8); PG8_WAIT_L(0); PG8_BAR; PG8_MMA(1, 0, At, B0); PG8_MMA(1, 1, At, B1); PG8_BAR; PG8_SCHED;
;             PG8_LDB(B0, 1, 0); PG8_LDB(B1, 1, 1); PG8_SCHED; PG8_LDA(At, 1, 0); PG8_STAGE(PG8_SA(0, 1), a2 + hstepA, voffA);
;             PG8_WAIT_V(8); PG8_WAIT_L(0); PG8_BAR; PG8_MMA(0, 0, At, B0); PG8_MMA(0, 1, At, B1); PG8_BAR; PG8_SCHED;
	s_add_i32 s61, s49, s39
	s_add_u32 s98, s34, 0x80
	s_addc_u32 s99, s35, 0
	s_mov_b32 m0, s61
	s_nop 0
	global_load_lds_dwordx4 v154, s[34:35]
	s_add_i32 m0, s61, 0x2000
	s_add_u32 s62, s34, 0x40000
	s_addc_u32 s63, s35, 0
	s_add_i32 s61, s56, s39
	global_load_lds_dwordx4 v158, s[34:35]
	s_mov_b32 m0, s61
	s_add_u32 s100, s36, 0x80
	s_addc_u32 s101, s37, 0
	global_load_lds_dwordx4 v154, s[62:63]
	s_add_i32 m0, s61, 0x2000
	s_nop 0
	global_load_lds_dwordx4 v158, s[62:63]
	s_mov_b32 m0, s40
	s_nop 0
	global_load_lds_dwordx4 v152, s[36:37]
	s_mov_b32 m0, s41
	s_nop 0
	global_load_lds_dwordx4 v156, s[36:37]
	ds_read_b128 v[180:183], v192 offset:16384
	ds_read_b128 v[184:187], v192 offset:17408
	ds_read_b128 v[194:197], v192 offset:18432
	ds_read_b128 v[198:201], v192 offset:19456
	ds_read_b128 v[202:205], v192 offset:20480
	ds_read_b128 v[206:209], v192 offset:21504
	ds_read_b128 v[210:213], v192 offset:22528
	ds_read_b128 v[214:217], v192 offset:23552
	s_waitcnt vmcnt(8) lgkmcnt(0)
	s_barrier
	s_setprio 1
	v_mfma_f32_16x16x32_bf16 v[60:63], v[128:131], v[180:183], v[60:63]
	v_mfma_f32_16x16x32_bf16 v[56:59], v[136:139], v[180:183], v[56:59]
	v_mfma_f32_16x16x32_bf16 v[44:47], v[128:131], v[194:197], v[44:47]
	v_mfma_f32_16x16x32_bf16 v[40:43], v[136:139], v[194:197], v[40:43]
	v_mfma_f32_16x16x32_bf16 v[28:31], v[128:131], v[202:205], v[28:31]
	v_mfma_f32_16x16x32_bf16 v[24:27], v[136:139], v[202:205], v[24:27]
	v_mfma_f32_16x16x32_bf16 v[12:15], v[128:131], v[210:213], v[12:15]
	v_mfma_f32_16x16x32_bf16 v[8:11], v[136:139], v[210:213], v[8:11]
	v_mfma_f32_16x16x32_bf16 v[60:63], v[132:135], v[184:187], v[60:63]
	v_mfma_f32_16x16x32_bf16 v[56:59], v[140:143], v[184:187], v[56:59]
	v_mfma_f32_16x16x32_bf16 v[44:47], v[132:135], v[198:201], v[44:47]
	v_mfma_f32_16x16x32_bf16 v[40:43], v[140:143], v[198:201], v[40:43]
	v_mfma_f32_16x16x32_bf16 v[28:31], v[132:135], v[206:209], v[28:31]
	v_mfma_f32_16x16x32_bf16 v[24:27], v[140:143], v[206:209], v[24:27]
	v_mfma_f32_16x16x32_bf16 v[12:15], v[132:135], v[214:217], v[12:15]
	v_mfma_f32_16x16x32_bf16 v[8:11], v[140:143], v[214:217], v[8:11]
	s_setprio 0
	s_setprio 1
	v_mfma_f32_16x16x32_bf16 v[52:55], v[144:147], v[180:183], v[52:55]
	v_mfma_f32_16x16x32_bf16 v[48:51], v[172:175], v[180:183], v[48:51]
	v_mfma_f32_16x16x32_bf16 v[36:39], v[144:147], v[194:197], v[36:39]
	v_mfma_f32_16x16x32_bf16 v[32:35], v[172:175], v[194:197], v[32:35]
	v_mfma_f32_16x16x32_bf16 v[20:23], v[144:147], v[202:205], v[20:23]
	v_mfma_f32_16x16x32_bf16 v[16:19], v[172:175], v[202:205], v[16:19]
	v_mfma_f32_16x16x32_bf16 v[4:7], v[144:147], v[210:213], v[4:7]
	v_mfma_f32_16x16x32_bf16 v[0:3], v[172:175], v[210:213], v[0:3]
	v_mfma_f32_16x16x32_bf16 v[52:55], v[148:151], v[184:187], v[52:55]
	v_mfma_f32_16x16x32_bf16 v[48:51], v[176:179], v[184:187], v[48:51]
	v_mfma_f32_16x16x32_bf16 v[36:39], v[148:151], v[198:201], v[36:39]
	v_mfma_f32_16x16x32_bf16 v[32:35], v[176:179], v[198:201], v[32:35]
	v_mfma_f32_16x16x32_bf16 v[20:23], v[148:151], v[206:209], v[20:23]
	v_mfma_f32_16x16x32_bf16 v[16:19], v[176:179], v[206:209], v[16:19]
	v_mfma_f32_16x16x32_bf16 v[4:7], v[148:151], v[214:217], v[4:7]
	v_mfma_f32_16x16x32_bf16 v[0:3], v[176:179], v[214:217], v[0:3]
	s_setprio 0
	s_barrier
	s_add_i32 s61, 0, 0x18000
	s_add_i32 s62, 0, 0x1c000
	s_add_u32 s36, s36, 0x40000
	s_addc_u32 s37, s37, 0
	s_mov_b32 m0, s42
	s_nop 0
	global_load_lds_dwordx4 v152, s[36:37]
	s_mov_b32 m0, s43
	s_nop 0
	global_load_lds_dwordx4 v156, s[36:37]
	ds_read_b128 v[128:131], v252
	ds_read_b128 v[132:135], v252 offset:1024
	ds_read_b128 v[136:139], v252 offset:2048
	ds_read_b128 v[140:143], v252 offset:3072
	ds_read_b128 v[144:147], v253
	ds_read_b128 v[148:151], v253 offset:1024
	ds_read_b128 v[172:175], v253 offset:2048
	ds_read_b128 v[176:179], v253 offset:3072
	ds_read_b128 v[180:183], v192 offset:32768
	ds_read_b128 v[184:187], v192 offset:33792
	ds_read_b128 v[194:197], v192 offset:34816
	ds_read_b128 v[198:201], v192 offset:35840
	ds_read_b128 v[202:205], v192 offset:36864
	ds_read_b128 v[206:209], v192 offset:37888
	ds_read_b128 v[210:213], v192 offset:38912
	ds_read_b128 v[214:217], v192 offset:39936
	s_waitcnt vmcnt(8) lgkmcnt(0)
	s_barrier
; #define PG8_STAGE(bufoff, gbase, voff) do { _Pragma("unroll") for (int _i = 0; _i < 2; ++_i) \
;         __builtin_amdgcn_global_load_lds((const unsigned*)((const char*)(gbase) + (voff)[_i]), (PG8_LAS unsigned*)(lds + (bufoff) + ldsw + _i * 8192), 16, 0, 0); } while (0)
; #define PG8_LDA(dst, b, h) do { _Pragma("unroll") for (int m = 0; m < 4; ++m) _Pragma("unroll") for (int k = 0; k < 2; ++k) dst[m][k] = *(const PG8_LAS bf16x8*)(lds + PG8_SA(b, h) + aoff + m * 2048 + k * 1024); } while (0)
; #define PG8_MMA(ai, bj, At, Bt) do { __builtin_amdgcn_s_setprio(1); _Pragma("unroll") for (int m = 0; m < 4; ++m) _Pragma("unroll") for (int n = 0; n < 2; ++n) _Pragma("unroll") for (int k = 0; k < 2; ++k) \
;         acc[ai][bj][m][n] = __builtin_amdgcn_mfma_f32_16x16x32_bf16(Bt[n][k], At[m][k], acc[ai][bj][m][n], 0, 0, 0); __builtin_amdgcn_s_setprio(0); } while (0)
; #define PG8_WAIT_V(n) asm volatile("s_waitcnt vmcnt(" #n ")" ::: "memory")
; #define PG8_WAIT_L(n) asm volatile("s_waitcnt lgkmcnt(" #n ")" ::: "memory")
; #define PG8_BAR __builtin_amdgcn_s_barrier()
; #define PG8_SCHED __builtin_amdgcn_sched_barrier(0)
; template <class Epi, class Sched, bool ALIGN_EPI = false, bool SP2 = false>
; __device__ __forceinline__ void gemm_phase(PG8_LAS unsigned char* lds, const Gemm g, const Sched& S, const Epi& E, const int wid) {
;     ...
;             PG8_WAIT_V(8); PG8_WAIT_L(0); PG8_BAR; PG8_MMA(0, 0, At, B0); PG8_MMA(0, 1, At, B1); PG8_BAR; PG8_SCHED;
;             PG8_LDA(At, 1, 1); PG8_STAGE(PG8_SB(1, 0), b3, voffB); PG8_STAGE(PG8_SB(1, 1), b3 + hstepB, voffB); PG8_STAGE(PG8_SA(1, 0), a3, voffA);
;             PG8_WAIT_V(8); PG8_WAIT_L(0); PG8_BAR; PG8_MMA(1, 0, At, B0); PG8_MMA(1, 1, At, B1); PG8_BAR; PG8_SCHED;
;     ...
;         if constexpr (ALIGN_EPI) { if (wr == 0) PG8_BAR; }
	s_setprio 1
	v_mfma_f32_16x16x32_bf16 v[124:127], v[128:131], v[180:183], v[124:127]
	v_mfma_f32_16x16x32_bf16 v[120:123], v[136:139], v[180:183], v[120:123]
	v_mfma_f32_16x16x32_bf16 v[108:111], v[128:131], v[194:197], v[108:111]
	v_mfma_f32_16x16x32_bf16 v[104:107], v[136:139], v[194:197], v[104:107]
	v_mfma_f32_16x16x32_bf16 v[92:95], v[128:131], v[202:205], v[92:95]
	v_mfma_f32_16x16x32_bf16 v[88:91], v[136:139], v[202:205], v[88:91]
	v_mfma_f32_16x16x32_bf16 v[76:79], v[128:131], v[210:213], v[76:79]
	v_mfma_f32_16x16x32_bf16 v[72:75], v[136:139], v[210:213], v[72:75]
	v_mfma_f32_16x16x32_bf16 v[124:127], v[132:135], v[184:187], v[124:127]
	v_mfma_f32_16x16x32_bf16 v[120:123], v[140:143], v[184:187], v[120:123]
	v_mfma_f32_16x16x32_bf16 v[108:111], v[132:135], v[198:201], v[108:111]
	v_mfma_f32_16x16x32_bf16 v[104:107], v[140:143], v[198:201], v[104:107]
	v_mfma_f32_16x16x32_bf16 v[92:95], v[132:135], v[206:209], v[92:95]
	v_mfma_f32_16x16x32_bf16 v[88:91], v[140:143], v[206:209], v[88:91]
	v_mfma_f32_16x16x32_bf16 v[76:79], v[132:135], v[214:217], v[76:79]
	v_mfma_f32_16x16x32_bf16 v[72:75], v[140:143], v[214:217], v[72:75]
	s_setprio 0
	s_setprio 1
	v_mfma_f32_16x16x32_bf16 v[116:119], v[144:147], v[180:183], v[116:119]
	v_mfma_f32_16x16x32_bf16 v[112:115], v[172:175], v[180:183], v[112:115]
	v_mfma_f32_16x16x32_bf16 v[100:103], v[144:147], v[194:197], v[100:103]
	v_mfma_f32_16x16x32_bf16 v[96:99], v[172:175], v[194:197], v[96:99]
	v_mfma_f32_16x16x32_bf16 v[84:87], v[144:147], v[202:205], v[84:87]
	v_mfma_f32_16x16x32_bf16 v[80:83], v[172:175], v[202:205], v[80:83]
	v_mfma_f32_16x16x32_bf16 v[68:71], v[144:147], v[210:213], v[68:71]
	v_mfma_f32_16x16x32_bf16 v[64:67], v[172:175], v[210:213], v[64:67]
	v_mfma_f32_16x16x32_bf16 v[116:119], v[148:151], v[184:187], v[116:119]
	v_mfma_f32_16x16x32_bf16 v[112:115], v[176:179], v[184:187], v[112:115]
	v_mfma_f32_16x16x32_bf16 v[100:103], v[148:151], v[198:201], v[100:103]
	v_mfma_f32_16x16x32_bf16 v[96:99], v[176:179], v[198:201], v[96:99]
	v_mfma_f32_16x16x32_bf16 v[84:87], v[148:151], v[206:209], v[84:87]
	v_mfma_f32_16x16x32_bf16 v[80:83], v[176:179], v[206:209], v[80:83]
	v_mfma_f32_16x16x32_bf16 v[68:71], v[148:151], v[214:217], v[68:71]
	v_mfma_f32_16x16x32_bf16 v[64:67], v[176:179], v[214:217], v[64:67]
	s_setprio 0
	s_barrier
	s_add_i32 s36, s61, s39
	s_mov_b32 m0, s36
	s_nop 0
	global_load_lds_dwordx4 v154, s[98:99]
	s_add_i32 m0, s36, 0x2000
	s_add_u32 s34, s34, 0x40080
	s_addc_u32 s35, s35, 0
	s_add_i32 s36, s62, s39
	global_load_lds_dwordx4 v158, s[98:99]
	s_mov_b32 m0, s36
	s_nop 0
	global_load_lds_dwordx4 v154, s[34:35]
	s_add_i32 m0, s36, 0x2000
	s_nop 0
	global_load_lds_dwordx4 v158, s[34:35]
	s_mov_b32 m0, s45
	s_nop 0
	global_load_lds_dwordx4 v152, s[100:101]
	s_mov_b32 m0, s46
	s_nop 0
	global_load_lds_dwordx4 v156, s[100:101]
	ds_read_b128 v[180:183], v192 offset:49152
	ds_read_b128 v[184:187], v192 offset:50176
	ds_read_b128 v[194:197], v192 offset:51200
	ds_read_b128 v[198:201], v192 offset:52224
	ds_read_b128 v[202:205], v192 offset:53248
	ds_read_b128 v[206:209], v192 offset:54272
	ds_read_b128 v[210:213], v192 offset:55296
	ds_read_b128 v[214:217], v192 offset:56320
	s_waitcnt vmcnt(8) lgkmcnt(0)
	s_barrier
	s_setprio 1
	v_mfma_f32_16x16x32_bf16 v[60:63], v[128:131], v[180:183], v[60:63]
	v_mfma_f32_16x16x32_bf16 v[56:59], v[136:139], v[180:183], v[56:59]
	v_mfma_f32_16x16x32_bf16 v[44:47], v[128:131], v[194:197], v[44:47]
	v_mfma_f32_16x16x32_bf16 v[40:43], v[136:139], v[194:197], v[40:43]
	v_mfma_f32_16x16x32_bf16 v[28:31], v[128:131], v[202:205], v[28:31]
	v_mfma_f32_16x16x32_bf16 v[24:27], v[136:139], v[202:205], v[24:27]
	v_mfma_f32_16x16x32_bf16 v[12:15], v[128:131], v[210:213], v[12:15]
	v_mfma_f32_16x16x32_bf16 v[8:11], v[136:139], v[210:213], v[8:11]
	v_mfma_f32_16x16x32_bf16 v[60:63], v[132:135], v[184:187], v[60:63]
	v_mfma_f32_16x16x32_bf16 v[56:59], v[140:143], v[184:187], v[56:59]
	v_mfma_f32_16x16x32_bf16 v[44:47], v[132:135], v[198:201], v[44:47]
	v_mfma_f32_16x16x32_bf16 v[40:43], v[140:143], v[198:201], v[40:43]
	v_mfma_f32_16x16x32_bf16 v[28:31], v[132:135], v[206:209], v[28:31]
	v_mfma_f32_16x16x32_bf16 v[24:27], v[140:143], v[206:209], v[24:27]
	v_mfma_f32_16x16x32_bf16 v[12:15], v[132:135], v[214:217], v[12:15]
	v_mfma_f32_16x16x32_bf16 v[8:11], v[140:143], v[214:217], v[8:11]
	s_setprio 0
	s_setprio 1
	v_mfma_f32_16x16x32_bf16 v[52:55], v[144:147], v[180:183], v[52:55]
	v_mfma_f32_16x16x32_bf16 v[48:51], v[172:175], v[180:183], v[48:51]
	v_mfma_f32_16x16x32_bf16 v[36:39], v[144:147], v[194:197], v[36:39]
	v_mfma_f32_16x16x32_bf16 v[32:35], v[172:175], v[194:197], v[32:35]
	v_mfma_f32_16x16x32_bf16 v[20:23], v[144:147], v[202:205], v[20:23]
	v_mfma_f32_16x16x32_bf16 v[16:19], v[172:175], v[202:205], v[16:19]
	v_mfma_f32_16x16x32_bf16 v[4:7], v[144:147], v[210:213], v[4:7]
	v_mfma_f32_16x16x32_bf16 v[0:3], v[172:175], v[210:213], v[0:3]
	v_mfma_f32_16x16x32_bf16 v[52:55], v[148:151], v[184:187], v[52:55]
	v_mfma_f32_16x16x32_bf16 v[48:51], v[176:179], v[184:187], v[48:51]
	v_mfma_f32_16x16x32_bf16 v[36:39], v[148:151], v[198:201], v[36:39]
	v_mfma_f32_16x16x32_bf16 v[32:35], v[176:179], v[198:201], v[32:35]
	v_mfma_f32_16x16x32_bf16 v[20:23], v[148:151], v[206:209], v[20:23]
	v_mfma_f32_16x16x32_bf16 v[16:19], v[176:179], v[206:209], v[16:19]
	v_mfma_f32_16x16x32_bf16 v[4:7], v[148:151], v[214:217], v[4:7]
	v_mfma_f32_16x16x32_bf16 v[0:3], v[176:179], v[214:217], v[0:3]
	s_setprio 0
	s_barrier
	s_add_i32 s60, s60, 2
	s_add_u32 s30, s30, 0x100
	s_addc_u32 s31, s31, 0
	s_add_u32 s58, s58, 0x100
	s_addc_u32 s59, s59, 0
	s_cmp_gt_u32 s60, 13
	s_cbranch_scc0 .LBB0_2725
	s_and_b64 vcc, exec, s[16:17]
	s_cbranch_vccz .LBB0_2728
	s_barrier

; #define PG8_STAGE(bufoff, gbase, voff) do { _Pragma("unroll") for (int _i = 0; _i < 2; ++_i) \
;         __builtin_amdgcn_global_load_lds((const unsigned*)((const char*)(gbase) + (voff)[_i]), (PG8_LAS unsigned*)(lds + (bufoff) + ldsw + _i * 8192), 16, 0, 0); } while (0)
; #define PG8_LDA(dst, b, h) do { _Pragma("unroll") for (int m = 0; m < 4; ++m) _Pragma("unroll") for (int k = 0; k < 2; ++k) dst[m][k] = *(const PG8_LAS bf16x8*)(lds + PG8_SA(b, h) + aoff + m * 2048 + k * 1024); } while (0)
; #define PG8_WAIT_V(n) asm volatile("s_waitcnt vmcnt(" #n ")" ::: "memory")
; #define PG8_WAIT_L(n) asm volatile("s_waitcnt lgkmcnt(" #n ")" ::: "memory")
;     __device__ __forceinline__ void operator()(const f32x4 (&acc)[2][2][4][2], const Unit& u, int wr, int wc, int fr, int fq) const {
;     ...
;             for (int ai = 0; ai < 2; ++ai)
; #pragma unroll
;                 for (int m = 0; m < 4; ++m) qd[ai][m] = row_quad(ssq, u.pm * BM + ai * HALF + wr * 64 + m * 16 + fr, fq);
; template <class Epi, class Sched, bool ALIGN_EPI = false, bool SP2 = false>
; __device__ __forceinline__ void gemm_phase(PG8_LAS unsigned char* lds, const Gemm g, const Sched& S, const Epi& E, const int wid) {
;     ...
;         const bool has_next = S.next(ui + 1, nxt);
;         const char* nA = has_next ? (const char*)g.A + (size_t)nxt.pm * tstepA : cA; const char* nB = has_next ? (const char*)g.Bt + (size_t)nxt.pn * tstepB : cB;
;         for (int t = 0; t < nt; t += 2) {
;             const bool last = (t == nt - 2);
;             const char* a1 = cA + (size_t)(t + 1) * kstep;
;             const char* a2 = last ? nA : cA + (size_t)(t + 2) * kstep; const char* b2 = last ? nB : cB + (size_t)(t + 2) * kstep;
;             const char* a3 = a2 + kstep; const char* b3 = b2 + kstep;
;             if (last && has_next) S.a_ready(nxt);
;             if constexpr (SP2) {
;             PG8_LDB(B0, 0, 0); PG8_LDB(B1, 0, 1); PG8_SCHED; PG8_LDA(At, 0, 0); PG8_STAGE(PG8_SA(1, 1), a1 + hstepA, voffA);
;             PG8_WAIT_V(8); PG8_WAIT_L(0); PG8_BAR; PG8_MMA(0, 0, At, B0); PG8_MMA(0, 1, At, B1); PG8_BAR; PG8_SCHED;
;             PG8_LDA(At, 0, 1); PG8_STAGE(PG8_SB(0, 0), b2, voffB); PG8_STAGE(PG8_SB(0, 1), b2 + hstepB, voffB); PG8_STAGE(PG8_SA(0, 0), a2, voffA);
;             PG8_WAIT_V(8); PG8_WAIT_L(0); PG8_BAR; PG8_MMA(1, 0, At, B0); PG8_MMA(1, 1, At, B1); PG8_BAR; PG8_SCHED;
.LBB0_2811:
	s_ashr_i32 s17, s16, 31
	s_lshl_b64 s[18:19], s[16:17], 19
	s_add_u32 s18, s0, s18
	s_addc_u32 s19, s1, s19
	s_and_b64 s[20:21], s[2:3], exec
	s_cselect_b32 s17, s19, s25
	s_cselect_b32 s47, s18, s24
	s_ashr_i32 s15, s14, 31
	s_lshl_b64 s[20:21], s[14:15], 19
	s_add_u32 s20, s30, s20
	s_addc_u32 s21, s31, s21
	s_and_b64 s[28:29], s[2:3], exec
	s_cselect_b32 s15, s21, s27
	s_cselect_b32 s48, s20, s26
	s_add_u32 s24, s24, 0x40080
	s_addc_u32 s25, s25, 0
	s_add_u32 s49, s26, 0x100
	s_addc_u32 s56, s27, 0
	s_mov_b32 s57, -2
	v_add_u32_e32 v252, 0x18000, v165
	v_add_u32_e32 v253, 0x1c000, v165
	s_add_u32 s26, s24, 0xfffc0080
	s_addc_u32 s27, s25, -1
	s_cmp_eq_u32 s57, 12
	s_cselect_b32 s29, s17, s27
	s_cselect_b32 s28, s47, s26
	s_cselect_b32 s27, s15, s56
	s_cselect_b32 s26, s48, s49
	s_add_i32 m0, s36, 0xc000
	s_nop 0
	global_load_lds_dwordx4 v140, s[24:25]
	s_add_i32 m0, s36, 0xe000
	s_nop 0
	global_load_lds_dwordx4 v142, s[24:25]
	ds_read_b128 v[148:151], v166
	ds_read_b128 v[152:155], v166 offset:1024
	ds_read_b128 v[156:159], v166 offset:2048
	ds_read_b128 v[160:163], v166 offset:3072
	ds_read_b128 v[172:175], v167
	ds_read_b128 v[176:179], v167 offset:1024
	ds_read_b128 v[180:183], v167 offset:2048
	ds_read_b128 v[184:187], v167 offset:3072
	ds_read_b128 v[188:191], v168
	ds_read_b128 v[192:195], v168 offset:1024
	ds_read_b128 v[196:199], v168 offset:2048
	ds_read_b128 v[200:203], v168 offset:3072
	ds_read_b128 v[204:207], v168 offset:4096
	ds_read_b128 v[208:211], v168 offset:5120
	ds_read_b128 v[212:215], v168 offset:6144
	ds_read_b128 v[216:219], v168 offset:7168
	s_waitcnt vmcnt(8) lgkmcnt(0)
	v_lshl_add_u32 v220, s22, 8, v164
	v_add_u32_e32 v236, 0x80, v220
	v_ashrrev_i32_e32 v221, 31, v220
	v_ashrrev_i32_e32 v237, 31, v236
	v_lshlrev_b64 v[220:221], 6, v[220:221]
	v_lshlrev_b64 v[236:237], 6, v[236:237]
	v_lshl_add_u64 v[220:221], v[138:139], 0, v[220:221]
	v_lshl_add_u64 v[236:237], v[138:139], 0, v[236:237]
	global_load_dwordx4 v[224:227], v[220:221], off offset:1024
	global_load_dwordx4 v[228:231], v[220:221], off offset:2048
	global_load_dwordx4 v[232:235], v[220:221], off offset:3072
	global_load_dwordx4 v[240:243], v[236:237], off offset:1024
	global_load_dwordx4 v[244:247], v[236:237], off offset:2048
	global_load_dwordx4 v[248:251], v[236:237], off offset:3072
	s_nop 0
	global_load_dwordx4 v[220:223], v[220:221], off
	s_nop 0
	global_load_dwordx4 v[236:239], v[236:237], off
	s_barrier
	s_setprio 1
	v_mfma_f32_16x16x32_bf16 v[124:127], v[148:151], v[188:191], 0
	v_mfma_f32_16x16x32_bf16 v[116:119], v[156:159], v[188:191], 0
	v_mfma_f32_16x16x32_bf16 v[108:111], v[148:151], v[196:199], 0
	v_mfma_f32_16x16x32_bf16 v[100:103], v[156:159], v[196:199], 0
	v_mfma_f32_16x16x32_bf16 v[92:95], v[148:151], v[204:207], 0
	v_mfma_f32_16x16x32_bf16 v[84:87], v[156:159], v[204:207], 0
	v_mfma_f32_16x16x32_bf16 v[76:79], v[148:151], v[212:215], 0
	v_mfma_f32_16x16x32_bf16 v[68:71], v[156:159], v[212:215], 0
	v_mfma_f32_16x16x32_bf16 v[124:127], v[152:155], v[192:195], v[124:127]
	v_mfma_f32_16x16x32_bf16 v[116:119], v[160:163], v[192:195], v[116:119]
	v_mfma_f32_16x16x32_bf16 v[108:111], v[152:155], v[200:203], v[108:111]
	v_mfma_f32_16x16x32_bf16 v[100:103], v[160:163], v[200:203], v[100:103]
	v_mfma_f32_16x16x32_bf16 v[92:95], v[152:155], v[208:211], v[92:95]
	v_mfma_f32_16x16x32_bf16 v[84:87], v[160:163], v[208:211], v[84:87]
	v_mfma_f32_16x16x32_bf16 v[76:79], v[152:155], v[216:219], v[76:79]
	v_mfma_f32_16x16x32_bf16 v[68:71], v[160:163], v[216:219], v[68:71]
	s_setprio 0
	s_setprio 1
	v_mfma_f32_16x16x32_bf16 v[120:123], v[172:175], v[188:191], 0
	v_mfma_f32_16x16x32_bf16 v[112:115], v[180:183], v[188:191], 0
	v_mfma_f32_16x16x32_bf16 v[104:107], v[172:175], v[196:199], 0
	v_mfma_f32_16x16x32_bf16 v[96:99], v[180:183], v[196:199], 0
	v_mfma_f32_16x16x32_bf16 v[88:91], v[172:175], v[204:207], 0
	v_mfma_f32_16x16x32_bf16 v[80:83], v[180:183], v[204:207], 0
	v_mfma_f32_16x16x32_bf16 v[72:75], v[172:175], v[212:215], 0
	v_mfma_f32_16x16x32_bf16 v[64:67], v[180:183], v[212:215], 0
	v_mfma_f32_16x16x32_bf16 v[120:123], v[176:179], v[192:195], v[120:123]
	v_mfma_f32_16x16x32_bf16 v[112:115], v[184:187], v[192:195], v[112:115]
	v_mfma_f32_16x16x32_bf16 v[104:107], v[176:179], v[200:203], v[104:107]
	v_mfma_f32_16x16x32_bf16 v[96:99], v[184:187], v[200:203], v[96:99]
	v_mfma_f32_16x16x32_bf16 v[88:91], v[176:179], v[208:211], v[88:91]
	v_mfma_f32_16x16x32_bf16 v[80:83], v[184:187], v[208:211], v[80:83]
	v_mfma_f32_16x16x32_bf16 v[72:75], v[176:179], v[216:219], v[72:75]
	v_mfma_f32_16x16x32_bf16 v[64:67], v[184:187], v[216:219], v[64:67]
	s_setprio 0
	s_barrier
	s_add_i32 s58, s43, s33
	s_add_u32 s98, s26, 0x80
	s_addc_u32 s99, s27, 0
	s_mov_b32 m0, s58
	s_nop 0
	global_load_lds_dwordx4 v132, s[26:27]
	s_add_i32 m0, s58, 0x2000
	s_add_u32 s58, s26, 0x40000
	s_addc_u32 s59, s27, 0
	s_add_i32 s60, s44, s33
	global_load_lds_dwordx4 v128, s[26:27]
	s_mov_b32 m0, s60
	s_add_u32 s100, s28, 0x80
	s_addc_u32 s101, s29, 0
	global_load_lds_dwordx4 v132, s[58:59]
	s_add_i32 m0, s60, 0x2000
	s_nop 0
	global_load_lds_dwordx4 v128, s[58:59]
	s_mov_b32 m0, s36
	s_nop 0
	global_load_lds_dwordx4 v134, s[28:29]
	s_mov_b32 m0, s37
	s_nop 0
	global_load_lds_dwordx4 v130, s[28:29]
	ds_read_b128 v[188:191], v168 offset:16384
	ds_read_b128 v[192:195], v168 offset:17408
	ds_read_b128 v[196:199], v168 offset:18432
	ds_read_b128 v[200:203], v168 offset:19456
	ds_read_b128 v[204:207], v168 offset:20480
	ds_read_b128 v[208:211], v168 offset:21504
	ds_read_b128 v[212:215], v168 offset:22528
	ds_read_b128 v[216:219], v168 offset:23552
	s_waitcnt vmcnt(8) lgkmcnt(0)
	s_barrier
; #define PG8_STAGE(bufoff, gbase, voff) do { _Pragma("unroll") for (int _i = 0; _i < 2; ++_i) \
;         __builtin_amdgcn_global_load_lds((const unsigned*)((const char*)(gbase) + (voff)[_i]), (PG8_LAS unsigned*)(lds + (bufoff) + ldsw + _i * 8192), 16, 0, 0); } while (0)
; #define PG8_LDA(dst, b, h) do { _Pragma("unroll") for (int m = 0; m < 4; ++m) _Pragma("unroll") for (int k = 0; k < 2; ++k) dst[m][k] = *(const PG8_LAS bf16x8*)(lds + PG8_SA(b, h) + aoff + m * 2048 + k * 1024); } while (0)
; #define PG8_LDB(dst, b, h) do { _Pragma("unroll") for (int n = 0; n < 2; ++n) _Pragma("unroll") for (int k = 0; k < 2; ++k) dst[n][k] = *(const PG8_LAS bf16x8*)(lds + PG8_SB(b, h) + boff + n * 2048 + k * 1024); } while (0)
; #define PG8_MMA(ai, bj, At, Bt) do { __builtin_amdgcn_s_setprio(1); _Pragma("unroll") for (int m = 0; m < 4; ++m) _Pragma("unroll") for (int n = 0; n < 2; ++n) _Pragma("unroll") for (int k = 0; k < 2; ++k) \
;         acc[ai][bj][m][n] = __builtin_amdgcn_mfma_f32_16x16x32_bf16(Bt[n][k], At[m][k], acc[ai][bj][m][n], 0, 0, 0); __builtin_amdgcn_s_setprio(0); } while (0)
; #define PG8_WAIT_V(n) asm volatile("s_waitcnt vmcnt(" #n ")" ::: "memory")
; #define PG8_WAIT_L(n) asm volatile("s_waitcnt lgkmcnt(" #n ")" ::: "memory")
; #define PG8_BAR __builtin_amdgcn_s_barrier()
; #define PG8_SCHED __builtin_amdgcn_sched_barrier(0)
; template <class Epi, class Sched, bool ALIGN_EPI = false, bool SP2 = false>
; __device__ __forceinline__ void gemm_phase(PG8_LAS unsigned char* lds, const Gemm g, const Sched& S, const Epi& E, const int wid) {
;     ...
;             PG8_WAIT_V(8); PG8_WAIT_L(0); PG8_BAR; PG8_MMA(1, 0, At, B0); PG8_MMA(1, 1, At, B1); PG8_BAR; PG8_SCHED;
;             PG8_LDB(B0, 1, 0); PG8_LDB(B1, 1, 1); PG8_SCHED; PG8_LDA(At, 1, 0); PG8_STAGE(PG8_SA(0, 1), a2 + hstepA, voffA);
;             PG8_WAIT_V(8); PG8_WAIT_L(0); PG8_BAR; PG8_MMA(0, 0, At, B0); PG8_MMA(0, 1, At, B1); PG8_BAR; PG8_SCHED;
	s_setprio 1
	v_mfma_f32_16x16x32_bf16 v[60:63], v[148:151], v[188:191], 0
	v_mfma_f32_16x16x32_bf16 v[52:55], v[156:159], v[188:191], 0
	v_mfma_f32_16x16x32_bf16 v[44:47], v[148:151], v[196:199], 0
	v_mfma_f32_16x16x32_bf16 v[36:39], v[156:159], v[196:199], 0
	v_mfma_f32_16x16x32_bf16 v[28:31], v[148:151], v[204:207], 0
	v_mfma_f32_16x16x32_bf16 v[20:23], v[156:159], v[204:207], 0
	v_mfma_f32_16x16x32_bf16 v[12:15], v[148:151], v[212:215], 0
	v_mfma_f32_16x16x32_bf16 v[4:7], v[156:159], v[212:215], 0
	v_mfma_f32_16x16x32_bf16 v[60:63], v[152:155], v[192:195], v[60:63]
	v_mfma_f32_16x16x32_bf16 v[52:55], v[160:163], v[192:195], v[52:55]
	v_mfma_f32_16x16x32_bf16 v[44:47], v[152:155], v[200:203], v[44:47]
	v_mfma_f32_16x16x32_bf16 v[36:39], v[160:163], v[200:203], v[36:39]
	v_mfma_f32_16x16x32_bf16 v[28:31], v[152:155], v[208:211], v[28:31]
	v_mfma_f32_16x16x32_bf16 v[20:23], v[160:163], v[208:211], v[20:23]
	v_mfma_f32_16x16x32_bf16 v[12:15], v[152:155], v[216:219], v[12:15]
	v_mfma_f32_16x16x32_bf16 v[4:7], v[160:163], v[216:219], v[4:7]
	s_setprio 0
	s_setprio 1
	v_mfma_f32_16x16x32_bf16 v[56:59], v[172:175], v[188:191], 0
	v_mfma_f32_16x16x32_bf16 v[48:51], v[180:183], v[188:191], 0
	v_mfma_f32_16x16x32_bf16 v[40:43], v[172:175], v[196:199], 0
	v_mfma_f32_16x16x32_bf16 v[32:35], v[180:183], v[196:199], 0
	v_mfma_f32_16x16x32_bf16 v[24:27], v[172:175], v[204:207], 0
	v_mfma_f32_16x16x32_bf16 v[16:19], v[180:183], v[204:207], 0
	v_mfma_f32_16x16x32_bf16 v[8:11], v[172:175], v[212:215], 0
	v_mfma_f32_16x16x32_bf16 v[0:3], v[180:183], v[212:215], 0
	v_mfma_f32_16x16x32_bf16 v[56:59], v[176:179], v[192:195], v[56:59]
	v_mfma_f32_16x16x32_bf16 v[48:51], v[184:187], v[192:195], v[48:51]
	v_mfma_f32_16x16x32_bf16 v[40:43], v[176:179], v[200:203], v[40:43]
	v_mfma_f32_16x16x32_bf16 v[32:35], v[184:187], v[200:203], v[32:35]
	v_mfma_f32_16x16x32_bf16 v[24:27], v[176:179], v[208:211], v[24:27]
	v_mfma_f32_16x16x32_bf16 v[16:19], v[184:187], v[208:211], v[16:19]
	v_mfma_f32_16x16x32_bf16 v[8:11], v[176:179], v[216:219], v[8:11]
	v_mfma_f32_16x16x32_bf16 v[0:3], v[184:187], v[216:219], v[0:3]
	s_setprio 0
	s_barrier
	s_add_i32 s58, 0, 0x18000
	s_add_i32 s59, 0, 0x1c000
	s_add_u32 s28, s28, 0x40000
	s_addc_u32 s29, s29, 0
	s_mov_b32 m0, s38
	s_nop 0
	global_load_lds_dwordx4 v134, s[28:29]
	s_mov_b32 m0, s39
	s_nop 0
	global_load_lds_dwordx4 v130, s[28:29]
	ds_read_b128 v[148:151], v252
	ds_read_b128 v[152:155], v252 offset:1024
	ds_read_b128 v[156:159], v252 offset:2048
	ds_read_b128 v[160:163], v252 offset:3072
	ds_read_b128 v[172:175], v253
	ds_read_b128 v[176:179], v253 offset:1024
	ds_read_b128 v[180:183], v253 offset:2048
	ds_read_b128 v[184:187], v253 offset:3072
	ds_read_b128 v[188:191], v168 offset:32768
	ds_read_b128 v[192:195], v168 offset:33792
	ds_read_b128 v[196:199], v168 offset:34816
	ds_read_b128 v[200:203], v168 offset:35840
	ds_read_b128 v[204:207], v168 offset:36864
	ds_read_b128 v[208:211], v168 offset:37888
	ds_read_b128 v[212:215], v168 offset:38912
	ds_read_b128 v[216:219], v168 offset:39936
	s_waitcnt vmcnt(8) lgkmcnt(0)
	s_barrier
	s_setprio 1
	v_mfma_f32_16x16x32_bf16 v[124:127], v[148:151], v[188:191], v[124:127]
	v_mfma_f32_16x16x32_bf16 v[116:119], v[156:159], v[188:191], v[116:119]
	v_mfma_f32_16x16x32_bf16 v[108:111], v[148:151], v[196:199], v[108:111]
	v_mfma_f32_16x16x32_bf16 v[100:103], v[156:159], v[196:199], v[100:103]
	v_mfma_f32_16x16x32_bf16 v[92:95], v[148:151], v[204:207], v[92:95]
	v_mfma_f32_16x16x32_bf16 v[84:87], v[156:159], v[204:207], v[84:87]
	v_mfma_f32_16x16x32_bf16 v[76:79], v[148:151], v[212:215], v[76:79]
	v_mfma_f32_16x16x32_bf16 v[68:71], v[156:159], v[212:215], v[68:71]
	v_mfma_f32_16x16x32_bf16 v[124:127], v[152:155], v[192:195], v[124:127]
	v_mfma_f32_16x16x32_bf16 v[116:119], v[160:163], v[192:195], v[116:119]
	v_mfma_f32_16x16x32_bf16 v[108:111], v[152:155], v[200:203], v[108:111]
	v_mfma_f32_16x16x32_bf16 v[100:103], v[160:163], v[200:203], v[100:103]
	v_mfma_f32_16x16x32_bf16 v[92:95], v[152:155], v[208:211], v[92:95]
	v_mfma_f32_16x16x32_bf16 v[84:87], v[160:163], v[208:211], v[84:87]
	v_mfma_f32_16x16x32_bf16 v[76:79], v[152:155], v[216:219], v[76:79]
	v_mfma_f32_16x16x32_bf16 v[68:71], v[160:163], v[216:219], v[68:71]
	s_setprio 0
	s_setprio 1
	v_mfma_f32_16x16x32_bf16 v[120:123], v[172:175], v[188:191], v[120:123]
	v_mfma_f32_16x16x32_bf16 v[112:115], v[180:183], v[188:191], v[112:115]
	v_mfma_f32_16x16x32_bf16 v[104:107], v[172:175], v[196:199], v[104:107]
	v_mfma_f32_16x16x32_bf16 v[96:99], v[180:183], v[196:199], v[96:99]
	v_mfma_f32_16x16x32_bf16 v[88:91], v[172:175], v[204:207], v[88:91]
	v_mfma_f32_16x16x32_bf16 v[80:83], v[180:183], v[204:207], v[80:83]
	v_mfma_f32_16x16x32_bf16 v[72:75], v[172:175], v[212:215], v[72:75]
	v_mfma_f32_16x16x32_bf16 v[64:67], v[180:183], v[212:215], v[64:67]
	v_mfma_f32_16x16x32_bf16 v[120:123], v[176:179], v[192:195], v[120:123]
	v_mfma_f32_16x16x32_bf16 v[112:115], v[184:187], v[192:195], v[112:115]
	v_mfma_f32_16x16x32_bf16 v[104:107], v[176:179], v[200:203], v[104:107]
	v_mfma_f32_16x16x32_bf16 v[96:99], v[184:187], v[200:203], v[96:99]
	v_mfma_f32_16x16x32_bf16 v[88:91], v[176:179], v[208:211], v[88:91]
	v_mfma_f32_16x16x32_bf16 v[80:83], v[184:187], v[208:211], v[80:83]
	v_mfma_f32_16x16x32_bf16 v[72:75], v[176:179], v[216:219], v[72:75]
	v_mfma_f32_16x16x32_bf16 v[64:67], v[184:187], v[216:219], v[64:67]
	s_setprio 0
	s_barrier
; #define PG8_STAGE(bufoff, gbase, voff) do { _Pragma("unroll") for (int _i = 0; _i < 2; ++_i) \
;         __builtin_amdgcn_global_load_lds((const unsigned*)((const char*)(gbase) + (voff)[_i]), (PG8_LAS unsigned*)(lds + (bufoff) + ldsw + _i * 8192), 16, 0, 0); } while (0)
; #define PG8_LDA(dst, b, h) do { _Pragma("unroll") for (int m = 0; m < 4; ++m) _Pragma("unroll") for (int k = 0; k < 2; ++k) dst[m][k] = *(const PG8_LAS bf16x8*)(lds + PG8_SA(b, h) + aoff + m * 2048 + k * 1024); } while (0)
; #define PG8_LDB(dst, b, h) do { _Pragma("unroll") for (int n = 0; n < 2; ++n) _Pragma("unroll") for (int k = 0; k < 2; ++k) dst[n][k] = *(const PG8_LAS bf16x8*)(lds + PG8_SB(b, h) + boff + n * 2048 + k * 1024); } while (0)
; #define PG8_MMA(ai, bj, At, Bt) do { __builtin_amdgcn_s_setprio(1); _Pragma("unroll") for (int m = 0; m < 4; ++m) _Pragma("unroll") for (int n = 0; n < 2; ++n) _Pragma("unroll") for (int k = 0; k < 2; ++k) \
;         acc[ai][bj][m][n] = __builtin_amdgcn_mfma_f32_16x16x32_bf16(Bt[n][k], At[m][k], acc[ai][bj][m][n], 0, 0, 0); __builtin_amdgcn_s_setprio(0); } while (0)
; #define PG8_WAIT_V(n) asm volatile("s_waitcnt vmcnt(" #n ")" ::: "memory")
; #define PG8_BAR __builtin_amdgcn_s_barrier()
; template <class Epi, class Sched, bool ALIGN_EPI = false, bool SP2 = false>
; __device__ __forceinline__ void gemm_phase(PG8_LAS unsigned char* lds, const Gemm g, const Sched& S, const Epi& E, const int wid) {
;     ...
;         for (int t = 0; t < nt; t += 2) {
;             const bool last = (t == nt - 2);
;             const char* a1 = cA + (size_t)(t + 1) * kstep;
;             const char* a2 = last ? nA : cA + (size_t)(t + 2) * kstep; const char* b2 = last ? nB : cB + (size_t)(t + 2) * kstep;
;             const char* a3 = a2 + kstep; const char* b3 = b2 + kstep;
;             if (last && has_next) S.a_ready(nxt);
;             if constexpr (SP2) {
;             PG8_LDB(B0, 0, 0); PG8_LDB(B1, 0, 1); PG8_SCHED; PG8_LDA(At, 0, 0); PG8_STAGE(PG8_SA(1, 1), a1 + hstepA, voffA);
;             PG8_WAIT_V(8); PG8_WAIT_L(0); PG8_BAR; PG8_MMA(0, 0, At, B0); PG8_MMA(0, 1, At, B1); PG8_BAR; PG8_SCHED;
;     ...
;             PG8_LDA(At, 1, 1); PG8_STAGE(PG8_SB(1, 0), b3, voffB); PG8_STAGE(PG8_SB(1, 1), b3 + hstepB, voffB); PG8_STAGE(PG8_SA(1, 0), a3, voffA);
;             PG8_WAIT_V(8); PG8_WAIT_L(0); PG8_BAR; PG8_MMA(1, 0, At, B0); PG8_MMA(1, 1, At, B1); PG8_BAR; PG8_SCHED;
	s_add_i32 s28, s58, s33
	s_mov_b32 m0, s28
	s_nop 0
	global_load_lds_dwordx4 v132, s[98:99]
	s_add_i32 m0, s28, 0x2000
	s_add_u32 s26, s26, 0x40080
	s_addc_u32 s27, s27, 0
	s_add_i32 s28, s59, s33
	global_load_lds_dwordx4 v128, s[98:99]
	s_mov_b32 m0, s28
	s_nop 0
	global_load_lds_dwordx4 v132, s[26:27]
	s_add_i32 m0, s28, 0x2000
	s_nop 0
	global_load_lds_dwordx4 v128, s[26:27]
	s_mov_b32 m0, s40
	s_nop 0
	global_load_lds_dwordx4 v134, s[100:101]
	s_mov_b32 m0, s41
	s_nop 0
	global_load_lds_dwordx4 v130, s[100:101]
	ds_read_b128 v[188:191], v168 offset:49152
	ds_read_b128 v[192:195], v168 offset:50176
	ds_read_b128 v[196:199], v168 offset:51200
	ds_read_b128 v[200:203], v168 offset:52224
	ds_read_b128 v[204:207], v168 offset:53248
	ds_read_b128 v[208:211], v168 offset:54272
	ds_read_b128 v[212:215], v168 offset:55296
	ds_read_b128 v[216:219], v168 offset:56320
	s_waitcnt vmcnt(8) lgkmcnt(0)
	s_barrier
	s_setprio 1
	v_mfma_f32_16x16x32_bf16 v[60:63], v[148:151], v[188:191], v[60:63]
	v_mfma_f32_16x16x32_bf16 v[52:55], v[156:159], v[188:191], v[52:55]
	v_mfma_f32_16x16x32_bf16 v[44:47], v[148:151], v[196:199], v[44:47]
	v_mfma_f32_16x16x32_bf16 v[36:39], v[156:159], v[196:199], v[36:39]
	v_mfma_f32_16x16x32_bf16 v[28:31], v[148:151], v[204:207], v[28:31]
	v_mfma_f32_16x16x32_bf16 v[20:23], v[156:159], v[204:207], v[20:23]
	v_mfma_f32_16x16x32_bf16 v[12:15], v[148:151], v[212:215], v[12:15]
	v_mfma_f32_16x16x32_bf16 v[4:7], v[156:159], v[212:215], v[4:7]
	v_mfma_f32_16x16x32_bf16 v[60:63], v[152:155], v[192:195], v[60:63]
	v_mfma_f32_16x16x32_bf16 v[52:55], v[160:163], v[192:195], v[52:55]
	v_mfma_f32_16x16x32_bf16 v[44:47], v[152:155], v[200:203], v[44:47]
	v_mfma_f32_16x16x32_bf16 v[36:39], v[160:163], v[200:203], v[36:39]
	v_mfma_f32_16x16x32_bf16 v[28:31], v[152:155], v[208:211], v[28:31]
	v_mfma_f32_16x16x32_bf16 v[20:23], v[160:163], v[208:211], v[20:23]
	v_mfma_f32_16x16x32_bf16 v[12:15], v[152:155], v[216:219], v[12:15]
	v_mfma_f32_16x16x32_bf16 v[4:7], v[160:163], v[216:219], v[4:7]
	s_setprio 0
	s_setprio 1
	v_mfma_f32_16x16x32_bf16 v[56:59], v[172:175], v[188:191], v[56:59]
	v_mfma_f32_16x16x32_bf16 v[48:51], v[180:183], v[188:191], v[48:51]
	v_mfma_f32_16x16x32_bf16 v[40:43], v[172:175], v[196:199], v[40:43]
	v_mfma_f32_16x16x32_bf16 v[32:35], v[180:183], v[196:199], v[32:35]
	v_mfma_f32_16x16x32_bf16 v[24:27], v[172:175], v[204:207], v[24:27]
	v_mfma_f32_16x16x32_bf16 v[16:19], v[180:183], v[204:207], v[16:19]
	v_mfma_f32_16x16x32_bf16 v[8:11], v[172:175], v[212:215], v[8:11]
	v_mfma_f32_16x16x32_bf16 v[0:3], v[180:183], v[212:215], v[0:3]
	v_mfma_f32_16x16x32_bf16 v[56:59], v[176:179], v[192:195], v[56:59]
	v_mfma_f32_16x16x32_bf16 v[48:51], v[184:187], v[192:195], v[48:51]
	v_mfma_f32_16x16x32_bf16 v[40:43], v[176:179], v[200:203], v[40:43]
	v_mfma_f32_16x16x32_bf16 v[32:35], v[184:187], v[200:203], v[32:35]
	v_mfma_f32_16x16x32_bf16 v[24:27], v[176:179], v[208:211], v[24:27]
	v_mfma_f32_16x16x32_bf16 v[16:19], v[184:187], v[208:211], v[16:19]
	v_mfma_f32_16x16x32_bf16 v[8:11], v[176:179], v[216:219], v[8:11]
	v_mfma_f32_16x16x32_bf16 v[0:3], v[184:187], v[216:219], v[0:3]
	s_setprio 0
	s_barrier
	s_add_i32 s57, s57, 2
	s_add_u32 s24, s24, 0x100
	s_addc_u32 s25, s25, 0
	s_add_u32 s49, s49, 0x100
	s_addc_u32 s56, s56, 0
	s_cmp_gt_u32 s57, 13
.LBB0_2812:
	s_add_u32 s26, s24, 0xfffc0080
	s_addc_u32 s27, s25, -1
	s_cmp_eq_u32 s57, 12
	s_cselect_b32 s29, s17, s27
	s_cselect_b32 s28, s47, s26
	s_cselect_b32 s27, s15, s56
	s_cselect_b32 s26, s48, s49
	s_add_i32 m0, s36, 0xc000
	s_nop 0
	global_load_lds_dwordx4 v140, s[24:25]
	s_add_i32 m0, s36, 0xe000
	s_nop 0
	global_load_lds_dwordx4 v142, s[24:25]
	ds_read_b128 v[148:151], v166
	ds_read_b128 v[152:155], v166 offset:1024
	ds_read_b128 v[156:159], v166 offset:2048
	ds_read_b128 v[160:163], v166 offset:3072
	ds_read_b128 v[172:175], v167
	ds_read_b128 v[176:179], v167 offset:1024
	ds_read_b128 v[180:183], v167 offset:2048
	ds_read_b128 v[184:187], v167 offset:3072
	ds_read_b128 v[188:191], v168
	ds_read_b128 v[192:195], v168 offset:1024
	ds_read_b128 v[196:199], v168 offset:2048
	ds_read_b128 v[200:203], v168 offset:3072
	ds_read_b128 v[204:207], v168 offset:4096
	ds_read_b128 v[208:211], v168 offset:5120
	ds_read_b128 v[212:215], v168 offset:6144
	ds_read_b128 v[216:219], v168 offset:7168
	s_waitcnt vmcnt(8) lgkmcnt(0)
	s_barrier
	s_setprio 1
	v_mfma_f32_16x16x32_bf16 v[124:127], v[148:151], v[188:191], v[124:127]
	v_mfma_f32_16x16x32_bf16 v[116:119], v[156:159], v[188:191], v[116:119]
	v_mfma_f32_16x16x32_bf16 v[108:111], v[148:151], v[196:199], v[108:111]
	v_mfma_f32_16x16x32_bf16 v[100:103], v[156:159], v[196:199], v[100:103]
	v_mfma_f32_16x16x32_bf16 v[92:95], v[148:151], v[204:207], v[92:95]
	v_mfma_f32_16x16x32_bf16 v[84:87], v[156:159], v[204:207], v[84:87]
	v_mfma_f32_16x16x32_bf16 v[76:79], v[148:151], v[212:215], v[76:79]
	v_mfma_f32_16x16x32_bf16 v[68:71], v[156:159], v[212:215], v[68:71]
	v_mfma_f32_16x16x32_bf16 v[124:127], v[152:155], v[192:195], v[124:127]
	v_mfma_f32_16x16x32_bf16 v[116:119], v[160:163], v[192:195], v[116:119]
	v_mfma_f32_16x16x32_bf16 v[108:111], v[152:155], v[200:203], v[108:111]
	v_mfma_f32_16x16x32_bf16 v[100:103], v[160:163], v[200:203], v[100:103]
	v_mfma_f32_16x16x32_bf16 v[92:95], v[152:155], v[208:211], v[92:95]
	v_mfma_f32_16x16x32_bf16 v[84:87], v[160:163], v[208:211], v[84:87]
	v_mfma_f32_16x16x32_bf16 v[76:79], v[152:155], v[216:219], v[76:79]
	v_mfma_f32_16x16x32_bf16 v[68:71], v[160:163], v[216:219], v[68:71]
	s_setprio 0
	s_setprio 1
	v_mfma_f32_16x16x32_bf16 v[120:123], v[172:175], v[188:191], v[120:123]
	v_mfma_f32_16x16x32_bf16 v[112:115], v[180:183], v[188:191], v[112:115]
	v_mfma_f32_16x16x32_bf16 v[104:107], v[172:175], v[196:199], v[104:107]
	v_mfma_f32_16x16x32_bf16 v[96:99], v[180:183], v[196:199], v[96:99]
	v_mfma_f32_16x16x32_bf16 v[88:91], v[172:175], v[204:207], v[88:91]
	v_mfma_f32_16x16x32_bf16 v[80:83], v[180:183], v[204:207], v[80:83]
	v_mfma_f32_16x16x32_bf16 v[72:75], v[172:175], v[212:215], v[72:75]
	v_mfma_f32_16x16x32_bf16 v[64:67], v[180:183], v[212:215], v[64:67]
	v_mfma_f32_16x16x32_bf16 v[120:123], v[176:179], v[192:195], v[120:123]
	v_mfma_f32_16x16x32_bf16 v[112:115], v[184:187], v[192:195], v[112:115]
	v_mfma_f32_16x16x32_bf16 v[104:107], v[176:179], v[200:203], v[104:107]
	v_mfma_f32_16x16x32_bf16 v[96:99], v[184:187], v[200:203], v[96:99]
	v_mfma_f32_16x16x32_bf16 v[88:91], v[176:179], v[208:211], v[88:91]
	v_mfma_f32_16x16x32_bf16 v[80:83], v[184:187], v[208:211], v[80:83]
	v_mfma_f32_16x16x32_bf16 v[72:75], v[176:179], v[216:219], v[72:75]
	v_mfma_f32_16x16x32_bf16 v[64:67], v[184:187], v[216:219], v[64:67]
	s_setprio 0
	s_barrier
; #define PG8_STAGE(bufoff, gbase, voff) do { _Pragma("unroll") for (int _i = 0; _i < 2; ++_i) \
;         __builtin_amdgcn_global_load_lds((const unsigned*)((const char*)(gbase) + (voff)[_i]), (PG8_LAS unsigned*)(lds + (bufoff) + ldsw + _i * 8192), 16, 0, 0); } while (0)
; #define PG8_LDA(dst, b, h) do { _Pragma("unroll") for (int m = 0; m < 4; ++m) _Pragma("unroll") for (int k = 0; k < 2; ++k) dst[m][k] = *(const PG8_LAS bf16x8*)(lds + PG8_SA(b, h) + aoff + m * 2048 + k * 1024); } while (0)
; #define PG8_LDB(dst, b, h) do { _Pragma("unroll") for (int n = 0; n < 2; ++n) _Pragma("unroll") for (int k = 0; k < 2; ++k) dst[n][k] = *(const PG8_LAS bf16x8*)(lds + PG8_SB(b, h) + boff + n * 2048 + k * 1024); } while (0)
; #define PG8_MMA(ai, bj, At, Bt) do { __builtin_amdgcn_s_setprio(1); _Pragma("unroll") for (int m = 0; m < 4; ++m) _Pragma("unroll") for (int n = 0; n < 2; ++n) _Pragma("unroll") for (int k = 0; k < 2; ++k) \
;         acc[ai][bj][m][n] = __builtin_amdgcn_mfma_f32_16x16x32_bf16(Bt[n][k], At[m][k], acc[ai][bj][m][n], 0, 0, 0); __builtin_amdgcn_s_setprio(0); } while (0)
; #define PG8_WAIT_V(n) asm volatile("s_waitcnt vmcnt(" #n ")" ::: "memory")
; #define PG8_WAIT_L(n) asm volatile("s_waitcnt lgkmcnt(" #n ")" ::: "memory")
; #define PG8_BAR __builtin_amdgcn_s_barrier()
; #define PG8_SCHED __builtin_amdgcn_sched_barrier(0)
; template <class Epi, class Sched, bool ALIGN_EPI = false, bool SP2 = false>
; __device__ __forceinline__ void gemm_phase(PG8_LAS unsigned char* lds, const Gemm g, const Sched& S, const Epi& E, const int wid) {
;     ...
;             PG8_WAIT_V(8); PG8_WAIT_L(0); PG8_BAR; PG8_MMA(0, 0, At, B0); PG8_MMA(0, 1, At, B1); PG8_BAR; PG8_SCHED;
;             PG8_LDA(At, 0, 1); PG8_STAGE(PG8_SB(0, 0), b2, voffB); PG8_STAGE(PG8_SB(0, 1), b2 + hstepB, voffB); PG8_STAGE(PG8_SA(0, 0), a2, voffA);
;             PG8_WAIT_V(8); PG8_WAIT_L(0); PG8_BAR; PG8_MMA(1, 0, At, B0); PG8_MMA(1, 1, At, B1); PG8_BAR; PG8_SCHED;
;             PG8_LDB(B0, 1, 0); PG8_LDB(B1, 1, 1); PG8_SCHED; PG8_LDA(At, 1, 0); PG8_STAGE(PG8_SA(0, 1), a2 + hstepA, voffA);
;             PG8_WAIT_V(8); PG8_WAIT_L(0); PG8_BAR; PG8_MMA(0, 0, At, B0); PG8_MMA(0, 1, At, B1); PG8_BAR; PG8_SCHED;
	s_add_i32 s58, s43, s33
	s_add_u32 s98, s26, 0x80
	s_addc_u32 s99, s27, 0
	s_mov_b32 m0, s58
	s_nop 0
	global_load_lds_dwordx4 v132, s[26:27]
	s_add_i32 m0, s58, 0x2000
	s_add_u32 s58, s26, 0x40000
	s_addc_u32 s59, s27, 0
	s_add_i32 s60, s44, s33
	global_load_lds_dwordx4 v128, s[26:27]
	s_mov_b32 m0, s60
	s_add_u32 s100, s28, 0x80
	s_addc_u32 s101, s29, 0
	global_load_lds_dwordx4 v132, s[58:59]
	s_add_i32 m0, s60, 0x2000
	s_nop 0
	global_load_lds_dwordx4 v128, s[58:59]
	s_mov_b32 m0, s36
	s_nop 0
	global_load_lds_dwordx4 v134, s[28:29]
	s_mov_b32 m0, s37
	s_nop 0
	global_load_lds_dwordx4 v130, s[28:29]
	ds_read_b128 v[188:191], v168 offset:16384
	ds_read_b128 v[192:195], v168 offset:17408
	ds_read_b128 v[196:199], v168 offset:18432
	ds_read_b128 v[200:203], v168 offset:19456
	ds_read_b128 v[204:207], v168 offset:20480
	ds_read_b128 v[208:211], v168 offset:21504
	ds_read_b128 v[212:215], v168 offset:22528
	ds_read_b128 v[216:219], v168 offset:23552
	s_waitcnt vmcnt(8) lgkmcnt(0)
	s_barrier
	s_setprio 1
	v_mfma_f32_16x16x32_bf16 v[60:63], v[148:151], v[188:191], v[60:63]
	v_mfma_f32_16x16x32_bf16 v[52:55], v[156:159], v[188:191], v[52:55]
	v_mfma_f32_16x16x32_bf16 v[44:47], v[148:151], v[196:199], v[44:47]
	v_mfma_f32_16x16x32_bf16 v[36:39], v[156:159], v[196:199], v[36:39]
	v_mfma_f32_16x16x32_bf16 v[28:31], v[148:151], v[204:207], v[28:31]
	v_mfma_f32_16x16x32_bf16 v[20:23], v[156:159], v[204:207], v[20:23]
	v_mfma_f32_16x16x32_bf16 v[12:15], v[148:151], v[212:215], v[12:15]
	v_mfma_f32_16x16x32_bf16 v[4:7], v[156:159], v[212:215], v[4:7]
	v_mfma_f32_16x16x32_bf16 v[60:63], v[152:155], v[192:195], v[60:63]
	v_mfma_f32_16x16x32_bf16 v[52:55], v[160:163], v[192:195], v[52:55]
	v_mfma_f32_16x16x32_bf16 v[44:47], v[152:155], v[200:203], v[44:47]
	v_mfma_f32_16x16x32_bf16 v[36:39], v[160:163], v[200:203], v[36:39]
	v_mfma_f32_16x16x32_bf16 v[28:31], v[152:155], v[208:211], v[28:31]
	v_mfma_f32_16x16x32_bf16 v[20:23], v[160:163], v[208:211], v[20:23]
	v_mfma_f32_16x16x32_bf16 v[12:15], v[152:155], v[216:219], v[12:15]
	v_mfma_f32_16x16x32_bf16 v[4:7], v[160:163], v[216:219], v[4:7]
	s_setprio 0
	s_setprio 1
	v_mfma_f32_16x16x32_bf16 v[56:59], v[172:175], v[188:191], v[56:59]
	v_mfma_f32_16x16x32_bf16 v[48:51], v[180:183], v[188:191], v[48:51]
	v_mfma_f32_16x16x32_bf16 v[40:43], v[172:175], v[196:199], v[40:43]
	v_mfma_f32_16x16x32_bf16 v[32:35], v[180:183], v[196:199], v[32:35]
	v_mfma_f32_16x16x32_bf16 v[24:27], v[172:175], v[204:207], v[24:27]
	v_mfma_f32_16x16x32_bf16 v[16:19], v[180:183], v[204:207], v[16:19]
	v_mfma_f32_16x16x32_bf16 v[8:11], v[172:175], v[212:215], v[8:11]
	v_mfma_f32_16x16x32_bf16 v[0:3], v[180:183], v[212:215], v[0:3]
	v_mfma_f32_16x16x32_bf16 v[56:59], v[176:179], v[192:195], v[56:59]
	v_mfma_f32_16x16x32_bf16 v[48:51], v[184:187], v[192:195], v[48:51]
	v_mfma_f32_16x16x32_bf16 v[40:43], v[176:179], v[200:203], v[40:43]
	v_mfma_f32_16x16x32_bf16 v[32:35], v[184:187], v[200:203], v[32:35]
	v_mfma_f32_16x16x32_bf16 v[24:27], v[176:179], v[208:211], v[24:27]
	v_mfma_f32_16x16x32_bf16 v[16:19], v[184:187], v[208:211], v[16:19]
	v_mfma_f32_16x16x32_bf16 v[8:11], v[176:179], v[216:219], v[8:11]
	v_mfma_f32_16x16x32_bf16 v[0:3], v[184:187], v[216:219], v[0:3]
	s_setprio 0
	s_barrier
	s_add_i32 s58, 0, 0x18000
	s_add_i32 s59, 0, 0x1c000
	s_add_u32 s28, s28, 0x40000
	s_addc_u32 s29, s29, 0
	s_mov_b32 m0, s38
	s_nop 0
	global_load_lds_dwordx4 v134, s[28:29]
	s_mov_b32 m0, s39
	s_nop 0
	global_load_lds_dwordx4 v130, s[28:29]
	ds_read_b128 v[148:151], v252
	ds_read_b128 v[152:155], v252 offset:1024
	ds_read_b128 v[156:159], v252 offset:2048
	ds_read_b128 v[160:163], v252 offset:3072
	ds_read_b128 v[172:175], v253
	ds_read_b128 v[176:179], v253 offset:1024
	ds_read_b128 v[180:183], v253 offset:2048
	ds_read_b128 v[184:187], v253 offset:3072
	ds_read_b128 v[188:191], v168 offset:32768
	ds_read_b128 v[192:195], v168 offset:33792
	ds_read_b128 v[196:199], v168 offset:34816
	ds_read_b128 v[200:203], v168 offset:35840
	ds_read_b128 v[204:207], v168 offset:36864
	ds_read_b128 v[208:211], v168 offset:37888
	ds_read_b128 v[212:215], v168 offset:38912
	ds_read_b128 v[216:219], v168 offset:39936
	s_waitcnt vmcnt(8) lgkmcnt(0)
	s_barrier
; #define PG8_STAGE(bufoff, gbase, voff) do { _Pragma("unroll") for (int _i = 0; _i < 2; ++_i) \
;         __builtin_amdgcn_global_load_lds((const unsigned*)((const char*)(gbase) + (voff)[_i]), (PG8_LAS unsigned*)(lds + (bufoff) + ldsw + _i * 8192), 16, 0, 0); } while (0)
; #define PG8_LDA(dst, b, h) do { _Pragma("unroll") for (int m = 0; m < 4; ++m) _Pragma("unroll") for (int k = 0; k < 2; ++k) dst[m][k] = *(const PG8_LAS bf16x8*)(lds + PG8_SA(b, h) + aoff + m * 2048 + k * 1024); } while (0)
; #define PG8_MMA(ai, bj, At, Bt) do { __builtin_amdgcn_s_setprio(1); _Pragma("unroll") for (int m = 0; m < 4; ++m) _Pragma("unroll") for (int n = 0; n < 2; ++n) _Pragma("unroll") for (int k = 0; k < 2; ++k) \
;         acc[ai][bj][m][n] = __builtin_amdgcn_mfma_f32_16x16x32_bf16(Bt[n][k], At[m][k], acc[ai][bj][m][n], 0, 0, 0); __builtin_amdgcn_s_setprio(0); } while (0)
; #define PG8_WAIT_V(n) asm volatile("s_waitcnt vmcnt(" #n ")" ::: "memory")
; #define PG8_WAIT_L(n) asm volatile("s_waitcnt lgkmcnt(" #n ")" ::: "memory")
; #define PG8_BAR __builtin_amdgcn_s_barrier()
; #define PG8_SCHED __builtin_amdgcn_sched_barrier(0)
; template <class Epi, class Sched, bool ALIGN_EPI = false, bool SP2 = false>
; __device__ __forceinline__ void gemm_phase(PG8_LAS unsigned char* lds, const Gemm g, const Sched& S, const Epi& E, const int wid) {
;     ...
;             PG8_WAIT_V(8); PG8_WAIT_L(0); PG8_BAR; PG8_MMA(0, 0, At, B0); PG8_MMA(0, 1, At, B1); PG8_BAR; PG8_SCHED;
;             PG8_LDA(At, 1, 1); PG8_STAGE(PG8_SB(1, 0), b3, voffB); PG8_STAGE(PG8_SB(1, 1), b3 + hstepB, voffB); PG8_STAGE(PG8_SA(1, 0), a3, voffA);
;             PG8_WAIT_V(8); PG8_WAIT_L(0); PG8_BAR; PG8_MMA(1, 0, At, B0); PG8_MMA(1, 1, At, B1); PG8_BAR; PG8_SCHED;
;     ...
;         if constexpr (ALIGN_EPI) { if (wr == 0) PG8_BAR; }
	s_setprio 1
	v_mfma_f32_16x16x32_bf16 v[124:127], v[148:151], v[188:191], v[124:127]
	v_mfma_f32_16x16x32_bf16 v[116:119], v[156:159], v[188:191], v[116:119]
	v_mfma_f32_16x16x32_bf16 v[108:111], v[148:151], v[196:199], v[108:111]
	v_mfma_f32_16x16x32_bf16 v[100:103], v[156:159], v[196:199], v[100:103]
	v_mfma_f32_16x16x32_bf16 v[92:95], v[148:151], v[204:207], v[92:95]
	v_mfma_f32_16x16x32_bf16 v[84:87], v[156:159], v[204:207], v[84:87]
	v_mfma_f32_16x16x32_bf16 v[76:79], v[148:151], v[212:215], v[76:79]
	v_mfma_f32_16x16x32_bf16 v[68:71], v[156:159], v[212:215], v[68:71]
	v_mfma_f32_16x16x32_bf16 v[124:127], v[152:155], v[192:195], v[124:127]
	v_mfma_f32_16x16x32_bf16 v[116:119], v[160:163], v[192:195], v[116:119]
	v_mfma_f32_16x16x32_bf16 v[108:111], v[152:155], v[200:203], v[108:111]
	v_mfma_f32_16x16x32_bf16 v[100:103], v[160:163], v[200:203], v[100:103]
	v_mfma_f32_16x16x32_bf16 v[92:95], v[152:155], v[208:211], v[92:95]
	v_mfma_f32_16x16x32_bf16 v[84:87], v[160:163], v[208:211], v[84:87]
	v_mfma_f32_16x16x32_bf16 v[76:79], v[152:155], v[216:219], v[76:79]
	v_mfma_f32_16x16x32_bf16 v[68:71], v[160:163], v[216:219], v[68:71]
	s_setprio 0
	s_setprio 1
	v_mfma_f32_16x16x32_bf16 v[120:123], v[172:175], v[188:191], v[120:123]
	v_mfma_f32_16x16x32_bf16 v[112:115], v[180:183], v[188:191], v[112:115]
	v_mfma_f32_16x16x32_bf16 v[104:107], v[172:175], v[196:199], v[104:107]
	v_mfma_f32_16x16x32_bf16 v[96:99], v[180:183], v[196:199], v[96:99]
	v_mfma_f32_16x16x32_bf16 v[88:91], v[172:175], v[204:207], v[88:91]
	v_mfma_f32_16x16x32_bf16 v[80:83], v[180:183], v[204:207], v[80:83]
	v_mfma_f32_16x16x32_bf16 v[72:75], v[172:175], v[212:215], v[72:75]
	v_mfma_f32_16x16x32_bf16 v[64:67], v[180:183], v[212:215], v[64:67]
	v_mfma_f32_16x16x32_bf16 v[120:123], v[176:179], v[192:195], v[120:123]
	v_mfma_f32_16x16x32_bf16 v[112:115], v[184:187], v[192:195], v[112:115]
	v_mfma_f32_16x16x32_bf16 v[104:107], v[176:179], v[200:203], v[104:107]
	v_mfma_f32_16x16x32_bf16 v[96:99], v[184:187], v[200:203], v[96:99]
	v_mfma_f32_16x16x32_bf16 v[88:91], v[176:179], v[208:211], v[88:91]
	v_mfma_f32_16x16x32_bf16 v[80:83], v[184:187], v[208:211], v[80:83]
	v_mfma_f32_16x16x32_bf16 v[72:75], v[176:179], v[216:219], v[72:75]
	v_mfma_f32_16x16x32_bf16 v[64:67], v[184:187], v[216:219], v[64:67]
	s_setprio 0
	s_barrier
	s_add_i32 s28, s58, s33
	s_mov_b32 m0, s28
	s_nop 0
	global_load_lds_dwordx4 v132, s[98:99]
	s_add_i32 m0, s28, 0x2000
	s_add_u32 s26, s26, 0x40080
	s_addc_u32 s27, s27, 0
	s_add_i32 s28, s59, s33
	global_load_lds_dwordx4 v128, s[98:99]
	s_mov_b32 m0, s28
	s_nop 0
	global_load_lds_dwordx4 v132, s[26:27]
	s_add_i32 m0, s28, 0x2000
	s_nop 0
	global_load_lds_dwordx4 v128, s[26:27]
	s_mov_b32 m0, s40
	s_nop 0
	global_load_lds_dwordx4 v134, s[100:101]
	s_mov_b32 m0, s41
	s_nop 0
	global_load_lds_dwordx4 v130, s[100:101]
	ds_read_b128 v[188:191], v168 offset:49152
	ds_read_b128 v[192:195], v168 offset:50176
	ds_read_b128 v[196:199], v168 offset:51200
	ds_read_b128 v[200:203], v168 offset:52224
	ds_read_b128 v[204:207], v168 offset:53248
	ds_read_b128 v[208:211], v168 offset:54272
	ds_read_b128 v[212:215], v168 offset:55296
	ds_read_b128 v[216:219], v168 offset:56320
	s_waitcnt vmcnt(8) lgkmcnt(0)
	s_barrier
	s_setprio 1
	v_mfma_f32_16x16x32_bf16 v[60:63], v[148:151], v[188:191], v[60:63]
	v_mfma_f32_16x16x32_bf16 v[52:55], v[156:159], v[188:191], v[52:55]
	v_mfma_f32_16x16x32_bf16 v[44:47], v[148:151], v[196:199], v[44:47]
	v_mfma_f32_16x16x32_bf16 v[36:39], v[156:159], v[196:199], v[36:39]
	v_mfma_f32_16x16x32_bf16 v[28:31], v[148:151], v[204:207], v[28:31]
	v_mfma_f32_16x16x32_bf16 v[20:23], v[156:159], v[204:207], v[20:23]
	v_mfma_f32_16x16x32_bf16 v[12:15], v[148:151], v[212:215], v[12:15]
	v_mfma_f32_16x16x32_bf16 v[4:7], v[156:159], v[212:215], v[4:7]
	v_mfma_f32_16x16x32_bf16 v[60:63], v[152:155], v[192:195], v[60:63]
	v_mfma_f32_16x16x32_bf16 v[52:55], v[160:163], v[192:195], v[52:55]
	v_mfma_f32_16x16x32_bf16 v[44:47], v[152:155], v[200:203], v[44:47]
	v_mfma_f32_16x16x32_bf16 v[36:39], v[160:163], v[200:203], v[36:39]
	v_mfma_f32_16x16x32_bf16 v[28:31], v[152:155], v[208:211], v[28:31]
	v_mfma_f32_16x16x32_bf16 v[20:23], v[160:163], v[208:211], v[20:23]
	v_mfma_f32_16x16x32_bf16 v[12:15], v[152:155], v[216:219], v[12:15]
	v_mfma_f32_16x16x32_bf16 v[4:7], v[160:163], v[216:219], v[4:7]
	s_setprio 0
	s_setprio 1
	v_mfma_f32_16x16x32_bf16 v[56:59], v[172:175], v[188:191], v[56:59]
	v_mfma_f32_16x16x32_bf16 v[48:51], v[180:183], v[188:191], v[48:51]
	v_mfma_f32_16x16x32_bf16 v[40:43], v[172:175], v[196:199], v[40:43]
	v_mfma_f32_16x16x32_bf16 v[32:35], v[180:183], v[196:199], v[32:35]
	v_mfma_f32_16x16x32_bf16 v[24:27], v[172:175], v[204:207], v[24:27]
	v_mfma_f32_16x16x32_bf16 v[16:19], v[180:183], v[204:207], v[16:19]
	v_mfma_f32_16x16x32_bf16 v[8:11], v[172:175], v[212:215], v[8:11]
	v_mfma_f32_16x16x32_bf16 v[0:3], v[180:183], v[212:215], v[0:3]
	v_mfma_f32_16x16x32_bf16 v[56:59], v[176:179], v[192:195], v[56:59]
	v_mfma_f32_16x16x32_bf16 v[48:51], v[184:187], v[192:195], v[48:51]
	v_mfma_f32_16x16x32_bf16 v[40:43], v[176:179], v[200:203], v[40:43]
	v_mfma_f32_16x16x32_bf16 v[32:35], v[184:187], v[200:203], v[32:35]
	v_mfma_f32_16x16x32_bf16 v[24:27], v[176:179], v[208:211], v[24:27]
	v_mfma_f32_16x16x32_bf16 v[16:19], v[184:187], v[208:211], v[16:19]
	v_mfma_f32_16x16x32_bf16 v[8:11], v[176:179], v[216:219], v[8:11]
	v_mfma_f32_16x16x32_bf16 v[0:3], v[184:187], v[216:219], v[0:3]
	s_setprio 0
	s_barrier
	s_add_i32 s57, s57, 2
	s_add_u32 s24, s24, 0x100
	s_addc_u32 s25, s25, 0
	s_add_u32 s49, s49, 0x100
	s_addc_u32 s56, s56, 0
	s_cmp_gt_u32 s57, 13
	s_cbranch_scc0 .LBB0_2812
	s_and_b64 vcc, exec, s[12:13]
	s_cbranch_vccz .LBB0_2815
	s_barrier

; #define PG8_STAGE(bufoff, gbase, voff) do { _Pragma("unroll") for (int _i = 0; _i < 2; ++_i) \
;         __builtin_amdgcn_global_load_lds((const unsigned*)((const char*)(gbase) + (voff)[_i]), (PG8_LAS unsigned*)(lds + (bufoff) + ldsw + _i * 8192), 16, 0, 0); } while (0)
; #define PG8_LDA(dst, b, h) do { _Pragma("unroll") for (int m = 0; m < 4; ++m) _Pragma("unroll") for (int k = 0; k < 2; ++k) dst[m][k] = *(const PG8_LAS bf16x8*)(lds + PG8_SA(b, h) + aoff + m * 2048 + k * 1024); } while (0)
; #define PG8_LDB(dst, b, h) do { _Pragma("unroll") for (int n = 0; n < 2; ++n) _Pragma("unroll") for (int k = 0; k < 2; ++k) dst[n][k] = *(const PG8_LAS bf16x8*)(lds + PG8_SB(b, h) + boff + n * 2048 + k * 1024); } while (0)
; #define PG8_WAIT_V(n) asm volatile("s_waitcnt vmcnt(" #n ")" ::: "memory")
; #define PG8_WAIT_L(n) asm volatile("s_waitcnt lgkmcnt(" #n ")" ::: "memory")
; #define PG8_BAR __builtin_amdgcn_s_barrier()
; #define PG8_SCHED __builtin_amdgcn_sched_barrier(0)
; template <class Epi, class Sched, bool ALIGN_EPI = false, bool SP2 = false>
; __device__ __forceinline__ void gemm_phase(PG8_LAS unsigned char* lds, const Gemm g, const Sched& S, const Epi& E, const int wid) {
;     ...
;         const bool has_next = S.next(ui + 1, nxt);
;         const char* nA = has_next ? (const char*)g.A + (size_t)nxt.pm * tstepA : cA; const char* nB = has_next ? (const char*)g.Bt + (size_t)nxt.pn * tstepB : cB;
;         for (int t = 0; t < nt; t += 2) {
;             const bool last = (t == nt - 2);
;             const char* a1 = cA + (size_t)(t + 1) * kstep;
;             const char* a2 = last ? nA : cA + (size_t)(t + 2) * kstep; const char* b2 = last ? nB : cB + (size_t)(t + 2) * kstep;
;             const char* a3 = a2 + kstep; const char* b3 = b2 + kstep;
;             if (last && has_next) S.a_ready(nxt);
;             if constexpr (SP2) {
;             PG8_LDB(B0, 0, 0); PG8_LDB(B1, 0, 1); PG8_SCHED; PG8_LDA(At, 0, 0); PG8_STAGE(PG8_SA(1, 1), a1 + hstepA, voffA);
;             PG8_WAIT_V(8); PG8_WAIT_L(0); PG8_BAR; PG8_MMA(0, 0, At, B0); PG8_MMA(0, 1, At, B1); PG8_BAR; PG8_SCHED;
;             PG8_LDA(At, 0, 1); PG8_STAGE(PG8_SB(0, 0), b2, voffB); PG8_STAGE(PG8_SB(0, 1), b2 + hstepB, voffB); PG8_STAGE(PG8_SA(0, 0), a2, voffA);
;             PG8_WAIT_V(8); PG8_WAIT_L(0); PG8_BAR; PG8_MMA(1, 0, At, B0); PG8_MMA(1, 1, At, B1); PG8_BAR; PG8_SCHED;
.LBB0_2896:
	s_add_u32 s56, s24, 0x100
	s_addc_u32 s57, s25, 0
	s_mov_b32 s58, -2
	s_waitcnt lgkmcnt(0)
	v_add_u32_e32 v252, 0x18000, v189
	v_add_u32_e32 v253, 0x1c000, v189
	s_add_u32 s24, s22, 0x100
	s_addc_u32 s25, s23, 0
	s_cmp_eq_u32 s58, 40
	s_cselect_b32 s29, s7, s25
	s_cselect_b32 s28, s6, s24
	s_cselect_b32 s27, s21, s57
	s_cselect_b32 s26, s20, s56
	s_add_i32 m0, s34, 0xc000
	s_nop 0
	global_load_lds_dwordx4 v164, s[22:23]
	s_add_i32 m0, s34, 0xe000
	s_nop 0
	global_load_lds_dwordx4 v166, s[22:23]
	ds_read_b128 v[128:131], v190
	ds_read_b128 v[132:135], v190 offset:1024
	ds_read_b128 v[136:139], v190 offset:2048
	ds_read_b128 v[140:143], v190 offset:3072
	ds_read_b128 v[144:147], v191
	ds_read_b128 v[148:151], v191 offset:1024
	ds_read_b128 v[172:175], v191 offset:2048
	ds_read_b128 v[176:179], v191 offset:3072
	ds_read_b128 v[180:183], v192
	ds_read_b128 v[184:187], v192 offset:1024
	ds_read_b128 v[194:197], v192 offset:2048
	ds_read_b128 v[198:201], v192 offset:3072
	ds_read_b128 v[202:205], v192 offset:4096
	ds_read_b128 v[206:209], v192 offset:5120
	ds_read_b128 v[210:213], v192 offset:6144
	ds_read_b128 v[214:217], v192 offset:7168
	s_waitcnt vmcnt(8) lgkmcnt(0)
	s_barrier
	s_setprio 1
	v_mfma_f32_16x16x32_bf16 v[124:127], v[128:131], v[180:183], 0
	v_mfma_f32_16x16x32_bf16 v[120:123], v[136:139], v[180:183], 0
	v_mfma_f32_16x16x32_bf16 v[108:111], v[128:131], v[194:197], 0
	v_mfma_f32_16x16x32_bf16 v[104:107], v[136:139], v[194:197], 0
	v_mfma_f32_16x16x32_bf16 v[92:95], v[128:131], v[202:205], 0
	v_mfma_f32_16x16x32_bf16 v[88:91], v[136:139], v[202:205], 0
	v_mfma_f32_16x16x32_bf16 v[76:79], v[128:131], v[210:213], 0
	v_mfma_f32_16x16x32_bf16 v[72:75], v[136:139], v[210:213], 0
	v_mfma_f32_16x16x32_bf16 v[124:127], v[132:135], v[184:187], v[124:127]
	v_mfma_f32_16x16x32_bf16 v[120:123], v[140:143], v[184:187], v[120:123]
	v_mfma_f32_16x16x32_bf16 v[108:111], v[132:135], v[198:201], v[108:111]
	v_mfma_f32_16x16x32_bf16 v[104:107], v[140:143], v[198:201], v[104:107]
	v_mfma_f32_16x16x32_bf16 v[92:95], v[132:135], v[206:209], v[92:95]
	v_mfma_f32_16x16x32_bf16 v[88:91], v[140:143], v[206:209], v[88:91]
	v_mfma_f32_16x16x32_bf16 v[76:79], v[132:135], v[214:217], v[76:79]
	v_mfma_f32_16x16x32_bf16 v[72:75], v[140:143], v[214:217], v[72:75]
	s_setprio 0
	s_setprio 1
	v_mfma_f32_16x16x32_bf16 v[116:119], v[144:147], v[180:183], 0
	v_mfma_f32_16x16x32_bf16 v[112:115], v[172:175], v[180:183], 0
	v_mfma_f32_16x16x32_bf16 v[100:103], v[144:147], v[194:197], 0
	v_mfma_f32_16x16x32_bf16 v[96:99], v[172:175], v[194:197], 0
	v_mfma_f32_16x16x32_bf16 v[84:87], v[144:147], v[202:205], 0
	v_mfma_f32_16x16x32_bf16 v[80:83], v[172:175], v[202:205], 0
	v_mfma_f32_16x16x32_bf16 v[68:71], v[144:147], v[210:213], 0
	v_mfma_f32_16x16x32_bf16 v[64:67], v[172:175], v[210:213], 0
	v_mfma_f32_16x16x32_bf16 v[116:119], v[148:151], v[184:187], v[116:119]
	v_mfma_f32_16x16x32_bf16 v[112:115], v[176:179], v[184:187], v[112:115]
	v_mfma_f32_16x16x32_bf16 v[100:103], v[148:151], v[198:201], v[100:103]
	v_mfma_f32_16x16x32_bf16 v[96:99], v[176:179], v[198:201], v[96:99]
	v_mfma_f32_16x16x32_bf16 v[84:87], v[148:151], v[206:209], v[84:87]
	v_mfma_f32_16x16x32_bf16 v[80:83], v[176:179], v[206:209], v[80:83]
	v_mfma_f32_16x16x32_bf16 v[68:71], v[148:151], v[214:217], v[68:71]
	v_mfma_f32_16x16x32_bf16 v[64:67], v[176:179], v[214:217], v[64:67]
	s_setprio 0
	s_barrier
	s_add_i32 s22, s43, s33
	s_add_u32 s98, s26, 0x80
	s_addc_u32 s99, s27, 0
	s_mov_b32 m0, s22
	s_nop 0
	global_load_lds_dwordx4 v154, s[26:27]
	s_add_i32 m0, s22, 0x2000
	s_add_u32 s22, s26, 0xb0000
	s_addc_u32 s23, s27, 0
	s_add_i32 s59, s44, s33
	global_load_lds_dwordx4 v158, s[26:27]
	s_mov_b32 m0, s59
	s_add_u32 s100, s28, 0x80
	s_addc_u32 s101, s29, 0
	global_load_lds_dwordx4 v154, s[22:23]
	s_add_i32 m0, s59, 0x2000
	s_nop 0
	global_load_lds_dwordx4 v158, s[22:23]
	s_mov_b32 m0, s34
	s_nop 0
	global_load_lds_dwordx4 v152, s[28:29]
	s_mov_b32 m0, s35
	s_nop 0
	global_load_lds_dwordx4 v156, s[28:29]
	ds_read_b128 v[180:183], v192 offset:16384
	ds_read_b128 v[184:187], v192 offset:17408
	ds_read_b128 v[194:197], v192 offset:18432
	ds_read_b128 v[198:201], v192 offset:19456
	ds_read_b128 v[202:205], v192 offset:20480
	ds_read_b128 v[206:209], v192 offset:21504
	ds_read_b128 v[210:213], v192 offset:22528
	ds_read_b128 v[214:217], v192 offset:23552
	s_waitcnt vmcnt(8) lgkmcnt(0)
	s_barrier
	s_setprio 1
	v_mfma_f32_16x16x32_bf16 v[60:63], v[128:131], v[180:183], 0
	v_mfma_f32_16x16x32_bf16 v[56:59], v[136:139], v[180:183], 0
	v_mfma_f32_16x16x32_bf16 v[44:47], v[128:131], v[194:197], 0
	v_mfma_f32_16x16x32_bf16 v[40:43], v[136:139], v[194:197], 0
	v_mfma_f32_16x16x32_bf16 v[28:31], v[128:131], v[202:205], 0
	v_mfma_f32_16x16x32_bf16 v[24:27], v[136:139], v[202:205], 0
	v_mfma_f32_16x16x32_bf16 v[12:15], v[128:131], v[210:213], 0
	v_mfma_f32_16x16x32_bf16 v[8:11], v[136:139], v[210:213], 0
	v_mfma_f32_16x16x32_bf16 v[60:63], v[132:135], v[184:187], v[60:63]
	v_mfma_f32_16x16x32_bf16 v[56:59], v[140:143], v[184:187], v[56:59]
	v_mfma_f32_16x16x32_bf16 v[44:47], v[132:135], v[198:201], v[44:47]
	v_mfma_f32_16x16x32_bf16 v[40:43], v[140:143], v[198:201], v[40:43]
	v_mfma_f32_16x16x32_bf16 v[28:31], v[132:135], v[206:209], v[28:31]
	v_mfma_f32_16x16x32_bf16 v[24:27], v[140:143], v[206:209], v[24:27]
	v_mfma_f32_16x16x32_bf16 v[12:15], v[132:135], v[214:217], v[12:15]
	v_mfma_f32_16x16x32_bf16 v[8:11], v[140:143], v[214:217], v[8:11]
	s_setprio 0
	s_setprio 1
	v_mfma_f32_16x16x32_bf16 v[52:55], v[144:147], v[180:183], 0
	v_mfma_f32_16x16x32_bf16 v[48:51], v[172:175], v[180:183], 0
	v_mfma_f32_16x16x32_bf16 v[36:39], v[144:147], v[194:197], 0
	v_mfma_f32_16x16x32_bf16 v[32:35], v[172:175], v[194:197], 0
	v_mfma_f32_16x16x32_bf16 v[20:23], v[144:147], v[202:205], 0
	v_mfma_f32_16x16x32_bf16 v[16:19], v[172:175], v[202:205], 0
	v_mfma_f32_16x16x32_bf16 v[4:7], v[144:147], v[210:213], 0
	v_mfma_f32_16x16x32_bf16 v[0:3], v[172:175], v[210:213], 0
	v_mfma_f32_16x16x32_bf16 v[52:55], v[148:151], v[184:187], v[52:55]
	v_mfma_f32_16x16x32_bf16 v[48:51], v[176:179], v[184:187], v[48:51]
	v_mfma_f32_16x16x32_bf16 v[36:39], v[148:151], v[198:201], v[36:39]
	v_mfma_f32_16x16x32_bf16 v[32:35], v[176:179], v[198:201], v[32:35]
	v_mfma_f32_16x16x32_bf16 v[20:23], v[148:151], v[206:209], v[20:23]
	v_mfma_f32_16x16x32_bf16 v[16:19], v[176:179], v[206:209], v[16:19]
	v_mfma_f32_16x16x32_bf16 v[4:7], v[148:151], v[214:217], v[4:7]
	v_mfma_f32_16x16x32_bf16 v[0:3], v[176:179], v[214:217], v[0:3]
	s_setprio 0
	s_barrier
; #define PG8_STAGE(bufoff, gbase, voff) do { _Pragma("unroll") for (int _i = 0; _i < 2; ++_i) \
;         __builtin_amdgcn_global_load_lds((const unsigned*)((const char*)(gbase) + (voff)[_i]), (PG8_LAS unsigned*)(lds + (bufoff) + ldsw + _i * 8192), 16, 0, 0); } while (0)
; #define PG8_LDA(dst, b, h) do { _Pragma("unroll") for (int m = 0; m < 4; ++m) _Pragma("unroll") for (int k = 0; k < 2; ++k) dst[m][k] = *(const PG8_LAS bf16x8*)(lds + PG8_SA(b, h) + aoff + m * 2048 + k * 1024); } while (0)
; #define PG8_LDB(dst, b, h) do { _Pragma("unroll") for (int n = 0; n < 2; ++n) _Pragma("unroll") for (int k = 0; k < 2; ++k) dst[n][k] = *(const PG8_LAS bf16x8*)(lds + PG8_SB(b, h) + boff + n * 2048 + k * 1024); } while (0)
; #define PG8_MMA(ai, bj, At, Bt) do { __builtin_amdgcn_s_setprio(1); _Pragma("unroll") for (int m = 0; m < 4; ++m) _Pragma("unroll") for (int n = 0; n < 2; ++n) _Pragma("unroll") for (int k = 0; k < 2; ++k) \
;         acc[ai][bj][m][n] = __builtin_amdgcn_mfma_f32_16x16x32_bf16(Bt[n][k], At[m][k], acc[ai][bj][m][n], 0, 0, 0); __builtin_amdgcn_s_setprio(0); } while (0)
; #define PG8_WAIT_V(n) asm volatile("s_waitcnt vmcnt(" #n ")" ::: "memory")
; #define PG8_WAIT_L(n) asm volatile("s_waitcnt lgkmcnt(" #n ")" ::: "memory")
; #define PG8_BAR __builtin_amdgcn_s_barrier()
; #define PG8_SCHED __builtin_amdgcn_sched_barrier(0)
; template <class Epi, class Sched, bool ALIGN_EPI = false, bool SP2 = false>
; __device__ __forceinline__ void gemm_phase(PG8_LAS unsigned char* lds, const Gemm g, const Sched& S, const Epi& E, const int wid) {
;     ...
;             PG8_LDB(B0, 1, 0); PG8_LDB(B1, 1, 1); PG8_SCHED; PG8_LDA(At, 1, 0); PG8_STAGE(PG8_SA(0, 1), a2 + hstepA, voffA);
;             PG8_WAIT_V(8); PG8_WAIT_L(0); PG8_BAR; PG8_MMA(0, 0, At, B0); PG8_MMA(0, 1, At, B1); PG8_BAR; PG8_SCHED;
;             PG8_LDA(At, 1, 1); PG8_STAGE(PG8_SB(1, 0), b3, voffB); PG8_STAGE(PG8_SB(1, 1), b3 + hstepB, voffB); PG8_STAGE(PG8_SA(1, 0), a3, voffA);
;             PG8_WAIT_V(8); PG8_WAIT_L(0); PG8_BAR; PG8_MMA(1, 0, At, B0); PG8_MMA(1, 1, At, B1); PG8_BAR; PG8_SCHED;
	s_add_i32 s59, 0, 0x18000
	s_add_i32 s60, 0, 0x1c000
	s_add_u32 s22, s28, 0xb0000
	s_addc_u32 s23, s29, 0
	s_mov_b32 m0, s36
	s_nop 0
	global_load_lds_dwordx4 v152, s[22:23]
	s_mov_b32 m0, s37
	s_nop 0
	global_load_lds_dwordx4 v156, s[22:23]
	ds_read_b128 v[128:131], v252
	ds_read_b128 v[132:135], v252 offset:1024
	ds_read_b128 v[136:139], v252 offset:2048
	ds_read_b128 v[140:143], v252 offset:3072
	ds_read_b128 v[144:147], v253
	ds_read_b128 v[148:151], v253 offset:1024
	ds_read_b128 v[172:175], v253 offset:2048
	ds_read_b128 v[176:179], v253 offset:3072
	ds_read_b128 v[180:183], v192 offset:32768
	ds_read_b128 v[184:187], v192 offset:33792
	ds_read_b128 v[194:197], v192 offset:34816
	ds_read_b128 v[198:201], v192 offset:35840
	ds_read_b128 v[202:205], v192 offset:36864
	ds_read_b128 v[206:209], v192 offset:37888
	ds_read_b128 v[210:213], v192 offset:38912
	ds_read_b128 v[214:217], v192 offset:39936
	s_waitcnt vmcnt(8) lgkmcnt(0)
	s_barrier
	s_setprio 1
	v_mfma_f32_16x16x32_bf16 v[124:127], v[128:131], v[180:183], v[124:127]
	v_mfma_f32_16x16x32_bf16 v[120:123], v[136:139], v[180:183], v[120:123]
	v_mfma_f32_16x16x32_bf16 v[108:111], v[128:131], v[194:197], v[108:111]
	v_mfma_f32_16x16x32_bf16 v[104:107], v[136:139], v[194:197], v[104:107]
	v_mfma_f32_16x16x32_bf16 v[92:95], v[128:131], v[202:205], v[92:95]
	v_mfma_f32_16x16x32_bf16 v[88:91], v[136:139], v[202:205], v[88:91]
	v_mfma_f32_16x16x32_bf16 v[76:79], v[128:131], v[210:213], v[76:79]
	v_mfma_f32_16x16x32_bf16 v[72:75], v[136:139], v[210:213], v[72:75]
	v_mfma_f32_16x16x32_bf16 v[124:127], v[132:135], v[184:187], v[124:127]
	v_mfma_f32_16x16x32_bf16 v[120:123], v[140:143], v[184:187], v[120:123]
	v_mfma_f32_16x16x32_bf16 v[108:111], v[132:135], v[198:201], v[108:111]
	v_mfma_f32_16x16x32_bf16 v[104:107], v[140:143], v[198:201], v[104:107]
	v_mfma_f32_16x16x32_bf16 v[92:95], v[132:135], v[206:209], v[92:95]
	v_mfma_f32_16x16x32_bf16 v[88:91], v[140:143], v[206:209], v[88:91]
	v_mfma_f32_16x16x32_bf16 v[76:79], v[132:135], v[214:217], v[76:79]
	v_mfma_f32_16x16x32_bf16 v[72:75], v[140:143], v[214:217], v[72:75]
	s_setprio 0
	s_setprio 1
	v_mfma_f32_16x16x32_bf16 v[116:119], v[144:147], v[180:183], v[116:119]
	v_mfma_f32_16x16x32_bf16 v[112:115], v[172:175], v[180:183], v[112:115]
	v_mfma_f32_16x16x32_bf16 v[100:103], v[144:147], v[194:197], v[100:103]
	v_mfma_f32_16x16x32_bf16 v[96:99], v[172:175], v[194:197], v[96:99]
	v_mfma_f32_16x16x32_bf16 v[84:87], v[144:147], v[202:205], v[84:87]
	v_mfma_f32_16x16x32_bf16 v[80:83], v[172:175], v[202:205], v[80:83]
	v_mfma_f32_16x16x32_bf16 v[68:71], v[144:147], v[210:213], v[68:71]
	v_mfma_f32_16x16x32_bf16 v[64:67], v[172:175], v[210:213], v[64:67]
	v_mfma_f32_16x16x32_bf16 v[116:119], v[148:151], v[184:187], v[116:119]
	v_mfma_f32_16x16x32_bf16 v[112:115], v[176:179], v[184:187], v[112:115]
	v_mfma_f32_16x16x32_bf16 v[100:103], v[148:151], v[198:201], v[100:103]
	v_mfma_f32_16x16x32_bf16 v[96:99], v[176:179], v[198:201], v[96:99]
	v_mfma_f32_16x16x32_bf16 v[84:87], v[148:151], v[206:209], v[84:87]
	v_mfma_f32_16x16x32_bf16 v[80:83], v[176:179], v[206:209], v[80:83]
	v_mfma_f32_16x16x32_bf16 v[68:71], v[148:151], v[214:217], v[68:71]
	v_mfma_f32_16x16x32_bf16 v[64:67], v[176:179], v[214:217], v[64:67]
	s_setprio 0
	s_barrier
	s_add_i32 s22, s59, s33
	s_mov_b32 m0, s22
	s_nop 0
	global_load_lds_dwordx4 v154, s[98:99]
	s_add_i32 m0, s22, 0x2000
	s_add_u32 s22, s26, 0xb0080
	s_addc_u32 s23, s27, 0
	s_add_i32 s26, s60, s33
	global_load_lds_dwordx4 v158, s[98:99]
	s_mov_b32 m0, s26
	s_nop 0
	global_load_lds_dwordx4 v154, s[22:23]
	s_add_i32 m0, s26, 0x2000
	s_nop 0
	global_load_lds_dwordx4 v158, s[22:23]
	s_mov_b32 m0, s39
	s_nop 0
	global_load_lds_dwordx4 v152, s[100:101]
	s_mov_b32 m0, s40
	s_nop 0
	global_load_lds_dwordx4 v156, s[100:101]
	ds_read_b128 v[180:183], v192 offset:49152
	ds_read_b128 v[184:187], v192 offset:50176
	ds_read_b128 v[194:197], v192 offset:51200
	ds_read_b128 v[198:201], v192 offset:52224
	ds_read_b128 v[202:205], v192 offset:53248
	ds_read_b128 v[206:209], v192 offset:54272
	ds_read_b128 v[210:213], v192 offset:55296
	ds_read_b128 v[214:217], v192 offset:56320
	s_waitcnt vmcnt(8) lgkmcnt(0)
	s_barrier
	s_setprio 1
	v_mfma_f32_16x16x32_bf16 v[60:63], v[128:131], v[180:183], v[60:63]
	v_mfma_f32_16x16x32_bf16 v[56:59], v[136:139], v[180:183], v[56:59]
	v_mfma_f32_16x16x32_bf16 v[44:47], v[128:131], v[194:197], v[44:47]
	v_mfma_f32_16x16x32_bf16 v[40:43], v[136:139], v[194:197], v[40:43]
	v_mfma_f32_16x16x32_bf16 v[28:31], v[128:131], v[202:205], v[28:31]
	v_mfma_f32_16x16x32_bf16 v[24:27], v[136:139], v[202:205], v[24:27]
	v_mfma_f32_16x16x32_bf16 v[12:15], v[128:131], v[210:213], v[12:15]
	v_mfma_f32_16x16x32_bf16 v[8:11], v[136:139], v[210:213], v[8:11]
	v_mfma_f32_16x16x32_bf16 v[60:63], v[132:135], v[184:187], v[60:63]
	v_mfma_f32_16x16x32_bf16 v[56:59], v[140:143], v[184:187], v[56:59]
	v_mfma_f32_16x16x32_bf16 v[44:47], v[132:135], v[198:201], v[44:47]
	v_mfma_f32_16x16x32_bf16 v[40:43], v[140:143], v[198:201], v[40:43]
	v_mfma_f32_16x16x32_bf16 v[28:31], v[132:135], v[206:209], v[28:31]
	v_mfma_f32_16x16x32_bf16 v[24:27], v[140:143], v[206:209], v[24:27]
	v_mfma_f32_16x16x32_bf16 v[12:15], v[132:135], v[214:217], v[12:15]
	v_mfma_f32_16x16x32_bf16 v[8:11], v[140:143], v[214:217], v[8:11]
	s_setprio 0
	s_setprio 1
	v_mfma_f32_16x16x32_bf16 v[52:55], v[144:147], v[180:183], v[52:55]
	v_mfma_f32_16x16x32_bf16 v[48:51], v[172:175], v[180:183], v[48:51]
	v_mfma_f32_16x16x32_bf16 v[36:39], v[144:147], v[194:197], v[36:39]
	v_mfma_f32_16x16x32_bf16 v[32:35], v[172:175], v[194:197], v[32:35]
	v_mfma_f32_16x16x32_bf16 v[20:23], v[144:147], v[202:205], v[20:23]
	v_mfma_f32_16x16x32_bf16 v[16:19], v[172:175], v[202:205], v[16:19]
	v_mfma_f32_16x16x32_bf16 v[4:7], v[144:147], v[210:213], v[4:7]
	v_mfma_f32_16x16x32_bf16 v[0:3], v[172:175], v[210:213], v[0:3]
	v_mfma_f32_16x16x32_bf16 v[52:55], v[148:151], v[184:187], v[52:55]
	v_mfma_f32_16x16x32_bf16 v[48:51], v[176:179], v[184:187], v[48:51]
	v_mfma_f32_16x16x32_bf16 v[36:39], v[148:151], v[198:201], v[36:39]
	v_mfma_f32_16x16x32_bf16 v[32:35], v[176:179], v[198:201], v[32:35]
	v_mfma_f32_16x16x32_bf16 v[20:23], v[148:151], v[206:209], v[20:23]
	v_mfma_f32_16x16x32_bf16 v[16:19], v[176:179], v[206:209], v[16:19]
	v_mfma_f32_16x16x32_bf16 v[4:7], v[148:151], v[214:217], v[4:7]
	v_mfma_f32_16x16x32_bf16 v[0:3], v[176:179], v[214:217], v[0:3]
	s_setprio 0
	s_barrier
	s_add_i32 s58, s58, 2
	s_add_u32 s56, s56, 0x100
	s_addc_u32 s57, s57, 0
	s_cmp_gt_u32 s58, 41
	s_mov_b64 s[22:23], s[24:25]
; #define PG8_STAGE(bufoff, gbase, voff) do { _Pragma("unroll") for (int _i = 0; _i < 2; ++_i) \
;         __builtin_amdgcn_global_load_lds((const unsigned*)((const char*)(gbase) + (voff)[_i]), (PG8_LAS unsigned*)(lds + (bufoff) + ldsw + _i * 8192), 16, 0, 0); } while (0)
; #define PG8_LDA(dst, b, h) do { _Pragma("unroll") for (int m = 0; m < 4; ++m) _Pragma("unroll") for (int k = 0; k < 2; ++k) dst[m][k] = *(const PG8_LAS bf16x8*)(lds + PG8_SA(b, h) + aoff + m * 2048 + k * 1024); } while (0)
; #define PG8_LDB(dst, b, h) do { _Pragma("unroll") for (int n = 0; n < 2; ++n) _Pragma("unroll") for (int k = 0; k < 2; ++k) dst[n][k] = *(const PG8_LAS bf16x8*)(lds + PG8_SB(b, h) + boff + n * 2048 + k * 1024); } while (0)
; #define PG8_MMA(ai, bj, At, Bt) do { __builtin_amdgcn_s_setprio(1); _Pragma("unroll") for (int m = 0; m < 4; ++m) _Pragma("unroll") for (int n = 0; n < 2; ++n) _Pragma("unroll") for (int k = 0; k < 2; ++k) \
;         acc[ai][bj][m][n] = __builtin_amdgcn_mfma_f32_16x16x32_bf16(Bt[n][k], At[m][k], acc[ai][bj][m][n], 0, 0, 0); __builtin_amdgcn_s_setprio(0); } while (0)
; #define PG8_WAIT_V(n) asm volatile("s_waitcnt vmcnt(" #n ")" ::: "memory")
; #define PG8_BAR __builtin_amdgcn_s_barrier()
; template <class Epi, class Sched, bool ALIGN_EPI = false, bool SP2 = false>
; __device__ __forceinline__ void gemm_phase(PG8_LAS unsigned char* lds, const Gemm g, const Sched& S, const Epi& E, const int wid) {
;     ...
;         for (int t = 0; t < nt; t += 2) {
;             const bool last = (t == nt - 2);
;             const char* a1 = cA + (size_t)(t + 1) * kstep;
;             const char* a2 = last ? nA : cA + (size_t)(t + 2) * kstep; const char* b2 = last ? nB : cB + (size_t)(t + 2) * kstep;
;             const char* a3 = a2 + kstep; const char* b3 = b2 + kstep;
;             if (last && has_next) S.a_ready(nxt);
;             if constexpr (SP2) {
;             PG8_LDB(B0, 0, 0); PG8_LDB(B1, 0, 1); PG8_SCHED; PG8_LDA(At, 0, 0); PG8_STAGE(PG8_SA(1, 1), a1 + hstepA, voffA);
;             PG8_WAIT_V(8); PG8_WAIT_L(0); PG8_BAR; PG8_MMA(0, 0, At, B0); PG8_MMA(0, 1, At, B1); PG8_BAR; PG8_SCHED;
;             PG8_LDA(At, 0, 1); PG8_STAGE(PG8_SB(0, 0), b2, voffB); PG8_STAGE(PG8_SB(0, 1), b2 + hstepB, voffB); PG8_STAGE(PG8_SA(0, 0), a2, voffA);
;             PG8_WAIT_V(8); PG8_WAIT_L(0); PG8_BAR; PG8_MMA(1, 0, At, B0); PG8_MMA(1, 1, At, B1); PG8_BAR; PG8_SCHED;
.LBB0_2897:
	s_add_u32 s24, s22, 0x100
	s_addc_u32 s25, s23, 0
	s_cmp_eq_u32 s58, 40
	s_cselect_b32 s29, s7, s25
	s_cselect_b32 s28, s6, s24
	s_cselect_b32 s27, s21, s57
	s_cselect_b32 s26, s20, s56
	s_add_i32 m0, s34, 0xc000
	s_nop 0
	global_load_lds_dwordx4 v164, s[22:23]
	s_add_i32 m0, s34, 0xe000
	s_nop 0
	global_load_lds_dwordx4 v166, s[22:23]
	ds_read_b128 v[128:131], v190
	ds_read_b128 v[132:135], v190 offset:1024
	ds_read_b128 v[136:139], v190 offset:2048
	ds_read_b128 v[140:143], v190 offset:3072
	ds_read_b128 v[144:147], v191
	ds_read_b128 v[148:151], v191 offset:1024
	ds_read_b128 v[172:175], v191 offset:2048
	ds_read_b128 v[176:179], v191 offset:3072
	ds_read_b128 v[180:183], v192
	ds_read_b128 v[184:187], v192 offset:1024
	ds_read_b128 v[194:197], v192 offset:2048
	ds_read_b128 v[198:201], v192 offset:3072
	ds_read_b128 v[202:205], v192 offset:4096
	ds_read_b128 v[206:209], v192 offset:5120
	ds_read_b128 v[210:213], v192 offset:6144
	ds_read_b128 v[214:217], v192 offset:7168
	s_waitcnt vmcnt(8) lgkmcnt(0)
	s_barrier
	s_setprio 1
	v_mfma_f32_16x16x32_bf16 v[124:127], v[128:131], v[180:183], v[124:127]
	v_mfma_f32_16x16x32_bf16 v[120:123], v[136:139], v[180:183], v[120:123]
	v_mfma_f32_16x16x32_bf16 v[108:111], v[128:131], v[194:197], v[108:111]
	v_mfma_f32_16x16x32_bf16 v[104:107], v[136:139], v[194:197], v[104:107]
	v_mfma_f32_16x16x32_bf16 v[92:95], v[128:131], v[202:205], v[92:95]
	v_mfma_f32_16x16x32_bf16 v[88:91], v[136:139], v[202:205], v[88:91]
	v_mfma_f32_16x16x32_bf16 v[76:79], v[128:131], v[210:213], v[76:79]
	v_mfma_f32_16x16x32_bf16 v[72:75], v[136:139], v[210:213], v[72:75]
	v_mfma_f32_16x16x32_bf16 v[124:127], v[132:135], v[184:187], v[124:127]
	v_mfma_f32_16x16x32_bf16 v[120:123], v[140:143], v[184:187], v[120:123]
	v_mfma_f32_16x16x32_bf16 v[108:111], v[132:135], v[198:201], v[108:111]
	v_mfma_f32_16x16x32_bf16 v[104:107], v[140:143], v[198:201], v[104:107]
	v_mfma_f32_16x16x32_bf16 v[92:95], v[132:135], v[206:209], v[92:95]
	v_mfma_f32_16x16x32_bf16 v[88:91], v[140:143], v[206:209], v[88:91]
	v_mfma_f32_16x16x32_bf16 v[76:79], v[132:135], v[214:217], v[76:79]
	v_mfma_f32_16x16x32_bf16 v[72:75], v[140:143], v[214:217], v[72:75]
	s_setprio 0
	s_setprio 1
	v_mfma_f32_16x16x32_bf16 v[116:119], v[144:147], v[180:183], v[116:119]
	v_mfma_f32_16x16x32_bf16 v[112:115], v[172:175], v[180:183], v[112:115]
	v_mfma_f32_16x16x32_bf16 v[100:103], v[144:147], v[194:197], v[100:103]
	v_mfma_f32_16x16x32_bf16 v[96:99], v[172:175], v[194:197], v[96:99]
	v_mfma_f32_16x16x32_bf16 v[84:87], v[144:147], v[202:205], v[84:87]
	v_mfma_f32_16x16x32_bf16 v[80:83], v[172:175], v[202:205], v[80:83]
	v_mfma_f32_16x16x32_bf16 v[68:71], v[144:147], v[210:213], v[68:71]
	v_mfma_f32_16x16x32_bf16 v[64:67], v[172:175], v[210:213], v[64:67]
	v_mfma_f32_16x16x32_bf16 v[116:119], v[148:151], v[184:187], v[116:119]
	v_mfma_f32_16x16x32_bf16 v[112:115], v[176:179], v[184:187], v[112:115]
	v_mfma_f32_16x16x32_bf16 v[100:103], v[148:151], v[198:201], v[100:103]
	v_mfma_f32_16x16x32_bf16 v[96:99], v[176:179], v[198:201], v[96:99]
	v_mfma_f32_16x16x32_bf16 v[84:87], v[148:151], v[206:209], v[84:87]
	v_mfma_f32_16x16x32_bf16 v[80:83], v[176:179], v[206:209], v[80:83]
	v_mfma_f32_16x16x32_bf16 v[68:71], v[148:151], v[214:217], v[68:71]
	v_mfma_f32_16x16x32_bf16 v[64:67], v[176:179], v[214:217], v[64:67]
	s_setprio 0
	s_barrier
	s_add_i32 s22, s43, s33
	s_add_u32 s98, s26, 0x80
	s_addc_u32 s99, s27, 0
	s_mov_b32 m0, s22
	s_nop 0
	global_load_lds_dwordx4 v154, s[26:27]
	s_add_i32 m0, s22, 0x2000
	s_add_u32 s22, s26, 0xb0000
	s_addc_u32 s23, s27, 0
	s_add_i32 s59, s44, s33
	global_load_lds_dwordx4 v158, s[26:27]
	s_mov_b32 m0, s59
	s_add_u32 s100, s28, 0x80
	s_addc_u32 s101, s29, 0
	global_load_lds_dwordx4 v154, s[22:23]
	s_add_i32 m0, s59, 0x2000
	s_nop 0
	global_load_lds_dwordx4 v158, s[22:23]
	s_mov_b32 m0, s34
	s_nop 0
	global_load_lds_dwordx4 v152, s[28:29]
	s_mov_b32 m0, s35
	s_nop 0
	global_load_lds_dwordx4 v156, s[28:29]
	ds_read_b128 v[180:183], v192 offset:16384
	ds_read_b128 v[184:187], v192 offset:17408
	ds_read_b128 v[194:197], v192 offset:18432
	ds_read_b128 v[198:201], v192 offset:19456
	ds_read_b128 v[202:205], v192 offset:20480
	ds_read_b128 v[206:209], v192 offset:21504
	ds_read_b128 v[210:213], v192 offset:22528
	ds_read_b128 v[214:217], v192 offset:23552
	s_waitcnt vmcnt(8) lgkmcnt(0)
	s_barrier
	s_setprio 1
	v_mfma_f32_16x16x32_bf16 v[60:63], v[128:131], v[180:183], v[60:63]
	v_mfma_f32_16x16x32_bf16 v[56:59], v[136:139], v[180:183], v[56:59]
	v_mfma_f32_16x16x32_bf16 v[44:47], v[128:131], v[194:197], v[44:47]
	v_mfma_f32_16x16x32_bf16 v[40:43], v[136:139], v[194:197], v[40:43]
	v_mfma_f32_16x16x32_bf16 v[28:31], v[128:131], v[202:205], v[28:31]
	v_mfma_f32_16x16x32_bf16 v[24:27], v[136:139], v[202:205], v[24:27]
	v_mfma_f32_16x16x32_bf16 v[12:15], v[128:131], v[210:213], v[12:15]
	v_mfma_f32_16x16x32_bf16 v[8:11], v[136:139], v[210:213], v[8:11]
	v_mfma_f32_16x16x32_bf16 v[60:63], v[132:135], v[184:187], v[60:63]
	v_mfma_f32_16x16x32_bf16 v[56:59], v[140:143], v[184:187], v[56:59]
	v_mfma_f32_16x16x32_bf16 v[44:47], v[132:135], v[198:201], v[44:47]
	v_mfma_f32_16x16x32_bf16 v[40:43], v[140:143], v[198:201], v[40:43]
	v_mfma_f32_16x16x32_bf16 v[28:31], v[132:135], v[206:209], v[28:31]
	v_mfma_f32_16x16x32_bf16 v[24:27], v[140:143], v[206:209], v[24:27]
	v_mfma_f32_16x16x32_bf16 v[12:15], v[132:135], v[214:217], v[12:15]
	v_mfma_f32_16x16x32_bf16 v[8:11], v[140:143], v[214:217], v[8:11]
	s_setprio 0
	s_setprio 1
	v_mfma_f32_16x16x32_bf16 v[52:55], v[144:147], v[180:183], v[52:55]
	v_mfma_f32_16x16x32_bf16 v[48:51], v[172:175], v[180:183], v[48:51]
	v_mfma_f32_16x16x32_bf16 v[36:39], v[144:147], v[194:197], v[36:39]
	v_mfma_f32_16x16x32_bf16 v[32:35], v[172:175], v[194:197], v[32:35]
	v_mfma_f32_16x16x32_bf16 v[20:23], v[144:147], v[202:205], v[20:23]
	v_mfma_f32_16x16x32_bf16 v[16:19], v[172:175], v[202:205], v[16:19]
	v_mfma_f32_16x16x32_bf16 v[4:7], v[144:147], v[210:213], v[4:7]
	v_mfma_f32_16x16x32_bf16 v[0:3], v[172:175], v[210:213], v[0:3]
	v_mfma_f32_16x16x32_bf16 v[52:55], v[148:151], v[184:187], v[52:55]
	v_mfma_f32_16x16x32_bf16 v[48:51], v[176:179], v[184:187], v[48:51]
	v_mfma_f32_16x16x32_bf16 v[36:39], v[148:151], v[198:201], v[36:39]
	v_mfma_f32_16x16x32_bf16 v[32:35], v[176:179], v[198:201], v[32:35]
	v_mfma_f32_16x16x32_bf16 v[20:23], v[148:151], v[206:209], v[20:23]
	v_mfma_f32_16x16x32_bf16 v[16:19], v[176:179], v[206:209], v[16:19]
	v_mfma_f32_16x16x32_bf16 v[4:7], v[148:151], v[214:217], v[4:7]
	v_mfma_f32_16x16x32_bf16 v[0:3], v[176:179], v[214:217], v[0:3]
	s_setprio 0
	s_barrier
; #define PG8_STAGE(bufoff, gbase, voff) do { _Pragma("unroll") for (int _i = 0; _i < 2; ++_i) \
;         __builtin_amdgcn_global_load_lds((const unsigned*)((const char*)(gbase) + (voff)[_i]), (PG8_LAS unsigned*)(lds + (bufoff) + ldsw + _i * 8192), 16, 0, 0); } while (0)
; #define PG8_LDA(dst, b, h) do { _Pragma("unroll") for (int m = 0; m < 4; ++m) _Pragma("unroll") for (int k = 0; k < 2; ++k) dst[m][k] = *(const PG8_LAS bf16x8*)(lds + PG8_SA(b, h) + aoff + m * 2048 + k * 1024); } while (0)
; #define PG8_LDB(dst, b, h) do { _Pragma("unroll") for (int n = 0; n < 2; ++n) _Pragma("unroll") for (int k = 0; k < 2; ++k) dst[n][k] = *(const PG8_LAS bf16x8*)(lds + PG8_SB(b, h) + boff + n * 2048 + k * 1024); } while (0)
; #define PG8_MMA(ai, bj, At, Bt) do { __builtin_amdgcn_s_setprio(1); _Pragma("unroll") for (int m = 0; m < 4; ++m) _Pragma("unroll") for (int n = 0; n < 2; ++n) _Pragma("unroll") for (int k = 0; k < 2; ++k) \
;         acc[ai][bj][m][n] = __builtin_amdgcn_mfma_f32_16x16x32_bf16(Bt[n][k], At[m][k], acc[ai][bj][m][n], 0, 0, 0); __builtin_amdgcn_s_setprio(0); } while (0)
; #define PG8_WAIT_V(n) asm volatile("s_waitcnt vmcnt(" #n ")" ::: "memory")
; #define PG8_WAIT_L(n) asm volatile("s_waitcnt lgkmcnt(" #n ")" ::: "memory")
; #define PG8_BAR __builtin_amdgcn_s_barrier()
; #define PG8_SCHED __builtin_amdgcn_sched_barrier(0)
; template <class Epi, class Sched, bool ALIGN_EPI = false, bool SP2 = false>
; __device__ __forceinline__ void gemm_phase(PG8_LAS unsigned char* lds, const Gemm g, const Sched& S, const Epi& E, const int wid) {
;     ...
;             PG8_LDB(B0, 1, 0); PG8_LDB(B1, 1, 1); PG8_SCHED; PG8_LDA(At, 1, 0); PG8_STAGE(PG8_SA(0, 1), a2 + hstepA, voffA);
;             PG8_WAIT_V(8); PG8_WAIT_L(0); PG8_BAR; PG8_MMA(0, 0, At, B0); PG8_MMA(0, 1, At, B1); PG8_BAR; PG8_SCHED;
;             PG8_LDA(At, 1, 1); PG8_STAGE(PG8_SB(1, 0), b3, voffB); PG8_STAGE(PG8_SB(1, 1), b3 + hstepB, voffB); PG8_STAGE(PG8_SA(1, 0), a3, voffA);
;             PG8_WAIT_V(8); PG8_WAIT_L(0); PG8_BAR; PG8_MMA(1, 0, At, B0); PG8_MMA(1, 1, At, B1); PG8_BAR; PG8_SCHED;
;     ...
;         if constexpr (ALIGN_EPI) { if (wr == 0) PG8_BAR; }
	s_add_i32 s59, 0, 0x18000
	s_add_i32 s60, 0, 0x1c000
	s_add_u32 s22, s28, 0xb0000
	s_addc_u32 s23, s29, 0
	s_mov_b32 m0, s36
	s_nop 0
	global_load_lds_dwordx4 v152, s[22:23]
	s_mov_b32 m0, s37
	s_nop 0
	global_load_lds_dwordx4 v156, s[22:23]
	ds_read_b128 v[128:131], v252
	ds_read_b128 v[132:135], v252 offset:1024
	ds_read_b128 v[136:139], v252 offset:2048
	ds_read_b128 v[140:143], v252 offset:3072
	ds_read_b128 v[144:147], v253
	ds_read_b128 v[148:151], v253 offset:1024
	ds_read_b128 v[172:175], v253 offset:2048
	ds_read_b128 v[176:179], v253 offset:3072
	ds_read_b128 v[180:183], v192 offset:32768
	ds_read_b128 v[184:187], v192 offset:33792
	ds_read_b128 v[194:197], v192 offset:34816
	ds_read_b128 v[198:201], v192 offset:35840
	ds_read_b128 v[202:205], v192 offset:36864
	ds_read_b128 v[206:209], v192 offset:37888
	ds_read_b128 v[210:213], v192 offset:38912
	ds_read_b128 v[214:217], v192 offset:39936
	s_waitcnt vmcnt(8) lgkmcnt(0)
	s_barrier
	s_setprio 1
	v_mfma_f32_16x16x32_bf16 v[124:127], v[128:131], v[180:183], v[124:127]
	v_mfma_f32_16x16x32_bf16 v[120:123], v[136:139], v[180:183], v[120:123]
	v_mfma_f32_16x16x32_bf16 v[108:111], v[128:131], v[194:197], v[108:111]
	v_mfma_f32_16x16x32_bf16 v[104:107], v[136:139], v[194:197], v[104:107]
	v_mfma_f32_16x16x32_bf16 v[92:95], v[128:131], v[202:205], v[92:95]
	v_mfma_f32_16x16x32_bf16 v[88:91], v[136:139], v[202:205], v[88:91]
	v_mfma_f32_16x16x32_bf16 v[76:79], v[128:131], v[210:213], v[76:79]
	v_mfma_f32_16x16x32_bf16 v[72:75], v[136:139], v[210:213], v[72:75]
	v_mfma_f32_16x16x32_bf16 v[124:127], v[132:135], v[184:187], v[124:127]
	v_mfma_f32_16x16x32_bf16 v[120:123], v[140:143], v[184:187], v[120:123]
	v_mfma_f32_16x16x32_bf16 v[108:111], v[132:135], v[198:201], v[108:111]
	v_mfma_f32_16x16x32_bf16 v[104:107], v[140:143], v[198:201], v[104:107]
	v_mfma_f32_16x16x32_bf16 v[92:95], v[132:135], v[206:209], v[92:95]
	v_mfma_f32_16x16x32_bf16 v[88:91], v[140:143], v[206:209], v[88:91]
	v_mfma_f32_16x16x32_bf16 v[76:79], v[132:135], v[214:217], v[76:79]
	v_mfma_f32_16x16x32_bf16 v[72:75], v[140:143], v[214:217], v[72:75]
	s_setprio 0
	s_setprio 1
	v_mfma_f32_16x16x32_bf16 v[116:119], v[144:147], v[180:183], v[116:119]
	v_mfma_f32_16x16x32_bf16 v[112:115], v[172:175], v[180:183], v[112:115]
	v_mfma_f32_16x16x32_bf16 v[100:103], v[144:147], v[194:197], v[100:103]
	v_mfma_f32_16x16x32_bf16 v[96:99], v[172:175], v[194:197], v[96:99]
	v_mfma_f32_16x16x32_bf16 v[84:87], v[144:147], v[202:205], v[84:87]
	v_mfma_f32_16x16x32_bf16 v[80:83], v[172:175], v[202:205], v[80:83]
	v_mfma_f32_16x16x32_bf16 v[68:71], v[144:147], v[210:213], v[68:71]
	v_mfma_f32_16x16x32_bf16 v[64:67], v[172:175], v[210:213], v[64:67]
	v_mfma_f32_16x16x32_bf16 v[116:119], v[148:151], v[184:187], v[116:119]
	v_mfma_f32_16x16x32_bf16 v[112:115], v[176:179], v[184:187], v[112:115]
	v_mfma_f32_16x16x32_bf16 v[100:103], v[148:151], v[198:201], v[100:103]
	v_mfma_f32_16x16x32_bf16 v[96:99], v[176:179], v[198:201], v[96:99]
	v_mfma_f32_16x16x32_bf16 v[84:87], v[148:151], v[206:209], v[84:87]
	v_mfma_f32_16x16x32_bf16 v[80:83], v[176:179], v[206:209], v[80:83]
	v_mfma_f32_16x16x32_bf16 v[68:71], v[148:151], v[214:217], v[68:71]
	v_mfma_f32_16x16x32_bf16 v[64:67], v[176:179], v[214:217], v[64:67]
	s_setprio 0
	s_barrier
	s_add_i32 s22, s59, s33
	s_mov_b32 m0, s22
	s_nop 0
	global_load_lds_dwordx4 v154, s[98:99]
	s_add_i32 m0, s22, 0x2000
	s_add_u32 s22, s26, 0xb0080
	s_addc_u32 s23, s27, 0
	s_add_i32 s26, s60, s33
	global_load_lds_dwordx4 v158, s[98:99]
	s_mov_b32 m0, s26
	s_nop 0
	global_load_lds_dwordx4 v154, s[22:23]
	s_add_i32 m0, s26, 0x2000
	s_nop 0
	global_load_lds_dwordx4 v158, s[22:23]
	s_mov_b32 m0, s39
	s_nop 0
	global_load_lds_dwordx4 v152, s[100:101]
	s_mov_b32 m0, s40
	s_nop 0
	global_load_lds_dwordx4 v156, s[100:101]
	ds_read_b128 v[180:183], v192 offset:49152
	ds_read_b128 v[184:187], v192 offset:50176
	ds_read_b128 v[194:197], v192 offset:51200
	ds_read_b128 v[198:201], v192 offset:52224
	ds_read_b128 v[202:205], v192 offset:53248
	ds_read_b128 v[206:209], v192 offset:54272
	ds_read_b128 v[210:213], v192 offset:55296
	ds_read_b128 v[214:217], v192 offset:56320
	s_waitcnt vmcnt(8) lgkmcnt(0)
	s_barrier
	s_setprio 1
	v_mfma_f32_16x16x32_bf16 v[60:63], v[128:131], v[180:183], v[60:63]
	v_mfma_f32_16x16x32_bf16 v[56:59], v[136:139], v[180:183], v[56:59]
	v_mfma_f32_16x16x32_bf16 v[44:47], v[128:131], v[194:197], v[44:47]
	v_mfma_f32_16x16x32_bf16 v[40:43], v[136:139], v[194:197], v[40:43]
	v_mfma_f32_16x16x32_bf16 v[28:31], v[128:131], v[202:205], v[28:31]
	v_mfma_f32_16x16x32_bf16 v[24:27], v[136:139], v[202:205], v[24:27]
	v_mfma_f32_16x16x32_bf16 v[12:15], v[128:131], v[210:213], v[12:15]
	v_mfma_f32_16x16x32_bf16 v[8:11], v[136:139], v[210:213], v[8:11]
	v_mfma_f32_16x16x32_bf16 v[60:63], v[132:135], v[184:187], v[60:63]
	v_mfma_f32_16x16x32_bf16 v[56:59], v[140:143], v[184:187], v[56:59]
	v_mfma_f32_16x16x32_bf16 v[44:47], v[132:135], v[198:201], v[44:47]
	v_mfma_f32_16x16x32_bf16 v[40:43], v[140:143], v[198:201], v[40:43]
	v_mfma_f32_16x16x32_bf16 v[28:31], v[132:135], v[206:209], v[28:31]
	v_mfma_f32_16x16x32_bf16 v[24:27], v[140:143], v[206:209], v[24:27]
	v_mfma_f32_16x16x32_bf16 v[12:15], v[132:135], v[214:217], v[12:15]
	v_mfma_f32_16x16x32_bf16 v[8:11], v[140:143], v[214:217], v[8:11]
	s_setprio 0
	s_setprio 1
	v_mfma_f32_16x16x32_bf16 v[52:55], v[144:147], v[180:183], v[52:55]
	v_mfma_f32_16x16x32_bf16 v[48:51], v[172:175], v[180:183], v[48:51]
	v_mfma_f32_16x16x32_bf16 v[36:39], v[144:147], v[194:197], v[36:39]
	v_mfma_f32_16x16x32_bf16 v[32:35], v[172:175], v[194:197], v[32:35]
	v_mfma_f32_16x16x32_bf16 v[20:23], v[144:147], v[202:205], v[20:23]
	v_mfma_f32_16x16x32_bf16 v[16:19], v[172:175], v[202:205], v[16:19]
	v_mfma_f32_16x16x32_bf16 v[4:7], v[144:147], v[210:213], v[4:7]
	v_mfma_f32_16x16x32_bf16 v[0:3], v[172:175], v[210:213], v[0:3]
	v_mfma_f32_16x16x32_bf16 v[52:55], v[148:151], v[184:187], v[52:55]
	v_mfma_f32_16x16x32_bf16 v[48:51], v[176:179], v[184:187], v[48:51]
	v_mfma_f32_16x16x32_bf16 v[36:39], v[148:151], v[198:201], v[36:39]
	v_mfma_f32_16x16x32_bf16 v[32:35], v[176:179], v[198:201], v[32:35]
	v_mfma_f32_16x16x32_bf16 v[20:23], v[148:151], v[206:209], v[20:23]
	v_mfma_f32_16x16x32_bf16 v[16:19], v[176:179], v[206:209], v[16:19]
	v_mfma_f32_16x16x32_bf16 v[4:7], v[148:151], v[214:217], v[4:7]
	v_mfma_f32_16x16x32_bf16 v[0:3], v[176:179], v[214:217], v[0:3]
	s_setprio 0
	s_barrier
	s_add_i32 s58, s58, 2
	s_add_u32 s56, s56, 0x100
	s_addc_u32 s57, s57, 0
	s_cmp_gt_u32 s58, 41
	s_mov_b64 s[22:23], s[24:25]
	s_cbranch_scc0 .LBB0_2897
	s_and_b64 vcc, exec, s[18:19]
	s_cbranch_vccz .LBB0_2900
	s_barrier
